# adds: carry scan spread over 64 WGs; MoE GEMM K steps: pre-barrier LDS wait counted so trailing fragment reads stay in flight across the barrier
# speedup vs baseline: 1.0232x; 1.0232x over previous
; #define LAS __attribute__((address_space(3)))
;     __device__ __forceinline__ static bf16x8 frag(const bfr* Bb, int wn, int ni, int ks, int lane) {
;         const int g = lane >> 4, q = (lane & 15) >> 2, pp = lane & 3;
;         const bfr* a = Bb + (ks * 16 + 8 * (g >> 1) + q) * KSTR + wn * 64 + ni * 32 + 16 * (g & 1) + 4 * pp;
;         union { v4s16 h[2]; bf16x8 v; } cv;
;         cv.h[0] = __builtin_amdgcn_ds_read_tr16_b64_v4i16((v4s16 LAS*)a);
;         cv.h[1] = __builtin_amdgcn_ds_read_tr16_b64_v4i16((v4s16 LAS*)(a + 4 * KSTR));
;         return cv.v;
;     }
.LBB0_1326:
	s_or_b64 exec, exec, s[2:3]
	v_add_co_u32_e32 v114, vcc, 0x20000, v220
	s_nop 1
	v_addc_co_u32_e32 v115, vcc, 0, v221, vcc
	global_load_dwordx4 v[142:145], v[114:115], off
	global_load_dwordx4 v[134:137], v[114:115], off offset:1024
	global_load_dwordx4 v[118:121], v[114:115], off offset:2048
	s_nop 0
	global_load_dwordx4 v[114:117], v[114:115], off offset:3072
	v_mfma_f32_32x32x16_bf16 v[34:49], v[154:157], v[182:185], v[34:49]
	ds_read_b128 v[154:157], v227 offset:17968
	v_mfma_f32_32x32x16_bf16 v[18:33], v[158:161], v[174:177], v[18:33]
	ds_read_b64_tr_b16 v[174:175], v229
	ds_read_b64_tr_b16 v[176:177], v229 offset:2304
	v_mfma_f32_32x32x16_bf16 v[2:17], v[158:161], v[182:185], v[2:17]
	s_waitcnt lgkmcnt(10)
	v_mfma_f32_32x32x16_bf16 v[82:97], v[162:165], v[178:181], v[82:97]
	ds_read_b128 v[158:161], v227 offset:20528
	ds_read_b64_tr_b16 v[186:187], v230 offset:64
	ds_read_b64_tr_b16 v[188:189], v230 offset:2368
	s_waitcnt lgkmcnt(3)
	s_barrier
	v_mfma_f32_32x32x16_bf16 v[66:81], v[162:165], v[170:173], v[66:81]
	ds_read_b128 v[162:165], v227 offset:30736
	v_mfma_f32_32x32x16_bf16 v[50:65], v[166:169], v[178:181], v[50:65]
	v_mfma_f32_32x32x16_bf16 v[34:49], v[166:169], v[170:173], v[34:49]
	ds_read_b128 v[166:169], v227 offset:33296
	v_mfma_f32_32x32x16_bf16 v[18:33], v[146:149], v[178:181], v[18:33]
	ds_read_b64_tr_b16 v[178:179], v232
	ds_read_b64_tr_b16 v[180:181], v232 offset:2304
	v_mfma_f32_32x32x16_bf16 v[2:17], v[146:149], v[170:173], v[2:17]
	ds_read_b128 v[170:173], v227 offset:35856
	ds_read_b64_tr_b16 v[182:183], v232 offset:64
	ds_read_b64_tr_b16 v[184:185], v232 offset:2368
	v_mfma_f32_32x32x16_bf16 v[82:97], v[150:153], v[174:177], v[82:97]
	s_waitcnt vmcnt(9)
	ds_write_b128 v222, v[138:141] offset:16
	s_and_saveexec_b64 s[2:3], s[4:5]
	ds_write_b128 v223, v[102:105] offset:10256
	s_or_b64 exec, exec, s[2:3]
	s_waitcnt lgkmcnt(9)
	v_mfma_f32_32x32x16_bf16 v[66:81], v[150:153], v[186:189], v[66:81]
	ds_read_b128 v[150:153], v227 offset:30768
	s_waitcnt vmcnt(8)
	v_cvt_pk_bf16_f32 v130, v130, v131
	v_cvt_pk_bf16_f32 v131, v132, v133
	s_waitcnt vmcnt(7)
	v_cvt_pk_bf16_f32 v122, v122, v123
	v_cvt_pk_bf16_f32 v123, v124, v125
	s_waitcnt vmcnt(6)
	v_cvt_pk_bf16_f32 v110, v110, v111
	v_cvt_pk_bf16_f32 v111, v112, v113
	s_waitcnt vmcnt(5)
	v_cvt_pk_bf16_f32 v106, v106, v107
	v_cvt_pk_bf16_f32 v107, v108, v109
	ds_write2_b64 v205, v[130:131], v[122:123] offset0:130 offset1:202
	ds_write2_b64 v206, v[110:111], v[106:107] offset0:18 offset1:90
	v_mfma_f32_32x32x16_bf16 v[50:65], v[154:157], v[174:177], v[50:65]
	global_load_dwordx4 v[130:133], v[208:209], off offset:320
	s_and_saveexec_b64 s[2:3], s[4:5]
	s_cbranch_execz .LBB0_1330
	global_load_dwordx4 v[102:105], v[210:211], off offset:320
.LBB0_1330:
	s_or_b64 exec, exec, s[2:3]
	v_add_co_u32_e32 v106, vcc, 0x28000, v220
	s_nop 1
	v_addc_co_u32_e32 v107, vcc, 0, v221, vcc
	global_load_dwordx4 v[146:149], v[106:107], off
	global_load_dwordx4 v[138:141], v[106:107], off offset:1024
	global_load_dwordx4 v[122:125], v[106:107], off offset:2048
	s_nop 0
	global_load_dwordx4 v[106:109], v[106:107], off offset:3072
	v_mfma_f32_32x32x16_bf16 v[34:49], v[154:157], v[186:189], v[34:49]
	ds_read_b128 v[154:157], v227 offset:33328
	v_mfma_f32_32x32x16_bf16 v[18:33], v[158:161], v[174:177], v[18:33]
	ds_read_b64_tr_b16 v[174:175], v233
	ds_read_b64_tr_b16 v[176:177], v233 offset:2304
	v_mfma_f32_32x32x16_bf16 v[2:17], v[158:161], v[186:189], v[2:17]
	s_waitcnt lgkmcnt(10)
	v_mfma_f32_32x32x16_bf16 v[82:97], v[162:165], v[178:181], v[82:97]
	ds_read_b128 v[158:161], v227 offset:35888
	ds_read_b64_tr_b16 v[186:187], v234 offset:64
	ds_read_b64_tr_b16 v[188:189], v234 offset:2368
	s_waitcnt lgkmcnt(3)
	s_barrier
	v_mfma_f32_32x32x16_bf16 v[66:81], v[162:165], v[182:185], v[66:81]
	ds_read_b128 v[162:165], v227 offset:16
	v_mfma_f32_32x32x16_bf16 v[50:65], v[166:169], v[178:181], v[50:65]
	v_mfma_f32_32x32x16_bf16 v[34:49], v[166:169], v[182:185], v[34:49]
	ds_read_b128 v[166:169], v227 offset:2576
	v_mfma_f32_32x32x16_bf16 v[18:33], v[170:173], v[178:181], v[18:33]
	ds_read_b64_tr_b16 v[178:179], v235 offset:46096
	ds_read_b64_tr_b16 v[180:181], v235 offset:48400
	v_mfma_f32_32x32x16_bf16 v[2:17], v[170:173], v[182:185], v[2:17]
	ds_read_b128 v[170:173], v227 offset:5136
	ds_read_b64_tr_b16 v[182:183], v235 offset:46160
	ds_read_b64_tr_b16 v[184:185], v235 offset:48464
	v_mfma_f32_32x32x16_bf16 v[82:97], v[150:153], v[174:177], v[82:97]
	s_waitcnt vmcnt(9)
	ds_write_b128 v222, v[126:129] offset:15376
	s_and_saveexec_b64 s[2:3], s[4:5]
	ds_write_b128 v223, v[98:101] offset:25616
	s_or_b64 exec, exec, s[2:3]
	s_waitcnt lgkmcnt(9)
	v_mfma_f32_32x32x16_bf16 v[66:81], v[150:153], v[186:189], v[66:81]
	ds_read_b128 v[150:153], v227 offset:48
	s_waitcnt vmcnt(8)
	v_cvt_pk_bf16_f32 v110, v142, v143
	v_cvt_pk_bf16_f32 v111, v144, v145
	s_waitcnt vmcnt(7)
	v_cvt_pk_bf16_f32 v112, v134, v135
	v_cvt_pk_bf16_f32 v113, v136, v137
	ds_write2_b64 v226, v[110:111], v[112:113] offset1:72
	s_waitcnt vmcnt(6)
	v_cvt_pk_bf16_f32 v110, v118, v119
	v_cvt_pk_bf16_f32 v111, v120, v121
	s_waitcnt vmcnt(5)
	v_cvt_pk_bf16_f32 v112, v114, v115
	v_cvt_pk_bf16_f32 v113, v116, v117
	ds_write2_b64 v226, v[110:111], v[112:113] offset0:144 offset1:216
	v_mfma_f32_32x32x16_bf16 v[50:65], v[154:157], v[174:177], v[50:65]
	global_load_dwordx4 v[126:129], v[208:209], off offset:384
	s_and_saveexec_b64 s[2:3], s[4:5]
	s_cbranch_execz .LBB0_1334
	global_load_dwordx4 v[98:101], v[210:211], off offset:384
; #define LAS __attribute__((address_space(3)))
;     __device__ __forceinline__ static bf16x8 frag(const bfr* Bb, int wn, int ni, int ks, int lane) {
;         const int g = lane >> 4, q = (lane & 15) >> 2, pp = lane & 3;
;         const bfr* a = Bb + (ks * 16 + 8 * (g >> 1) + q) * KSTR + wn * 64 + ni * 32 + 16 * (g & 1) + 4 * pp;
;         union { v4s16 h[2]; bf16x8 v; } cv;
;         cv.h[0] = __builtin_amdgcn_ds_read_tr16_b64_v4i16((v4s16 LAS*)a);
;         cv.h[1] = __builtin_amdgcn_ds_read_tr16_b64_v4i16((v4s16 LAS*)(a + 4 * KSTR));
;         return cv.v;
;     }
.LBB0_1334:
	s_or_b64 exec, exec, s[2:3]
	v_add_co_u32_e32 v110, vcc, 0x30000, v220
	s_nop 1
	v_addc_co_u32_e32 v111, vcc, 0, v221, vcc
	global_load_dwordx4 v[142:145], v[110:111], off
	global_load_dwordx4 v[134:137], v[110:111], off offset:1024
	global_load_dwordx4 v[114:117], v[110:111], off offset:2048
	s_nop 0
	global_load_dwordx4 v[110:113], v[110:111], off offset:3072
	v_mfma_f32_32x32x16_bf16 v[34:49], v[154:157], v[186:189], v[34:49]
	ds_read_b128 v[154:157], v227 offset:2608
	v_mfma_f32_32x32x16_bf16 v[18:33], v[158:161], v[174:177], v[18:33]
	ds_read_b64_tr_b16 v[174:175], v235 offset:55312
	ds_read_b64_tr_b16 v[176:177], v235 offset:57616
	v_mfma_f32_32x32x16_bf16 v[2:17], v[158:161], v[186:189], v[2:17]
	s_waitcnt lgkmcnt(10)
	v_mfma_f32_32x32x16_bf16 v[82:97], v[162:165], v[178:181], v[82:97]
	ds_read_b128 v[158:161], v227 offset:5168
	ds_read_b64_tr_b16 v[186:187], v235 offset:55376
	ds_read_b64_tr_b16 v[188:189], v235 offset:57680
	s_waitcnt lgkmcnt(3)
	s_barrier
	v_mfma_f32_32x32x16_bf16 v[66:81], v[162:165], v[182:185], v[66:81]
	ds_read_b128 v[162:165], v227 offset:15376
	v_mfma_f32_32x32x16_bf16 v[50:65], v[166:169], v[178:181], v[50:65]
	v_mfma_f32_32x32x16_bf16 v[34:49], v[166:169], v[182:185], v[34:49]
	ds_read_b128 v[166:169], v227 offset:17936
	v_mfma_f32_32x32x16_bf16 v[18:33], v[170:173], v[178:181], v[18:33]
	ds_read_b64_tr_b16 v[178:179], v228
	ds_read_b64_tr_b16 v[180:181], v228 offset:2304
	v_mfma_f32_32x32x16_bf16 v[2:17], v[170:173], v[182:185], v[2:17]
	ds_read_b128 v[170:173], v227 offset:20496
	ds_read_b64_tr_b16 v[182:183], v228 offset:64
	ds_read_b64_tr_b16 v[184:185], v228 offset:2368
	v_mfma_f32_32x32x16_bf16 v[82:97], v[150:153], v[174:177], v[82:97]
	s_waitcnt vmcnt(9)
	ds_write_b128 v222, v[130:133] offset:30736
	s_and_saveexec_b64 s[2:3], s[4:5]
	ds_write_b128 v223, v[102:105] offset:40976
	s_or_b64 exec, exec, s[2:3]
	s_waitcnt lgkmcnt(9)
	v_mfma_f32_32x32x16_bf16 v[66:81], v[150:153], v[186:189], v[66:81]
	ds_read_b128 v[150:153], v227 offset:15408
	s_waitcnt vmcnt(8)
	v_cvt_pk_bf16_f32 v118, v146, v147
	v_cvt_pk_bf16_f32 v119, v148, v149
	s_waitcnt vmcnt(7)
	v_cvt_pk_bf16_f32 v120, v138, v139
	v_cvt_pk_bf16_f32 v121, v140, v141
	ds_write2_b64 v231, v[118:119], v[120:121] offset1:72
	s_waitcnt vmcnt(6)
	v_cvt_pk_bf16_f32 v118, v122, v123
	v_cvt_pk_bf16_f32 v119, v124, v125
	s_waitcnt vmcnt(5)
	v_cvt_pk_bf16_f32 v106, v106, v107
	v_cvt_pk_bf16_f32 v107, v108, v109
	ds_write2_b64 v231, v[118:119], v[106:107] offset0:144 offset1:216
	v_mfma_f32_32x32x16_bf16 v[50:65], v[154:157], v[174:177], v[50:65]
	global_load_dwordx4 v[122:125], v[208:209], off offset:448
	s_and_saveexec_b64 s[2:3], s[4:5]
	s_cbranch_execz .LBB0_1338
	global_load_dwordx4 v[102:105], v[210:211], off offset:448
.LBB0_1338:
	s_or_b64 exec, exec, s[2:3]
	v_add_co_u32_e32 v106, vcc, 0x38000, v220
	s_nop 1
	v_addc_co_u32_e32 v107, vcc, 0, v221, vcc
	global_load_dwordx4 v[138:141], v[106:107], off
	global_load_dwordx4 v[130:133], v[106:107], off offset:1024
	global_load_dwordx4 v[118:121], v[106:107], off offset:2048
	s_nop 0
	global_load_dwordx4 v[106:109], v[106:107], off offset:3072
	v_mfma_f32_32x32x16_bf16 v[34:49], v[154:157], v[186:189], v[34:49]
	ds_read_b128 v[146:149], v227 offset:17968
	v_mfma_f32_32x32x16_bf16 v[18:33], v[158:161], v[174:177], v[18:33]
	ds_read_b64_tr_b16 v[174:175], v229
	ds_read_b64_tr_b16 v[176:177], v229 offset:2304
	v_mfma_f32_32x32x16_bf16 v[2:17], v[158:161], v[186:189], v[2:17]
	s_waitcnt lgkmcnt(10)
	v_mfma_f32_32x32x16_bf16 v[82:97], v[162:165], v[178:181], v[82:97]
	ds_read_b128 v[154:157], v227 offset:20528
	ds_read_b64_tr_b16 v[186:187], v230 offset:64
	ds_read_b64_tr_b16 v[188:189], v230 offset:2368
	s_waitcnt lgkmcnt(3)
	s_barrier
	v_mfma_f32_32x32x16_bf16 v[66:81], v[162:165], v[182:185], v[66:81]
	ds_read_b128 v[158:161], v227 offset:30736
	v_mfma_f32_32x32x16_bf16 v[50:65], v[166:169], v[178:181], v[50:65]
	v_mfma_f32_32x32x16_bf16 v[34:49], v[166:169], v[182:185], v[34:49]
	ds_read_b128 v[162:165], v227 offset:33296
	v_mfma_f32_32x32x16_bf16 v[18:33], v[170:173], v[178:181], v[18:33]
	ds_read_b64_tr_b16 v[178:179], v232
	ds_read_b64_tr_b16 v[180:181], v232 offset:2304
	v_mfma_f32_32x32x16_bf16 v[2:17], v[170:173], v[182:185], v[2:17]
	ds_read_b128 v[166:169], v227 offset:35856
	ds_read_b64_tr_b16 v[182:183], v232 offset:64
	ds_read_b64_tr_b16 v[184:185], v232 offset:2368
	v_mfma_f32_32x32x16_bf16 v[82:97], v[150:153], v[174:177], v[82:97]
	s_waitcnt vmcnt(9)
	ds_write_b128 v222, v[126:129] offset:16
	s_and_saveexec_b64 s[2:3], s[4:5]
	ds_write_b128 v223, v[98:101] offset:10256
	s_or_b64 exec, exec, s[2:3]
	s_waitcnt lgkmcnt(9)
	v_mfma_f32_32x32x16_bf16 v[66:81], v[150:153], v[186:189], v[66:81]
	ds_read_b128 v[150:153], v227 offset:30768
	s_waitcnt vmcnt(8)
	v_cvt_pk_bf16_f32 v126, v142, v143
	v_cvt_pk_bf16_f32 v127, v144, v145
	s_waitcnt vmcnt(7)
	v_cvt_pk_bf16_f32 v128, v134, v135
	v_cvt_pk_bf16_f32 v129, v136, v137
	s_waitcnt vmcnt(6)
	v_cvt_pk_bf16_f32 v114, v114, v115
	v_cvt_pk_bf16_f32 v115, v116, v117
	s_waitcnt vmcnt(5)
	v_cvt_pk_bf16_f32 v110, v110, v111
	v_cvt_pk_bf16_f32 v111, v112, v113
	ds_write2_b64 v205, v[126:127], v[128:129] offset0:130 offset1:202
	ds_write2_b64 v206, v[114:115], v[110:111] offset0:18 offset1:90
	v_mfma_f32_32x32x16_bf16 v[50:65], v[146:149], v[174:177], v[50:65]
	global_load_dwordx4 v[126:129], v[208:209], off offset:512
	s_and_saveexec_b64 s[2:3], s[4:5]
	s_cbranch_execz .LBB0_1342
	global_load_dwordx4 v[98:101], v[210:211], off offset:512
; #define LAS __attribute__((address_space(3)))
;     __device__ __forceinline__ void st(bfr* base, int id) const {
;         bfr* d = base + ((id >> 6) * 4) * KSTR + (id & 63) * 4;
;         *(u32x2*)(d)            = (u32x2){pack2(v0.x, v0.y), pack2(v0.z, v0.w)};
;         *(u32x2*)(d + KSTR)     = (u32x2){pack2(v1.x, v1.y), pack2(v1.z, v1.w)};
;         *(u32x2*)(d + 2 * KSTR) = (u32x2){pack2(v2.x, v2.y), pack2(v2.z, v2.w)};
;         *(u32x2*)(d + 3 * KSTR) = (u32x2){pack2(v3.x, v3.y), pack2(v3.z, v3.w)};
;     }
;     __device__ __forceinline__ static bf16x8 frag(const bfr* Bb, int wn, int ni, int ks, int lane) {
;         const int g = lane >> 4, q = (lane & 15) >> 2, pp = lane & 3;
;         const bfr* a = Bb + (ks * 16 + 8 * (g >> 1) + q) * KSTR + wn * 64 + ni * 32 + 16 * (g & 1) + 4 * pp;
;         union { v4s16 h[2]; bf16x8 v; } cv;
;         cv.h[0] = __builtin_amdgcn_ds_read_tr16_b64_v4i16((v4s16 LAS*)a);
;         cv.h[1] = __builtin_amdgcn_ds_read_tr16_b64_v4i16((v4s16 LAS*)(a + 4 * KSTR));
;         return cv.v;
;     }
.LBB0_1342:
	s_or_b64 exec, exec, s[2:3]
	v_add_co_u32_e32 v110, vcc, 0x40000, v220
	s_nop 1
	v_addc_co_u32_e32 v111, vcc, 0, v221, vcc
	global_load_dwordx4 v[142:145], v[110:111], off
	global_load_dwordx4 v[134:137], v[110:111], off offset:1024
	global_load_dwordx4 v[114:117], v[110:111], off offset:2048
	s_nop 0
	global_load_dwordx4 v[110:113], v[110:111], off offset:3072
	v_mfma_f32_32x32x16_bf16 v[34:49], v[146:149], v[186:189], v[34:49]
	ds_read_b128 v[146:149], v227 offset:33328
	v_mfma_f32_32x32x16_bf16 v[18:33], v[154:157], v[174:177], v[18:33]
	ds_read_b64_tr_b16 v[174:175], v233
	ds_read_b64_tr_b16 v[176:177], v233 offset:2304
	v_mfma_f32_32x32x16_bf16 v[2:17], v[154:157], v[186:189], v[2:17]
	s_waitcnt lgkmcnt(10)
	v_mfma_f32_32x32x16_bf16 v[82:97], v[158:161], v[178:181], v[82:97]
	ds_read_b128 v[154:157], v227 offset:35888
	ds_read_b64_tr_b16 v[186:187], v234 offset:64
	ds_read_b64_tr_b16 v[188:189], v234 offset:2368
	s_waitcnt lgkmcnt(3)
	s_barrier
	v_mfma_f32_32x32x16_bf16 v[66:81], v[158:161], v[182:185], v[66:81]
	ds_read_b128 v[158:161], v227 offset:16
	v_mfma_f32_32x32x16_bf16 v[50:65], v[162:165], v[178:181], v[50:65]
	v_mfma_f32_32x32x16_bf16 v[34:49], v[162:165], v[182:185], v[34:49]
	ds_read_b128 v[162:165], v227 offset:2576
	v_mfma_f32_32x32x16_bf16 v[18:33], v[166:169], v[178:181], v[18:33]
	ds_read_b64_tr_b16 v[170:171], v235 offset:46096
	ds_read_b64_tr_b16 v[172:173], v235 offset:48400
	v_mfma_f32_32x32x16_bf16 v[2:17], v[166:169], v[182:185], v[2:17]
	ds_read_b128 v[166:169], v227 offset:5136
	ds_read_b64_tr_b16 v[182:183], v235 offset:46160
	ds_read_b64_tr_b16 v[184:185], v235 offset:48464
	v_mfma_f32_32x32x16_bf16 v[82:97], v[150:153], v[174:177], v[82:97]
	s_waitcnt vmcnt(9)
	ds_write_b128 v222, v[122:125] offset:15376
	s_and_saveexec_b64 s[2:3], s[4:5]
	ds_write_b128 v223, v[102:105] offset:25616
	s_or_b64 exec, exec, s[2:3]
	s_waitcnt lgkmcnt(9)
	v_mfma_f32_32x32x16_bf16 v[66:81], v[150:153], v[186:189], v[66:81]
	ds_read_b128 v[150:153], v227 offset:48
	s_waitcnt vmcnt(8)
	v_cvt_pk_bf16_f32 v122, v138, v139
	v_cvt_pk_bf16_f32 v123, v140, v141
	s_waitcnt vmcnt(7)
	v_cvt_pk_bf16_f32 v124, v130, v131
	v_cvt_pk_bf16_f32 v125, v132, v133
	s_waitcnt vmcnt(6)
	v_cvt_pk_bf16_f32 v118, v118, v119
	v_cvt_pk_bf16_f32 v119, v120, v121
	s_waitcnt vmcnt(5)
	v_cvt_pk_bf16_f32 v106, v106, v107
	v_cvt_pk_bf16_f32 v107, v108, v109
	ds_write2_b64 v226, v[122:123], v[124:125] offset1:72
	ds_write2_b64 v226, v[118:119], v[106:107] offset0:144 offset1:216
	v_mfma_f32_32x32x16_bf16 v[50:65], v[146:149], v[174:177], v[50:65]
	global_load_dwordx4 v[122:125], v[208:209], off offset:576
	s_and_saveexec_b64 s[2:3], s[4:5]
	s_cbranch_execz .LBB0_1346
	global_load_dwordx4 v[102:105], v[210:211], off offset:576
.LBB0_1346:
	s_or_b64 exec, exec, s[2:3]
	v_add_co_u32_e32 v106, vcc, 0x48000, v220
	s_nop 1
	v_addc_co_u32_e32 v107, vcc, 0, v221, vcc
	global_load_dwordx4 v[138:141], v[106:107], off
	global_load_dwordx4 v[130:133], v[106:107], off offset:1024
	global_load_dwordx4 v[118:121], v[106:107], off offset:2048
	s_nop 0
	global_load_dwordx4 v[106:109], v[106:107], off offset:3072
	v_mfma_f32_32x32x16_bf16 v[34:49], v[146:149], v[186:189], v[34:49]
	ds_read_b128 v[146:149], v227 offset:2608
	v_mfma_f32_32x32x16_bf16 v[18:33], v[154:157], v[174:177], v[18:33]
	ds_read_b64_tr_b16 v[174:175], v235 offset:55312
	ds_read_b64_tr_b16 v[176:177], v235 offset:57616
	v_mfma_f32_32x32x16_bf16 v[2:17], v[154:157], v[186:189], v[2:17]
	s_waitcnt lgkmcnt(10)
	v_mfma_f32_32x32x16_bf16 v[82:97], v[158:161], v[170:173], v[82:97]
	ds_read_b128 v[154:157], v227 offset:5168
	ds_read_b64_tr_b16 v[178:179], v235 offset:55376
	ds_read_b64_tr_b16 v[180:181], v235 offset:57680
	s_waitcnt lgkmcnt(3)
	s_barrier
	v_mfma_f32_32x32x16_bf16 v[66:81], v[158:161], v[182:185], v[66:81]
	ds_read_b128 v[158:161], v227 offset:15376
	v_mfma_f32_32x32x16_bf16 v[50:65], v[162:165], v[170:173], v[50:65]
	v_mfma_f32_32x32x16_bf16 v[34:49], v[162:165], v[182:185], v[34:49]
	ds_read_b128 v[162:165], v227 offset:17936
	v_mfma_f32_32x32x16_bf16 v[18:33], v[166:169], v[170:173], v[18:33]
	ds_read_b64_tr_b16 v[170:171], v228
	ds_read_b64_tr_b16 v[172:173], v228 offset:2304
	v_mfma_f32_32x32x16_bf16 v[2:17], v[166:169], v[182:185], v[2:17]
	ds_read_b128 v[166:169], v227 offset:20496
	ds_read_b64_tr_b16 v[182:183], v228 offset:64
	ds_read_b64_tr_b16 v[184:185], v228 offset:2368
	v_mfma_f32_32x32x16_bf16 v[82:97], v[150:153], v[174:177], v[82:97]
	s_waitcnt vmcnt(9)
	ds_write_b128 v222, v[126:129] offset:30736
	s_and_saveexec_b64 s[2:3], s[4:5]
	ds_write_b128 v223, v[98:101] offset:40976
	s_or_b64 exec, exec, s[2:3]
	s_waitcnt lgkmcnt(9)
	v_mfma_f32_32x32x16_bf16 v[66:81], v[150:153], v[178:181], v[66:81]
	ds_read_b128 v[150:153], v227 offset:15408
	s_waitcnt vmcnt(8)
	v_cvt_pk_bf16_f32 v126, v142, v143
	v_cvt_pk_bf16_f32 v127, v144, v145
	s_waitcnt vmcnt(7)
	v_cvt_pk_bf16_f32 v128, v134, v135
	v_cvt_pk_bf16_f32 v129, v136, v137
	s_waitcnt vmcnt(6)
	v_cvt_pk_bf16_f32 v114, v114, v115
	v_cvt_pk_bf16_f32 v115, v116, v117
	s_waitcnt vmcnt(5)
	v_cvt_pk_bf16_f32 v110, v110, v111
	v_cvt_pk_bf16_f32 v111, v112, v113
	ds_write2_b64 v231, v[126:127], v[128:129] offset1:72
	ds_write2_b64 v231, v[114:115], v[110:111] offset0:144 offset1:216
	v_mfma_f32_32x32x16_bf16 v[50:65], v[146:149], v[174:177], v[50:65]
	global_load_dwordx4 v[126:129], v[208:209], off offset:640
	s_and_saveexec_b64 s[2:3], s[4:5]
	s_cbranch_execz .LBB0_1350
	global_load_dwordx4 v[98:101], v[210:211], off offset:640
; #define LAS __attribute__((address_space(3)))
;     __device__ __forceinline__ void st(bfr* base, int id) const {
;         bfr* d = base + ((id >> 6) * 4) * KSTR + (id & 63) * 4;
;         *(u32x2*)(d)            = (u32x2){pack2(v0.x, v0.y), pack2(v0.z, v0.w)};
;         *(u32x2*)(d + KSTR)     = (u32x2){pack2(v1.x, v1.y), pack2(v1.z, v1.w)};
;         *(u32x2*)(d + 2 * KSTR) = (u32x2){pack2(v2.x, v2.y), pack2(v2.z, v2.w)};
;         *(u32x2*)(d + 3 * KSTR) = (u32x2){pack2(v3.x, v3.y), pack2(v3.z, v3.w)};
;     }
;     __device__ __forceinline__ static bf16x8 frag(const bfr* Bb, int wn, int ni, int ks, int lane) {
;         const int g = lane >> 4, q = (lane & 15) >> 2, pp = lane & 3;
;         const bfr* a = Bb + (ks * 16 + 8 * (g >> 1) + q) * KSTR + wn * 64 + ni * 32 + 16 * (g & 1) + 4 * pp;
;         union { v4s16 h[2]; bf16x8 v; } cv;
;         cv.h[0] = __builtin_amdgcn_ds_read_tr16_b64_v4i16((v4s16 LAS*)a);
;         cv.h[1] = __builtin_amdgcn_ds_read_tr16_b64_v4i16((v4s16 LAS*)(a + 4 * KSTR));
;         return cv.v;
;     }
.LBB0_1350:
	s_or_b64 exec, exec, s[2:3]
	v_add_co_u32_e32 v110, vcc, 0x50000, v220
	s_nop 1
	v_addc_co_u32_e32 v111, vcc, 0, v221, vcc
	global_load_dwordx4 v[142:145], v[110:111], off
	global_load_dwordx4 v[134:137], v[110:111], off offset:1024
	global_load_dwordx4 v[114:117], v[110:111], off offset:2048
	s_nop 0
	global_load_dwordx4 v[110:113], v[110:111], off offset:3072
	v_mfma_f32_32x32x16_bf16 v[34:49], v[146:149], v[178:181], v[34:49]
	ds_read_b128 v[146:149], v227 offset:17968
	v_mfma_f32_32x32x16_bf16 v[18:33], v[154:157], v[174:177], v[18:33]
	ds_read_b64_tr_b16 v[174:175], v229
	ds_read_b64_tr_b16 v[176:177], v229 offset:2304
	v_mfma_f32_32x32x16_bf16 v[2:17], v[154:157], v[178:181], v[2:17]
	s_waitcnt lgkmcnt(10)
	v_mfma_f32_32x32x16_bf16 v[82:97], v[158:161], v[170:173], v[82:97]
	ds_read_b128 v[154:157], v227 offset:20528
	ds_read_b64_tr_b16 v[178:179], v230 offset:64
	ds_read_b64_tr_b16 v[180:181], v230 offset:2368
	s_waitcnt lgkmcnt(3)
	s_barrier
	v_mfma_f32_32x32x16_bf16 v[66:81], v[158:161], v[182:185], v[66:81]
	ds_read_b128 v[158:161], v227 offset:30736
	v_mfma_f32_32x32x16_bf16 v[50:65], v[162:165], v[170:173], v[50:65]
	v_mfma_f32_32x32x16_bf16 v[34:49], v[162:165], v[182:185], v[34:49]
	ds_read_b128 v[162:165], v227 offset:33296
	v_mfma_f32_32x32x16_bf16 v[18:33], v[166:169], v[170:173], v[18:33]
	ds_read_b64_tr_b16 v[170:171], v232
	ds_read_b64_tr_b16 v[172:173], v232 offset:2304
	v_mfma_f32_32x32x16_bf16 v[2:17], v[166:169], v[182:185], v[2:17]
	ds_read_b128 v[166:169], v227 offset:35856
	ds_read_b64_tr_b16 v[182:183], v232 offset:64
	ds_read_b64_tr_b16 v[184:185], v232 offset:2368
	v_mfma_f32_32x32x16_bf16 v[82:97], v[150:153], v[174:177], v[82:97]
	s_waitcnt vmcnt(9)
	ds_write_b128 v222, v[122:125] offset:16
	s_and_saveexec_b64 s[2:3], s[4:5]
	ds_write_b128 v223, v[102:105] offset:10256
	s_or_b64 exec, exec, s[2:3]
	s_waitcnt lgkmcnt(9)
	v_mfma_f32_32x32x16_bf16 v[66:81], v[150:153], v[178:181], v[66:81]
	ds_read_b128 v[150:153], v227 offset:30768
	s_waitcnt vmcnt(8)
	v_cvt_pk_bf16_f32 v122, v138, v139
	v_cvt_pk_bf16_f32 v123, v140, v141
	s_waitcnt vmcnt(7)
	v_cvt_pk_bf16_f32 v124, v130, v131
	v_cvt_pk_bf16_f32 v125, v132, v133
	s_waitcnt vmcnt(6)
	v_cvt_pk_bf16_f32 v118, v118, v119
	v_cvt_pk_bf16_f32 v119, v120, v121
	s_waitcnt vmcnt(5)
	v_cvt_pk_bf16_f32 v106, v106, v107
	v_cvt_pk_bf16_f32 v107, v108, v109
	ds_write2_b64 v205, v[122:123], v[124:125] offset0:130 offset1:202
	ds_write2_b64 v206, v[118:119], v[106:107] offset0:18 offset1:90
	v_mfma_f32_32x32x16_bf16 v[50:65], v[146:149], v[174:177], v[50:65]
	global_load_dwordx4 v[122:125], v[208:209], off offset:704
	s_and_saveexec_b64 s[2:3], s[4:5]
	s_cbranch_execz .LBB0_1354
	global_load_dwordx4 v[102:105], v[210:211], off offset:704
.LBB0_1354:
	s_or_b64 exec, exec, s[2:3]
	v_add_co_u32_e32 v106, vcc, 0x58000, v220
	s_nop 1
	v_addc_co_u32_e32 v107, vcc, 0, v221, vcc
	global_load_dwordx4 v[138:141], v[106:107], off
	global_load_dwordx4 v[130:133], v[106:107], off offset:1024
	global_load_dwordx4 v[118:121], v[106:107], off offset:2048
	s_nop 0
	global_load_dwordx4 v[106:109], v[106:107], off offset:3072
	v_mfma_f32_32x32x16_bf16 v[34:49], v[146:149], v[178:181], v[34:49]
	ds_read_b128 v[146:149], v227 offset:33328
	v_mfma_f32_32x32x16_bf16 v[18:33], v[154:157], v[174:177], v[18:33]
	ds_read_b64_tr_b16 v[174:175], v233
	ds_read_b64_tr_b16 v[176:177], v233 offset:2304
	v_mfma_f32_32x32x16_bf16 v[2:17], v[154:157], v[178:181], v[2:17]
	s_waitcnt lgkmcnt(10)
	v_mfma_f32_32x32x16_bf16 v[82:97], v[158:161], v[170:173], v[82:97]
	ds_read_b128 v[154:157], v227 offset:35888
	ds_read_b64_tr_b16 v[178:179], v234 offset:64
	ds_read_b64_tr_b16 v[180:181], v234 offset:2368
	s_waitcnt lgkmcnt(3)
	s_barrier
	v_mfma_f32_32x32x16_bf16 v[66:81], v[158:161], v[182:185], v[66:81]
	ds_read_b128 v[158:161], v227 offset:16
	v_mfma_f32_32x32x16_bf16 v[50:65], v[162:165], v[170:173], v[50:65]
	v_mfma_f32_32x32x16_bf16 v[34:49], v[162:165], v[182:185], v[34:49]
	ds_read_b128 v[162:165], v227 offset:2576
	v_mfma_f32_32x32x16_bf16 v[18:33], v[166:169], v[170:173], v[18:33]
	ds_read_b64_tr_b16 v[170:171], v235 offset:46096
	ds_read_b64_tr_b16 v[172:173], v235 offset:48400
	v_mfma_f32_32x32x16_bf16 v[2:17], v[166:169], v[182:185], v[2:17]
	ds_read_b128 v[166:169], v227 offset:5136
	ds_read_b64_tr_b16 v[182:183], v235 offset:46160
	ds_read_b64_tr_b16 v[184:185], v235 offset:48464
	v_mfma_f32_32x32x16_bf16 v[82:97], v[150:153], v[174:177], v[82:97]
	s_waitcnt vmcnt(9)
	ds_write_b128 v222, v[126:129] offset:15376
	s_and_saveexec_b64 s[2:3], s[4:5]
	ds_write_b128 v223, v[98:101] offset:25616
	s_or_b64 exec, exec, s[2:3]
	s_waitcnt lgkmcnt(9)
	v_mfma_f32_32x32x16_bf16 v[66:81], v[150:153], v[178:181], v[66:81]
	ds_read_b128 v[150:153], v227 offset:48
	s_waitcnt vmcnt(8)
	v_cvt_pk_bf16_f32 v126, v142, v143
	v_cvt_pk_bf16_f32 v127, v144, v145
	s_waitcnt vmcnt(7)
	v_cvt_pk_bf16_f32 v128, v134, v135
	v_cvt_pk_bf16_f32 v129, v136, v137
	s_waitcnt vmcnt(6)
	v_cvt_pk_bf16_f32 v114, v114, v115
	v_cvt_pk_bf16_f32 v115, v116, v117
	s_waitcnt vmcnt(5)
	v_cvt_pk_bf16_f32 v110, v110, v111
	v_cvt_pk_bf16_f32 v111, v112, v113
	ds_write2_b64 v226, v[126:127], v[128:129] offset1:72
	ds_write2_b64 v226, v[114:115], v[110:111] offset0:144 offset1:216
	v_mfma_f32_32x32x16_bf16 v[50:65], v[146:149], v[174:177], v[50:65]
	global_load_dwordx4 v[126:129], v[208:209], off offset:768
	s_and_saveexec_b64 s[2:3], s[4:5]
	s_cbranch_execz .LBB0_1358
	global_load_dwordx4 v[98:101], v[210:211], off offset:768
; #define LAS __attribute__((address_space(3)))
;     __device__ __forceinline__ void st(bfr* base, int id) const {
;         bfr* d = base + ((id >> 6) * 4) * KSTR + (id & 63) * 4;
;         *(u32x2*)(d)            = (u32x2){pack2(v0.x, v0.y), pack2(v0.z, v0.w)};
;         *(u32x2*)(d + KSTR)     = (u32x2){pack2(v1.x, v1.y), pack2(v1.z, v1.w)};
;         *(u32x2*)(d + 2 * KSTR) = (u32x2){pack2(v2.x, v2.y), pack2(v2.z, v2.w)};
;         *(u32x2*)(d + 3 * KSTR) = (u32x2){pack2(v3.x, v3.y), pack2(v3.z, v3.w)};
;     }
;     __device__ __forceinline__ static bf16x8 frag(const bfr* Bb, int wn, int ni, int ks, int lane) {
;         const int g = lane >> 4, q = (lane & 15) >> 2, pp = lane & 3;
;         const bfr* a = Bb + (ks * 16 + 8 * (g >> 1) + q) * KSTR + wn * 64 + ni * 32 + 16 * (g & 1) + 4 * pp;
;         union { v4s16 h[2]; bf16x8 v; } cv;
;         cv.h[0] = __builtin_amdgcn_ds_read_tr16_b64_v4i16((v4s16 LAS*)a);
;         cv.h[1] = __builtin_amdgcn_ds_read_tr16_b64_v4i16((v4s16 LAS*)(a + 4 * KSTR));
;         return cv.v;
;     }
.LBB0_1358:
	s_or_b64 exec, exec, s[2:3]
	v_add_co_u32_e32 v110, vcc, 0x60000, v220
	s_nop 1
	v_addc_co_u32_e32 v111, vcc, 0, v221, vcc
	global_load_dwordx4 v[142:145], v[110:111], off
	global_load_dwordx4 v[134:137], v[110:111], off offset:1024
	global_load_dwordx4 v[114:117], v[110:111], off offset:2048
	s_nop 0
	global_load_dwordx4 v[110:113], v[110:111], off offset:3072
	v_mfma_f32_32x32x16_bf16 v[34:49], v[146:149], v[178:181], v[34:49]
	ds_read_b128 v[146:149], v227 offset:2608
	v_mfma_f32_32x32x16_bf16 v[18:33], v[154:157], v[174:177], v[18:33]
	ds_read_b64_tr_b16 v[174:175], v235 offset:55312
	ds_read_b64_tr_b16 v[176:177], v235 offset:57616
	v_mfma_f32_32x32x16_bf16 v[2:17], v[154:157], v[178:181], v[2:17]
	s_waitcnt lgkmcnt(10)
	v_mfma_f32_32x32x16_bf16 v[82:97], v[158:161], v[170:173], v[82:97]
	ds_read_b128 v[154:157], v227 offset:5168
	ds_read_b64_tr_b16 v[178:179], v235 offset:55376
	ds_read_b64_tr_b16 v[180:181], v235 offset:57680
	s_waitcnt lgkmcnt(3)
	s_barrier
	v_mfma_f32_32x32x16_bf16 v[66:81], v[158:161], v[182:185], v[66:81]
	ds_read_b128 v[158:161], v227 offset:15376
	v_mfma_f32_32x32x16_bf16 v[50:65], v[162:165], v[170:173], v[50:65]
	v_mfma_f32_32x32x16_bf16 v[34:49], v[162:165], v[182:185], v[34:49]
	ds_read_b128 v[162:165], v227 offset:17936
	v_mfma_f32_32x32x16_bf16 v[18:33], v[166:169], v[170:173], v[18:33]
	ds_read_b64_tr_b16 v[170:171], v228
	ds_read_b64_tr_b16 v[172:173], v228 offset:2304
	v_mfma_f32_32x32x16_bf16 v[2:17], v[166:169], v[182:185], v[2:17]
	ds_read_b128 v[166:169], v227 offset:20496
	ds_read_b64_tr_b16 v[182:183], v228 offset:64
	ds_read_b64_tr_b16 v[184:185], v228 offset:2368
	v_mfma_f32_32x32x16_bf16 v[82:97], v[150:153], v[174:177], v[82:97]
	s_waitcnt vmcnt(9)
	ds_write_b128 v222, v[122:125] offset:30736
	s_and_saveexec_b64 s[2:3], s[4:5]
	ds_write_b128 v223, v[102:105] offset:40976
	s_or_b64 exec, exec, s[2:3]
	s_waitcnt lgkmcnt(9)
	v_mfma_f32_32x32x16_bf16 v[66:81], v[150:153], v[178:181], v[66:81]
	ds_read_b128 v[150:153], v227 offset:15408
	s_waitcnt vmcnt(8)
	v_cvt_pk_bf16_f32 v122, v138, v139
	v_cvt_pk_bf16_f32 v123, v140, v141
	s_waitcnt vmcnt(7)
	v_cvt_pk_bf16_f32 v124, v130, v131
	v_cvt_pk_bf16_f32 v125, v132, v133
	s_waitcnt vmcnt(6)
	v_cvt_pk_bf16_f32 v118, v118, v119
	v_cvt_pk_bf16_f32 v119, v120, v121
	s_waitcnt vmcnt(5)
	v_cvt_pk_bf16_f32 v106, v106, v107
	v_cvt_pk_bf16_f32 v107, v108, v109
	ds_write2_b64 v231, v[122:123], v[124:125] offset1:72
	ds_write2_b64 v231, v[118:119], v[106:107] offset0:144 offset1:216
	v_mfma_f32_32x32x16_bf16 v[50:65], v[146:149], v[174:177], v[50:65]
	global_load_dwordx4 v[122:125], v[208:209], off offset:832
	s_and_saveexec_b64 s[2:3], s[4:5]
	s_cbranch_execz .LBB0_1362
	global_load_dwordx4 v[102:105], v[210:211], off offset:832
.LBB0_1362:
	s_or_b64 exec, exec, s[2:3]
	v_add_co_u32_e32 v106, vcc, 0x68000, v220
	s_nop 1
	v_addc_co_u32_e32 v107, vcc, 0, v221, vcc
	global_load_dwordx4 v[138:141], v[106:107], off
	global_load_dwordx4 v[130:133], v[106:107], off offset:1024
	global_load_dwordx4 v[118:121], v[106:107], off offset:2048
	s_nop 0
	global_load_dwordx4 v[106:109], v[106:107], off offset:3072
	v_mfma_f32_32x32x16_bf16 v[34:49], v[146:149], v[178:181], v[34:49]
	ds_read_b128 v[146:149], v227 offset:17968
	v_mfma_f32_32x32x16_bf16 v[18:33], v[154:157], v[174:177], v[18:33]
	ds_read_b64_tr_b16 v[174:175], v229
	ds_read_b64_tr_b16 v[176:177], v229 offset:2304
	v_mfma_f32_32x32x16_bf16 v[2:17], v[154:157], v[178:181], v[2:17]
	s_waitcnt lgkmcnt(10)
	v_mfma_f32_32x32x16_bf16 v[82:97], v[158:161], v[170:173], v[82:97]
	ds_read_b128 v[154:157], v227 offset:20528
	ds_read_b64_tr_b16 v[178:179], v230 offset:64
	ds_read_b64_tr_b16 v[180:181], v230 offset:2368
	s_waitcnt lgkmcnt(3)
	s_barrier
	v_mfma_f32_32x32x16_bf16 v[66:81], v[158:161], v[182:185], v[66:81]
	ds_read_b128 v[158:161], v227 offset:30736
	v_mfma_f32_32x32x16_bf16 v[50:65], v[162:165], v[170:173], v[50:65]
	v_mfma_f32_32x32x16_bf16 v[34:49], v[162:165], v[182:185], v[34:49]
	ds_read_b128 v[162:165], v227 offset:33296
	v_mfma_f32_32x32x16_bf16 v[18:33], v[166:169], v[170:173], v[18:33]
	ds_read_b64_tr_b16 v[170:171], v232
	ds_read_b64_tr_b16 v[172:173], v232 offset:2304
	v_mfma_f32_32x32x16_bf16 v[2:17], v[166:169], v[182:185], v[2:17]
	ds_read_b128 v[166:169], v227 offset:35856
	ds_read_b64_tr_b16 v[182:183], v232 offset:64
	ds_read_b64_tr_b16 v[184:185], v232 offset:2368
	v_mfma_f32_32x32x16_bf16 v[82:97], v[150:153], v[174:177], v[82:97]
	s_waitcnt vmcnt(9)
	ds_write_b128 v222, v[126:129] offset:16
	s_and_saveexec_b64 s[2:3], s[4:5]
	ds_write_b128 v223, v[98:101] offset:10256
	s_or_b64 exec, exec, s[2:3]
	s_waitcnt lgkmcnt(9)
	v_mfma_f32_32x32x16_bf16 v[66:81], v[150:153], v[178:181], v[66:81]
	ds_read_b128 v[150:153], v227 offset:30768
	s_waitcnt vmcnt(8)
	v_cvt_pk_bf16_f32 v126, v142, v143
	v_cvt_pk_bf16_f32 v127, v144, v145
	s_waitcnt vmcnt(7)
	v_cvt_pk_bf16_f32 v128, v134, v135
	v_cvt_pk_bf16_f32 v129, v136, v137
	s_waitcnt vmcnt(6)
	v_cvt_pk_bf16_f32 v114, v114, v115
	v_cvt_pk_bf16_f32 v115, v116, v117
	s_waitcnt vmcnt(5)
	v_cvt_pk_bf16_f32 v110, v110, v111
	v_cvt_pk_bf16_f32 v111, v112, v113
	ds_write2_b64 v205, v[126:127], v[128:129] offset0:130 offset1:202
	ds_write2_b64 v206, v[114:115], v[110:111] offset0:18 offset1:90
	v_mfma_f32_32x32x16_bf16 v[50:65], v[146:149], v[174:177], v[50:65]
	global_load_dwordx4 v[126:129], v[208:209], off offset:896
	s_and_saveexec_b64 s[2:3], s[4:5]
	s_cbranch_execz .LBB0_1366
	global_load_dwordx4 v[98:101], v[210:211], off offset:896
; #define LAS __attribute__((address_space(3)))
;     __device__ __forceinline__ void st(bfr* base, int id) const {
;         bfr* d = base + ((id >> 6) * 4) * KSTR + (id & 63) * 4;
;         *(u32x2*)(d)            = (u32x2){pack2(v0.x, v0.y), pack2(v0.z, v0.w)};
;         *(u32x2*)(d + KSTR)     = (u32x2){pack2(v1.x, v1.y), pack2(v1.z, v1.w)};
;         *(u32x2*)(d + 2 * KSTR) = (u32x2){pack2(v2.x, v2.y), pack2(v2.z, v2.w)};
;         *(u32x2*)(d + 3 * KSTR) = (u32x2){pack2(v3.x, v3.y), pack2(v3.z, v3.w)};
;     }
;     __device__ __forceinline__ static bf16x8 frag(const bfr* Bb, int wn, int ni, int ks, int lane) {
;         const int g = lane >> 4, q = (lane & 15) >> 2, pp = lane & 3;
;         const bfr* a = Bb + (ks * 16 + 8 * (g >> 1) + q) * KSTR + wn * 64 + ni * 32 + 16 * (g & 1) + 4 * pp;
;         union { v4s16 h[2]; bf16x8 v; } cv;
;         cv.h[0] = __builtin_amdgcn_ds_read_tr16_b64_v4i16((v4s16 LAS*)a);
;         cv.h[1] = __builtin_amdgcn_ds_read_tr16_b64_v4i16((v4s16 LAS*)(a + 4 * KSTR));
;         return cv.v;
;     }
.LBB0_1366:
	s_or_b64 exec, exec, s[2:3]
	v_add_co_u32_e32 v110, vcc, 0x70000, v220
	s_nop 1
	v_addc_co_u32_e32 v111, vcc, 0, v221, vcc
	global_load_dwordx4 v[142:145], v[110:111], off
	global_load_dwordx4 v[134:137], v[110:111], off offset:1024
	global_load_dwordx4 v[114:117], v[110:111], off offset:2048
	s_nop 0
	global_load_dwordx4 v[110:113], v[110:111], off offset:3072
	v_mfma_f32_32x32x16_bf16 v[34:49], v[146:149], v[178:181], v[34:49]
	ds_read_b128 v[146:149], v227 offset:33328
	v_mfma_f32_32x32x16_bf16 v[18:33], v[154:157], v[174:177], v[18:33]
	ds_read_b64_tr_b16 v[174:175], v233
	ds_read_b64_tr_b16 v[176:177], v233 offset:2304
	v_mfma_f32_32x32x16_bf16 v[2:17], v[154:157], v[178:181], v[2:17]
	s_waitcnt lgkmcnt(10)
	v_mfma_f32_32x32x16_bf16 v[82:97], v[158:161], v[170:173], v[82:97]
	ds_read_b128 v[154:157], v227 offset:35888
	ds_read_b64_tr_b16 v[178:179], v234 offset:64
	ds_read_b64_tr_b16 v[180:181], v234 offset:2368
	s_waitcnt lgkmcnt(3)
	s_barrier
	v_mfma_f32_32x32x16_bf16 v[66:81], v[158:161], v[182:185], v[66:81]
	ds_read_b128 v[158:161], v227 offset:16
	v_mfma_f32_32x32x16_bf16 v[50:65], v[162:165], v[170:173], v[50:65]
	v_mfma_f32_32x32x16_bf16 v[34:49], v[162:165], v[182:185], v[34:49]
	ds_read_b128 v[162:165], v227 offset:2576
	v_mfma_f32_32x32x16_bf16 v[18:33], v[166:169], v[170:173], v[18:33]
	ds_read_b64_tr_b16 v[170:171], v235 offset:46096
	ds_read_b64_tr_b16 v[172:173], v235 offset:48400
	v_mfma_f32_32x32x16_bf16 v[2:17], v[166:169], v[182:185], v[2:17]
	ds_read_b128 v[166:169], v227 offset:5136
	ds_read_b64_tr_b16 v[182:183], v235 offset:46160
	ds_read_b64_tr_b16 v[184:185], v235 offset:48464
	v_mfma_f32_32x32x16_bf16 v[82:97], v[150:153], v[174:177], v[82:97]
	s_waitcnt vmcnt(9)
	ds_write_b128 v222, v[122:125] offset:15376
	s_and_saveexec_b64 s[2:3], s[4:5]
	ds_write_b128 v223, v[102:105] offset:25616
	s_or_b64 exec, exec, s[2:3]
	s_waitcnt lgkmcnt(9)
	v_mfma_f32_32x32x16_bf16 v[66:81], v[150:153], v[178:181], v[66:81]
	ds_read_b128 v[150:153], v227 offset:48
	s_waitcnt vmcnt(8)
	v_cvt_pk_bf16_f32 v122, v138, v139
	v_cvt_pk_bf16_f32 v123, v140, v141
	s_waitcnt vmcnt(7)
	v_cvt_pk_bf16_f32 v124, v130, v131
	v_cvt_pk_bf16_f32 v125, v132, v133
	s_waitcnt vmcnt(6)
	v_cvt_pk_bf16_f32 v118, v118, v119
	v_cvt_pk_bf16_f32 v119, v120, v121
	s_waitcnt vmcnt(5)
	v_cvt_pk_bf16_f32 v106, v106, v107
	v_cvt_pk_bf16_f32 v107, v108, v109
	ds_write2_b64 v226, v[122:123], v[124:125] offset1:72
	ds_write2_b64 v226, v[118:119], v[106:107] offset0:144 offset1:216
	v_mfma_f32_32x32x16_bf16 v[50:65], v[146:149], v[174:177], v[50:65]
	global_load_dwordx4 v[122:125], v[208:209], off offset:960
	s_and_saveexec_b64 s[2:3], s[4:5]
	s_cbranch_execz .LBB0_1370
	global_load_dwordx4 v[102:105], v[210:211], off offset:960
.LBB0_1370:
	s_or_b64 exec, exec, s[2:3]
	v_add_co_u32_e32 v106, vcc, 0x78000, v220
	s_nop 1
	v_addc_co_u32_e32 v107, vcc, 0, v221, vcc
	global_load_dwordx4 v[138:141], v[106:107], off
	global_load_dwordx4 v[130:133], v[106:107], off offset:1024
	global_load_dwordx4 v[118:121], v[106:107], off offset:2048
	s_nop 0
	global_load_dwordx4 v[106:109], v[106:107], off offset:3072
	v_mfma_f32_32x32x16_bf16 v[34:49], v[146:149], v[178:181], v[34:49]
	ds_read_b128 v[146:149], v227 offset:2608
	v_mfma_f32_32x32x16_bf16 v[18:33], v[154:157], v[174:177], v[18:33]
	ds_read_b64_tr_b16 v[174:175], v235 offset:55312
	ds_read_b64_tr_b16 v[176:177], v235 offset:57616
	v_mfma_f32_32x32x16_bf16 v[2:17], v[154:157], v[178:181], v[2:17]
	s_waitcnt lgkmcnt(10)
	v_mfma_f32_32x32x16_bf16 v[82:97], v[158:161], v[170:173], v[82:97]
	ds_read_b128 v[154:157], v227 offset:5168
	ds_read_b64_tr_b16 v[178:179], v235 offset:55376
	ds_read_b64_tr_b16 v[180:181], v235 offset:57680
	s_waitcnt lgkmcnt(3)
	s_barrier
	v_mfma_f32_32x32x16_bf16 v[66:81], v[158:161], v[182:185], v[66:81]
	ds_read_b128 v[158:161], v227 offset:15376
	v_mfma_f32_32x32x16_bf16 v[50:65], v[162:165], v[170:173], v[50:65]
	v_mfma_f32_32x32x16_bf16 v[34:49], v[162:165], v[182:185], v[34:49]
	ds_read_b128 v[162:165], v227 offset:17936
	v_mfma_f32_32x32x16_bf16 v[18:33], v[166:169], v[170:173], v[18:33]
	ds_read_b64_tr_b16 v[170:171], v228
	ds_read_b64_tr_b16 v[172:173], v228 offset:2304
	v_mfma_f32_32x32x16_bf16 v[2:17], v[166:169], v[182:185], v[2:17]
	ds_read_b128 v[166:169], v227 offset:20496
	ds_read_b64_tr_b16 v[182:183], v228 offset:64
	ds_read_b64_tr_b16 v[184:185], v228 offset:2368
	v_mfma_f32_32x32x16_bf16 v[82:97], v[150:153], v[174:177], v[82:97]
	s_waitcnt vmcnt(9)
	ds_write_b128 v222, v[126:129] offset:30736
	s_and_saveexec_b64 s[2:3], s[4:5]
	ds_write_b128 v223, v[98:101] offset:40976
	s_or_b64 exec, exec, s[2:3]
	s_waitcnt lgkmcnt(9)
	v_mfma_f32_32x32x16_bf16 v[66:81], v[150:153], v[178:181], v[66:81]
	ds_read_b128 v[150:153], v227 offset:15408
	s_waitcnt vmcnt(8)
	v_cvt_pk_bf16_f32 v126, v142, v143
	v_cvt_pk_bf16_f32 v127, v144, v145
	s_waitcnt vmcnt(7)
	v_cvt_pk_bf16_f32 v128, v134, v135
	v_cvt_pk_bf16_f32 v129, v136, v137
	s_waitcnt vmcnt(6)
	v_cvt_pk_bf16_f32 v114, v114, v115
	v_cvt_pk_bf16_f32 v115, v116, v117
	s_waitcnt vmcnt(5)
	v_cvt_pk_bf16_f32 v110, v110, v111
	v_cvt_pk_bf16_f32 v111, v112, v113
	ds_write2_b64 v231, v[126:127], v[128:129] offset1:72
	ds_write2_b64 v231, v[114:115], v[110:111] offset0:144 offset1:216
	v_mfma_f32_32x32x16_bf16 v[50:65], v[146:149], v[174:177], v[50:65]
	global_load_dwordx4 v[126:129], v[208:209], off offset:1024
	s_and_saveexec_b64 s[2:3], s[4:5]
	s_cbranch_execz .LBB0_1374
	global_load_dwordx4 v[98:101], v[210:211], off offset:1024
; #define LAS __attribute__((address_space(3)))
;     __device__ __forceinline__ void st(bfr* base, int id) const {
;         bfr* d = base + ((id >> 6) * 4) * KSTR + (id & 63) * 4;
;         *(u32x2*)(d)            = (u32x2){pack2(v0.x, v0.y), pack2(v0.z, v0.w)};
;         *(u32x2*)(d + KSTR)     = (u32x2){pack2(v1.x, v1.y), pack2(v1.z, v1.w)};
;         *(u32x2*)(d + 2 * KSTR) = (u32x2){pack2(v2.x, v2.y), pack2(v2.z, v2.w)};
;         *(u32x2*)(d + 3 * KSTR) = (u32x2){pack2(v3.x, v3.y), pack2(v3.z, v3.w)};
;     }
;     __device__ __forceinline__ static bf16x8 frag(const bfr* Bb, int wn, int ni, int ks, int lane) {
;         const int g = lane >> 4, q = (lane & 15) >> 2, pp = lane & 3;
;         const bfr* a = Bb + (ks * 16 + 8 * (g >> 1) + q) * KSTR + wn * 64 + ni * 32 + 16 * (g & 1) + 4 * pp;
;         union { v4s16 h[2]; bf16x8 v; } cv;
;         cv.h[0] = __builtin_amdgcn_ds_read_tr16_b64_v4i16((v4s16 LAS*)a);
;         cv.h[1] = __builtin_amdgcn_ds_read_tr16_b64_v4i16((v4s16 LAS*)(a + 4 * KSTR));
;         return cv.v;
;     }
.LBB0_1374:
	s_or_b64 exec, exec, s[2:3]
	v_add_co_u32_e32 v110, vcc, 0x80000, v220
	s_nop 1
	v_addc_co_u32_e32 v111, vcc, 0, v221, vcc
	global_load_dwordx4 v[142:145], v[110:111], off
	global_load_dwordx4 v[134:137], v[110:111], off offset:1024
	global_load_dwordx4 v[114:117], v[110:111], off offset:2048
	s_nop 0
	global_load_dwordx4 v[110:113], v[110:111], off offset:3072
	v_mfma_f32_32x32x16_bf16 v[34:49], v[146:149], v[178:181], v[34:49]
	ds_read_b128 v[146:149], v227 offset:17968
	v_mfma_f32_32x32x16_bf16 v[18:33], v[154:157], v[174:177], v[18:33]
	ds_read_b64_tr_b16 v[174:175], v229
	ds_read_b64_tr_b16 v[176:177], v229 offset:2304
	v_mfma_f32_32x32x16_bf16 v[2:17], v[154:157], v[178:181], v[2:17]
	s_waitcnt lgkmcnt(10)
	v_mfma_f32_32x32x16_bf16 v[82:97], v[158:161], v[170:173], v[82:97]
	ds_read_b128 v[154:157], v227 offset:20528
	ds_read_b64_tr_b16 v[178:179], v230 offset:64
	ds_read_b64_tr_b16 v[180:181], v230 offset:2368
	s_waitcnt lgkmcnt(3)
	s_barrier
	v_mfma_f32_32x32x16_bf16 v[66:81], v[158:161], v[182:185], v[66:81]
	ds_read_b128 v[158:161], v227 offset:30736
	v_mfma_f32_32x32x16_bf16 v[50:65], v[162:165], v[170:173], v[50:65]
	v_mfma_f32_32x32x16_bf16 v[34:49], v[162:165], v[182:185], v[34:49]
	ds_read_b128 v[162:165], v227 offset:33296
	v_mfma_f32_32x32x16_bf16 v[18:33], v[166:169], v[170:173], v[18:33]
	ds_read_b64_tr_b16 v[170:171], v232
	ds_read_b64_tr_b16 v[172:173], v232 offset:2304
	v_mfma_f32_32x32x16_bf16 v[2:17], v[166:169], v[182:185], v[2:17]
	ds_read_b128 v[166:169], v227 offset:35856
	ds_read_b64_tr_b16 v[182:183], v232 offset:64
	ds_read_b64_tr_b16 v[184:185], v232 offset:2368
	v_mfma_f32_32x32x16_bf16 v[82:97], v[150:153], v[174:177], v[82:97]
	s_waitcnt vmcnt(9)
	ds_write_b128 v222, v[122:125] offset:16
	s_and_saveexec_b64 s[2:3], s[4:5]
	ds_write_b128 v223, v[102:105] offset:10256
	s_or_b64 exec, exec, s[2:3]
	s_waitcnt lgkmcnt(9)
	v_mfma_f32_32x32x16_bf16 v[66:81], v[150:153], v[178:181], v[66:81]
	ds_read_b128 v[150:153], v227 offset:30768
	s_waitcnt vmcnt(8)
	v_cvt_pk_bf16_f32 v122, v138, v139
	v_cvt_pk_bf16_f32 v123, v140, v141
	s_waitcnt vmcnt(7)
	v_cvt_pk_bf16_f32 v124, v130, v131
	v_cvt_pk_bf16_f32 v125, v132, v133
	s_waitcnt vmcnt(6)
	v_cvt_pk_bf16_f32 v118, v118, v119
	v_cvt_pk_bf16_f32 v119, v120, v121
	s_waitcnt vmcnt(5)
	v_cvt_pk_bf16_f32 v106, v106, v107
	v_cvt_pk_bf16_f32 v107, v108, v109
	ds_write2_b64 v205, v[122:123], v[124:125] offset0:130 offset1:202
	ds_write2_b64 v206, v[118:119], v[106:107] offset0:18 offset1:90
	v_mfma_f32_32x32x16_bf16 v[50:65], v[146:149], v[174:177], v[50:65]
	global_load_dwordx4 v[122:125], v[208:209], off offset:1088
	s_and_saveexec_b64 s[2:3], s[4:5]
	s_cbranch_execz .LBB0_1378
	global_load_dwordx4 v[102:105], v[210:211], off offset:1088
.LBB0_1378:
	s_or_b64 exec, exec, s[2:3]
	v_add_co_u32_e32 v106, vcc, 0x88000, v220
	s_nop 1
	v_addc_co_u32_e32 v107, vcc, 0, v221, vcc
	global_load_dwordx4 v[138:141], v[106:107], off
	global_load_dwordx4 v[130:133], v[106:107], off offset:1024
	global_load_dwordx4 v[118:121], v[106:107], off offset:2048
	s_nop 0
	global_load_dwordx4 v[106:109], v[106:107], off offset:3072
	v_mfma_f32_32x32x16_bf16 v[34:49], v[146:149], v[178:181], v[34:49]
	ds_read_b128 v[146:149], v227 offset:33328
	v_mfma_f32_32x32x16_bf16 v[18:33], v[154:157], v[174:177], v[18:33]
	ds_read_b64_tr_b16 v[174:175], v233
	ds_read_b64_tr_b16 v[176:177], v233 offset:2304
	v_mfma_f32_32x32x16_bf16 v[2:17], v[154:157], v[178:181], v[2:17]
	s_waitcnt lgkmcnt(10)
	v_mfma_f32_32x32x16_bf16 v[82:97], v[158:161], v[170:173], v[82:97]
	ds_read_b128 v[154:157], v227 offset:35888
	ds_read_b64_tr_b16 v[178:179], v234 offset:64
	ds_read_b64_tr_b16 v[180:181], v234 offset:2368
	s_waitcnt lgkmcnt(3)
	s_barrier
	v_mfma_f32_32x32x16_bf16 v[66:81], v[158:161], v[182:185], v[66:81]
	ds_read_b128 v[158:161], v227 offset:16
	v_mfma_f32_32x32x16_bf16 v[50:65], v[162:165], v[170:173], v[50:65]
	v_mfma_f32_32x32x16_bf16 v[34:49], v[162:165], v[182:185], v[34:49]
	ds_read_b128 v[162:165], v227 offset:2576
	v_mfma_f32_32x32x16_bf16 v[18:33], v[166:169], v[170:173], v[18:33]
	ds_read_b64_tr_b16 v[170:171], v235 offset:46096
	ds_read_b64_tr_b16 v[172:173], v235 offset:48400
	v_mfma_f32_32x32x16_bf16 v[2:17], v[166:169], v[182:185], v[2:17]
	ds_read_b128 v[166:169], v227 offset:5136
	ds_read_b64_tr_b16 v[182:183], v235 offset:46160
	ds_read_b64_tr_b16 v[184:185], v235 offset:48464
	v_mfma_f32_32x32x16_bf16 v[82:97], v[150:153], v[174:177], v[82:97]
	s_waitcnt vmcnt(9)
	ds_write_b128 v222, v[126:129] offset:15376
	s_and_saveexec_b64 s[2:3], s[4:5]
	ds_write_b128 v223, v[98:101] offset:25616
	s_or_b64 exec, exec, s[2:3]
	s_waitcnt lgkmcnt(9)
	v_mfma_f32_32x32x16_bf16 v[66:81], v[150:153], v[178:181], v[66:81]
	ds_read_b128 v[150:153], v227 offset:48
	s_waitcnt vmcnt(8)
	v_cvt_pk_bf16_f32 v126, v142, v143
	v_cvt_pk_bf16_f32 v127, v144, v145
	s_waitcnt vmcnt(7)
	v_cvt_pk_bf16_f32 v128, v134, v135
	v_cvt_pk_bf16_f32 v129, v136, v137
	s_waitcnt vmcnt(6)
	v_cvt_pk_bf16_f32 v114, v114, v115
	v_cvt_pk_bf16_f32 v115, v116, v117
	s_waitcnt vmcnt(5)
	v_cvt_pk_bf16_f32 v110, v110, v111
	v_cvt_pk_bf16_f32 v111, v112, v113
	ds_write2_b64 v226, v[126:127], v[128:129] offset1:72
	ds_write2_b64 v226, v[114:115], v[110:111] offset0:144 offset1:216
	v_mfma_f32_32x32x16_bf16 v[50:65], v[146:149], v[174:177], v[50:65]
	global_load_dwordx4 v[126:129], v[208:209], off offset:1152
	s_and_saveexec_b64 s[2:3], s[4:5]
	s_cbranch_execz .LBB0_1382
	global_load_dwordx4 v[98:101], v[210:211], off offset:1152
; #define LAS __attribute__((address_space(3)))
;     __device__ __forceinline__ void st(bfr* base, int id) const {
;         bfr* d = base + ((id >> 6) * 4) * KSTR + (id & 63) * 4;
;         *(u32x2*)(d)            = (u32x2){pack2(v0.x, v0.y), pack2(v0.z, v0.w)};
;         *(u32x2*)(d + KSTR)     = (u32x2){pack2(v1.x, v1.y), pack2(v1.z, v1.w)};
;         *(u32x2*)(d + 2 * KSTR) = (u32x2){pack2(v2.x, v2.y), pack2(v2.z, v2.w)};
;         *(u32x2*)(d + 3 * KSTR) = (u32x2){pack2(v3.x, v3.y), pack2(v3.z, v3.w)};
;     }
;     __device__ __forceinline__ static bf16x8 frag(const bfr* Bb, int wn, int ni, int ks, int lane) {
;         const int g = lane >> 4, q = (lane & 15) >> 2, pp = lane & 3;
;         const bfr* a = Bb + (ks * 16 + 8 * (g >> 1) + q) * KSTR + wn * 64 + ni * 32 + 16 * (g & 1) + 4 * pp;
;         union { v4s16 h[2]; bf16x8 v; } cv;
;         cv.h[0] = __builtin_amdgcn_ds_read_tr16_b64_v4i16((v4s16 LAS*)a);
;         cv.h[1] = __builtin_amdgcn_ds_read_tr16_b64_v4i16((v4s16 LAS*)(a + 4 * KSTR));
;         return cv.v;
;     }
.LBB0_1382:
	s_or_b64 exec, exec, s[2:3]
	v_add_co_u32_e32 v110, vcc, 0x90000, v220
	s_nop 1
	v_addc_co_u32_e32 v111, vcc, 0, v221, vcc
	global_load_dwordx4 v[142:145], v[110:111], off
	global_load_dwordx4 v[134:137], v[110:111], off offset:1024
	global_load_dwordx4 v[114:117], v[110:111], off offset:2048
	s_nop 0
	global_load_dwordx4 v[110:113], v[110:111], off offset:3072
	v_mfma_f32_32x32x16_bf16 v[34:49], v[146:149], v[178:181], v[34:49]
	ds_read_b128 v[146:149], v227 offset:2608
	v_mfma_f32_32x32x16_bf16 v[18:33], v[154:157], v[174:177], v[18:33]
	ds_read_b64_tr_b16 v[174:175], v235 offset:55312
	ds_read_b64_tr_b16 v[176:177], v235 offset:57616
	v_mfma_f32_32x32x16_bf16 v[2:17], v[154:157], v[178:181], v[2:17]
	s_waitcnt lgkmcnt(10)
	v_mfma_f32_32x32x16_bf16 v[82:97], v[158:161], v[170:173], v[82:97]
	ds_read_b128 v[154:157], v227 offset:5168
	ds_read_b64_tr_b16 v[178:179], v235 offset:55376
	ds_read_b64_tr_b16 v[180:181], v235 offset:57680
	s_waitcnt lgkmcnt(3)
	s_barrier
	v_mfma_f32_32x32x16_bf16 v[66:81], v[158:161], v[182:185], v[66:81]
	ds_read_b128 v[158:161], v227 offset:15376
	v_mfma_f32_32x32x16_bf16 v[50:65], v[162:165], v[170:173], v[50:65]
	v_mfma_f32_32x32x16_bf16 v[34:49], v[162:165], v[182:185], v[34:49]
	ds_read_b128 v[162:165], v227 offset:17936
	v_mfma_f32_32x32x16_bf16 v[18:33], v[166:169], v[170:173], v[18:33]
	ds_read_b64_tr_b16 v[170:171], v228
	ds_read_b64_tr_b16 v[172:173], v228 offset:2304
	v_mfma_f32_32x32x16_bf16 v[2:17], v[166:169], v[182:185], v[2:17]
	ds_read_b128 v[166:169], v227 offset:20496
	ds_read_b64_tr_b16 v[182:183], v228 offset:64
	ds_read_b64_tr_b16 v[184:185], v228 offset:2368
	v_mfma_f32_32x32x16_bf16 v[82:97], v[150:153], v[174:177], v[82:97]
	s_waitcnt vmcnt(9)
	ds_write_b128 v222, v[122:125] offset:30736
	s_and_saveexec_b64 s[2:3], s[4:5]
	ds_write_b128 v223, v[102:105] offset:40976
	s_or_b64 exec, exec, s[2:3]
	s_waitcnt lgkmcnt(9)
	v_mfma_f32_32x32x16_bf16 v[66:81], v[150:153], v[178:181], v[66:81]
	ds_read_b128 v[150:153], v227 offset:15408
	s_waitcnt vmcnt(8)
	v_cvt_pk_bf16_f32 v122, v138, v139
	v_cvt_pk_bf16_f32 v123, v140, v141
	s_waitcnt vmcnt(7)
	v_cvt_pk_bf16_f32 v124, v130, v131
	v_cvt_pk_bf16_f32 v125, v132, v133
	s_waitcnt vmcnt(6)
	v_cvt_pk_bf16_f32 v118, v118, v119
	v_cvt_pk_bf16_f32 v119, v120, v121
	s_waitcnt vmcnt(5)
	v_cvt_pk_bf16_f32 v106, v106, v107
	v_cvt_pk_bf16_f32 v107, v108, v109
	ds_write2_b64 v231, v[122:123], v[124:125] offset1:72
	ds_write2_b64 v231, v[118:119], v[106:107] offset0:144 offset1:216
	v_mfma_f32_32x32x16_bf16 v[50:65], v[146:149], v[174:177], v[50:65]
	global_load_dwordx4 v[122:125], v[208:209], off offset:1216
	s_and_saveexec_b64 s[2:3], s[4:5]
	s_cbranch_execz .LBB0_1386
	global_load_dwordx4 v[102:105], v[210:211], off offset:1216
.LBB0_1386:
	s_or_b64 exec, exec, s[2:3]
	v_add_co_u32_e32 v106, vcc, 0x98000, v220
	s_nop 1
	v_addc_co_u32_e32 v107, vcc, 0, v221, vcc
	global_load_dwordx4 v[138:141], v[106:107], off
	global_load_dwordx4 v[130:133], v[106:107], off offset:1024
	global_load_dwordx4 v[118:121], v[106:107], off offset:2048
	s_nop 0
	global_load_dwordx4 v[106:109], v[106:107], off offset:3072
	v_mfma_f32_32x32x16_bf16 v[34:49], v[146:149], v[178:181], v[34:49]
	ds_read_b128 v[146:149], v227 offset:17968
	v_mfma_f32_32x32x16_bf16 v[18:33], v[154:157], v[174:177], v[18:33]
	ds_read_b64_tr_b16 v[174:175], v229
	ds_read_b64_tr_b16 v[176:177], v229 offset:2304
	v_mfma_f32_32x32x16_bf16 v[2:17], v[154:157], v[178:181], v[2:17]
	s_waitcnt lgkmcnt(10)
	v_mfma_f32_32x32x16_bf16 v[82:97], v[158:161], v[170:173], v[82:97]
	ds_read_b128 v[154:157], v227 offset:20528
	ds_read_b64_tr_b16 v[178:179], v230 offset:64
	ds_read_b64_tr_b16 v[180:181], v230 offset:2368
	s_waitcnt lgkmcnt(3)
	s_barrier
	v_mfma_f32_32x32x16_bf16 v[66:81], v[158:161], v[182:185], v[66:81]
	ds_read_b128 v[158:161], v227 offset:30736
	v_mfma_f32_32x32x16_bf16 v[50:65], v[162:165], v[170:173], v[50:65]
	v_mfma_f32_32x32x16_bf16 v[34:49], v[162:165], v[182:185], v[34:49]
	ds_read_b128 v[162:165], v227 offset:33296
	v_mfma_f32_32x32x16_bf16 v[18:33], v[166:169], v[170:173], v[18:33]
	ds_read_b64_tr_b16 v[170:171], v232
	ds_read_b64_tr_b16 v[172:173], v232 offset:2304
	v_mfma_f32_32x32x16_bf16 v[2:17], v[166:169], v[182:185], v[2:17]
	ds_read_b128 v[166:169], v227 offset:35856
	ds_read_b64_tr_b16 v[182:183], v232 offset:64
	ds_read_b64_tr_b16 v[184:185], v232 offset:2368
	v_mfma_f32_32x32x16_bf16 v[82:97], v[150:153], v[174:177], v[82:97]
	s_waitcnt vmcnt(9)
	ds_write_b128 v222, v[126:129] offset:16
	s_and_saveexec_b64 s[2:3], s[4:5]
	ds_write_b128 v223, v[98:101] offset:10256
	s_or_b64 exec, exec, s[2:3]
	s_waitcnt lgkmcnt(9)
	v_mfma_f32_32x32x16_bf16 v[66:81], v[150:153], v[178:181], v[66:81]
	ds_read_b128 v[150:153], v227 offset:30768
	s_waitcnt vmcnt(8)
	v_cvt_pk_bf16_f32 v126, v142, v143
	v_cvt_pk_bf16_f32 v127, v144, v145
	s_waitcnt vmcnt(7)
	v_cvt_pk_bf16_f32 v128, v134, v135
	v_cvt_pk_bf16_f32 v129, v136, v137
	s_waitcnt vmcnt(6)
	v_cvt_pk_bf16_f32 v114, v114, v115
	v_cvt_pk_bf16_f32 v115, v116, v117
	s_waitcnt vmcnt(5)
	v_cvt_pk_bf16_f32 v110, v110, v111
	v_cvt_pk_bf16_f32 v111, v112, v113
	ds_write2_b64 v205, v[126:127], v[128:129] offset0:130 offset1:202
	ds_write2_b64 v206, v[114:115], v[110:111] offset0:18 offset1:90
	v_mfma_f32_32x32x16_bf16 v[50:65], v[146:149], v[174:177], v[50:65]
	global_load_dwordx4 v[126:129], v[208:209], off offset:1280
	s_and_saveexec_b64 s[2:3], s[4:5]
	s_cbranch_execz .LBB0_1390
	global_load_dwordx4 v[98:101], v[210:211], off offset:1280
; #define LAS __attribute__((address_space(3)))
;     __device__ __forceinline__ void st(bfr* base, int id) const {
;         bfr* d = base + ((id >> 6) * 4) * KSTR + (id & 63) * 4;
;         *(u32x2*)(d)            = (u32x2){pack2(v0.x, v0.y), pack2(v0.z, v0.w)};
;         *(u32x2*)(d + KSTR)     = (u32x2){pack2(v1.x, v1.y), pack2(v1.z, v1.w)};
;         *(u32x2*)(d + 2 * KSTR) = (u32x2){pack2(v2.x, v2.y), pack2(v2.z, v2.w)};
;         *(u32x2*)(d + 3 * KSTR) = (u32x2){pack2(v3.x, v3.y), pack2(v3.z, v3.w)};
;     }
;     __device__ __forceinline__ static bf16x8 frag(const bfr* Bb, int wn, int ni, int ks, int lane) {
;         const int g = lane >> 4, q = (lane & 15) >> 2, pp = lane & 3;
;         const bfr* a = Bb + (ks * 16 + 8 * (g >> 1) + q) * KSTR + wn * 64 + ni * 32 + 16 * (g & 1) + 4 * pp;
;         union { v4s16 h[2]; bf16x8 v; } cv;
;         cv.h[0] = __builtin_amdgcn_ds_read_tr16_b64_v4i16((v4s16 LAS*)a);
;         cv.h[1] = __builtin_amdgcn_ds_read_tr16_b64_v4i16((v4s16 LAS*)(a + 4 * KSTR));
;         return cv.v;
;     }
.LBB0_1390:
	s_or_b64 exec, exec, s[2:3]
	v_add_co_u32_e32 v110, vcc, 0xa0000, v220
	s_nop 1
	v_addc_co_u32_e32 v111, vcc, 0, v221, vcc
	global_load_dwordx4 v[142:145], v[110:111], off
	global_load_dwordx4 v[134:137], v[110:111], off offset:1024
	global_load_dwordx4 v[114:117], v[110:111], off offset:2048
	s_nop 0
	global_load_dwordx4 v[110:113], v[110:111], off offset:3072
	v_mfma_f32_32x32x16_bf16 v[34:49], v[146:149], v[178:181], v[34:49]
	ds_read_b128 v[146:149], v227 offset:33328
	v_mfma_f32_32x32x16_bf16 v[18:33], v[154:157], v[174:177], v[18:33]
	ds_read_b64_tr_b16 v[174:175], v233
	ds_read_b64_tr_b16 v[176:177], v233 offset:2304
	v_mfma_f32_32x32x16_bf16 v[2:17], v[154:157], v[178:181], v[2:17]
	s_waitcnt lgkmcnt(10)
	v_mfma_f32_32x32x16_bf16 v[82:97], v[158:161], v[170:173], v[82:97]
	ds_read_b128 v[154:157], v227 offset:35888
	ds_read_b64_tr_b16 v[178:179], v234 offset:64
	ds_read_b64_tr_b16 v[180:181], v234 offset:2368
	s_waitcnt lgkmcnt(3)
	s_barrier
	v_mfma_f32_32x32x16_bf16 v[66:81], v[158:161], v[182:185], v[66:81]
	ds_read_b128 v[158:161], v227 offset:16
	v_mfma_f32_32x32x16_bf16 v[50:65], v[162:165], v[170:173], v[50:65]
	v_mfma_f32_32x32x16_bf16 v[34:49], v[162:165], v[182:185], v[34:49]
	ds_read_b128 v[162:165], v227 offset:2576
	v_mfma_f32_32x32x16_bf16 v[18:33], v[166:169], v[170:173], v[18:33]
	ds_read_b64_tr_b16 v[170:171], v235 offset:46096
	ds_read_b64_tr_b16 v[172:173], v235 offset:48400
	v_mfma_f32_32x32x16_bf16 v[2:17], v[166:169], v[182:185], v[2:17]
	ds_read_b128 v[166:169], v227 offset:5136
	ds_read_b64_tr_b16 v[182:183], v235 offset:46160
	ds_read_b64_tr_b16 v[184:185], v235 offset:48464
	v_mfma_f32_32x32x16_bf16 v[82:97], v[150:153], v[174:177], v[82:97]
	s_waitcnt vmcnt(9)
	ds_write_b128 v222, v[122:125] offset:15376
	s_and_saveexec_b64 s[2:3], s[4:5]
	ds_write_b128 v223, v[102:105] offset:25616
	s_or_b64 exec, exec, s[2:3]
	s_waitcnt lgkmcnt(9)
	v_mfma_f32_32x32x16_bf16 v[66:81], v[150:153], v[178:181], v[66:81]
	ds_read_b128 v[150:153], v227 offset:48
	s_waitcnt vmcnt(8)
	v_cvt_pk_bf16_f32 v122, v138, v139
	v_cvt_pk_bf16_f32 v123, v140, v141
	s_waitcnt vmcnt(7)
	v_cvt_pk_bf16_f32 v124, v130, v131
	v_cvt_pk_bf16_f32 v125, v132, v133
	s_waitcnt vmcnt(6)
	v_cvt_pk_bf16_f32 v118, v118, v119
	v_cvt_pk_bf16_f32 v119, v120, v121
	s_waitcnt vmcnt(5)
	v_cvt_pk_bf16_f32 v106, v106, v107
	v_cvt_pk_bf16_f32 v107, v108, v109
	ds_write2_b64 v226, v[122:123], v[124:125] offset1:72
	ds_write2_b64 v226, v[118:119], v[106:107] offset0:144 offset1:216
	v_mfma_f32_32x32x16_bf16 v[50:65], v[146:149], v[174:177], v[50:65]
	global_load_dwordx4 v[122:125], v[208:209], off offset:1344
	s_and_saveexec_b64 s[2:3], s[4:5]
	s_cbranch_execz .LBB0_1394
	global_load_dwordx4 v[102:105], v[210:211], off offset:1344
.LBB0_1394:
	s_or_b64 exec, exec, s[2:3]
	v_add_co_u32_e32 v106, vcc, 0xa8000, v220
	s_nop 1
	v_addc_co_u32_e32 v107, vcc, 0, v221, vcc
	global_load_dwordx4 v[138:141], v[106:107], off
	global_load_dwordx4 v[130:133], v[106:107], off offset:1024
	global_load_dwordx4 v[118:121], v[106:107], off offset:2048
	s_nop 0
	global_load_dwordx4 v[106:109], v[106:107], off offset:3072
	v_mfma_f32_32x32x16_bf16 v[34:49], v[146:149], v[178:181], v[34:49]
	ds_read_b128 v[146:149], v227 offset:2608
	v_mfma_f32_32x32x16_bf16 v[18:33], v[154:157], v[174:177], v[18:33]
	ds_read_b64_tr_b16 v[174:175], v235 offset:55312
	ds_read_b64_tr_b16 v[176:177], v235 offset:57616
	v_mfma_f32_32x32x16_bf16 v[2:17], v[154:157], v[178:181], v[2:17]
	s_waitcnt lgkmcnt(10)
	v_mfma_f32_32x32x16_bf16 v[82:97], v[158:161], v[170:173], v[82:97]
	ds_read_b128 v[154:157], v227 offset:5168
	ds_read_b64_tr_b16 v[178:179], v235 offset:55376
	ds_read_b64_tr_b16 v[180:181], v235 offset:57680
	s_waitcnt lgkmcnt(3)
	s_barrier
	v_mfma_f32_32x32x16_bf16 v[66:81], v[158:161], v[182:185], v[66:81]
	ds_read_b128 v[158:161], v227 offset:15376
	v_mfma_f32_32x32x16_bf16 v[50:65], v[162:165], v[170:173], v[50:65]
	v_mfma_f32_32x32x16_bf16 v[34:49], v[162:165], v[182:185], v[34:49]
	ds_read_b128 v[162:165], v227 offset:17936
	v_mfma_f32_32x32x16_bf16 v[18:33], v[166:169], v[170:173], v[18:33]
	ds_read_b64_tr_b16 v[170:171], v228
	ds_read_b64_tr_b16 v[172:173], v228 offset:2304
	v_mfma_f32_32x32x16_bf16 v[2:17], v[166:169], v[182:185], v[2:17]
	ds_read_b128 v[166:169], v227 offset:20496
	ds_read_b64_tr_b16 v[182:183], v228 offset:64
	ds_read_b64_tr_b16 v[184:185], v228 offset:2368
	v_mfma_f32_32x32x16_bf16 v[82:97], v[150:153], v[174:177], v[82:97]
	s_waitcnt vmcnt(9)
	ds_write_b128 v222, v[126:129] offset:30736
	s_and_saveexec_b64 s[2:3], s[4:5]
	ds_write_b128 v223, v[98:101] offset:40976
	s_or_b64 exec, exec, s[2:3]
	s_waitcnt lgkmcnt(9)
	v_mfma_f32_32x32x16_bf16 v[66:81], v[150:153], v[178:181], v[66:81]
	ds_read_b128 v[150:153], v227 offset:15408
	s_waitcnt vmcnt(8)
	v_cvt_pk_bf16_f32 v126, v142, v143
	v_cvt_pk_bf16_f32 v127, v144, v145
	s_waitcnt vmcnt(7)
	v_cvt_pk_bf16_f32 v128, v134, v135
	v_cvt_pk_bf16_f32 v129, v136, v137
	s_waitcnt vmcnt(6)
	v_cvt_pk_bf16_f32 v114, v114, v115
	v_cvt_pk_bf16_f32 v115, v116, v117
	s_waitcnt vmcnt(5)
	v_cvt_pk_bf16_f32 v110, v110, v111
	v_cvt_pk_bf16_f32 v111, v112, v113
	ds_write2_b64 v231, v[126:127], v[128:129] offset1:72
	ds_write2_b64 v231, v[114:115], v[110:111] offset0:144 offset1:216
	v_mfma_f32_32x32x16_bf16 v[50:65], v[146:149], v[174:177], v[50:65]
	global_load_dwordx4 v[126:129], v[208:209], off offset:1408
	s_and_saveexec_b64 s[2:3], s[4:5]
	s_cbranch_execz .LBB0_1398
	global_load_dwordx4 v[98:101], v[210:211], off offset:1408
; #define LAS __attribute__((address_space(3)))
;     __device__ __forceinline__ void st(bfr* base, int id) const {
;         bfr* d = base + ((id >> 6) * 4) * KSTR + (id & 63) * 4;
;         *(u32x2*)(d)            = (u32x2){pack2(v0.x, v0.y), pack2(v0.z, v0.w)};
;         *(u32x2*)(d + KSTR)     = (u32x2){pack2(v1.x, v1.y), pack2(v1.z, v1.w)};
;         *(u32x2*)(d + 2 * KSTR) = (u32x2){pack2(v2.x, v2.y), pack2(v2.z, v2.w)};
;         *(u32x2*)(d + 3 * KSTR) = (u32x2){pack2(v3.x, v3.y), pack2(v3.z, v3.w)};
;     }
;     __device__ __forceinline__ static bf16x8 frag(const bfr* Bb, int wn, int ni, int ks, int lane) {
;         const int g = lane >> 4, q = (lane & 15) >> 2, pp = lane & 3;
;         const bfr* a = Bb + (ks * 16 + 8 * (g >> 1) + q) * KSTR + wn * 64 + ni * 32 + 16 * (g & 1) + 4 * pp;
;         union { v4s16 h[2]; bf16x8 v; } cv;
;         cv.h[0] = __builtin_amdgcn_ds_read_tr16_b64_v4i16((v4s16 LAS*)a);
;         cv.h[1] = __builtin_amdgcn_ds_read_tr16_b64_v4i16((v4s16 LAS*)(a + 4 * KSTR));
;         return cv.v;
;     }
.LBB0_1398:
	s_or_b64 exec, exec, s[2:3]
	v_add_co_u32_e32 v110, vcc, 0xb0000, v220
	s_nop 1
	v_addc_co_u32_e32 v111, vcc, 0, v221, vcc
	global_load_dwordx4 v[142:145], v[110:111], off
	global_load_dwordx4 v[134:137], v[110:111], off offset:1024
	global_load_dwordx4 v[114:117], v[110:111], off offset:2048
	s_nop 0
	global_load_dwordx4 v[110:113], v[110:111], off offset:3072
	v_mfma_f32_32x32x16_bf16 v[34:49], v[146:149], v[178:181], v[34:49]
	ds_read_b128 v[146:149], v227 offset:17968
	v_mfma_f32_32x32x16_bf16 v[18:33], v[154:157], v[174:177], v[18:33]
	ds_read_b64_tr_b16 v[174:175], v229
	ds_read_b64_tr_b16 v[176:177], v229 offset:2304
	v_mfma_f32_32x32x16_bf16 v[2:17], v[154:157], v[178:181], v[2:17]
	s_waitcnt lgkmcnt(10)
	v_mfma_f32_32x32x16_bf16 v[82:97], v[158:161], v[170:173], v[82:97]
	ds_read_b128 v[154:157], v227 offset:20528
	ds_read_b64_tr_b16 v[178:179], v230 offset:64
	ds_read_b64_tr_b16 v[180:181], v230 offset:2368
	s_waitcnt lgkmcnt(3)
	s_barrier
	v_mfma_f32_32x32x16_bf16 v[66:81], v[158:161], v[182:185], v[66:81]
	ds_read_b128 v[158:161], v227 offset:30736
	v_mfma_f32_32x32x16_bf16 v[50:65], v[162:165], v[170:173], v[50:65]
	v_mfma_f32_32x32x16_bf16 v[34:49], v[162:165], v[182:185], v[34:49]
	ds_read_b128 v[162:165], v227 offset:33296
	v_mfma_f32_32x32x16_bf16 v[18:33], v[166:169], v[170:173], v[18:33]
	ds_read_b64_tr_b16 v[170:171], v232
	ds_read_b64_tr_b16 v[172:173], v232 offset:2304
	v_mfma_f32_32x32x16_bf16 v[2:17], v[166:169], v[182:185], v[2:17]
	ds_read_b128 v[166:169], v227 offset:35856
	ds_read_b64_tr_b16 v[182:183], v232 offset:64
	ds_read_b64_tr_b16 v[184:185], v232 offset:2368
	v_mfma_f32_32x32x16_bf16 v[82:97], v[150:153], v[174:177], v[82:97]
	s_waitcnt vmcnt(9)
	ds_write_b128 v222, v[122:125] offset:16
	s_and_saveexec_b64 s[2:3], s[4:5]
	ds_write_b128 v223, v[102:105] offset:10256
	s_or_b64 exec, exec, s[2:3]
	s_waitcnt lgkmcnt(9)
	v_mfma_f32_32x32x16_bf16 v[66:81], v[150:153], v[178:181], v[66:81]
	ds_read_b128 v[150:153], v227 offset:30768
	s_waitcnt vmcnt(8)
	v_cvt_pk_bf16_f32 v122, v138, v139
	v_cvt_pk_bf16_f32 v123, v140, v141
	s_waitcnt vmcnt(7)
	v_cvt_pk_bf16_f32 v124, v130, v131
	v_cvt_pk_bf16_f32 v125, v132, v133
	s_waitcnt vmcnt(6)
	v_cvt_pk_bf16_f32 v118, v118, v119
	v_cvt_pk_bf16_f32 v119, v120, v121
	s_waitcnt vmcnt(5)
	v_cvt_pk_bf16_f32 v106, v106, v107
	v_cvt_pk_bf16_f32 v107, v108, v109
	ds_write2_b64 v205, v[122:123], v[124:125] offset0:130 offset1:202
	ds_write2_b64 v206, v[118:119], v[106:107] offset0:18 offset1:90
	v_mfma_f32_32x32x16_bf16 v[50:65], v[146:149], v[174:177], v[50:65]
	global_load_dwordx4 v[122:125], v[208:209], off offset:1472
	s_and_saveexec_b64 s[2:3], s[4:5]
	s_cbranch_execz .LBB0_1402
	global_load_dwordx4 v[102:105], v[210:211], off offset:1472
.LBB0_1402:
	s_or_b64 exec, exec, s[2:3]
	v_add_co_u32_e32 v106, vcc, 0xb8000, v220
	s_nop 1
	v_addc_co_u32_e32 v107, vcc, 0, v221, vcc
	global_load_dwordx4 v[138:141], v[106:107], off
	global_load_dwordx4 v[130:133], v[106:107], off offset:1024
	global_load_dwordx4 v[118:121], v[106:107], off offset:2048
	s_nop 0
	global_load_dwordx4 v[106:109], v[106:107], off offset:3072
	v_mfma_f32_32x32x16_bf16 v[34:49], v[146:149], v[178:181], v[34:49]
	ds_read_b128 v[146:149], v227 offset:33328
	v_mfma_f32_32x32x16_bf16 v[18:33], v[154:157], v[174:177], v[18:33]
	ds_read_b64_tr_b16 v[174:175], v233
	ds_read_b64_tr_b16 v[176:177], v233 offset:2304
	v_mfma_f32_32x32x16_bf16 v[2:17], v[154:157], v[178:181], v[2:17]
	s_waitcnt lgkmcnt(10)
	v_mfma_f32_32x32x16_bf16 v[82:97], v[158:161], v[170:173], v[82:97]
	ds_read_b128 v[154:157], v227 offset:35888
	ds_read_b64_tr_b16 v[178:179], v234 offset:64
	ds_read_b64_tr_b16 v[180:181], v234 offset:2368
	s_waitcnt lgkmcnt(3)
	s_barrier
	v_mfma_f32_32x32x16_bf16 v[66:81], v[158:161], v[182:185], v[66:81]
	ds_read_b128 v[158:161], v227 offset:16
	v_mfma_f32_32x32x16_bf16 v[50:65], v[162:165], v[170:173], v[50:65]
	v_mfma_f32_32x32x16_bf16 v[34:49], v[162:165], v[182:185], v[34:49]
	ds_read_b128 v[162:165], v227 offset:2576
	v_mfma_f32_32x32x16_bf16 v[18:33], v[166:169], v[170:173], v[18:33]
	ds_read_b64_tr_b16 v[170:171], v235 offset:46096
	ds_read_b64_tr_b16 v[172:173], v235 offset:48400
	v_mfma_f32_32x32x16_bf16 v[2:17], v[166:169], v[182:185], v[2:17]
	ds_read_b128 v[166:169], v227 offset:5136
	ds_read_b64_tr_b16 v[182:183], v235 offset:46160
	ds_read_b64_tr_b16 v[184:185], v235 offset:48464
	v_mfma_f32_32x32x16_bf16 v[82:97], v[150:153], v[174:177], v[82:97]
	s_waitcnt vmcnt(9)
	ds_write_b128 v222, v[126:129] offset:15376
	s_and_saveexec_b64 s[2:3], s[4:5]
	ds_write_b128 v223, v[98:101] offset:25616
	s_or_b64 exec, exec, s[2:3]
	s_waitcnt lgkmcnt(9)
	v_mfma_f32_32x32x16_bf16 v[66:81], v[150:153], v[178:181], v[66:81]
	ds_read_b128 v[150:153], v227 offset:48
	s_waitcnt vmcnt(8)
	v_cvt_pk_bf16_f32 v126, v142, v143
	v_cvt_pk_bf16_f32 v127, v144, v145
	s_waitcnt vmcnt(7)
	v_cvt_pk_bf16_f32 v128, v134, v135
	v_cvt_pk_bf16_f32 v129, v136, v137
	s_waitcnt vmcnt(6)
	v_cvt_pk_bf16_f32 v114, v114, v115
	v_cvt_pk_bf16_f32 v115, v116, v117
	s_waitcnt vmcnt(5)
	v_cvt_pk_bf16_f32 v110, v110, v111
	v_cvt_pk_bf16_f32 v111, v112, v113
	ds_write2_b64 v226, v[126:127], v[128:129] offset1:72
	ds_write2_b64 v226, v[114:115], v[110:111] offset0:144 offset1:216
	v_mfma_f32_32x32x16_bf16 v[50:65], v[146:149], v[174:177], v[50:65]
	global_load_dwordx4 v[126:129], v[208:209], off offset:1536
	s_and_saveexec_b64 s[2:3], s[4:5]
	s_cbranch_execz .LBB0_1406
	global_load_dwordx4 v[98:101], v[210:211], off offset:1536
; #define LAS __attribute__((address_space(3)))
;     __device__ __forceinline__ void st(bfr* base, int id) const {
;         bfr* d = base + ((id >> 6) * 4) * KSTR + (id & 63) * 4;
;         *(u32x2*)(d)            = (u32x2){pack2(v0.x, v0.y), pack2(v0.z, v0.w)};
;         *(u32x2*)(d + KSTR)     = (u32x2){pack2(v1.x, v1.y), pack2(v1.z, v1.w)};
;         *(u32x2*)(d + 2 * KSTR) = (u32x2){pack2(v2.x, v2.y), pack2(v2.z, v2.w)};
;         *(u32x2*)(d + 3 * KSTR) = (u32x2){pack2(v3.x, v3.y), pack2(v3.z, v3.w)};
;     }
;     __device__ __forceinline__ static bf16x8 frag(const bfr* Bb, int wn, int ni, int ks, int lane) {
;         const int g = lane >> 4, q = (lane & 15) >> 2, pp = lane & 3;
;         const bfr* a = Bb + (ks * 16 + 8 * (g >> 1) + q) * KSTR + wn * 64 + ni * 32 + 16 * (g & 1) + 4 * pp;
;         union { v4s16 h[2]; bf16x8 v; } cv;
;         cv.h[0] = __builtin_amdgcn_ds_read_tr16_b64_v4i16((v4s16 LAS*)a);
;         cv.h[1] = __builtin_amdgcn_ds_read_tr16_b64_v4i16((v4s16 LAS*)(a + 4 * KSTR));
;         return cv.v;
;     }
.LBB0_1406:
	s_or_b64 exec, exec, s[2:3]
	v_add_co_u32_e32 v110, vcc, 0xc0000, v220
	s_nop 1
	v_addc_co_u32_e32 v111, vcc, 0, v221, vcc
	global_load_dwordx4 v[142:145], v[110:111], off
	global_load_dwordx4 v[134:137], v[110:111], off offset:1024
	global_load_dwordx4 v[114:117], v[110:111], off offset:2048
	s_nop 0
	global_load_dwordx4 v[110:113], v[110:111], off offset:3072
	v_mfma_f32_32x32x16_bf16 v[34:49], v[146:149], v[178:181], v[34:49]
	ds_read_b128 v[146:149], v227 offset:2608
	v_mfma_f32_32x32x16_bf16 v[18:33], v[154:157], v[174:177], v[18:33]
	ds_read_b64_tr_b16 v[174:175], v235 offset:55312
	ds_read_b64_tr_b16 v[176:177], v235 offset:57616
	v_mfma_f32_32x32x16_bf16 v[2:17], v[154:157], v[178:181], v[2:17]
	s_waitcnt lgkmcnt(10)
	v_mfma_f32_32x32x16_bf16 v[82:97], v[158:161], v[170:173], v[82:97]
	ds_read_b128 v[154:157], v227 offset:5168
	ds_read_b64_tr_b16 v[178:179], v235 offset:55376
	ds_read_b64_tr_b16 v[180:181], v235 offset:57680
	s_waitcnt lgkmcnt(3)
	s_barrier
	v_mfma_f32_32x32x16_bf16 v[66:81], v[158:161], v[182:185], v[66:81]
	ds_read_b128 v[158:161], v227 offset:15376
	v_mfma_f32_32x32x16_bf16 v[50:65], v[162:165], v[170:173], v[50:65]
	v_mfma_f32_32x32x16_bf16 v[34:49], v[162:165], v[182:185], v[34:49]
	ds_read_b128 v[162:165], v227 offset:17936
	v_mfma_f32_32x32x16_bf16 v[18:33], v[166:169], v[170:173], v[18:33]
	ds_read_b64_tr_b16 v[170:171], v228
	ds_read_b64_tr_b16 v[172:173], v228 offset:2304
	v_mfma_f32_32x32x16_bf16 v[2:17], v[166:169], v[182:185], v[2:17]
	ds_read_b128 v[166:169], v227 offset:20496
	ds_read_b64_tr_b16 v[182:183], v228 offset:64
	ds_read_b64_tr_b16 v[184:185], v228 offset:2368
	v_mfma_f32_32x32x16_bf16 v[82:97], v[150:153], v[174:177], v[82:97]
	s_waitcnt vmcnt(9)
	ds_write_b128 v222, v[122:125] offset:30736
	s_and_saveexec_b64 s[2:3], s[4:5]
	ds_write_b128 v223, v[102:105] offset:40976
	s_or_b64 exec, exec, s[2:3]
	s_waitcnt lgkmcnt(9)
	v_mfma_f32_32x32x16_bf16 v[66:81], v[150:153], v[178:181], v[66:81]
	ds_read_b128 v[150:153], v227 offset:15408
	s_waitcnt vmcnt(8)
	v_cvt_pk_bf16_f32 v122, v138, v139
	v_cvt_pk_bf16_f32 v123, v140, v141
	s_waitcnt vmcnt(7)
	v_cvt_pk_bf16_f32 v124, v130, v131
	v_cvt_pk_bf16_f32 v125, v132, v133
	s_waitcnt vmcnt(6)
	v_cvt_pk_bf16_f32 v118, v118, v119
	v_cvt_pk_bf16_f32 v119, v120, v121
	s_waitcnt vmcnt(5)
	v_cvt_pk_bf16_f32 v106, v106, v107
	v_cvt_pk_bf16_f32 v107, v108, v109
	ds_write2_b64 v231, v[122:123], v[124:125] offset1:72
	ds_write2_b64 v231, v[118:119], v[106:107] offset0:144 offset1:216
	v_mfma_f32_32x32x16_bf16 v[50:65], v[146:149], v[174:177], v[50:65]
	global_load_dwordx4 v[122:125], v[208:209], off offset:1600
	s_and_saveexec_b64 s[2:3], s[4:5]
	s_cbranch_execz .LBB0_1410
	global_load_dwordx4 v[102:105], v[210:211], off offset:1600
.LBB0_1410:
	s_or_b64 exec, exec, s[2:3]
	v_add_co_u32_e32 v106, vcc, 0xc8000, v220
	s_nop 1
	v_addc_co_u32_e32 v107, vcc, 0, v221, vcc
	global_load_dwordx4 v[138:141], v[106:107], off
	global_load_dwordx4 v[130:133], v[106:107], off offset:1024
	global_load_dwordx4 v[118:121], v[106:107], off offset:2048
	s_nop 0
	global_load_dwordx4 v[106:109], v[106:107], off offset:3072
	v_mfma_f32_32x32x16_bf16 v[34:49], v[146:149], v[178:181], v[34:49]
	ds_read_b128 v[146:149], v227 offset:17968
	v_mfma_f32_32x32x16_bf16 v[18:33], v[154:157], v[174:177], v[18:33]
	ds_read_b64_tr_b16 v[174:175], v229
	ds_read_b64_tr_b16 v[176:177], v229 offset:2304
	v_mfma_f32_32x32x16_bf16 v[2:17], v[154:157], v[178:181], v[2:17]
	s_waitcnt lgkmcnt(10)
	v_mfma_f32_32x32x16_bf16 v[82:97], v[158:161], v[170:173], v[82:97]
	ds_read_b128 v[154:157], v227 offset:20528
	ds_read_b64_tr_b16 v[178:179], v230 offset:64
	ds_read_b64_tr_b16 v[180:181], v230 offset:2368
	s_waitcnt lgkmcnt(3)
	s_barrier
	v_mfma_f32_32x32x16_bf16 v[66:81], v[158:161], v[182:185], v[66:81]
	ds_read_b128 v[158:161], v227 offset:30736
	v_mfma_f32_32x32x16_bf16 v[50:65], v[162:165], v[170:173], v[50:65]
	v_mfma_f32_32x32x16_bf16 v[34:49], v[162:165], v[182:185], v[34:49]
	ds_read_b128 v[162:165], v227 offset:33296
	v_mfma_f32_32x32x16_bf16 v[18:33], v[166:169], v[170:173], v[18:33]
	ds_read_b64_tr_b16 v[170:171], v232
	ds_read_b64_tr_b16 v[172:173], v232 offset:2304
	v_mfma_f32_32x32x16_bf16 v[2:17], v[166:169], v[182:185], v[2:17]
	ds_read_b128 v[166:169], v227 offset:35856
	ds_read_b64_tr_b16 v[182:183], v232 offset:64
	ds_read_b64_tr_b16 v[184:185], v232 offset:2368
	v_mfma_f32_32x32x16_bf16 v[82:97], v[150:153], v[174:177], v[82:97]
	s_waitcnt vmcnt(9)
	ds_write_b128 v222, v[126:129] offset:16
	s_and_saveexec_b64 s[2:3], s[4:5]
	ds_write_b128 v223, v[98:101] offset:10256
	s_or_b64 exec, exec, s[2:3]
	s_waitcnt lgkmcnt(9)
	v_mfma_f32_32x32x16_bf16 v[66:81], v[150:153], v[178:181], v[66:81]
	ds_read_b128 v[150:153], v227 offset:30768
	s_waitcnt vmcnt(8)
	v_cvt_pk_bf16_f32 v126, v142, v143
	v_cvt_pk_bf16_f32 v127, v144, v145
	s_waitcnt vmcnt(7)
	v_cvt_pk_bf16_f32 v128, v134, v135
	v_cvt_pk_bf16_f32 v129, v136, v137
	s_waitcnt vmcnt(6)
	v_cvt_pk_bf16_f32 v114, v114, v115
	v_cvt_pk_bf16_f32 v115, v116, v117
	s_waitcnt vmcnt(5)
	v_cvt_pk_bf16_f32 v110, v110, v111
	v_cvt_pk_bf16_f32 v111, v112, v113
	ds_write2_b64 v205, v[126:127], v[128:129] offset0:130 offset1:202
	ds_write2_b64 v206, v[114:115], v[110:111] offset0:18 offset1:90
	v_mfma_f32_32x32x16_bf16 v[50:65], v[146:149], v[174:177], v[50:65]
	global_load_dwordx4 v[126:129], v[208:209], off offset:1664
	s_and_saveexec_b64 s[2:3], s[4:5]
	s_cbranch_execz .LBB0_1414
	global_load_dwordx4 v[98:101], v[210:211], off offset:1664
; #define LAS __attribute__((address_space(3)))
;     __device__ __forceinline__ void st(bfr* base, int id) const {
;         bfr* d = base + ((id >> 6) * 4) * KSTR + (id & 63) * 4;
;         *(u32x2*)(d)            = (u32x2){pack2(v0.x, v0.y), pack2(v0.z, v0.w)};
;         *(u32x2*)(d + KSTR)     = (u32x2){pack2(v1.x, v1.y), pack2(v1.z, v1.w)};
;         *(u32x2*)(d + 2 * KSTR) = (u32x2){pack2(v2.x, v2.y), pack2(v2.z, v2.w)};
;         *(u32x2*)(d + 3 * KSTR) = (u32x2){pack2(v3.x, v3.y), pack2(v3.z, v3.w)};
;     }
;     __device__ __forceinline__ static bf16x8 frag(const bfr* Bb, int wn, int ni, int ks, int lane) {
;         const int g = lane >> 4, q = (lane & 15) >> 2, pp = lane & 3;
;         const bfr* a = Bb + (ks * 16 + 8 * (g >> 1) + q) * KSTR + wn * 64 + ni * 32 + 16 * (g & 1) + 4 * pp;
;         union { v4s16 h[2]; bf16x8 v; } cv;
;         cv.h[0] = __builtin_amdgcn_ds_read_tr16_b64_v4i16((v4s16 LAS*)a);
;         cv.h[1] = __builtin_amdgcn_ds_read_tr16_b64_v4i16((v4s16 LAS*)(a + 4 * KSTR));
;         return cv.v;
;     }
.LBB0_1414:
	s_or_b64 exec, exec, s[2:3]
	v_add_co_u32_e32 v110, vcc, 0xd0000, v220
	s_nop 1
	v_addc_co_u32_e32 v111, vcc, 0, v221, vcc
	global_load_dwordx4 v[142:145], v[110:111], off
	global_load_dwordx4 v[134:137], v[110:111], off offset:1024
	global_load_dwordx4 v[114:117], v[110:111], off offset:2048
	s_nop 0
	global_load_dwordx4 v[110:113], v[110:111], off offset:3072
	v_mfma_f32_32x32x16_bf16 v[34:49], v[146:149], v[178:181], v[34:49]
	ds_read_b128 v[146:149], v227 offset:33328
	v_mfma_f32_32x32x16_bf16 v[18:33], v[154:157], v[174:177], v[18:33]
	ds_read_b64_tr_b16 v[174:175], v233
	ds_read_b64_tr_b16 v[176:177], v233 offset:2304
	v_mfma_f32_32x32x16_bf16 v[2:17], v[154:157], v[178:181], v[2:17]
	s_waitcnt lgkmcnt(10)
	v_mfma_f32_32x32x16_bf16 v[82:97], v[158:161], v[170:173], v[82:97]
	ds_read_b128 v[154:157], v227 offset:35888
	ds_read_b64_tr_b16 v[178:179], v234 offset:64
	ds_read_b64_tr_b16 v[180:181], v234 offset:2368
	s_waitcnt lgkmcnt(3)
	s_barrier
	v_mfma_f32_32x32x16_bf16 v[66:81], v[158:161], v[182:185], v[66:81]
	ds_read_b128 v[158:161], v227 offset:16
	v_mfma_f32_32x32x16_bf16 v[50:65], v[162:165], v[170:173], v[50:65]
	v_mfma_f32_32x32x16_bf16 v[34:49], v[162:165], v[182:185], v[34:49]
	ds_read_b128 v[162:165], v227 offset:2576
	v_mfma_f32_32x32x16_bf16 v[18:33], v[166:169], v[170:173], v[18:33]
	ds_read_b64_tr_b16 v[170:171], v235 offset:46096
	ds_read_b64_tr_b16 v[172:173], v235 offset:48400
	v_mfma_f32_32x32x16_bf16 v[2:17], v[166:169], v[182:185], v[2:17]
	ds_read_b128 v[166:169], v227 offset:5136
	ds_read_b64_tr_b16 v[182:183], v235 offset:46160
	ds_read_b64_tr_b16 v[184:185], v235 offset:48464
	v_mfma_f32_32x32x16_bf16 v[82:97], v[150:153], v[174:177], v[82:97]
	s_waitcnt vmcnt(9)
	ds_write_b128 v222, v[122:125] offset:15376
	s_and_saveexec_b64 s[2:3], s[4:5]
	ds_write_b128 v223, v[102:105] offset:25616
	s_or_b64 exec, exec, s[2:3]
	s_waitcnt lgkmcnt(9)
	v_mfma_f32_32x32x16_bf16 v[66:81], v[150:153], v[178:181], v[66:81]
	ds_read_b128 v[150:153], v227 offset:48
	s_waitcnt vmcnt(8)
	v_cvt_pk_bf16_f32 v122, v138, v139
	v_cvt_pk_bf16_f32 v123, v140, v141
	s_waitcnt vmcnt(7)
	v_cvt_pk_bf16_f32 v124, v130, v131
	v_cvt_pk_bf16_f32 v125, v132, v133
	s_waitcnt vmcnt(6)
	v_cvt_pk_bf16_f32 v118, v118, v119
	v_cvt_pk_bf16_f32 v119, v120, v121
	s_waitcnt vmcnt(5)
	v_cvt_pk_bf16_f32 v106, v106, v107
	v_cvt_pk_bf16_f32 v107, v108, v109
	ds_write2_b64 v226, v[122:123], v[124:125] offset1:72
	ds_write2_b64 v226, v[118:119], v[106:107] offset0:144 offset1:216
	v_mfma_f32_32x32x16_bf16 v[50:65], v[146:149], v[174:177], v[50:65]
	global_load_dwordx4 v[122:125], v[208:209], off offset:1728
	s_and_saveexec_b64 s[2:3], s[4:5]
	s_cbranch_execz .LBB0_1418
	global_load_dwordx4 v[102:105], v[210:211], off offset:1728
.LBB0_1418:
	s_or_b64 exec, exec, s[2:3]
	v_add_co_u32_e32 v106, vcc, 0xd8000, v220
	s_nop 1
	v_addc_co_u32_e32 v107, vcc, 0, v221, vcc
	global_load_dwordx4 v[138:141], v[106:107], off
	global_load_dwordx4 v[130:133], v[106:107], off offset:1024
	global_load_dwordx4 v[118:121], v[106:107], off offset:2048
	s_nop 0
	global_load_dwordx4 v[106:109], v[106:107], off offset:3072
	v_mfma_f32_32x32x16_bf16 v[34:49], v[146:149], v[178:181], v[34:49]
	ds_read_b128 v[146:149], v227 offset:2608
	v_mfma_f32_32x32x16_bf16 v[18:33], v[154:157], v[174:177], v[18:33]
	ds_read_b64_tr_b16 v[174:175], v235 offset:55312
	ds_read_b64_tr_b16 v[176:177], v235 offset:57616
	v_mfma_f32_32x32x16_bf16 v[2:17], v[154:157], v[178:181], v[2:17]
	s_waitcnt lgkmcnt(10)
	v_mfma_f32_32x32x16_bf16 v[82:97], v[158:161], v[170:173], v[82:97]
	ds_read_b128 v[154:157], v227 offset:5168
	ds_read_b64_tr_b16 v[190:191], v235 offset:55376
	ds_read_b64_tr_b16 v[192:193], v235 offset:57680
	s_waitcnt lgkmcnt(3)
	s_barrier
	v_mfma_f32_32x32x16_bf16 v[66:81], v[158:161], v[182:185], v[66:81]
	ds_read_b128 v[158:161], v227 offset:15376
	v_mfma_f32_32x32x16_bf16 v[50:65], v[162:165], v[170:173], v[50:65]
	v_mfma_f32_32x32x16_bf16 v[34:49], v[162:165], v[182:185], v[34:49]
	ds_read_b128 v[162:165], v227 offset:17936
	v_mfma_f32_32x32x16_bf16 v[18:33], v[166:169], v[170:173], v[18:33]
	ds_read_b64_tr_b16 v[178:179], v228
	ds_read_b64_tr_b16 v[180:181], v228 offset:2304
	v_mfma_f32_32x32x16_bf16 v[2:17], v[166:169], v[182:185], v[2:17]
	ds_read_b128 v[166:169], v227 offset:20496
	ds_read_b64_tr_b16 v[186:187], v228 offset:64
	ds_read_b64_tr_b16 v[188:189], v228 offset:2368
	v_mfma_f32_32x32x16_bf16 v[82:97], v[150:153], v[174:177], v[82:97]
	s_waitcnt vmcnt(9)
	ds_write_b128 v222, v[126:129] offset:30736
	s_and_saveexec_b64 s[2:3], s[4:5]
	ds_write_b128 v223, v[98:101] offset:40976
	s_or_b64 exec, exec, s[2:3]
	s_waitcnt lgkmcnt(9)
	v_mfma_f32_32x32x16_bf16 v[66:81], v[150:153], v[190:193], v[66:81]
	ds_read_b128 v[126:129], v227 offset:15408
	s_waitcnt vmcnt(8)
	v_cvt_pk_bf16_f32 v142, v142, v143
	v_cvt_pk_bf16_f32 v143, v144, v145
	s_waitcnt vmcnt(7)
	v_cvt_pk_bf16_f32 v134, v134, v135
	v_cvt_pk_bf16_f32 v135, v136, v137
	s_waitcnt vmcnt(6)
	v_cvt_pk_bf16_f32 v114, v114, v115
	v_cvt_pk_bf16_f32 v115, v116, v117
	s_waitcnt vmcnt(5)
	v_cvt_pk_bf16_f32 v110, v110, v111
	v_cvt_pk_bf16_f32 v111, v112, v113
	ds_write2_b64 v231, v[142:143], v[134:135] offset1:72
	ds_write2_b64 v231, v[114:115], v[110:111] offset0:144 offset1:216
	v_mfma_f32_32x32x16_bf16 v[50:65], v[146:149], v[174:177], v[50:65]
	global_load_dwordx4 v[134:137], v[208:209], off offset:1792
	s_and_saveexec_b64 s[2:3], s[4:5]
	s_cbranch_execz .LBB0_1422
	global_load_dwordx4 v[98:101], v[210:211], off offset:1792
; #define LAS __attribute__((address_space(3)))
;     __device__ __forceinline__ void st(bfr* base, int id) const {
;         bfr* d = base + ((id >> 6) * 4) * KSTR + (id & 63) * 4;
;         *(u32x2*)(d)            = (u32x2){pack2(v0.x, v0.y), pack2(v0.z, v0.w)};
;         *(u32x2*)(d + KSTR)     = (u32x2){pack2(v1.x, v1.y), pack2(v1.z, v1.w)};
;         *(u32x2*)(d + 2 * KSTR) = (u32x2){pack2(v2.x, v2.y), pack2(v2.z, v2.w)};
;         *(u32x2*)(d + 3 * KSTR) = (u32x2){pack2(v3.x, v3.y), pack2(v3.z, v3.w)};
;     }
;     __device__ __forceinline__ static bf16x8 frag(const bfr* Bb, int wn, int ni, int ks, int lane) {
;         const int g = lane >> 4, q = (lane & 15) >> 2, pp = lane & 3;
;         const bfr* a = Bb + (ks * 16 + 8 * (g >> 1) + q) * KSTR + wn * 64 + ni * 32 + 16 * (g & 1) + 4 * pp;
;         union { v4s16 h[2]; bf16x8 v; } cv;
;         cv.h[0] = __builtin_amdgcn_ds_read_tr16_b64_v4i16((v4s16 LAS*)a);
;         cv.h[1] = __builtin_amdgcn_ds_read_tr16_b64_v4i16((v4s16 LAS*)(a + 4 * KSTR));
;         return cv.v;
;     }
.LBB0_1422:
	s_or_b64 exec, exec, s[2:3]
	v_add_co_u32_e32 v110, vcc, 0xe0000, v220
	s_nop 1
	v_addc_co_u32_e32 v111, vcc, 0, v221, vcc
	global_load_dwordx4 v[150:153], v[110:111], off
	global_load_dwordx4 v[142:145], v[110:111], off offset:1024
	global_load_dwordx4 v[114:117], v[110:111], off offset:2048
	s_nop 0
	global_load_dwordx4 v[110:113], v[110:111], off offset:3072
	v_mfma_f32_32x32x16_bf16 v[34:49], v[146:149], v[190:193], v[34:49]
	ds_read_b128 v[170:173], v227 offset:17968
	v_mfma_f32_32x32x16_bf16 v[18:33], v[154:157], v[174:177], v[18:33]
	ds_read_b64_tr_b16 v[182:183], v229
	ds_read_b64_tr_b16 v[184:185], v229 offset:2304
	v_mfma_f32_32x32x16_bf16 v[2:17], v[154:157], v[190:193], v[2:17]
	s_waitcnt lgkmcnt(10)
	v_mfma_f32_32x32x16_bf16 v[82:97], v[158:161], v[178:181], v[82:97]
	ds_read_b128 v[174:177], v227 offset:20528
	ds_read_b64_tr_b16 v[190:191], v230 offset:64
	ds_read_b64_tr_b16 v[192:193], v230 offset:2368
	s_waitcnt lgkmcnt(3)
	s_barrier
	v_mfma_f32_32x32x16_bf16 v[66:81], v[158:161], v[186:189], v[66:81]
	ds_read_b128 v[158:161], v227 offset:30736
	v_mfma_f32_32x32x16_bf16 v[50:65], v[162:165], v[178:181], v[50:65]
	v_mfma_f32_32x32x16_bf16 v[34:49], v[162:165], v[186:189], v[34:49]
	ds_read_b128 v[162:165], v227 offset:33296
	v_mfma_f32_32x32x16_bf16 v[18:33], v[166:169], v[178:181], v[18:33]
	ds_read_b64_tr_b16 v[178:179], v232
	ds_read_b64_tr_b16 v[180:181], v232 offset:2304
	v_mfma_f32_32x32x16_bf16 v[2:17], v[166:169], v[186:189], v[2:17]
	ds_read_b128 v[166:169], v227 offset:35856
	ds_read_b64_tr_b16 v[186:187], v232 offset:64
	ds_read_b64_tr_b16 v[188:189], v232 offset:2368
	v_mfma_f32_32x32x16_bf16 v[82:97], v[126:129], v[182:185], v[82:97]
	s_waitcnt vmcnt(9)
	ds_write_b128 v222, v[122:125] offset:16
	s_and_saveexec_b64 s[2:3], s[4:5]
	ds_write_b128 v223, v[102:105] offset:10256
	s_or_b64 exec, exec, s[2:3]
	s_waitcnt lgkmcnt(9)
	v_mfma_f32_32x32x16_bf16 v[66:81], v[126:129], v[190:193], v[66:81]
	ds_read_b128 v[122:125], v227 offset:30768
	s_waitcnt vmcnt(8)
	v_cvt_pk_bf16_f32 v126, v138, v139
	v_cvt_pk_bf16_f32 v127, v140, v141
	s_waitcnt vmcnt(7)
	v_cvt_pk_bf16_f32 v128, v130, v131
	v_cvt_pk_bf16_f32 v129, v132, v133
	s_waitcnt vmcnt(6)
	v_cvt_pk_bf16_f32 v118, v118, v119
	v_cvt_pk_bf16_f32 v119, v120, v121
	s_waitcnt vmcnt(5)
	v_cvt_pk_bf16_f32 v106, v106, v107
	v_cvt_pk_bf16_f32 v107, v108, v109
	ds_write2_b64 v205, v[126:127], v[128:129] offset0:130 offset1:202
	ds_write2_b64 v206, v[118:119], v[106:107] offset0:18 offset1:90
	v_mfma_f32_32x32x16_bf16 v[50:65], v[170:173], v[182:185], v[50:65]
	global_load_dwordx4 v[138:141], v[208:209], off offset:1856
	s_and_saveexec_b64 s[2:3], s[4:5]
	s_cbranch_execz .LBB0_1426
	global_load_dwordx4 v[102:105], v[210:211], off offset:1856
.LBB0_1426:
	s_or_b64 exec, exec, s[2:3]
	v_add_co_u32_e32 v106, vcc, 0xe8000, v220
	s_nop 1
	v_addc_co_u32_e32 v107, vcc, 0, v221, vcc
	global_load_dwordx4 v[154:157], v[106:107], off
	global_load_dwordx4 v[146:149], v[106:107], off offset:1024
	global_load_dwordx4 v[130:133], v[106:107], off offset:2048
	global_load_dwordx4 v[126:129], v[106:107], off offset:3072
	v_mfma_f32_32x32x16_bf16 v[34:49], v[170:173], v[190:193], v[34:49]
	ds_read_b128 v[170:173], v227 offset:33328
	v_mfma_f32_32x32x16_bf16 v[18:33], v[174:177], v[182:185], v[18:33]
	ds_read_b64_tr_b16 v[182:183], v233
	ds_read_b64_tr_b16 v[184:185], v233 offset:2304
	v_mfma_f32_32x32x16_bf16 v[2:17], v[174:177], v[190:193], v[2:17]
	s_waitcnt lgkmcnt(10)
	v_mfma_f32_32x32x16_bf16 v[82:97], v[158:161], v[178:181], v[82:97]
	ds_read_b128 v[174:177], v227 offset:35888
	ds_read_b64_tr_b16 v[190:191], v234 offset:64
	ds_read_b64_tr_b16 v[192:193], v234 offset:2368
	s_waitcnt lgkmcnt(3)
	s_barrier
	v_mfma_f32_32x32x16_bf16 v[66:81], v[158:161], v[186:189], v[66:81]
	ds_read_b128 v[158:161], v227 offset:16
	v_mfma_f32_32x32x16_bf16 v[50:65], v[162:165], v[178:181], v[50:65]
	v_mfma_f32_32x32x16_bf16 v[34:49], v[162:165], v[186:189], v[34:49]
	ds_read_b128 v[162:165], v227 offset:2576
	v_mfma_f32_32x32x16_bf16 v[18:33], v[166:169], v[178:181], v[18:33]
	ds_read_b64_tr_b16 v[178:179], v235 offset:46096
	ds_read_b64_tr_b16 v[180:181], v235 offset:48400
	v_mfma_f32_32x32x16_bf16 v[2:17], v[166:169], v[186:189], v[2:17]
	ds_read_b128 v[166:169], v227 offset:5136
	ds_read_b64_tr_b16 v[186:187], v235 offset:46160
	ds_read_b64_tr_b16 v[188:189], v235 offset:48464
	v_mfma_f32_32x32x16_bf16 v[82:97], v[122:125], v[182:185], v[82:97]
	s_waitcnt vmcnt(9)
	ds_write_b128 v222, v[134:137] offset:15376
	s_and_saveexec_b64 s[2:3], s[4:5]
	ds_write_b128 v223, v[98:101] offset:25616
	s_or_b64 exec, exec, s[2:3]
	s_waitcnt lgkmcnt(9)
	v_mfma_f32_32x32x16_bf16 v[66:81], v[122:125], v[190:193], v[66:81]
	ds_read_b128 v[134:137], v227 offset:48
	s_waitcnt vmcnt(8)
	v_cvt_pk_bf16_f32 v106, v150, v151
	v_cvt_pk_bf16_f32 v107, v152, v153
	s_waitcnt vmcnt(7)
	v_cvt_pk_bf16_f32 v108, v142, v143
	v_cvt_pk_bf16_f32 v109, v144, v145
	ds_write2_b64 v226, v[106:107], v[108:109] offset1:72
	s_waitcnt vmcnt(6)
	v_cvt_pk_bf16_f32 v106, v114, v115
	v_cvt_pk_bf16_f32 v107, v116, v117
	s_waitcnt vmcnt(5)
	v_cvt_pk_bf16_f32 v108, v110, v111
	v_cvt_pk_bf16_f32 v109, v112, v113
	ds_write2_b64 v226, v[106:107], v[108:109] offset0:144 offset1:216
	v_mfma_f32_32x32x16_bf16 v[50:65], v[170:173], v[182:185], v[50:65]
	global_load_dwordx4 v[106:109], v[208:209], off offset:1920
	s_and_saveexec_b64 s[2:3], s[4:5]
	s_cbranch_execz .LBB0_1430
	global_load_dwordx4 v[98:101], v[210:211], off offset:1920
; #define LAS __attribute__((address_space(3)))
;     __device__ __forceinline__ void st(bfr* base, int id) const {
;         bfr* d = base + ((id >> 6) * 4) * KSTR + (id & 63) * 4;
;         *(u32x2*)(d)            = (u32x2){pack2(v0.x, v0.y), pack2(v0.z, v0.w)};
;         *(u32x2*)(d + KSTR)     = (u32x2){pack2(v1.x, v1.y), pack2(v1.z, v1.w)};
;         *(u32x2*)(d + 2 * KSTR) = (u32x2){pack2(v2.x, v2.y), pack2(v2.z, v2.w)};
;         *(u32x2*)(d + 3 * KSTR) = (u32x2){pack2(v3.x, v3.y), pack2(v3.z, v3.w)};
;     }
;     __device__ __forceinline__ static bf16x8 frag(const bfr* Bb, int wn, int ni, int ks, int lane) {
;         const int g = lane >> 4, q = (lane & 15) >> 2, pp = lane & 3;
;         const bfr* a = Bb + (ks * 16 + 8 * (g >> 1) + q) * KSTR + wn * 64 + ni * 32 + 16 * (g & 1) + 4 * pp;
;         union { v4s16 h[2]; bf16x8 v; } cv;
;         cv.h[0] = __builtin_amdgcn_ds_read_tr16_b64_v4i16((v4s16 LAS*)a);
;         cv.h[1] = __builtin_amdgcn_ds_read_tr16_b64_v4i16((v4s16 LAS*)(a + 4 * KSTR));
;         return cv.v;
;     }
.LBB0_1430:
	s_or_b64 exec, exec, s[2:3]
	v_add_co_u32_e32 v114, vcc, 0xf0000, v220
	s_nop 1
	v_addc_co_u32_e32 v115, vcc, 0, v221, vcc
	global_load_dwordx4 v[118:121], v[114:115], off
	global_load_dwordx4 v[122:125], v[114:115], off offset:1024
	global_load_dwordx4 v[110:113], v[114:115], off offset:2048
	s_nop 0
	global_load_dwordx4 v[114:117], v[114:115], off offset:3072
	v_mfma_f32_32x32x16_bf16 v[34:49], v[170:173], v[190:193], v[34:49]
	ds_read_b128 v[170:173], v227 offset:2608
	v_mfma_f32_32x32x16_bf16 v[18:33], v[174:177], v[182:185], v[18:33]
	ds_read_b64_tr_b16 v[182:183], v235 offset:55312
	ds_read_b64_tr_b16 v[184:185], v235 offset:57616
	v_mfma_f32_32x32x16_bf16 v[2:17], v[174:177], v[190:193], v[2:17]
	s_waitcnt lgkmcnt(10)
	v_mfma_f32_32x32x16_bf16 v[82:97], v[158:161], v[178:181], v[82:97]
	ds_read_b128 v[174:177], v227 offset:5168
	ds_read_b64_tr_b16 v[190:191], v235 offset:55376
	ds_read_b64_tr_b16 v[192:193], v235 offset:57680
	s_waitcnt lgkmcnt(3)
	s_barrier
	v_mfma_f32_32x32x16_bf16 v[66:81], v[158:161], v[186:189], v[66:81]
	ds_read_b128 v[158:161], v227 offset:15376
	v_mfma_f32_32x32x16_bf16 v[50:65], v[162:165], v[178:181], v[50:65]
	v_mfma_f32_32x32x16_bf16 v[34:49], v[162:165], v[186:189], v[34:49]
	ds_read_b128 v[162:165], v227 offset:17936
	v_mfma_f32_32x32x16_bf16 v[18:33], v[166:169], v[178:181], v[18:33]
	ds_read_b64_tr_b16 v[178:179], v228
	ds_read_b64_tr_b16 v[180:181], v228 offset:2304
	v_mfma_f32_32x32x16_bf16 v[2:17], v[166:169], v[186:189], v[2:17]
	ds_read_b128 v[166:169], v227 offset:20496
	ds_read_b64_tr_b16 v[186:187], v228 offset:64
	ds_read_b64_tr_b16 v[188:189], v228 offset:2368
	v_mfma_f32_32x32x16_bf16 v[82:97], v[134:137], v[182:185], v[82:97]
	s_waitcnt vmcnt(9)
	ds_write_b128 v222, v[138:141] offset:30736
	s_and_saveexec_b64 s[2:3], s[4:5]
	ds_write_b128 v223, v[102:105] offset:40976
	s_or_b64 exec, exec, s[2:3]
	s_waitcnt lgkmcnt(9)
	v_mfma_f32_32x32x16_bf16 v[66:81], v[134:137], v[190:193], v[66:81]
	ds_read_b128 v[150:153], v227 offset:15408
	s_waitcnt vmcnt(8)
	v_cvt_pk_bf16_f32 v134, v154, v155
	v_cvt_pk_bf16_f32 v135, v156, v157
	s_waitcnt vmcnt(7)
	v_cvt_pk_bf16_f32 v136, v146, v147
	v_cvt_pk_bf16_f32 v137, v148, v149
	s_waitcnt vmcnt(6)
	v_cvt_pk_bf16_f32 v130, v130, v131
	v_cvt_pk_bf16_f32 v131, v132, v133
	s_waitcnt vmcnt(5)
	v_cvt_pk_bf16_f32 v126, v126, v127
	v_cvt_pk_bf16_f32 v127, v128, v129
	ds_write2_b64 v231, v[134:135], v[136:137] offset1:72
	ds_write2_b64 v231, v[130:131], v[126:127] offset0:144 offset1:216
	v_mfma_f32_32x32x16_bf16 v[50:65], v[170:173], v[182:185], v[50:65]
	global_load_dwordx4 v[126:129], v[208:209], off offset:1984
	s_and_saveexec_b64 s[2:3], s[4:5]
	s_cbranch_execz .LBB0_1434
	global_load_dwordx4 v[102:105], v[210:211], off offset:1984
.LBB0_1434:
	s_or_b64 exec, exec, s[2:3]
	v_add_co_u32_e32 v130, vcc, 0xf8000, v220
	s_nop 1
	v_addc_co_u32_e32 v131, vcc, 0, v221, vcc
	global_load_dwordx4 v[138:141], v[130:131], off
	global_load_dwordx4 v[142:145], v[130:131], off offset:1024
	global_load_dwordx4 v[134:137], v[130:131], off offset:2048
	s_nop 0
	global_load_dwordx4 v[130:133], v[130:131], off offset:3072
	v_mfma_f32_32x32x16_bf16 v[34:49], v[170:173], v[190:193], v[34:49]
	ds_read_b128 v[146:149], v227 offset:17968
	v_mfma_f32_32x32x16_bf16 v[18:33], v[174:177], v[182:185], v[18:33]
	ds_read_b64_tr_b16 v[182:183], v229
	ds_read_b64_tr_b16 v[184:185], v229 offset:2304
	v_mfma_f32_32x32x16_bf16 v[2:17], v[174:177], v[190:193], v[2:17]
	s_waitcnt lgkmcnt(10)
	v_mfma_f32_32x32x16_bf16 v[82:97], v[158:161], v[178:181], v[82:97]
	ds_read_b128 v[154:157], v227 offset:20528
	ds_read_b64_tr_b16 v[198:199], v230 offset:64
	ds_read_b64_tr_b16 v[200:201], v230 offset:2368
	s_waitcnt lgkmcnt(3)
	s_barrier
	v_mfma_f32_32x32x16_bf16 v[66:81], v[158:161], v[186:189], v[66:81]
	ds_read_b128 v[158:161], v227 offset:30736
	v_mfma_f32_32x32x16_bf16 v[50:65], v[162:165], v[178:181], v[50:65]
	v_mfma_f32_32x32x16_bf16 v[34:49], v[162:165], v[186:189], v[34:49]
	ds_read_b128 v[162:165], v227 offset:33296
	v_mfma_f32_32x32x16_bf16 v[18:33], v[166:169], v[178:181], v[18:33]
	ds_read_b64_tr_b16 v[190:191], v232
	ds_read_b64_tr_b16 v[192:193], v232 offset:2304
	v_mfma_f32_32x32x16_bf16 v[2:17], v[166:169], v[186:189], v[2:17]
	ds_read_b128 v[166:169], v227 offset:35856
	ds_read_b64_tr_b16 v[194:195], v232 offset:64
	ds_read_b64_tr_b16 v[196:197], v232 offset:2368
	v_mfma_f32_32x32x16_bf16 v[82:97], v[150:153], v[182:185], v[82:97]
	s_waitcnt vmcnt(9)
	ds_write_b128 v222, v[106:109] offset:16
	s_and_saveexec_b64 s[2:3], s[4:5]
	ds_write_b128 v223, v[98:101] offset:10256
	s_or_b64 exec, exec, s[2:3]
	s_waitcnt lgkmcnt(9)
	v_mfma_f32_32x32x16_bf16 v[66:81], v[150:153], v[198:201], v[66:81]
	ds_read_b128 v[170:173], v227 offset:30768
	s_waitcnt vmcnt(8)
	v_cvt_pk_bf16_f32 v150, v118, v119
	v_cvt_pk_bf16_f32 v151, v120, v121
	s_waitcnt vmcnt(7)
	v_cvt_pk_bf16_f32 v152, v122, v123
	v_cvt_pk_bf16_f32 v153, v124, v125
	ds_write2_b64 v205, v[150:151], v[152:153] offset0:130 offset1:202
	s_waitcnt vmcnt(6)
	v_cvt_pk_bf16_f32 v150, v110, v111
	v_cvt_pk_bf16_f32 v151, v112, v113
	s_waitcnt vmcnt(5)
	v_cvt_pk_bf16_f32 v152, v114, v115
	v_cvt_pk_bf16_f32 v153, v116, v117
	ds_write2_b64 v206, v[150:151], v[152:153] offset0:18 offset1:90
	v_mfma_f32_32x32x16_bf16 v[50:65], v[146:149], v[182:185], v[50:65]
	v_mfma_f32_32x32x16_bf16 v[34:49], v[146:149], v[198:201], v[34:49]
	ds_read_b128 v[174:177], v227 offset:33328
	v_mfma_f32_32x32x16_bf16 v[18:33], v[154:157], v[182:185], v[18:33]
	ds_read_b64_tr_b16 v[182:183], v233
	ds_read_b64_tr_b16 v[184:185], v233 offset:2304
	v_mfma_f32_32x32x16_bf16 v[2:17], v[154:157], v[198:201], v[2:17]
	s_waitcnt lgkmcnt(10)
	v_mfma_f32_32x32x16_bf16 v[82:97], v[158:161], v[190:193], v[82:97]
	ds_read_b128 v[178:181], v227 offset:35888
	ds_read_b64_tr_b16 v[186:187], v234 offset:64
	ds_read_b64_tr_b16 v[188:189], v234 offset:2368
	s_waitcnt lgkmcnt(3)
	s_barrier
; __device__ __forceinline__ void moe_unit(const int* pre, const int* lpre, int x, int lb, int& e, int& rb) {
;     if (lb < lpre[32]) {
;         int lo = 0, hi = 32;
;         while (hi - lo > 1) { const int mid = (lo + hi) >> 1; if (lpre[mid] <= lb) lo = mid; else hi = mid; }
;         e = x + 8 * lo; rb = lb - lpre[lo];
;     } else { e = 256; rb = (lb - lpre[32]) * 8 + x; }
	v_mfma_f32_32x32x16_bf16 v[66:81], v[158:161], v[194:197], v[66:81]
	ds_read_b128 v[154:157], v227 offset:16
	v_mfma_f32_32x32x16_bf16 v[50:65], v[162:165], v[190:193], v[50:65]
	v_mfma_f32_32x32x16_bf16 v[34:49], v[162:165], v[194:197], v[34:49]
	ds_read_b128 v[158:161], v227 offset:2576
	v_mfma_f32_32x32x16_bf16 v[18:33], v[166:169], v[190:193], v[18:33]
	ds_read_b64_tr_b16 v[162:163], v235 offset:46096
	ds_read_b64_tr_b16 v[164:165], v235 offset:48400
	v_mfma_f32_32x32x16_bf16 v[2:17], v[166:169], v[194:197], v[2:17]
	ds_read_b128 v[146:149], v227 offset:5136
	ds_read_b64_tr_b16 v[150:151], v235 offset:46160
	ds_read_b64_tr_b16 v[152:153], v235 offset:48464
	v_mfma_f32_32x32x16_bf16 v[82:97], v[170:173], v[182:185], v[82:97]
	s_waitcnt vmcnt(4)
	ds_write_b128 v222, v[126:129] offset:15376
	s_and_saveexec_b64 s[2:3], s[4:5]
	ds_write_b128 v223, v[102:105] offset:25616
	s_or_b64 exec, exec, s[2:3]
	s_waitcnt lgkmcnt(9)
	v_mfma_f32_32x32x16_bf16 v[66:81], v[170:173], v[186:189], v[66:81]
	ds_read_b128 v[166:169], v227 offset:48
	s_waitcnt vmcnt(3)
	v_cvt_pk_bf16_f32 v170, v138, v139
	v_cvt_pk_bf16_f32 v171, v140, v141
	s_waitcnt vmcnt(2)
	v_cvt_pk_bf16_f32 v172, v142, v143
	v_cvt_pk_bf16_f32 v173, v144, v145
	ds_write2_b64 v226, v[170:171], v[172:173] offset1:72
	s_waitcnt vmcnt(1)
	v_cvt_pk_bf16_f32 v170, v134, v135
	v_cvt_pk_bf16_f32 v171, v136, v137
	s_waitcnt vmcnt(0)
	v_cvt_pk_bf16_f32 v172, v130, v131
	v_cvt_pk_bf16_f32 v173, v132, v133
	ds_write2_b64 v226, v[170:171], v[172:173] offset0:144 offset1:216
	v_mfma_f32_32x32x16_bf16 v[50:65], v[174:177], v[182:185], v[50:65]
	v_mfma_f32_32x32x16_bf16 v[34:49], v[174:177], v[186:189], v[34:49]
	ds_read_b128 v[170:173], v227 offset:2608
	v_mfma_f32_32x32x16_bf16 v[18:33], v[178:181], v[182:185], v[18:33]
	ds_read_b64_tr_b16 v[174:175], v235 offset:55312
	ds_read_b64_tr_b16 v[176:177], v235 offset:57616
	v_mfma_f32_32x32x16_bf16 v[2:17], v[178:181], v[186:189], v[2:17]
	s_waitcnt lgkmcnt(10)
	v_mfma_f32_32x32x16_bf16 v[82:97], v[154:157], v[162:165], v[82:97]
	ds_read_b128 v[178:181], v227 offset:5168
	ds_read_b64_tr_b16 v[182:183], v235 offset:55376
	ds_read_b64_tr_b16 v[184:185], v235 offset:57680
	s_waitcnt lgkmcnt(3)
	s_barrier
	v_mfma_f32_32x32x16_bf16 v[66:81], v[154:157], v[150:153], v[66:81]
	ds_read_b128 v[154:157], v227 offset:15376
	v_mfma_f32_32x32x16_bf16 v[50:65], v[158:161], v[162:165], v[50:65]
	v_mfma_f32_32x32x16_bf16 v[34:49], v[158:161], v[150:153], v[34:49]
	ds_read_b128 v[158:161], v227 offset:17936
	v_mfma_f32_32x32x16_bf16 v[18:33], v[146:149], v[162:165], v[18:33]
	ds_read_b64_tr_b16 v[162:163], v228
	ds_read_b64_tr_b16 v[164:165], v228 offset:2304
	v_mfma_f32_32x32x16_bf16 v[2:17], v[146:149], v[150:153], v[2:17]
	ds_read_b128 v[146:149], v227 offset:20496
	ds_read_b64_tr_b16 v[150:151], v228 offset:64
	ds_read_b64_tr_b16 v[152:153], v228 offset:2368
	v_mfma_f32_32x32x16_bf16 v[82:97], v[166:169], v[174:177], v[82:97]
	s_waitcnt lgkmcnt(7)
	v_mfma_f32_32x32x16_bf16 v[66:81], v[166:169], v[182:185], v[66:81]
	ds_read_b128 v[166:169], v227 offset:15408
	v_mfma_f32_32x32x16_bf16 v[50:65], v[170:173], v[174:177], v[50:65]
	v_mfma_f32_32x32x16_bf16 v[34:49], v[170:173], v[182:185], v[34:49]
	ds_read_b128 v[170:173], v227 offset:17968
	v_mfma_f32_32x32x16_bf16 v[18:33], v[178:181], v[174:177], v[18:33]
	ds_read_b64_tr_b16 v[174:175], v229
	ds_read_b64_tr_b16 v[176:177], v229 offset:2304
	v_mfma_f32_32x32x16_bf16 v[2:17], v[178:181], v[182:185], v[2:17]
	s_waitcnt lgkmcnt(7)
	v_mfma_f32_32x32x16_bf16 v[82:97], v[154:157], v[162:165], v[82:97]
	ds_read_b128 v[178:181], v227 offset:20528
	ds_read_b64_tr_b16 v[182:183], v230 offset:64
	ds_read_b64_tr_b16 v[184:185], v230 offset:2368
	s_waitcnt lgkmcnt(3)
	s_barrier
	v_mfma_f32_32x32x16_bf16 v[66:81], v[154:157], v[150:153], v[66:81]
	v_mfma_f32_32x32x16_bf16 v[50:65], v[158:161], v[162:165], v[50:65]
	v_mfma_f32_32x32x16_bf16 v[34:49], v[158:161], v[150:153], v[34:49]
	v_mfma_f32_32x32x16_bf16 v[18:33], v[146:149], v[162:165], v[18:33]
	v_mfma_f32_32x32x16_bf16 v[2:17], v[146:149], v[150:153], v[2:17]
	v_mfma_f32_32x32x16_bf16 v[82:97], v[166:169], v[174:177], v[82:97]
	s_waitcnt lgkmcnt(0)
	v_mfma_f32_32x32x16_bf16 v[66:81], v[166:169], v[182:185], v[66:81]
	v_mfma_f32_32x32x16_bf16 v[50:65], v[170:173], v[174:177], v[50:65]
	v_mfma_f32_32x32x16_bf16 v[34:49], v[170:173], v[182:185], v[34:49]
	v_mfma_f32_32x32x16_bf16 v[18:33], v[178:181], v[174:177], v[18:33]
	v_mfma_f32_32x32x16_bf16 v[2:17], v[178:181], v[182:185], v[2:17]
	s_add_i32 s21, s21, s23
	s_cmp_ge_i32 s21, s22
	s_cselect_b64 s[2:3], -1, 0
	s_and_b64 vcc, exec, s[2:3]
	s_barrier
	s_cbranch_vccnz .LBB0_1456
	v_mov_b32_e32 v106, s28
	ds_read_b32 v106, v106
	s_ashr_i32 s0, s21, 1
	s_waitcnt lgkmcnt(0)
	v_cmp_ge_i32_e32 vcc, s0, v106
	s_cbranch_vccz .LBB0_1441
	v_sub_u32_e32 v106, s0, v106
	v_lshlrev_b32_e32 v106, 3, v106
	v_or_b32_e32 v146, s20, v106
	s_movk_i32 s14, 0x100
	s_cbranch_execz .LBB0_1442
	s_branch .LBB0_1445

; #define LAS __attribute__((address_space(3)))
;     __device__ __forceinline__ void st(bfr* base, int id) const {
;         bfr* d = base + ((id >> 6) * 4) * KSTR + (id & 63) * 4;
;         *(u32x2*)(d)            = (u32x2){pack2(v0.x, v0.y), pack2(v0.z, v0.w)};
;         *(u32x2*)(d + KSTR)     = (u32x2){pack2(v1.x, v1.y), pack2(v1.z, v1.w)};
;         *(u32x2*)(d + 2 * KSTR) = (u32x2){pack2(v2.x, v2.y), pack2(v2.z, v2.w)};
;         *(u32x2*)(d + 3 * KSTR) = (u32x2){pack2(v3.x, v3.y), pack2(v3.z, v3.w)};
;     }
;     __device__ __forceinline__ static bf16x8 frag(const bfr* Bb, int wn, int ni, int ks, int lane) {
;         const int g = lane >> 4, q = (lane & 15) >> 2, pp = lane & 3;
;         const bfr* a = Bb + (ks * 16 + 8 * (g >> 1) + q) * KSTR + wn * 64 + ni * 32 + 16 * (g & 1) + 4 * pp;
;         union { v4s16 h[2]; bf16x8 v; } cv;
;         cv.h[0] = __builtin_amdgcn_ds_read_tr16_b64_v4i16((v4s16 LAS*)a);
;         cv.h[1] = __builtin_amdgcn_ds_read_tr16_b64_v4i16((v4s16 LAS*)(a + 4 * KSTR));
;         return cv.v;
;     }
.LBB0_1577:
	s_or_b64 exec, exec, s[12:13]
	v_add_co_u32_e32 v122, vcc, 0x80000, v214
	s_nop 1
	v_addc_co_u32_e32 v123, vcc, 0, v215, vcc
	v_add_co_u32_e32 v124, vcc, 0x81000, v214
	s_nop 1
	v_addc_co_u32_e32 v125, vcc, 0, v215, vcc
	v_add_co_u32_e32 v142, vcc, 0x82000, v214
	global_load_dwordx4 v[134:137], v[122:123], off
	s_nop 0
	global_load_dwordx4 v[122:125], v[124:125], off
	v_addc_co_u32_e32 v143, vcc, 0, v215, vcc
	v_add_co_u32_e32 v144, vcc, 0x83000, v214
	s_nop 1
	v_addc_co_u32_e32 v145, vcc, 0, v215, vcc
	global_load_dwordx4 v[150:153], v[142:143], off
	s_nop 0
	global_load_dwordx4 v[142:145], v[144:145], off
	v_mfma_f32_32x32x16_bf16 v[34:49], v[158:161], v[178:181], v[34:49]
	ds_read_b128 v[158:161], v219 offset:17968
	v_mfma_f32_32x32x16_bf16 v[18:33], v[162:165], v[182:185], v[18:33]
	ds_read_b64_tr_b16 v[182:183], v221
	ds_read_b64_tr_b16 v[184:185], v221 offset:2304
	v_mfma_f32_32x32x16_bf16 v[2:17], v[162:165], v[178:181], v[2:17]
	s_waitcnt lgkmcnt(10)
	v_mfma_f32_32x32x16_bf16 v[82:97], v[166:169], v[174:177], v[82:97]
	ds_read_b128 v[162:165], v219 offset:20528
	ds_read_b64_tr_b16 v[194:195], v222 offset:64
	ds_read_b64_tr_b16 v[196:197], v222 offset:2368
	s_waitcnt lgkmcnt(3)
	s_barrier
	v_mfma_f32_32x32x16_bf16 v[66:81], v[166:169], v[154:157], v[66:81]
	ds_read_b128 v[166:169], v219 offset:30736
	v_mfma_f32_32x32x16_bf16 v[50:65], v[170:173], v[174:177], v[50:65]
	v_mfma_f32_32x32x16_bf16 v[34:49], v[170:173], v[154:157], v[34:49]
	ds_read_b128 v[170:173], v219 offset:33296
	v_mfma_f32_32x32x16_bf16 v[18:33], v[138:141], v[174:177], v[18:33]
	ds_read_b64_tr_b16 v[178:179], v224
	ds_read_b64_tr_b16 v[180:181], v224 offset:2304
	v_mfma_f32_32x32x16_bf16 v[2:17], v[138:141], v[154:157], v[2:17]
	ds_read_b128 v[174:177], v219 offset:35856
	ds_read_b64_tr_b16 v[190:191], v224 offset:64
	ds_read_b64_tr_b16 v[192:193], v224 offset:2368
	v_mfma_f32_32x32x16_bf16 v[82:97], v[146:149], v[182:185], v[82:97]
	s_waitcnt vmcnt(9)
	ds_write_b128 v203, v[110:113] offset:16
	s_and_saveexec_b64 s[12:13], s[4:5]
	ds_write_b128 v216, v[102:105] offset:10256
	s_or_b64 exec, exec, s[12:13]
	s_waitcnt lgkmcnt(9)
	v_mfma_f32_32x32x16_bf16 v[66:81], v[146:149], v[194:197], v[66:81]
	ds_read_b128 v[110:113], v219 offset:30768
	s_waitcnt vmcnt(8)
	v_cvt_pk_bf16_f32 v118, v118, v119
	v_cvt_pk_bf16_f32 v119, v120, v121
	s_waitcnt vmcnt(7)
	v_cvt_pk_bf16_f32 v114, v114, v115
	v_cvt_pk_bf16_f32 v115, v116, v117
	ds_write2_b64 v198, v[118:119], v[114:115] offset0:130 offset1:202
	s_waitcnt vmcnt(6)
	v_cvt_pk_bf16_f32 v114, v130, v131
	v_cvt_pk_bf16_f32 v115, v132, v133
	s_waitcnt vmcnt(5)
	v_cvt_pk_bf16_f32 v116, v126, v127
	v_cvt_pk_bf16_f32 v117, v128, v129
	ds_write2_b64 v211, v[114:115], v[116:117] offset0:18 offset1:90
	v_mfma_f32_32x32x16_bf16 v[50:65], v[158:161], v[182:185], v[50:65]
	global_load_dwordx4 v[126:129], v[200:201], off offset:320
	s_and_saveexec_b64 s[12:13], s[4:5]
	s_cbranch_execz .LBB0_1581
	global_load_dwordx4 v[102:105], v[206:207], off offset:320
.LBB0_1581:
	s_or_b64 exec, exec, s[12:13]
	v_add_co_u32_e32 v114, vcc, 0xa0000, v214
	s_nop 1
	v_addc_co_u32_e32 v115, vcc, 0, v215, vcc
	v_add_co_u32_e32 v116, vcc, 0xa1000, v214
	s_nop 1
	v_addc_co_u32_e32 v117, vcc, 0, v215, vcc
	global_load_dwordx4 v[138:141], v[114:115], off
	global_load_dwordx4 v[130:133], v[116:117], off
	v_add_co_u32_e32 v114, vcc, 0xa2000, v214
	s_nop 1
	v_addc_co_u32_e32 v115, vcc, 0, v215, vcc
	v_add_co_u32_e32 v116, vcc, 0xa3000, v214
	s_nop 1
	v_addc_co_u32_e32 v117, vcc, 0, v215, vcc
	global_load_dwordx4 v[154:157], v[114:115], off
	global_load_dwordx4 v[146:149], v[116:117], off
	v_mfma_f32_32x32x16_bf16 v[34:49], v[158:161], v[194:197], v[34:49]
	ds_read_b128 v[158:161], v219 offset:33328
	v_mfma_f32_32x32x16_bf16 v[18:33], v[162:165], v[182:185], v[18:33]
	ds_read_b64_tr_b16 v[186:187], v225
	ds_read_b64_tr_b16 v[188:189], v225 offset:2304
	v_mfma_f32_32x32x16_bf16 v[2:17], v[162:165], v[194:197], v[2:17]
	s_waitcnt lgkmcnt(10)
	v_mfma_f32_32x32x16_bf16 v[82:97], v[166:169], v[178:181], v[82:97]
	ds_read_b128 v[162:165], v219 offset:35888
	ds_read_b64_tr_b16 v[194:195], v226 offset:64
	ds_read_b64_tr_b16 v[196:197], v226 offset:2368
	s_waitcnt lgkmcnt(3)
	s_barrier
	v_mfma_f32_32x32x16_bf16 v[66:81], v[166:169], v[190:193], v[66:81]
	ds_read_b128 v[166:169], v219 offset:16
	v_mfma_f32_32x32x16_bf16 v[50:65], v[170:173], v[178:181], v[50:65]
	v_mfma_f32_32x32x16_bf16 v[34:49], v[170:173], v[190:193], v[34:49]
	ds_read_b128 v[170:173], v219 offset:2576
	v_mfma_f32_32x32x16_bf16 v[18:33], v[174:177], v[178:181], v[18:33]
	ds_read_b64_tr_b16 v[182:183], v227 offset:46096
	ds_read_b64_tr_b16 v[184:185], v227 offset:48400
	v_mfma_f32_32x32x16_bf16 v[2:17], v[174:177], v[190:193], v[2:17]
	ds_read_b128 v[174:177], v219 offset:5136
	ds_read_b64_tr_b16 v[190:191], v227 offset:46160
	ds_read_b64_tr_b16 v[192:193], v227 offset:48464
	v_mfma_f32_32x32x16_bf16 v[82:97], v[110:113], v[186:189], v[82:97]
	s_waitcnt vmcnt(9)
	ds_write_b128 v203, v[106:109] offset:15376
	s_and_saveexec_b64 s[12:13], s[4:5]
	ds_write_b128 v216, v[98:101] offset:25616
	s_or_b64 exec, exec, s[12:13]
	s_waitcnt lgkmcnt(9)
	v_mfma_f32_32x32x16_bf16 v[66:81], v[110:113], v[194:197], v[66:81]
	ds_read_b128 v[178:181], v219 offset:48
	s_waitcnt vmcnt(8)
	v_cvt_pk_bf16_f32 v106, v134, v135
	v_cvt_pk_bf16_f32 v107, v136, v137
	s_waitcnt vmcnt(7)
	v_cvt_pk_bf16_f32 v108, v122, v123
	v_cvt_pk_bf16_f32 v109, v124, v125
	ds_write2_b64 v218, v[106:107], v[108:109] offset1:72
	s_waitcnt vmcnt(6)
	v_cvt_pk_bf16_f32 v106, v150, v151
	v_cvt_pk_bf16_f32 v107, v152, v153
	s_waitcnt vmcnt(5)
	v_cvt_pk_bf16_f32 v108, v142, v143
	v_cvt_pk_bf16_f32 v109, v144, v145
	ds_write2_b64 v218, v[106:107], v[108:109] offset0:144 offset1:216
	v_mfma_f32_32x32x16_bf16 v[50:65], v[158:161], v[186:189], v[50:65]
	global_load_dwordx4 v[106:109], v[200:201], off offset:384
	s_and_saveexec_b64 s[12:13], s[4:5]
	s_cbranch_execz .LBB0_1585
	global_load_dwordx4 v[98:101], v[206:207], off offset:384
; #define LAS __attribute__((address_space(3)))
;     __device__ __forceinline__ void st(bfr* base, int id) const {
;         bfr* d = base + ((id >> 6) * 4) * KSTR + (id & 63) * 4;
;         *(u32x2*)(d)            = (u32x2){pack2(v0.x, v0.y), pack2(v0.z, v0.w)};
;         *(u32x2*)(d + KSTR)     = (u32x2){pack2(v1.x, v1.y), pack2(v1.z, v1.w)};
;         *(u32x2*)(d + 2 * KSTR) = (u32x2){pack2(v2.x, v2.y), pack2(v2.z, v2.w)};
;         *(u32x2*)(d + 3 * KSTR) = (u32x2){pack2(v3.x, v3.y), pack2(v3.z, v3.w)};
;     }
;     __device__ __forceinline__ static bf16x8 frag(const bfr* Bb, int wn, int ni, int ks, int lane) {
;         const int g = lane >> 4, q = (lane & 15) >> 2, pp = lane & 3;
;         const bfr* a = Bb + (ks * 16 + 8 * (g >> 1) + q) * KSTR + wn * 64 + ni * 32 + 16 * (g & 1) + 4 * pp;
;         union { v4s16 h[2]; bf16x8 v; } cv;
;         cv.h[0] = __builtin_amdgcn_ds_read_tr16_b64_v4i16((v4s16 LAS*)a);
;         cv.h[1] = __builtin_amdgcn_ds_read_tr16_b64_v4i16((v4s16 LAS*)(a + 4 * KSTR));
;         return cv.v;
;     }
.LBB0_1585:
	s_or_b64 exec, exec, s[12:13]
	v_add_co_u32_e32 v110, vcc, 0xc0000, v214
	s_nop 1
	v_addc_co_u32_e32 v111, vcc, 0, v215, vcc
	v_add_co_u32_e32 v112, vcc, 0xc1000, v214
	s_nop 1
	v_addc_co_u32_e32 v113, vcc, 0, v215, vcc
	v_add_co_u32_e32 v114, vcc, 0xc2000, v214
	global_load_dwordx4 v[118:121], v[110:111], off
	s_nop 0
	global_load_dwordx4 v[110:113], v[112:113], off
	v_addc_co_u32_e32 v115, vcc, 0, v215, vcc
	v_add_co_u32_e32 v122, vcc, 0xc3000, v214
	s_nop 1
	v_addc_co_u32_e32 v123, vcc, 0, v215, vcc
	global_load_dwordx4 v[114:117], v[114:115], off
	s_nop 0
	global_load_dwordx4 v[122:125], v[122:123], off
	v_mfma_f32_32x32x16_bf16 v[34:49], v[158:161], v[194:197], v[34:49]
	ds_read_b128 v[158:161], v219 offset:2608
	v_mfma_f32_32x32x16_bf16 v[18:33], v[162:165], v[186:189], v[18:33]
	ds_read_b64_tr_b16 v[186:187], v227 offset:55312
	ds_read_b64_tr_b16 v[188:189], v227 offset:57616
	v_mfma_f32_32x32x16_bf16 v[2:17], v[162:165], v[194:197], v[2:17]
	s_waitcnt lgkmcnt(10)
	v_mfma_f32_32x32x16_bf16 v[82:97], v[166:169], v[182:185], v[82:97]
	ds_read_b128 v[162:165], v219 offset:5168
	ds_read_b64_tr_b16 v[194:195], v227 offset:55376
	ds_read_b64_tr_b16 v[196:197], v227 offset:57680
	s_waitcnt lgkmcnt(3)
	s_barrier
	v_mfma_f32_32x32x16_bf16 v[66:81], v[166:169], v[190:193], v[66:81]
	ds_read_b128 v[166:169], v219 offset:15376
	v_mfma_f32_32x32x16_bf16 v[50:65], v[170:173], v[182:185], v[50:65]
	v_mfma_f32_32x32x16_bf16 v[34:49], v[170:173], v[190:193], v[34:49]
	ds_read_b128 v[170:173], v219 offset:17936
	v_mfma_f32_32x32x16_bf16 v[18:33], v[174:177], v[182:185], v[18:33]
	ds_read_b64_tr_b16 v[182:183], v220
	ds_read_b64_tr_b16 v[184:185], v220 offset:2304
	v_mfma_f32_32x32x16_bf16 v[2:17], v[174:177], v[190:193], v[2:17]
	ds_read_b128 v[174:177], v219 offset:20496
	ds_read_b64_tr_b16 v[190:191], v220 offset:64
	ds_read_b64_tr_b16 v[192:193], v220 offset:2368
	v_mfma_f32_32x32x16_bf16 v[82:97], v[178:181], v[186:189], v[82:97]
	s_waitcnt vmcnt(9)
	ds_write_b128 v203, v[126:129] offset:30736
	s_and_saveexec_b64 s[12:13], s[4:5]
	ds_write_b128 v216, v[102:105] offset:40976
	s_or_b64 exec, exec, s[12:13]
	s_waitcnt lgkmcnt(9)
	v_mfma_f32_32x32x16_bf16 v[66:81], v[178:181], v[194:197], v[66:81]
	ds_read_b128 v[150:153], v219 offset:15408
	s_waitcnt vmcnt(8)
	v_cvt_pk_bf16_f32 v126, v138, v139
	v_cvt_pk_bf16_f32 v127, v140, v141
	s_waitcnt vmcnt(7)
	v_cvt_pk_bf16_f32 v128, v130, v131
	v_cvt_pk_bf16_f32 v129, v132, v133
	ds_write2_b64 v223, v[126:127], v[128:129] offset1:72
	s_waitcnt vmcnt(6)
	v_cvt_pk_bf16_f32 v126, v154, v155
	v_cvt_pk_bf16_f32 v127, v156, v157
	s_waitcnt vmcnt(5)
	v_cvt_pk_bf16_f32 v128, v146, v147
	v_cvt_pk_bf16_f32 v129, v148, v149
	ds_write2_b64 v223, v[126:127], v[128:129] offset0:144 offset1:216
	v_mfma_f32_32x32x16_bf16 v[50:65], v[158:161], v[186:189], v[50:65]
	global_load_dwordx4 v[126:129], v[200:201], off offset:448
	s_and_saveexec_b64 s[12:13], s[4:5]
	s_cbranch_execz .LBB0_1589
	global_load_dwordx4 v[102:105], v[206:207], off offset:448
.LBB0_1589:
	s_or_b64 exec, exec, s[12:13]
	v_add_co_u32_e32 v130, vcc, 0xe0000, v214
	s_nop 1
	v_addc_co_u32_e32 v131, vcc, 0, v215, vcc
	v_add_co_u32_e32 v134, vcc, 0xe1000, v214
	s_nop 1
	v_addc_co_u32_e32 v135, vcc, 0, v215, vcc
	v_add_co_u32_e32 v138, vcc, 0xe2000, v214
	global_load_dwordx4 v[130:133], v[130:131], off
	s_nop 0
	global_load_dwordx4 v[134:137], v[134:135], off
	v_addc_co_u32_e32 v139, vcc, 0, v215, vcc
	v_add_co_u32_e32 v142, vcc, 0xe3000, v214
	s_nop 1
	v_addc_co_u32_e32 v143, vcc, 0, v215, vcc
	global_load_dwordx4 v[138:141], v[138:139], off
	s_nop 0
	global_load_dwordx4 v[142:145], v[142:143], off
	v_mfma_f32_32x32x16_bf16 v[34:49], v[158:161], v[194:197], v[34:49]
	ds_read_b128 v[146:149], v219 offset:17968
	v_mfma_f32_32x32x16_bf16 v[18:33], v[162:165], v[186:189], v[18:33]
	ds_read_b64_tr_b16 v[178:179], v221
	ds_read_b64_tr_b16 v[180:181], v221 offset:2304
	v_mfma_f32_32x32x16_bf16 v[2:17], v[162:165], v[194:197], v[2:17]
	s_waitcnt lgkmcnt(10)
	v_mfma_f32_32x32x16_bf16 v[82:97], v[166:169], v[182:185], v[82:97]
	ds_read_b128 v[154:157], v219 offset:20528
	ds_read_b64_tr_b16 v[194:195], v222 offset:64
	ds_read_b64_tr_b16 v[196:197], v222 offset:2368
	s_waitcnt lgkmcnt(3)
	s_barrier
	v_mfma_f32_32x32x16_bf16 v[66:81], v[166:169], v[190:193], v[66:81]
	ds_read_b128 v[158:161], v219 offset:30736
	v_mfma_f32_32x32x16_bf16 v[50:65], v[170:173], v[182:185], v[50:65]
	v_mfma_f32_32x32x16_bf16 v[34:49], v[170:173], v[190:193], v[34:49]
	ds_read_b128 v[162:165], v219 offset:33296
	v_mfma_f32_32x32x16_bf16 v[18:33], v[174:177], v[182:185], v[18:33]
	ds_read_b64_tr_b16 v[182:183], v224
	ds_read_b64_tr_b16 v[184:185], v224 offset:2304
	v_mfma_f32_32x32x16_bf16 v[2:17], v[174:177], v[190:193], v[2:17]
	ds_read_b128 v[166:169], v219 offset:35856
	ds_read_b64_tr_b16 v[186:187], v224 offset:64
	ds_read_b64_tr_b16 v[188:189], v224 offset:2368
	v_mfma_f32_32x32x16_bf16 v[82:97], v[150:153], v[178:181], v[82:97]
	s_waitcnt vmcnt(9)
	ds_write_b128 v203, v[106:109] offset:16
	s_and_saveexec_b64 s[12:13], s[4:5]
	ds_write_b128 v216, v[98:101] offset:10256
	s_or_b64 exec, exec, s[12:13]
	s_waitcnt lgkmcnt(9)
	v_mfma_f32_32x32x16_bf16 v[66:81], v[150:153], v[194:197], v[66:81]
	ds_read_b128 v[170:173], v219 offset:30768
	s_waitcnt vmcnt(8)
	v_cvt_pk_bf16_f32 v150, v118, v119
	v_cvt_pk_bf16_f32 v151, v120, v121
	s_waitcnt vmcnt(7)
	v_cvt_pk_bf16_f32 v152, v110, v111
	v_cvt_pk_bf16_f32 v153, v112, v113
	ds_write2_b64 v198, v[150:151], v[152:153] offset0:130 offset1:202
	s_waitcnt vmcnt(6)
	v_cvt_pk_bf16_f32 v150, v114, v115
	v_cvt_pk_bf16_f32 v151, v116, v117
	s_waitcnt vmcnt(5)
	v_cvt_pk_bf16_f32 v152, v122, v123
	v_cvt_pk_bf16_f32 v153, v124, v125
	ds_write2_b64 v211, v[150:151], v[152:153] offset0:18 offset1:90
	v_mfma_f32_32x32x16_bf16 v[50:65], v[146:149], v[178:181], v[50:65]
	v_mfma_f32_32x32x16_bf16 v[34:49], v[146:149], v[194:197], v[34:49]
	ds_read_b128 v[174:177], v219 offset:33328
	v_mfma_f32_32x32x16_bf16 v[18:33], v[154:157], v[178:181], v[18:33]
	ds_read_b64_tr_b16 v[178:179], v225
	ds_read_b64_tr_b16 v[180:181], v225 offset:2304
	v_mfma_f32_32x32x16_bf16 v[2:17], v[154:157], v[194:197], v[2:17]
	s_waitcnt lgkmcnt(10)
	v_mfma_f32_32x32x16_bf16 v[82:97], v[158:161], v[182:185], v[82:97]
	ds_read_b128 v[190:193], v219 offset:35888
	ds_read_b64_tr_b16 v[194:195], v226 offset:64
	ds_read_b64_tr_b16 v[196:197], v226 offset:2368
	s_waitcnt lgkmcnt(3)
	s_barrier
; __device__ __forceinline__ void moe_unit(const int* pre, const int* lpre, int x, int lb, int& e, int& rb) {
;     if (lb < lpre[32]) {
;         int lo = 0, hi = 32;
;         while (hi - lo > 1) { const int mid = (lo + hi) >> 1; if (lpre[mid] <= lb) lo = mid; else hi = mid; }
;         e = x + 8 * lo; rb = lb - lpre[lo];
;     } else { e = 256; rb = (lb - lpre[32]) * 8 + x; }
	v_mfma_f32_32x32x16_bf16 v[66:81], v[158:161], v[186:189], v[66:81]
	ds_read_b128 v[154:157], v219 offset:16
	v_mfma_f32_32x32x16_bf16 v[50:65], v[162:165], v[182:185], v[50:65]
	v_mfma_f32_32x32x16_bf16 v[34:49], v[162:165], v[186:189], v[34:49]
	ds_read_b128 v[158:161], v219 offset:2576
	v_mfma_f32_32x32x16_bf16 v[18:33], v[166:169], v[182:185], v[18:33]
	ds_read_b64_tr_b16 v[162:163], v227 offset:46096
	ds_read_b64_tr_b16 v[164:165], v227 offset:48400
	v_mfma_f32_32x32x16_bf16 v[2:17], v[166:169], v[186:189], v[2:17]
	ds_read_b128 v[146:149], v219 offset:5136
	ds_read_b64_tr_b16 v[150:151], v227 offset:46160
	ds_read_b64_tr_b16 v[152:153], v227 offset:48464
	v_mfma_f32_32x32x16_bf16 v[82:97], v[170:173], v[178:181], v[82:97]
	s_waitcnt vmcnt(4)
	ds_write_b128 v203, v[126:129] offset:15376
	s_and_saveexec_b64 s[12:13], s[4:5]
	ds_write_b128 v216, v[102:105] offset:25616
	s_or_b64 exec, exec, s[12:13]
	s_waitcnt lgkmcnt(9)
	v_mfma_f32_32x32x16_bf16 v[66:81], v[170:173], v[194:197], v[66:81]
	ds_read_b128 v[166:169], v219 offset:48
	s_waitcnt vmcnt(3)
	v_cvt_pk_bf16_f32 v170, v130, v131
	v_cvt_pk_bf16_f32 v171, v132, v133
	s_waitcnt vmcnt(2)
	v_cvt_pk_bf16_f32 v172, v134, v135
	v_cvt_pk_bf16_f32 v173, v136, v137
	ds_write2_b64 v218, v[170:171], v[172:173] offset1:72
	s_waitcnt vmcnt(1)
	v_cvt_pk_bf16_f32 v170, v138, v139
	v_cvt_pk_bf16_f32 v171, v140, v141
	s_waitcnt vmcnt(0)
	v_cvt_pk_bf16_f32 v172, v142, v143
	v_cvt_pk_bf16_f32 v173, v144, v145
	ds_write2_b64 v218, v[170:171], v[172:173] offset0:144 offset1:216
	v_mfma_f32_32x32x16_bf16 v[50:65], v[174:177], v[178:181], v[50:65]
	v_mfma_f32_32x32x16_bf16 v[34:49], v[174:177], v[194:197], v[34:49]
	ds_read_b128 v[170:173], v219 offset:2608
	v_mfma_f32_32x32x16_bf16 v[18:33], v[190:193], v[178:181], v[18:33]
	ds_read_b64_tr_b16 v[174:175], v227 offset:55312
	ds_read_b64_tr_b16 v[176:177], v227 offset:57616
	v_mfma_f32_32x32x16_bf16 v[2:17], v[190:193], v[194:197], v[2:17]
	s_waitcnt lgkmcnt(10)
	v_mfma_f32_32x32x16_bf16 v[82:97], v[154:157], v[162:165], v[82:97]
	ds_read_b128 v[178:181], v219 offset:5168
	ds_read_b64_tr_b16 v[182:183], v227 offset:55376
	ds_read_b64_tr_b16 v[184:185], v227 offset:57680
	s_waitcnt lgkmcnt(3)
	s_barrier
	v_mfma_f32_32x32x16_bf16 v[66:81], v[154:157], v[150:153], v[66:81]
	ds_read_b128 v[154:157], v219 offset:15376
	v_mfma_f32_32x32x16_bf16 v[50:65], v[158:161], v[162:165], v[50:65]
	v_mfma_f32_32x32x16_bf16 v[34:49], v[158:161], v[150:153], v[34:49]
	ds_read_b128 v[158:161], v219 offset:17936
	v_mfma_f32_32x32x16_bf16 v[18:33], v[146:149], v[162:165], v[18:33]
	ds_read_b64_tr_b16 v[162:163], v220
	ds_read_b64_tr_b16 v[164:165], v220 offset:2304
	v_mfma_f32_32x32x16_bf16 v[2:17], v[146:149], v[150:153], v[2:17]
	ds_read_b128 v[146:149], v219 offset:20496
	ds_read_b64_tr_b16 v[150:151], v220 offset:64
	ds_read_b64_tr_b16 v[152:153], v220 offset:2368
	v_mfma_f32_32x32x16_bf16 v[82:97], v[166:169], v[174:177], v[82:97]
	s_waitcnt lgkmcnt(7)
	v_mfma_f32_32x32x16_bf16 v[66:81], v[166:169], v[182:185], v[66:81]
	ds_read_b128 v[166:169], v219 offset:15408
	v_mfma_f32_32x32x16_bf16 v[50:65], v[170:173], v[174:177], v[50:65]
	v_mfma_f32_32x32x16_bf16 v[34:49], v[170:173], v[182:185], v[34:49]
	ds_read_b128 v[170:173], v219 offset:17968
	v_mfma_f32_32x32x16_bf16 v[18:33], v[178:181], v[174:177], v[18:33]
	ds_read_b64_tr_b16 v[174:175], v221
	ds_read_b64_tr_b16 v[176:177], v221 offset:2304
	v_mfma_f32_32x32x16_bf16 v[2:17], v[178:181], v[182:185], v[2:17]
	s_waitcnt lgkmcnt(7)
	v_mfma_f32_32x32x16_bf16 v[82:97], v[154:157], v[162:165], v[82:97]
	ds_read_b128 v[178:181], v219 offset:20528
	ds_read_b64_tr_b16 v[182:183], v222 offset:64
	ds_read_b64_tr_b16 v[184:185], v222 offset:2368
	s_waitcnt lgkmcnt(3)
	s_barrier
	v_mfma_f32_32x32x16_bf16 v[66:81], v[154:157], v[150:153], v[66:81]
	v_mfma_f32_32x32x16_bf16 v[50:65], v[158:161], v[162:165], v[50:65]
	v_mfma_f32_32x32x16_bf16 v[34:49], v[158:161], v[150:153], v[34:49]
	v_mfma_f32_32x32x16_bf16 v[18:33], v[146:149], v[162:165], v[18:33]
	v_mfma_f32_32x32x16_bf16 v[2:17], v[146:149], v[150:153], v[2:17]
	v_mfma_f32_32x32x16_bf16 v[82:97], v[166:169], v[174:177], v[82:97]
	s_waitcnt lgkmcnt(0)
	v_mfma_f32_32x32x16_bf16 v[66:81], v[166:169], v[182:185], v[66:81]
	v_mfma_f32_32x32x16_bf16 v[50:65], v[170:173], v[174:177], v[50:65]
	v_mfma_f32_32x32x16_bf16 v[34:49], v[170:173], v[182:185], v[34:49]
	v_mfma_f32_32x32x16_bf16 v[18:33], v[178:181], v[174:177], v[18:33]
	v_mfma_f32_32x32x16_bf16 v[2:17], v[178:181], v[182:185], v[2:17]
	s_add_i32 s23, s23, s27
	s_cmp_ge_i32 s23, s24
	s_cselect_b64 s[12:13], -1, 0
	s_and_b64 vcc, exec, s[12:13]
	s_barrier
	s_cbranch_vccnz .LBB0_1614
	v_mov_b32_e32 v106, s29
	ds_read_b32 v106, v106
	s_ashr_i32 s0, s23, 2
	s_waitcnt lgkmcnt(0)
	v_cmp_ge_i32_e32 vcc, s0, v106
	s_cbranch_vccz .LBB0_1596
	v_sub_u32_e32 v106, s0, v106
	v_lshlrev_b32_e32 v106, 3, v106
	v_or_b32_e32 v108, s22, v106
	s_movk_i32 s14, 0x100
	s_cbranch_execz .LBB0_1597
	s_branch .LBB0_1600

; __device__ __forceinline__ void phase_s5b_gqa(const Params& P, unsigned char* smraw, int bid, int nb) {
;     if (bid < 8) {
;         const int i = bid * NTHR + threadIdx.x;
;         const float2 a = ((const float2*)(P.ws + WS_A64))[i];
;         const float2* SE = (const float2*)(P.ws + WS_SE);
;         float2* CIN = (float2*)(P.ws + WS_CIN);
;         float sr = 0.f, si = 0.f;
;         for (int c0 = 0; c0 < 260; c0 += 20) {
;             float2 e[20];
; #pragma unroll
;             for (int j = 0; j < 20; ++j) e[j] = SE[(size_t)(c0 + j) * 4096 + i];
; #pragma unroll
;             for (int j = 0; j < 20; ++j) {
;                 CIN[(size_t)(c0 + j) * 4096 + i] = make_float2(sr, si);
;                 const float nr = a.x * sr - a.y * si + e[j].x, ni = a.x * si + a.y * sr + e[j].y;
;                 sr = nr; si = ni;
;             }
;         }
;     }
.LBB0_1884:
	s_cmp_lt_i32 s6, 13
	s_cselect_b64 s[0:1], -1, 0
	s_cmp_gt_i32 s7, 12
	s_cselect_b64 s[2:3], -1, 0
	s_and_b64 s[0:1], s[0:1], s[2:3]
	s_andn2_b64 vcc, exec, s[0:1]
	s_cbranch_vccnz .LBB0_1950
	s_cmp_gt_i32 s44, 63
	s_cbranch_scc1 .LBB0_1887
	s_mov_b64 s[98:99], exec
	v_cmp_gt_u32_e32 vcc, 64, v0
	s_and_b64 exec, exec, vcc
	s_cbranch_execz .Lscan_skip
	v_lshl_or_b32 v2, s44, 6, v0
	v_ashrrev_i32_e32 v3, 31, v2
	v_lshl_add_u64 v[2:3], v[2:3], 3, s[42:43]
	v_add_co_u32_e32 v4, vcc, 0x3a932000, v2
	v_mov_b32_e32 v6, 0
	s_nop 0
	v_addc_co_u32_e32 v5, vcc, 0, v3, vcc
	v_mov_b32_e32 v7, v6
	global_store_dwordx2 v[4:5], v[6:7], off offset:1024
	v_add_co_u32_e32 v4, vcc, 0x3a112000, v2
	s_nop 1
	v_addc_co_u32_e32 v5, vcc, 0, v3, vcc
	v_add_co_u32_e32 v6, vcc, 0x3a11a000, v2
	s_nop 1
	v_addc_co_u32_e32 v7, vcc, 0, v3, vcc
	v_add_co_u32_e32 v10, vcc, 0x3a122000, v2
	s_nop 1
	v_addc_co_u32_e32 v11, vcc, 0, v3, vcc
	v_add_co_u32_e32 v14, vcc, 0x3a12a000, v2
	s_nop 1
	v_addc_co_u32_e32 v15, vcc, 0, v3, vcc
	global_load_dwordx2 v[32:33], v[4:5], off offset:1024
	global_load_dwordx2 v[22:23], v[6:7], off offset:1024
	global_load_dwordx2 v[12:13], v[10:11], off offset:1024
	global_load_dwordx2 v[8:9], v[14:15], off offset:1024
	v_add_co_u32_e32 v4, vcc, 0x3a132000, v2
	s_nop 1
	v_addc_co_u32_e32 v5, vcc, 0, v3, vcc
	v_add_co_u32_e32 v6, vcc, 0x3a13a000, v2
	s_nop 1
	v_addc_co_u32_e32 v7, vcc, 0, v3, vcc
	v_add_co_u32_e32 v14, vcc, 0x3a142000, v2
	s_nop 1
	v_addc_co_u32_e32 v15, vcc, 0, v3, vcc
	v_add_co_u32_e32 v18, vcc, 0x3a14a000, v2
	s_nop 1
	v_addc_co_u32_e32 v19, vcc, 0, v3, vcc
	global_load_dwordx2 v[36:37], v[4:5], off offset:1024
	global_load_dwordx2 v[26:27], v[6:7], off offset:1024
	global_load_dwordx2 v[16:17], v[14:15], off offset:1024
	global_load_dwordx2 v[10:11], v[18:19], off offset:1024
	v_add_co_u32_e32 v4, vcc, 0x3a152000, v2
	s_nop 1
	v_addc_co_u32_e32 v5, vcc, 0, v3, vcc
	v_add_co_u32_e32 v6, vcc, 0x3a15a000, v2
	s_nop 1
	v_addc_co_u32_e32 v7, vcc, 0, v3, vcc
	v_add_co_u32_e32 v18, vcc, 0x3a162000, v2
	s_nop 1
	v_addc_co_u32_e32 v19, vcc, 0, v3, vcc
	v_add_co_u32_e32 v20, vcc, 0x3a16a000, v2
	s_nop 1
	v_addc_co_u32_e32 v21, vcc, 0, v3, vcc
	global_load_dwordx2 v[40:41], v[4:5], off offset:1024
	global_load_dwordx2 v[34:35], v[6:7], off offset:1024
	global_load_dwordx2 v[24:25], v[18:19], off offset:1024
	global_load_dwordx2 v[14:15], v[20:21], off offset:1024
	v_add_co_u32_e32 v4, vcc, 0x3a172000, v2
	s_nop 1
	v_addc_co_u32_e32 v5, vcc, 0, v3, vcc
	v_add_co_u32_e32 v6, vcc, 0x3a17a000, v2
	s_nop 1
	v_addc_co_u32_e32 v7, vcc, 0, v3, vcc
	v_add_co_u32_e32 v20, vcc, 0x3a182000, v2
	s_nop 1
	v_addc_co_u32_e32 v21, vcc, 0, v3, vcc
	v_add_co_u32_e32 v30, vcc, 0x3a18a000, v2
	s_nop 1
	v_addc_co_u32_e32 v31, vcc, 0, v3, vcc
	global_load_dwordx2 v[44:45], v[4:5], off offset:1024
	global_load_dwordx2 v[38:39], v[6:7], off offset:1024
	global_load_dwordx2 v[28:29], v[20:21], off offset:1024
	global_load_dwordx2 v[18:19], v[30:31], off offset:1024
	v_add_co_u32_e32 v4, vcc, 0x3a192000, v2
	s_nop 1
	v_addc_co_u32_e32 v5, vcc, 0, v3, vcc
	v_add_co_u32_e32 v46, vcc, 0x3a19a000, v2
	s_nop 1
	v_addc_co_u32_e32 v47, vcc, 0, v3, vcc
	v_add_co_u32_e32 v48, vcc, 0x3a1a2000, v2
	s_nop 1
	v_addc_co_u32_e32 v49, vcc, 0, v3, vcc
	v_add_co_u32_e32 v50, vcc, 0x3a1aa000, v2
	s_nop 1
	v_addc_co_u32_e32 v51, vcc, 0, v3, vcc
	global_load_dwordx2 v[42:43], v[4:5], off offset:1024
	global_load_dwordx2 v[30:31], v[46:47], off offset:1024
	global_load_dwordx2 v[20:21], v[48:49], off offset:1024
	global_load_dwordx2 v[6:7], v[50:51], off offset:1024
	v_add_co_u32_e32 v46, vcc, 0x3a1b2000, v2
	s_nop 1
	v_addc_co_u32_e32 v47, vcc, 0, v3, vcc
	v_add_co_u32_e32 v4, vcc, 0x4f30000, v2
	s_nop 1
	v_addc_co_u32_e32 v5, vcc, 0, v3, vcc
	global_load_dwordx2 v[4:5], v[4:5], off
	v_add_co_u32_e32 v52, vcc, 0x3a93a000, v2
	s_mov_b64 s[4:5], vcc
	v_add_co_u32_e32 v54, vcc, 0x3a942000, v2
	s_mov_b64 s[8:9], vcc
	v_add_co_u32_e32 v56, vcc, 0x3a94a000, v2
	s_mov_b64 s[10:11], vcc
	v_add_co_u32_e32 v62, vcc, 0x3a952000, v2
	s_mov_b64 s[12:13], vcc
	v_add_co_u32_e32 v64, vcc, 0x3a95a000, v2
	s_mov_b64 s[14:15], vcc
	s_waitcnt vmcnt(25)
	v_add_co_u32_e32 v68, vcc, 0x3a962000, v2
	s_mov_b64 s[16:17], vcc
	s_waitcnt vmcnt(22)
	v_add_co_u32_e32 v70, vcc, 0x3a96a000, v2
	s_mov_b64 s[20:21], vcc
	v_add_co_u32_e32 v72, vcc, 0x3a972000, v2
	s_mov_b64 s[24:25], vcc
	v_add_co_u32_e32 v74, vcc, 0x3a97a000, v2
	s_mov_b64 s[26:27], vcc
	v_add_co_u32_e32 v76, vcc, 0x3a982000, v2
	s_mov_b64 s[28:29], vcc
	v_add_co_u32_e32 v78, vcc, 0x3a98a000, v2
	s_mov_b64 s[30:31], vcc
	v_add_co_u32_e32 v80, vcc, 0x3a992000, v2
	s_mov_b64 s[34:35], vcc
	v_add_co_u32_e32 v82, vcc, 0x3a99a000, v2
	s_mov_b64 s[36:37], vcc
	v_add_co_u32_e32 v84, vcc, 0x3a9a2000, v2
	s_mov_b64 s[38:39], vcc
	v_add_co_u32_e32 v86, vcc, 0x3a9aa000, v2
	s_mov_b64 s[40:41], vcc
	v_add_co_u32_e32 v88, vcc, 0x3a9b2000, v2
	s_mov_b64 s[42:43], vcc
	v_add_co_u32_e32 v90, vcc, 0x3a9ba000, v2
	s_mov_b64 s[44:45], vcc
	v_add_co_u32_e32 v92, vcc, 0x3a9c2000, v2
	s_mov_b64 s[46:47], vcc
	v_add_co_u32_e32 v60, vcc, 0x3a9ca000, v2
	s_mov_b64 s[48:49], vcc
	v_add_co_u32_e32 v58, vcc, 0x3a1ba000, v2
	s_waitcnt vmcnt(0)
; __device__ __forceinline__ void phase_s5b_gqa(const Params& P, unsigned char* smraw, int bid, int nb) {
;     if (bid < 8) {
;         const int i = bid * NTHR + threadIdx.x;
;         const float2 a = ((const float2*)(P.ws + WS_A64))[i];
;         const float2* SE = (const float2*)(P.ws + WS_SE);
;         float2* CIN = (float2*)(P.ws + WS_CIN);
;         float sr = 0.f, si = 0.f;
;         for (int c0 = 0; c0 < 260; c0 += 20) {
;             float2 e[20];
; #pragma unroll
;             for (int j = 0; j < 20; ++j) e[j] = SE[(size_t)(c0 + j) * 4096 + i];
; #pragma unroll
;             for (int j = 0; j < 20; ++j) {
;                 CIN[(size_t)(c0 + j) * 4096 + i] = make_float2(sr, si);
;                 const float nr = a.x * sr - a.y * si + e[j].x, ni = a.x * si + a.y * sr + e[j].y;
;                 sr = nr; si = ni;
;             }
;         }
;     }
	v_mul_f32_e32 v1, 0, v4
	v_addc_co_u32_e32 v59, vcc, 0, v3, vcc
	v_add_co_u32_e32 v66, vcc, 0x3a9d2000, v2
	s_mov_b64 s[18:19], vcc
	v_add_co_u32_e32 v48, vcc, 0x3a9da000, v2
	s_mov_b64 s[22:23], vcc
	v_add_co_u32_e32 v50, vcc, 0x3a9e2000, v2
	s_mov_b64 s[6:7], vcc
	v_add_co_u32_e32 v94, vcc, 0x3a1c2000, v2
	s_nop 1
	v_addc_co_u32_e32 v95, vcc, 0, v3, vcc
	global_load_dwordx2 v[96:97], v[46:47], off offset:1024
	s_nop 0
	global_load_dwordx2 v[58:59], v[58:59], off offset:1024
	s_nop 0
	global_load_dwordx2 v[46:47], v[94:95], off offset:1024
	v_mul_f32_e32 v95, 0, v5
	v_sub_f32_e32 v94, v1, v95
	v_fmac_f32_e32 v95, 0, v4
	v_pk_add_f32 v[32:33], v[32:33], v[94:95]
	v_addc_co_u32_e64 v53, vcc, 0, v3, s[4:5]
	global_store_dwordx2 v[52:53], v[32:33], off offset:1024
	v_pk_mul_f32 v[52:53], v[4:5], v[32:33] op_sel:[1,0]
	v_addc_co_u32_e64 v55, vcc, 0, v3, s[8:9]
	v_pk_fma_f32 v[94:95], v[4:5], v[32:33], v[52:53] op_sel:[0,0,1] op_sel_hi:[1,1,0] neg_lo:[0,0,1] neg_hi:[0,0,1]
	v_pk_fma_f32 v[32:33], v[4:5], v[32:33], v[52:53] op_sel:[0,0,1] op_sel_hi:[0,1,0]
	v_mov_b32_e32 v95, v33
	v_pk_add_f32 v[22:23], v[22:23], v[94:95]
	global_store_dwordx2 v[54:55], v[22:23], off offset:1024
	v_pk_mul_f32 v[32:33], v[4:5], v[22:23] op_sel:[1,0]
	v_addc_co_u32_e64 v57, vcc, 0, v3, s[10:11]
	v_pk_fma_f32 v[52:53], v[4:5], v[22:23], v[32:33] op_sel:[0,0,1] op_sel_hi:[1,1,0] neg_lo:[0,0,1] neg_hi:[0,0,1]
	v_pk_fma_f32 v[22:23], v[4:5], v[22:23], v[32:33] op_sel:[0,0,1] op_sel_hi:[0,1,0]
	v_mov_b32_e32 v53, v23
	v_pk_add_f32 v[12:13], v[12:13], v[52:53]
	global_store_dwordx2 v[56:57], v[12:13], off offset:1024
	v_pk_mul_f32 v[22:23], v[4:5], v[12:13] op_sel:[1,0]
	v_addc_co_u32_e64 v63, vcc, 0, v3, s[12:13]
	v_pk_fma_f32 v[32:33], v[4:5], v[12:13], v[22:23] op_sel:[0,0,1] op_sel_hi:[1,1,0] neg_lo:[0,0,1] neg_hi:[0,0,1]
	v_pk_fma_f32 v[12:13], v[4:5], v[12:13], v[22:23] op_sel:[0,0,1] op_sel_hi:[0,1,0]
	v_mov_b32_e32 v33, v13
	v_pk_add_f32 v[8:9], v[8:9], v[32:33]
	global_store_dwordx2 v[62:63], v[8:9], off offset:1024
	v_pk_mul_f32 v[12:13], v[4:5], v[8:9] op_sel:[1,0]
	v_addc_co_u32_e64 v65, vcc, 0, v3, s[14:15]
	v_pk_fma_f32 v[22:23], v[4:5], v[8:9], v[12:13] op_sel:[0,0,1] op_sel_hi:[1,1,0] neg_lo:[0,0,1] neg_hi:[0,0,1]
	v_pk_fma_f32 v[8:9], v[4:5], v[8:9], v[12:13] op_sel:[0,0,1] op_sel_hi:[0,1,0]
	v_mov_b32_e32 v23, v9
	v_pk_add_f32 v[8:9], v[36:37], v[22:23]
	global_store_dwordx2 v[64:65], v[8:9], off offset:1024
	v_pk_mul_f32 v[12:13], v[4:5], v[8:9] op_sel:[1,0]
	v_addc_co_u32_e64 v69, vcc, 0, v3, s[16:17]
	v_pk_fma_f32 v[22:23], v[4:5], v[8:9], v[12:13] op_sel:[0,0,1] op_sel_hi:[1,1,0] neg_lo:[0,0,1] neg_hi:[0,0,1]
	v_pk_fma_f32 v[8:9], v[4:5], v[8:9], v[12:13] op_sel:[0,0,1] op_sel_hi:[0,1,0]
	v_mov_b32_e32 v23, v9
	v_pk_add_f32 v[8:9], v[26:27], v[22:23]
	global_store_dwordx2 v[68:69], v[8:9], off offset:1024
	v_pk_mul_f32 v[12:13], v[4:5], v[8:9] op_sel:[1,0]
	v_addc_co_u32_e64 v71, vcc, 0, v3, s[20:21]
	v_pk_fma_f32 v[22:23], v[4:5], v[8:9], v[12:13] op_sel:[0,0,1] op_sel_hi:[1,1,0] neg_lo:[0,0,1] neg_hi:[0,0,1]
	v_pk_fma_f32 v[8:9], v[4:5], v[8:9], v[12:13] op_sel:[0,0,1] op_sel_hi:[0,1,0]
	v_mov_b32_e32 v23, v9
	v_pk_add_f32 v[8:9], v[16:17], v[22:23]
	global_store_dwordx2 v[70:71], v[8:9], off offset:1024
	v_pk_mul_f32 v[12:13], v[4:5], v[8:9] op_sel:[1,0]
	v_addc_co_u32_e64 v73, vcc, 0, v3, s[24:25]
	v_pk_fma_f32 v[16:17], v[4:5], v[8:9], v[12:13] op_sel:[0,0,1] op_sel_hi:[1,1,0] neg_lo:[0,0,1] neg_hi:[0,0,1]
	v_pk_fma_f32 v[8:9], v[4:5], v[8:9], v[12:13] op_sel:[0,0,1] op_sel_hi:[0,1,0]
	v_mov_b32_e32 v17, v9
	v_pk_add_f32 v[8:9], v[10:11], v[16:17]
	global_store_dwordx2 v[72:73], v[8:9], off offset:1024
	v_pk_mul_f32 v[10:11], v[4:5], v[8:9] op_sel:[1,0]
	v_addc_co_u32_e64 v75, vcc, 0, v3, s[26:27]
	v_pk_fma_f32 v[12:13], v[4:5], v[8:9], v[10:11] op_sel:[0,0,1] op_sel_hi:[1,1,0] neg_lo:[0,0,1] neg_hi:[0,0,1]
	v_pk_fma_f32 v[8:9], v[4:5], v[8:9], v[10:11] op_sel:[0,0,1] op_sel_hi:[0,1,0]
	v_mov_b32_e32 v13, v9
	v_pk_add_f32 v[8:9], v[40:41], v[12:13]
	global_store_dwordx2 v[74:75], v[8:9], off offset:1024
	v_pk_mul_f32 v[10:11], v[4:5], v[8:9] op_sel:[1,0]
	v_addc_co_u32_e64 v77, vcc, 0, v3, s[28:29]
	v_pk_fma_f32 v[12:13], v[4:5], v[8:9], v[10:11] op_sel:[0,0,1] op_sel_hi:[1,1,0] neg_lo:[0,0,1] neg_hi:[0,0,1]
	v_pk_fma_f32 v[8:9], v[4:5], v[8:9], v[10:11] op_sel:[0,0,1] op_sel_hi:[0,1,0]
	v_mov_b32_e32 v13, v9
	v_pk_add_f32 v[8:9], v[34:35], v[12:13]
	global_store_dwordx2 v[76:77], v[8:9], off offset:1024
	v_pk_mul_f32 v[10:11], v[4:5], v[8:9] op_sel:[1,0]
	v_addc_co_u32_e64 v79, vcc, 0, v3, s[30:31]
	v_pk_fma_f32 v[12:13], v[4:5], v[8:9], v[10:11] op_sel:[0,0,1] op_sel_hi:[1,1,0] neg_lo:[0,0,1] neg_hi:[0,0,1]
	v_pk_fma_f32 v[8:9], v[4:5], v[8:9], v[10:11] op_sel:[0,0,1] op_sel_hi:[0,1,0]
	v_mov_b32_e32 v13, v9
	v_pk_add_f32 v[8:9], v[24:25], v[12:13]
	global_store_dwordx2 v[78:79], v[8:9], off offset:1024
	v_pk_mul_f32 v[10:11], v[4:5], v[8:9] op_sel:[1,0]
	v_addc_co_u32_e64 v81, vcc, 0, v3, s[34:35]
	v_pk_fma_f32 v[12:13], v[4:5], v[8:9], v[10:11] op_sel:[0,0,1] op_sel_hi:[1,1,0] neg_lo:[0,0,1] neg_hi:[0,0,1]
	v_pk_fma_f32 v[8:9], v[4:5], v[8:9], v[10:11] op_sel:[0,0,1] op_sel_hi:[0,1,0]
	v_mov_b32_e32 v13, v9
	v_pk_add_f32 v[8:9], v[14:15], v[12:13]
	global_store_dwordx2 v[80:81], v[8:9], off offset:1024
	v_pk_mul_f32 v[10:11], v[4:5], v[8:9] op_sel:[1,0]
	v_addc_co_u32_e64 v83, vcc, 0, v3, s[36:37]
	v_pk_fma_f32 v[12:13], v[4:5], v[8:9], v[10:11] op_sel:[0,0,1] op_sel_hi:[1,1,0] neg_lo:[0,0,1] neg_hi:[0,0,1]
	v_pk_fma_f32 v[8:9], v[4:5], v[8:9], v[10:11] op_sel:[0,0,1] op_sel_hi:[0,1,0]
	v_mov_b32_e32 v13, v9
	v_pk_add_f32 v[8:9], v[44:45], v[12:13]
; __device__ __forceinline__ void phase_s5b_gqa(const Params& P, unsigned char* smraw, int bid, int nb) {
;     if (bid < 8) {
;         const int i = bid * NTHR + threadIdx.x;
;         const float2 a = ((const float2*)(P.ws + WS_A64))[i];
;         const float2* SE = (const float2*)(P.ws + WS_SE);
;         float2* CIN = (float2*)(P.ws + WS_CIN);
;         float sr = 0.f, si = 0.f;
;         for (int c0 = 0; c0 < 260; c0 += 20) {
;             float2 e[20];
; #pragma unroll
;             for (int j = 0; j < 20; ++j) e[j] = SE[(size_t)(c0 + j) * 4096 + i];
; #pragma unroll
;             for (int j = 0; j < 20; ++j) {
;                 CIN[(size_t)(c0 + j) * 4096 + i] = make_float2(sr, si);
;                 const float nr = a.x * sr - a.y * si + e[j].x, ni = a.x * si + a.y * sr + e[j].y;
;                 sr = nr; si = ni;
;             }
;         }
;     }
	global_store_dwordx2 v[82:83], v[8:9], off offset:1024
	v_pk_mul_f32 v[10:11], v[4:5], v[8:9] op_sel:[1,0]
	v_addc_co_u32_e64 v85, vcc, 0, v3, s[38:39]
	v_pk_fma_f32 v[12:13], v[4:5], v[8:9], v[10:11] op_sel:[0,0,1] op_sel_hi:[1,1,0] neg_lo:[0,0,1] neg_hi:[0,0,1]
	v_pk_fma_f32 v[8:9], v[4:5], v[8:9], v[10:11] op_sel:[0,0,1] op_sel_hi:[0,1,0]
	v_mov_b32_e32 v13, v9
	v_pk_add_f32 v[8:9], v[38:39], v[12:13]
	global_store_dwordx2 v[84:85], v[8:9], off offset:1024
	v_pk_mul_f32 v[10:11], v[4:5], v[8:9] op_sel:[1,0]
	v_addc_co_u32_e64 v87, vcc, 0, v3, s[40:41]
	v_pk_fma_f32 v[12:13], v[4:5], v[8:9], v[10:11] op_sel:[0,0,1] op_sel_hi:[1,1,0] neg_lo:[0,0,1] neg_hi:[0,0,1]
	v_pk_fma_f32 v[8:9], v[4:5], v[8:9], v[10:11] op_sel:[0,0,1] op_sel_hi:[0,1,0]
	v_mov_b32_e32 v13, v9
	v_pk_add_f32 v[8:9], v[28:29], v[12:13]
	global_store_dwordx2 v[86:87], v[8:9], off offset:1024
	v_pk_mul_f32 v[10:11], v[4:5], v[8:9] op_sel:[1,0]
	v_addc_co_u32_e64 v89, vcc, 0, v3, s[42:43]
	v_pk_fma_f32 v[12:13], v[4:5], v[8:9], v[10:11] op_sel:[0,0,1] op_sel_hi:[1,1,0] neg_lo:[0,0,1] neg_hi:[0,0,1]
	v_pk_fma_f32 v[8:9], v[4:5], v[8:9], v[10:11] op_sel:[0,0,1] op_sel_hi:[0,1,0]
	v_mov_b32_e32 v13, v9
	v_pk_add_f32 v[8:9], v[18:19], v[12:13]
	global_store_dwordx2 v[88:89], v[8:9], off offset:1024
	v_pk_mul_f32 v[10:11], v[4:5], v[8:9] op_sel:[1,0]
	v_addc_co_u32_e64 v91, vcc, 0, v3, s[44:45]
	v_pk_fma_f32 v[12:13], v[4:5], v[8:9], v[10:11] op_sel:[0,0,1] op_sel_hi:[1,1,0] neg_lo:[0,0,1] neg_hi:[0,0,1]
	v_pk_fma_f32 v[8:9], v[4:5], v[8:9], v[10:11] op_sel:[0,0,1] op_sel_hi:[0,1,0]
	v_mov_b32_e32 v13, v9
	v_pk_add_f32 v[8:9], v[42:43], v[12:13]
	global_store_dwordx2 v[90:91], v[8:9], off offset:1024
	v_pk_mul_f32 v[10:11], v[4:5], v[8:9] op_sel:[1,0]
	v_addc_co_u32_e64 v93, vcc, 0, v3, s[46:47]
	v_pk_fma_f32 v[12:13], v[4:5], v[8:9], v[10:11] op_sel:[0,0,1] op_sel_hi:[1,1,0] neg_lo:[0,0,1] neg_hi:[0,0,1]
	v_pk_fma_f32 v[8:9], v[4:5], v[8:9], v[10:11] op_sel:[0,0,1] op_sel_hi:[0,1,0]
	v_mov_b32_e32 v13, v9
	v_pk_add_f32 v[8:9], v[30:31], v[12:13]
	global_store_dwordx2 v[92:93], v[8:9], off offset:1024
	v_pk_mul_f32 v[10:11], v[4:5], v[8:9] op_sel:[1,0]
	v_addc_co_u32_e64 v61, vcc, 0, v3, s[48:49]
	v_pk_fma_f32 v[12:13], v[4:5], v[8:9], v[10:11] op_sel:[0,0,1] op_sel_hi:[1,1,0] neg_lo:[0,0,1] neg_hi:[0,0,1]
	v_pk_fma_f32 v[8:9], v[4:5], v[8:9], v[10:11] op_sel:[0,0,1] op_sel_hi:[0,1,0]
	v_mov_b32_e32 v13, v9
	v_add_co_u32_e32 v10, vcc, 0x3a9ea000, v2
	v_pk_add_f32 v[8:9], v[20:21], v[12:13]
	s_mov_b64 s[4:5], vcc
	v_add_co_u32_e32 v12, vcc, 0x3a1ca000, v2
	v_pk_mul_f32 v[26:27], v[4:5], v[8:9] op_sel:[1,0]
	s_nop 0
	v_addc_co_u32_e32 v13, vcc, 0, v3, vcc
	global_load_dwordx2 v[12:13], v[12:13], off offset:1024
	v_add_co_u32_e32 v14, vcc, 0x3a9f2000, v2
	s_mov_b64 s[8:9], vcc
	v_add_co_u32_e32 v16, vcc, 0x3a1d2000, v2
	global_store_dwordx2 v[60:61], v[8:9], off offset:1024
	s_nop 0
	v_addc_co_u32_e32 v17, vcc, 0, v3, vcc
	global_load_dwordx2 v[16:17], v[16:17], off offset:1024
	v_add_co_u32_e32 v18, vcc, 0x3a9fa000, v2
	s_mov_b64 s[0:1], vcc
	v_add_co_u32_e32 v20, vcc, 0x3a1da000, v2
	v_pk_fma_f32 v[28:29], v[4:5], v[8:9], v[26:27] op_sel:[0,0,1] op_sel_hi:[1,1,0] neg_lo:[0,0,1] neg_hi:[0,0,1]
	s_nop 0
	v_addc_co_u32_e32 v21, vcc, 0, v3, vcc
	global_load_dwordx2 v[20:21], v[20:21], off offset:1024
	v_add_co_u32_e32 v22, vcc, 0x3aa02000, v2
	s_mov_b64 s[10:11], vcc
	v_add_co_u32_e32 v24, vcc, 0x3a1e2000, v2
	v_pk_fma_f32 v[8:9], v[4:5], v[8:9], v[26:27] op_sel:[0,0,1] op_sel_hi:[0,1,0]
	s_nop 0
	v_addc_co_u32_e32 v25, vcc, 0, v3, vcc
	global_load_dwordx2 v[24:25], v[24:25], off offset:1024
	v_mov_b32_e32 v29, v9
	v_pk_add_f32 v[6:7], v[6:7], v[28:29]
	v_addc_co_u32_e64 v67, vcc, 0, v3, s[18:19]
	v_pk_mul_f32 v[8:9], v[4:5], v[6:7] op_sel:[1,0]
	global_store_dwordx2 v[66:67], v[6:7], off offset:1024
	v_pk_fma_f32 v[26:27], v[4:5], v[6:7], v[8:9] op_sel:[0,0,1] op_sel_hi:[1,1,0] neg_lo:[0,0,1] neg_hi:[0,0,1]
	v_pk_fma_f32 v[6:7], v[4:5], v[6:7], v[8:9] op_sel:[0,0,1] op_sel_hi:[0,1,0]
	v_addc_co_u32_e64 v49, vcc, 0, v3, s[22:23]
	v_mov_b32_e32 v27, v7
	v_add_co_u32_e32 v8, vcc, 0x3aa0a000, v2
	s_waitcnt vmcnt(26)
	v_pk_add_f32 v[6:7], v[26:27], v[96:97]
	s_mov_b64 s[12:13], vcc
	v_add_co_u32_e32 v26, vcc, 0x3a1ea000, v2
	v_pk_mul_f32 v[32:33], v[4:5], v[6:7] op_sel:[1,1] op_sel_hi:[0,1]
	s_nop 0
	v_addc_co_u32_e32 v27, vcc, 0, v3, vcc
	global_load_dwordx2 v[26:27], v[26:27], off offset:1024
	v_add_co_u32_e32 v28, vcc, 0x3aa12000, v2
	s_mov_b64 s[14:15], vcc
	v_add_co_u32_e32 v30, vcc, 0x3a1f2000, v2
	global_store_dwordx2 v[48:49], v[6:7], off offset:1024
	s_nop 0
	v_addc_co_u32_e32 v31, vcc, 0, v3, vcc
	global_load_dwordx2 v[30:31], v[30:31], off offset:1024
	v_pk_fma_f32 v[34:35], v[4:5], v[6:7], v[32:33] neg_lo:[0,0,1] neg_hi:[0,0,1]
	v_pk_fma_f32 v[6:7], v[4:5], v[6:7], v[32:33] op_sel_hi:[1,0,1]
	v_addc_co_u32_e64 v51, vcc, 0, v3, s[6:7]
	v_mov_b32_e32 v35, v7
	s_waitcnt vmcnt(28)
	v_pk_add_f32 v[6:7], v[58:59], v[34:35]
	global_store_dwordx2 v[50:51], v[6:7], off offset:1024
	v_pk_mul_f32 v[32:33], v[4:5], v[6:7] op_sel:[1,0]
	v_addc_co_u32_e64 v11, vcc, 0, v3, s[4:5]
	v_pk_fma_f32 v[34:35], v[4:5], v[6:7], v[32:33] op_sel:[0,0,1] op_sel_hi:[1,1,0] neg_lo:[0,0,1] neg_hi:[0,0,1]
	v_pk_fma_f32 v[6:7], v[4:5], v[6:7], v[32:33] op_sel:[0,0,1] op_sel_hi:[0,1,0]
	v_mov_b32_e32 v35, v7
	s_waitcnt vmcnt(28)
	v_pk_add_f32 v[6:7], v[46:47], v[34:35]
	global_store_dwordx2 v[10:11], v[6:7], off offset:1024
	v_pk_mul_f32 v[10:11], v[4:5], v[6:7] op_sel:[1,0]
	v_addc_co_u32_e64 v15, vcc, 0, v3, s[8:9]
	v_pk_fma_f32 v[32:33], v[4:5], v[6:7], v[10:11] op_sel:[0,0,1] op_sel_hi:[1,1,0] neg_lo:[0,0,1] neg_hi:[0,0,1]
	v_pk_fma_f32 v[6:7], v[4:5], v[6:7], v[10:11] op_sel:[0,0,1] op_sel_hi:[0,1,0]
	v_mov_b32_e32 v33, v7
	v_addc_co_u32_e64 v19, vcc, 0, v3, s[0:1]
	s_waitcnt vmcnt(10)
; __device__ __forceinline__ void phase_s5b_gqa(const Params& P, unsigned char* smraw, int bid, int nb) {
;     if (bid < 8) {
;         const int i = bid * NTHR + threadIdx.x;
;         const float2 a = ((const float2*)(P.ws + WS_A64))[i];
;         const float2* SE = (const float2*)(P.ws + WS_SE);
;         float2* CIN = (float2*)(P.ws + WS_CIN);
;         float sr = 0.f, si = 0.f;
;         for (int c0 = 0; c0 < 260; c0 += 20) {
;             float2 e[20];
; #pragma unroll
;             for (int j = 0; j < 20; ++j) e[j] = SE[(size_t)(c0 + j) * 4096 + i];
; #pragma unroll
;             for (int j = 0; j < 20; ++j) {
;                 CIN[(size_t)(c0 + j) * 4096 + i] = make_float2(sr, si);
;                 const float nr = a.x * sr - a.y * si + e[j].x, ni = a.x * si + a.y * sr + e[j].y;
;                 sr = nr; si = ni;
;             }
;         }
;     }
	v_pk_add_f32 v[6:7], v[12:13], v[32:33]
	global_store_dwordx2 v[14:15], v[6:7], off offset:1024
	v_pk_mul_f32 v[10:11], v[4:5], v[6:7] op_sel:[1,0]
	v_addc_co_u32_e64 v23, vcc, 0, v3, s[10:11]
	v_pk_fma_f32 v[12:13], v[4:5], v[6:7], v[10:11] op_sel:[0,0,1] op_sel_hi:[1,1,0] neg_lo:[0,0,1] neg_hi:[0,0,1]
	v_pk_fma_f32 v[6:7], v[4:5], v[6:7], v[10:11] op_sel:[0,0,1] op_sel_hi:[0,1,0]
	v_mov_b32_e32 v13, v7
	s_waitcnt vmcnt(9)
	v_pk_add_f32 v[6:7], v[16:17], v[12:13]
	global_store_dwordx2 v[18:19], v[6:7], off offset:1024
	v_pk_mul_f32 v[10:11], v[4:5], v[6:7] op_sel:[1,0]
	v_addc_co_u32_e64 v9, vcc, 0, v3, s[12:13]
	v_pk_fma_f32 v[12:13], v[4:5], v[6:7], v[10:11] op_sel:[0,0,1] op_sel_hi:[1,1,0] neg_lo:[0,0,1] neg_hi:[0,0,1]
	v_pk_fma_f32 v[6:7], v[4:5], v[6:7], v[10:11] op_sel:[0,0,1] op_sel_hi:[0,1,0]
	v_mov_b32_e32 v13, v7
	v_readlane_b32 s40, v252, 19
	s_waitcnt vmcnt(9)
	v_pk_add_f32 v[6:7], v[20:21], v[12:13]
	global_store_dwordx2 v[22:23], v[6:7], off offset:1024
	v_pk_mul_f32 v[10:11], v[4:5], v[6:7] op_sel:[1,0]
	v_readlane_b32 s41, v252, 20
	v_pk_fma_f32 v[12:13], v[4:5], v[6:7], v[10:11] op_sel:[0,0,1] op_sel_hi:[1,1,0] neg_lo:[0,0,1] neg_hi:[0,0,1]
	v_pk_fma_f32 v[6:7], v[4:5], v[6:7], v[10:11] op_sel:[0,0,1] op_sel_hi:[0,1,0]
	v_mov_b32_e32 v13, v7
	v_readlane_b32 s42, v252, 21
	v_readlane_b32 s43, v252, 22
	s_waitcnt vmcnt(9)
	v_pk_add_f32 v[6:7], v[24:25], v[12:13]
	global_store_dwordx2 v[8:9], v[6:7], off offset:1024
	v_pk_mul_f32 v[8:9], v[4:5], v[6:7] op_sel:[1,0]
	v_readlane_b32 s44, v252, 23
	v_pk_fma_f32 v[10:11], v[4:5], v[6:7], v[8:9] op_sel:[0,0,1] op_sel_hi:[1,1,0] neg_lo:[0,0,1] neg_hi:[0,0,1]
	v_pk_fma_f32 v[6:7], v[4:5], v[6:7], v[8:9] op_sel:[0,0,1] op_sel_hi:[0,1,0]
	v_add_co_u32_e32 v6, vcc, 0x3aa1a000, v2
	s_mov_b64 s[0:1], vcc
	v_add_co_u32_e32 v8, vcc, 0x3a1fa000, v2
	v_mov_b32_e32 v11, v7
	s_nop 0
	v_addc_co_u32_e32 v9, vcc, 0, v3, vcc
	global_load_dwordx2 v[8:9], v[8:9], off offset:1024
	v_add_co_u32_e32 v12, vcc, 0x3aa22000, v2
	s_mov_b64 s[6:7], vcc
	v_add_co_u32_e32 v14, vcc, 0x3a202000, v2
	v_readlane_b32 s45, v252, 24
	s_waitcnt vmcnt(9)
	v_pk_add_f32 v[10:11], v[26:27], v[10:11]
	v_addc_co_u32_e32 v15, vcc, 0, v3, vcc
	v_addc_co_u32_e64 v29, vcc, 0, v3, s[14:15]
	v_pk_mul_f32 v[16:17], v[4:5], v[10:11] op_sel:[1,0]
	global_load_dwordx2 v[14:15], v[14:15], off offset:1024
	v_pk_fma_f32 v[18:19], v[4:5], v[10:11], v[16:17] op_sel:[0,0,1] op_sel_hi:[1,1,0] neg_lo:[0,0,1] neg_hi:[0,0,1]
	global_store_dwordx2 v[28:29], v[10:11], off offset:1024
	v_pk_fma_f32 v[10:11], v[4:5], v[10:11], v[16:17] op_sel:[0,0,1] op_sel_hi:[0,1,0]
	v_addc_co_u32_e64 v7, vcc, 0, v3, s[0:1]
	v_mov_b32_e32 v19, v11
	v_add_co_u32_e32 v16, vcc, 0x3aa2a000, v2
	s_waitcnt vmcnt(9)
	v_pk_add_f32 v[10:11], v[30:31], v[18:19]
	s_mov_b64 s[12:13], vcc
	v_add_co_u32_e32 v18, vcc, 0x3a20a000, v2
	global_store_dwordx2 v[6:7], v[10:11], off offset:1024
	s_nop 0
	v_addc_co_u32_e32 v19, vcc, 0, v3, vcc
	global_load_dwordx2 v[18:19], v[18:19], off offset:1024
	v_add_co_u32_e32 v20, vcc, 0x3aa32000, v2
	s_mov_b64 s[4:5], vcc
	v_add_co_u32_e32 v22, vcc, 0x3a212000, v2
	v_pk_mul_f32 v[6:7], v[4:5], v[10:11] op_sel:[1,0]
	s_nop 0
	v_addc_co_u32_e32 v23, vcc, 0, v3, vcc
	global_load_dwordx2 v[22:23], v[22:23], off offset:1024
	v_add_co_u32_e32 v24, vcc, 0x3aa3a000, v2
	s_mov_b64 s[8:9], vcc
	v_add_co_u32_e32 v26, vcc, 0x3a21a000, v2
	v_pk_fma_f32 v[40:41], v[4:5], v[10:11], v[6:7] op_sel:[0,0,1] op_sel_hi:[1,1,0] neg_lo:[0,0,1] neg_hi:[0,0,1]
	s_nop 0
	v_addc_co_u32_e32 v27, vcc, 0, v3, vcc
	global_load_dwordx2 v[26:27], v[26:27], off offset:1024
	v_add_co_u32_e32 v28, vcc, 0x3aa42000, v2
	s_mov_b64 s[10:11], vcc
	v_add_co_u32_e32 v30, vcc, 0x3a222000, v2
	v_pk_fma_f32 v[6:7], v[4:5], v[10:11], v[6:7] op_sel:[0,0,1] op_sel_hi:[0,1,0]
	s_nop 0
	v_addc_co_u32_e32 v31, vcc, 0, v3, vcc
	global_load_dwordx2 v[30:31], v[30:31], off offset:1024
	v_add_co_u32_e32 v32, vcc, 0x3aa4a000, v2
	s_mov_b64 s[0:1], vcc
	v_add_co_u32_e32 v34, vcc, 0x3a22a000, v2
	v_mov_b32_e32 v41, v7
	s_nop 0
	v_addc_co_u32_e32 v35, vcc, 0, v3, vcc
	global_load_dwordx2 v[34:35], v[34:35], off offset:1024
	v_add_co_u32_e32 v36, vcc, 0x3aa52000, v2
	s_mov_b64 s[14:15], vcc
	v_add_co_u32_e32 v38, vcc, 0x3a232000, v2
	s_waitcnt vmcnt(8)
	v_pk_add_f32 v[6:7], v[8:9], v[40:41]
	v_addc_co_u32_e32 v39, vcc, 0, v3, vcc
	global_load_dwordx2 v[38:39], v[38:39], off offset:1024
	v_addc_co_u32_e64 v13, vcc, 0, v3, s[6:7]
	v_pk_mul_f32 v[8:9], v[4:5], v[6:7] op_sel:[1,0]
	global_store_dwordx2 v[12:13], v[6:7], off offset:1024
	v_pk_fma_f32 v[10:11], v[4:5], v[6:7], v[8:9] op_sel:[0,0,1] op_sel_hi:[1,1,0] neg_lo:[0,0,1] neg_hi:[0,0,1]
	v_pk_fma_f32 v[6:7], v[4:5], v[6:7], v[8:9] op_sel:[0,0,1] op_sel_hi:[0,1,0]
	v_mov_b32_e32 v11, v7
	v_addc_co_u32_e64 v17, vcc, 0, v3, s[12:13]
	s_waitcnt vmcnt(9)
	v_pk_add_f32 v[6:7], v[14:15], v[10:11]
	v_add_co_u32_e32 v8, vcc, 0x3aa5a000, v2
	s_mov_b64 s[6:7], vcc
	v_add_co_u32_e32 v10, vcc, 0x3a23a000, v2
	global_store_dwordx2 v[16:17], v[6:7], off offset:1024
	v_pk_mul_f32 v[16:17], v[4:5], v[6:7] op_sel:[1,0]
	v_addc_co_u32_e32 v11, vcc, 0, v3, vcc
	v_pk_fma_f32 v[40:41], v[4:5], v[6:7], v[16:17] op_sel:[0,0,1] op_sel_hi:[1,1,0] neg_lo:[0,0,1] neg_hi:[0,0,1]
	v_pk_fma_f32 v[6:7], v[4:5], v[6:7], v[16:17] op_sel:[0,0,1] op_sel_hi:[0,1,0]
	global_load_dwordx2 v[10:11], v[10:11], off offset:1024
	v_add_co_u32_e32 v12, vcc, 0x3aa62000, v2
	v_mov_b32_e32 v41, v7
	s_mov_b64 s[12:13], vcc
	v_add_co_u32_e32 v14, vcc, 0x3a242000, v2
	s_waitcnt vmcnt(8)
; __device__ __forceinline__ void phase_s5b_gqa(const Params& P, unsigned char* smraw, int bid, int nb) {
;     if (bid < 8) {
;         const int i = bid * NTHR + threadIdx.x;
;         const float2 a = ((const float2*)(P.ws + WS_A64))[i];
;         const float2* SE = (const float2*)(P.ws + WS_SE);
;         float2* CIN = (float2*)(P.ws + WS_CIN);
;         float sr = 0.f, si = 0.f;
;         for (int c0 = 0; c0 < 260; c0 += 20) {
;             float2 e[20];
; #pragma unroll
;             for (int j = 0; j < 20; ++j) e[j] = SE[(size_t)(c0 + j) * 4096 + i];
; #pragma unroll
;             for (int j = 0; j < 20; ++j) {
;                 CIN[(size_t)(c0 + j) * 4096 + i] = make_float2(sr, si);
;                 const float nr = a.x * sr - a.y * si + e[j].x, ni = a.x * si + a.y * sr + e[j].y;
;                 sr = nr; si = ni;
;             }
;         }
;     }
	v_pk_add_f32 v[6:7], v[18:19], v[40:41]
	v_addc_co_u32_e32 v15, vcc, 0, v3, vcc
	v_addc_co_u32_e64 v21, vcc, 0, v3, s[4:5]
	v_pk_mul_f32 v[16:17], v[4:5], v[6:7] op_sel:[1,0]
	global_store_dwordx2 v[20:21], v[6:7], off offset:1024
	v_pk_fma_f32 v[18:19], v[4:5], v[6:7], v[16:17] op_sel:[0,0,1] op_sel_hi:[1,1,0] neg_lo:[0,0,1] neg_hi:[0,0,1]
	v_pk_fma_f32 v[6:7], v[4:5], v[6:7], v[16:17] op_sel:[0,0,1] op_sel_hi:[0,1,0]
	global_load_dwordx2 v[14:15], v[14:15], off offset:1024
	v_mov_b32_e32 v19, v7
	s_waitcnt vmcnt(9)
	v_pk_add_f32 v[6:7], v[22:23], v[18:19]
	v_addc_co_u32_e64 v25, vcc, 0, v3, s[8:9]
	v_pk_mul_f32 v[16:17], v[4:5], v[6:7] op_sel:[1,0]
	global_store_dwordx2 v[24:25], v[6:7], off offset:1024
	v_pk_fma_f32 v[18:19], v[4:5], v[6:7], v[16:17] op_sel:[0,0,1] op_sel_hi:[1,1,0] neg_lo:[0,0,1] neg_hi:[0,0,1]
	v_pk_fma_f32 v[6:7], v[4:5], v[6:7], v[16:17] op_sel:[0,0,1] op_sel_hi:[0,1,0]
	v_mov_b32_e32 v19, v7
	s_waitcnt vmcnt(9)
	v_pk_add_f32 v[6:7], v[26:27], v[18:19]
	v_addc_co_u32_e64 v29, vcc, 0, v3, s[10:11]
	v_pk_mul_f32 v[16:17], v[4:5], v[6:7] op_sel:[1,0]
	global_store_dwordx2 v[28:29], v[6:7], off offset:1024
	v_pk_fma_f32 v[18:19], v[4:5], v[6:7], v[16:17] op_sel:[0,0,1] op_sel_hi:[1,1,0] neg_lo:[0,0,1] neg_hi:[0,0,1]
	v_pk_fma_f32 v[6:7], v[4:5], v[6:7], v[16:17] op_sel:[0,0,1] op_sel_hi:[0,1,0]
	v_mov_b32_e32 v19, v7
	s_waitcnt vmcnt(9)
	v_pk_add_f32 v[6:7], v[30:31], v[18:19]
	v_addc_co_u32_e64 v33, vcc, 0, v3, s[0:1]
	v_pk_mul_f32 v[16:17], v[4:5], v[6:7] op_sel:[1,0]
	global_store_dwordx2 v[32:33], v[6:7], off offset:1024
	v_pk_fma_f32 v[18:19], v[4:5], v[6:7], v[16:17] op_sel:[0,0,1] op_sel_hi:[1,1,0] neg_lo:[0,0,1] neg_hi:[0,0,1]
	v_pk_fma_f32 v[6:7], v[4:5], v[6:7], v[16:17] op_sel:[0,0,1] op_sel_hi:[0,1,0]
	v_mov_b32_e32 v19, v7
	s_waitcnt vmcnt(9)
	v_pk_add_f32 v[6:7], v[34:35], v[18:19]
	v_addc_co_u32_e64 v37, vcc, 0, v3, s[14:15]
	v_pk_mul_f32 v[16:17], v[4:5], v[6:7] op_sel:[1,0]
	global_store_dwordx2 v[36:37], v[6:7], off offset:1024
	v_pk_fma_f32 v[18:19], v[4:5], v[6:7], v[16:17] op_sel:[0,0,1] op_sel_hi:[1,1,0] neg_lo:[0,0,1] neg_hi:[0,0,1]
	v_pk_fma_f32 v[6:7], v[4:5], v[6:7], v[16:17] op_sel:[0,0,1] op_sel_hi:[0,1,0]
	v_mov_b32_e32 v19, v7
	v_addc_co_u32_e64 v9, vcc, 0, v3, s[6:7]
	s_waitcnt vmcnt(9)
	v_pk_add_f32 v[6:7], v[38:39], v[18:19]
	global_store_dwordx2 v[8:9], v[6:7], off offset:1024
	v_pk_mul_f32 v[8:9], v[4:5], v[6:7] op_sel:[1,0]
	s_nop 0
	v_pk_fma_f32 v[16:17], v[4:5], v[6:7], v[8:9] op_sel:[0,0,1] op_sel_hi:[1,1,0] neg_lo:[0,0,1] neg_hi:[0,0,1]
	v_pk_fma_f32 v[6:7], v[4:5], v[6:7], v[8:9] op_sel:[0,0,1] op_sel_hi:[0,1,0]
	v_add_co_u32_e32 v6, vcc, 0x3aa6a000, v2
	s_mov_b64 s[0:1], vcc
	v_add_co_u32_e32 v8, vcc, 0x3a24a000, v2
	v_mov_b32_e32 v17, v7
	s_nop 0
	v_addc_co_u32_e32 v9, vcc, 0, v3, vcc
	v_add_co_u32_e32 v18, vcc, 0x3aa72000, v2
	s_mov_b64 s[6:7], vcc
	v_add_co_u32_e32 v20, vcc, 0x3a252000, v2
	s_nop 1
	v_addc_co_u32_e32 v21, vcc, 0, v3, vcc
	global_load_dwordx2 v[20:21], v[20:21], off offset:1024
	v_addc_co_u32_e64 v13, vcc, 0, v3, s[12:13]
	global_load_dwordx2 v[8:9], v[8:9], off offset:1024
	s_waitcnt vmcnt(9)
	v_pk_add_f32 v[10:11], v[10:11], v[16:17]
	global_store_dwordx2 v[12:13], v[10:11], off offset:1024
	v_pk_mul_f32 v[12:13], v[4:5], v[10:11] op_sel:[1,0]
	v_addc_co_u32_e64 v7, vcc, 0, v3, s[0:1]
	v_pk_fma_f32 v[16:17], v[4:5], v[10:11], v[12:13] op_sel:[0,0,1] op_sel_hi:[1,1,0] neg_lo:[0,0,1] neg_hi:[0,0,1]
	v_pk_fma_f32 v[10:11], v[4:5], v[10:11], v[12:13] op_sel:[0,0,1] op_sel_hi:[0,1,0]
	v_mov_b32_e32 v17, v11
	v_add_co_u32_e32 v12, vcc, 0x3aa7a000, v2
	s_mov_b64 s[12:13], vcc
	s_waitcnt vmcnt(8)
	v_pk_add_f32 v[10:11], v[14:15], v[16:17]
	v_add_co_u32_e32 v14, vcc, 0x3a25a000, v2
	global_store_dwordx2 v[6:7], v[10:11], off offset:1024
	s_nop 0
	v_addc_co_u32_e32 v15, vcc, 0, v3, vcc
	global_load_dwordx2 v[14:15], v[14:15], off offset:1024
	v_add_co_u32_e32 v16, vcc, 0x3aa82000, v2
	s_mov_b64 s[4:5], vcc
	v_add_co_u32_e32 v22, vcc, 0x3a262000, v2
	v_pk_mul_f32 v[6:7], v[4:5], v[10:11] op_sel:[1,0]
	s_nop 0
	v_addc_co_u32_e32 v23, vcc, 0, v3, vcc
	global_load_dwordx2 v[22:23], v[22:23], off offset:1024
	v_add_co_u32_e32 v24, vcc, 0x3aa8a000, v2
	s_mov_b64 s[8:9], vcc
	v_add_co_u32_e32 v26, vcc, 0x3a26a000, v2
	v_pk_fma_f32 v[40:41], v[4:5], v[10:11], v[6:7] op_sel:[0,0,1] op_sel_hi:[1,1,0] neg_lo:[0,0,1] neg_hi:[0,0,1]
	s_nop 0
	v_addc_co_u32_e32 v27, vcc, 0, v3, vcc
	global_load_dwordx2 v[26:27], v[26:27], off offset:1024
	v_add_co_u32_e32 v28, vcc, 0x3aa92000, v2
	s_mov_b64 s[10:11], vcc
	v_add_co_u32_e32 v30, vcc, 0x3a272000, v2
	v_pk_fma_f32 v[6:7], v[4:5], v[10:11], v[6:7] op_sel:[0,0,1] op_sel_hi:[0,1,0]
	s_nop 0
	v_addc_co_u32_e32 v31, vcc, 0, v3, vcc
	global_load_dwordx2 v[30:31], v[30:31], off offset:1024
	v_add_co_u32_e32 v32, vcc, 0x3aa9a000, v2
	s_mov_b64 s[0:1], vcc
	v_add_co_u32_e32 v34, vcc, 0x3a27a000, v2
	v_mov_b32_e32 v41, v7
	s_nop 0
	v_addc_co_u32_e32 v35, vcc, 0, v3, vcc
	global_load_dwordx2 v[34:35], v[34:35], off offset:1024
	v_add_co_u32_e32 v36, vcc, 0x3aaa2000, v2
	s_mov_b64 s[14:15], vcc
	v_add_co_u32_e32 v38, vcc, 0x3a282000, v2
	s_waitcnt vmcnt(7)
; __device__ __forceinline__ void phase_s5b_gqa(const Params& P, unsigned char* smraw, int bid, int nb) {
;     if (bid < 8) {
;         const int i = bid * NTHR + threadIdx.x;
;         const float2 a = ((const float2*)(P.ws + WS_A64))[i];
;         const float2* SE = (const float2*)(P.ws + WS_SE);
;         float2* CIN = (float2*)(P.ws + WS_CIN);
;         float sr = 0.f, si = 0.f;
;         for (int c0 = 0; c0 < 260; c0 += 20) {
;             float2 e[20];
; #pragma unroll
;             for (int j = 0; j < 20; ++j) e[j] = SE[(size_t)(c0 + j) * 4096 + i];
; #pragma unroll
;             for (int j = 0; j < 20; ++j) {
;                 CIN[(size_t)(c0 + j) * 4096 + i] = make_float2(sr, si);
;                 const float nr = a.x * sr - a.y * si + e[j].x, ni = a.x * si + a.y * sr + e[j].y;
;                 sr = nr; si = ni;
;             }
;         }
;     }
	v_pk_add_f32 v[6:7], v[8:9], v[40:41]
	v_addc_co_u32_e32 v39, vcc, 0, v3, vcc
	global_load_dwordx2 v[38:39], v[38:39], off offset:1024
	v_addc_co_u32_e64 v19, vcc, 0, v3, s[6:7]
	v_pk_mul_f32 v[8:9], v[4:5], v[6:7] op_sel:[1,0]
	global_store_dwordx2 v[18:19], v[6:7], off offset:1024
	v_pk_fma_f32 v[10:11], v[4:5], v[6:7], v[8:9] op_sel:[0,0,1] op_sel_hi:[1,1,0] neg_lo:[0,0,1] neg_hi:[0,0,1]
	v_pk_fma_f32 v[6:7], v[4:5], v[6:7], v[8:9] op_sel:[0,0,1] op_sel_hi:[0,1,0]
	v_addc_co_u32_e64 v13, vcc, 0, v3, s[12:13]
	v_mov_b32_e32 v11, v7
	v_add_co_u32_e32 v8, vcc, 0x3aaaa000, v2
	v_pk_add_f32 v[6:7], v[10:11], v[20:21]
	s_mov_b64 s[6:7], vcc
	v_add_co_u32_e32 v10, vcc, 0x3a28a000, v2
	global_store_dwordx2 v[12:13], v[6:7], off offset:1024
	s_nop 0
	v_addc_co_u32_e32 v11, vcc, 0, v3, vcc
	v_add_co_u32_e32 v18, vcc, 0x3aab2000, v2
	s_mov_b64 s[12:13], vcc
	v_add_co_u32_e32 v20, vcc, 0x3a292000, v2
	v_pk_mul_f32 v[12:13], v[4:5], v[6:7] op_sel:[1,1] op_sel_hi:[0,1]
	s_nop 0
	v_addc_co_u32_e32 v21, vcc, 0, v3, vcc
	global_load_dwordx2 v[20:21], v[20:21], off offset:1024
	v_pk_fma_f32 v[40:41], v[4:5], v[6:7], v[12:13] neg_lo:[0,0,1] neg_hi:[0,0,1]
	global_load_dwordx2 v[10:11], v[10:11], off offset:1024
	v_pk_fma_f32 v[6:7], v[4:5], v[6:7], v[12:13] op_sel_hi:[1,0,1]
	v_addc_co_u32_e64 v17, vcc, 0, v3, s[4:5]
	v_mov_b32_e32 v41, v7
	s_waitcnt vmcnt(9)
	v_pk_add_f32 v[6:7], v[14:15], v[40:41]
	global_store_dwordx2 v[16:17], v[6:7], off offset:1024
	v_pk_mul_f32 v[12:13], v[4:5], v[6:7] op_sel:[1,0]
	v_addc_co_u32_e64 v25, vcc, 0, v3, s[8:9]
	v_pk_fma_f32 v[14:15], v[4:5], v[6:7], v[12:13] op_sel:[0,0,1] op_sel_hi:[1,1,0] neg_lo:[0,0,1] neg_hi:[0,0,1]
	v_pk_fma_f32 v[6:7], v[4:5], v[6:7], v[12:13] op_sel:[0,0,1] op_sel_hi:[0,1,0]
	v_mov_b32_e32 v15, v7
	s_waitcnt vmcnt(9)
	v_pk_add_f32 v[6:7], v[22:23], v[14:15]
	global_store_dwordx2 v[24:25], v[6:7], off offset:1024
	v_pk_mul_f32 v[12:13], v[4:5], v[6:7] op_sel:[1,0]
	v_addc_co_u32_e64 v29, vcc, 0, v3, s[10:11]
	v_pk_fma_f32 v[14:15], v[4:5], v[6:7], v[12:13] op_sel:[0,0,1] op_sel_hi:[1,1,0] neg_lo:[0,0,1] neg_hi:[0,0,1]
	v_pk_fma_f32 v[6:7], v[4:5], v[6:7], v[12:13] op_sel:[0,0,1] op_sel_hi:[0,1,0]
	v_mov_b32_e32 v15, v7
	s_waitcnt vmcnt(9)
	v_pk_add_f32 v[6:7], v[26:27], v[14:15]
	global_store_dwordx2 v[28:29], v[6:7], off offset:1024
	v_pk_mul_f32 v[12:13], v[4:5], v[6:7] op_sel:[1,0]
	v_addc_co_u32_e64 v33, vcc, 0, v3, s[0:1]
	v_pk_fma_f32 v[14:15], v[4:5], v[6:7], v[12:13] op_sel:[0,0,1] op_sel_hi:[1,1,0] neg_lo:[0,0,1] neg_hi:[0,0,1]
	v_pk_fma_f32 v[6:7], v[4:5], v[6:7], v[12:13] op_sel:[0,0,1] op_sel_hi:[0,1,0]
	v_mov_b32_e32 v15, v7
	s_waitcnt vmcnt(9)
	v_pk_add_f32 v[6:7], v[30:31], v[14:15]
	global_store_dwordx2 v[32:33], v[6:7], off offset:1024
	v_pk_mul_f32 v[12:13], v[4:5], v[6:7] op_sel:[1,0]
	v_addc_co_u32_e64 v37, vcc, 0, v3, s[14:15]
	v_pk_fma_f32 v[14:15], v[4:5], v[6:7], v[12:13] op_sel:[0,0,1] op_sel_hi:[1,1,0] neg_lo:[0,0,1] neg_hi:[0,0,1]
	v_pk_fma_f32 v[6:7], v[4:5], v[6:7], v[12:13] op_sel:[0,0,1] op_sel_hi:[0,1,0]
	v_mov_b32_e32 v15, v7
	s_waitcnt vmcnt(9)
	v_pk_add_f32 v[6:7], v[34:35], v[14:15]
	global_store_dwordx2 v[36:37], v[6:7], off offset:1024
	v_pk_mul_f32 v[12:13], v[4:5], v[6:7] op_sel:[1,0]
	v_addc_co_u32_e64 v9, vcc, 0, v3, s[6:7]
	v_pk_fma_f32 v[14:15], v[4:5], v[6:7], v[12:13] op_sel:[0,0,1] op_sel_hi:[1,1,0] neg_lo:[0,0,1] neg_hi:[0,0,1]
	v_pk_fma_f32 v[6:7], v[4:5], v[6:7], v[12:13] op_sel:[0,0,1] op_sel_hi:[0,1,0]
	v_mov_b32_e32 v15, v7
	s_waitcnt vmcnt(9)
	v_pk_add_f32 v[6:7], v[38:39], v[14:15]
	global_store_dwordx2 v[8:9], v[6:7], off offset:1024
	v_pk_mul_f32 v[8:9], v[4:5], v[6:7] op_sel:[1,0]
	s_nop 0
	v_pk_fma_f32 v[12:13], v[4:5], v[6:7], v[8:9] op_sel:[0,0,1] op_sel_hi:[1,1,0] neg_lo:[0,0,1] neg_hi:[0,0,1]
	v_pk_fma_f32 v[6:7], v[4:5], v[6:7], v[8:9] op_sel:[0,0,1] op_sel_hi:[0,1,0]
	v_add_co_u32_e32 v6, vcc, 0x3aaba000, v2
	s_mov_b64 s[0:1], vcc
	v_add_co_u32_e32 v8, vcc, 0x3a29a000, v2
	v_mov_b32_e32 v13, v7
	s_nop 0
	v_addc_co_u32_e32 v9, vcc, 0, v3, vcc
	global_load_dwordx2 v[8:9], v[8:9], off offset:1024
	v_add_co_u32_e32 v14, vcc, 0x3aac2000, v2
	s_mov_b64 s[6:7], vcc
	v_add_co_u32_e32 v16, vcc, 0x3a2a2000, v2
	s_waitcnt vmcnt(7)
	v_pk_add_f32 v[10:11], v[10:11], v[12:13]
	v_addc_co_u32_e32 v17, vcc, 0, v3, vcc
	global_load_dwordx2 v[16:17], v[16:17], off offset:1024
	v_addc_co_u32_e64 v19, vcc, 0, v3, s[12:13]
	v_pk_mul_f32 v[12:13], v[4:5], v[10:11] op_sel:[1,0]
	global_store_dwordx2 v[18:19], v[10:11], off offset:1024
	v_pk_fma_f32 v[18:19], v[4:5], v[10:11], v[12:13] op_sel:[0,0,1] op_sel_hi:[1,1,0] neg_lo:[0,0,1] neg_hi:[0,0,1]
	v_pk_fma_f32 v[10:11], v[4:5], v[10:11], v[12:13] op_sel:[0,0,1] op_sel_hi:[0,1,0]
	v_addc_co_u32_e64 v7, vcc, 0, v3, s[0:1]
	v_mov_b32_e32 v19, v11
	v_add_co_u32_e32 v12, vcc, 0x3aaca000, v2
	v_pk_add_f32 v[10:11], v[20:21], v[18:19]
	s_mov_b64 s[12:13], vcc
	v_add_co_u32_e32 v18, vcc, 0x3a2aa000, v2
	global_store_dwordx2 v[6:7], v[10:11], off offset:1024
	s_nop 0
	v_addc_co_u32_e32 v19, vcc, 0, v3, vcc
	global_load_dwordx2 v[18:19], v[18:19], off offset:1024
	v_add_co_u32_e32 v20, vcc, 0x3aad2000, v2
	s_mov_b64 s[4:5], vcc
	v_add_co_u32_e32 v22, vcc, 0x3a2b2000, v2
	v_pk_mul_f32 v[6:7], v[4:5], v[10:11] op_sel:[1,0]
	s_nop 0
	v_addc_co_u32_e32 v23, vcc, 0, v3, vcc
	global_load_dwordx2 v[22:23], v[22:23], off offset:1024
	v_add_co_u32_e32 v24, vcc, 0x3aada000, v2
	s_mov_b64 s[8:9], vcc
	v_add_co_u32_e32 v26, vcc, 0x3a2ba000, v2
	v_pk_fma_f32 v[40:41], v[4:5], v[10:11], v[6:7] op_sel:[0,0,1] op_sel_hi:[1,1,0] neg_lo:[0,0,1] neg_hi:[0,0,1]
	s_nop 0
	v_addc_co_u32_e32 v27, vcc, 0, v3, vcc
	global_load_dwordx2 v[26:27], v[26:27], off offset:1024
	v_add_co_u32_e32 v28, vcc, 0x3aae2000, v2
	s_mov_b64 s[10:11], vcc
	v_add_co_u32_e32 v30, vcc, 0x3a2c2000, v2
	v_pk_fma_f32 v[6:7], v[4:5], v[10:11], v[6:7] op_sel:[0,0,1] op_sel_hi:[0,1,0]
	s_nop 0
	v_addc_co_u32_e32 v31, vcc, 0, v3, vcc
	global_load_dwordx2 v[30:31], v[30:31], off offset:1024
	v_add_co_u32_e32 v32, vcc, 0x3aaea000, v2
	s_mov_b64 s[0:1], vcc
	v_add_co_u32_e32 v34, vcc, 0x3a2ca000, v2
	v_mov_b32_e32 v41, v7
	s_nop 0
	v_addc_co_u32_e32 v35, vcc, 0, v3, vcc
	global_load_dwordx2 v[34:35], v[34:35], off offset:1024
	v_add_co_u32_e32 v36, vcc, 0x3aaf2000, v2
	s_mov_b64 s[14:15], vcc
	v_add_co_u32_e32 v38, vcc, 0x3a2d2000, v2
	s_waitcnt vmcnt(8)
; __device__ __forceinline__ void phase_s5b_gqa(const Params& P, unsigned char* smraw, int bid, int nb) {
;     ...
;         float sr = 0.f, si = 0.f;
;         for (int c0 = 0; c0 < 260; c0 += 20) {
;             float2 e[20];
; #pragma unroll
;             for (int j = 0; j < 20; ++j) e[j] = SE[(size_t)(c0 + j) * 4096 + i];
; #pragma unroll
;             for (int j = 0; j < 20; ++j) {
;                 CIN[(size_t)(c0 + j) * 4096 + i] = make_float2(sr, si);
;                 const float nr = a.x * sr - a.y * si + e[j].x, ni = a.x * si + a.y * sr + e[j].y;
;                 sr = nr; si = ni;
;             }
	v_pk_add_f32 v[6:7], v[8:9], v[40:41]
	v_addc_co_u32_e32 v39, vcc, 0, v3, vcc
	global_load_dwordx2 v[38:39], v[38:39], off offset:1024
	v_addc_co_u32_e64 v15, vcc, 0, v3, s[6:7]
	v_pk_mul_f32 v[8:9], v[4:5], v[6:7] op_sel:[1,0]
	global_store_dwordx2 v[14:15], v[6:7], off offset:1024
	v_pk_fma_f32 v[10:11], v[4:5], v[6:7], v[8:9] op_sel:[0,0,1] op_sel_hi:[1,1,0] neg_lo:[0,0,1] neg_hi:[0,0,1]
	v_pk_fma_f32 v[6:7], v[4:5], v[6:7], v[8:9] op_sel:[0,0,1] op_sel_hi:[0,1,0]
	v_addc_co_u32_e64 v13, vcc, 0, v3, s[12:13]
	v_mov_b32_e32 v11, v7
	v_add_co_u32_e32 v8, vcc, 0x3aafa000, v2
	s_mov_b64 s[6:7], vcc
	s_waitcnt vmcnt(9)
	v_pk_add_f32 v[6:7], v[16:17], v[10:11]
	v_add_co_u32_e32 v10, vcc, 0x3a2da000, v2
	global_store_dwordx2 v[12:13], v[6:7], off offset:1024
	s_nop 0
	v_addc_co_u32_e32 v11, vcc, 0, v3, vcc
	global_load_dwordx2 v[10:11], v[10:11], off offset:1024
	v_add_co_u32_e32 v14, vcc, 0x3ab02000, v2
	s_mov_b64 s[12:13], vcc
	v_add_co_u32_e32 v16, vcc, 0x3a2e2000, v2
	v_pk_mul_f32 v[12:13], v[4:5], v[6:7] op_sel:[1,0]
	s_nop 0
	v_addc_co_u32_e32 v17, vcc, 0, v3, vcc
	global_load_dwordx2 v[16:17], v[16:17], off offset:1024
	v_pk_fma_f32 v[40:41], v[4:5], v[6:7], v[12:13] op_sel:[0,0,1] op_sel_hi:[1,1,0] neg_lo:[0,0,1] neg_hi:[0,0,1]
	v_pk_fma_f32 v[6:7], v[4:5], v[6:7], v[12:13] op_sel:[0,0,1] op_sel_hi:[0,1,0]
	v_mov_b32_e32 v41, v7
	s_waitcnt vmcnt(9)
	v_pk_add_f32 v[6:7], v[18:19], v[40:41]
	v_addc_co_u32_e64 v21, vcc, 0, v3, s[4:5]
	v_pk_mul_f32 v[12:13], v[4:5], v[6:7] op_sel:[1,0]
	global_store_dwordx2 v[20:21], v[6:7], off offset:1024
	v_pk_fma_f32 v[18:19], v[4:5], v[6:7], v[12:13] op_sel:[0,0,1] op_sel_hi:[1,1,0] neg_lo:[0,0,1] neg_hi:[0,0,1]
	v_pk_fma_f32 v[6:7], v[4:5], v[6:7], v[12:13] op_sel:[0,0,1] op_sel_hi:[0,1,0]
	v_mov_b32_e32 v19, v7
	v_addc_co_u32_e64 v25, vcc, 0, v3, s[8:9]
	s_waitcnt vmcnt(9)
	v_pk_add_f32 v[6:7], v[22:23], v[18:19]
	global_store_dwordx2 v[24:25], v[6:7], off offset:1024
	v_pk_mul_f32 v[12:13], v[4:5], v[6:7] op_sel:[1,0]
	v_addc_co_u32_e64 v29, vcc, 0, v3, s[10:11]
	v_pk_fma_f32 v[18:19], v[4:5], v[6:7], v[12:13] op_sel:[0,0,1] op_sel_hi:[1,1,0] neg_lo:[0,0,1] neg_hi:[0,0,1]
	v_pk_fma_f32 v[6:7], v[4:5], v[6:7], v[12:13] op_sel:[0,0,1] op_sel_hi:[0,1,0]
	v_mov_b32_e32 v19, v7
	s_waitcnt vmcnt(9)
	v_pk_add_f32 v[6:7], v[26:27], v[18:19]
	global_store_dwordx2 v[28:29], v[6:7], off offset:1024
	v_pk_mul_f32 v[12:13], v[4:5], v[6:7] op_sel:[1,0]
	v_addc_co_u32_e64 v33, vcc, 0, v3, s[0:1]
	v_pk_fma_f32 v[18:19], v[4:5], v[6:7], v[12:13] op_sel:[0,0,1] op_sel_hi:[1,1,0] neg_lo:[0,0,1] neg_hi:[0,0,1]
	v_pk_fma_f32 v[6:7], v[4:5], v[6:7], v[12:13] op_sel:[0,0,1] op_sel_hi:[0,1,0]
	v_mov_b32_e32 v19, v7
	v_addc_co_u32_e64 v37, vcc, 0, v3, s[14:15]
	s_waitcnt vmcnt(9)
	v_pk_add_f32 v[6:7], v[30:31], v[18:19]
	global_store_dwordx2 v[32:33], v[6:7], off offset:1024
	v_pk_mul_f32 v[12:13], v[4:5], v[6:7] op_sel:[1,0]
	v_addc_co_u32_e64 v9, vcc, 0, v3, s[6:7]
	v_pk_fma_f32 v[18:19], v[4:5], v[6:7], v[12:13] op_sel:[0,0,1] op_sel_hi:[1,1,0] neg_lo:[0,0,1] neg_hi:[0,0,1]
	v_pk_fma_f32 v[6:7], v[4:5], v[6:7], v[12:13] op_sel:[0,0,1] op_sel_hi:[0,1,0]
	v_mov_b32_e32 v19, v7
	s_waitcnt vmcnt(9)
	v_pk_add_f32 v[6:7], v[34:35], v[18:19]
	global_store_dwordx2 v[36:37], v[6:7], off offset:1024
	v_pk_mul_f32 v[12:13], v[4:5], v[6:7] op_sel:[1,0]
	s_nop 0
	v_pk_fma_f32 v[18:19], v[4:5], v[6:7], v[12:13] op_sel:[0,0,1] op_sel_hi:[1,1,0] neg_lo:[0,0,1] neg_hi:[0,0,1]
	v_pk_fma_f32 v[6:7], v[4:5], v[6:7], v[12:13] op_sel:[0,0,1] op_sel_hi:[0,1,0]
	v_mov_b32_e32 v19, v7
	s_waitcnt vmcnt(9)
	v_pk_add_f32 v[6:7], v[38:39], v[18:19]
	global_store_dwordx2 v[8:9], v[6:7], off offset:1024
	v_pk_mul_f32 v[8:9], v[4:5], v[6:7] op_sel:[1,0]
	s_nop 0
	v_pk_fma_f32 v[12:13], v[4:5], v[6:7], v[8:9] op_sel:[0,0,1] op_sel_hi:[1,1,0] neg_lo:[0,0,1] neg_hi:[0,0,1]
	v_pk_fma_f32 v[6:7], v[4:5], v[6:7], v[8:9] op_sel:[0,0,1] op_sel_hi:[0,1,0]
	v_add_co_u32_e32 v6, vcc, 0x3ab0a000, v2
	s_mov_b64 s[0:1], vcc
	v_add_co_u32_e32 v8, vcc, 0x3a2ea000, v2
	v_mov_b32_e32 v13, v7
	s_nop 0
	v_addc_co_u32_e32 v9, vcc, 0, v3, vcc
	global_load_dwordx2 v[8:9], v[8:9], off offset:1024
	v_add_co_u32_e32 v18, vcc, 0x3ab12000, v2
	s_mov_b64 s[6:7], vcc
	v_add_co_u32_e32 v20, vcc, 0x3a2f2000, v2
	s_waitcnt vmcnt(8)
	v_pk_add_f32 v[10:11], v[10:11], v[12:13]
	v_addc_co_u32_e32 v21, vcc, 0, v3, vcc
	global_load_dwordx2 v[20:21], v[20:21], off offset:1024
	v_addc_co_u32_e64 v15, vcc, 0, v3, s[12:13]
	v_pk_mul_f32 v[12:13], v[4:5], v[10:11] op_sel:[1,0]
	global_store_dwordx2 v[14:15], v[10:11], off offset:1024
	v_pk_fma_f32 v[14:15], v[4:5], v[10:11], v[12:13] op_sel:[0,0,1] op_sel_hi:[1,1,0] neg_lo:[0,0,1] neg_hi:[0,0,1]
	v_pk_fma_f32 v[10:11], v[4:5], v[10:11], v[12:13] op_sel:[0,0,1] op_sel_hi:[0,1,0]
	v_addc_co_u32_e64 v7, vcc, 0, v3, s[0:1]
	v_mov_b32_e32 v15, v11
	v_add_co_u32_e32 v12, vcc, 0x3ab1a000, v2
	s_waitcnt vmcnt(9)
; __device__ __forceinline__ void phase_s5b_gqa(const Params& P, unsigned char* smraw, int bid, int nb) {
;     ...
;         float sr = 0.f, si = 0.f;
;         for (int c0 = 0; c0 < 260; c0 += 20) {
;             float2 e[20];
; #pragma unroll
;             for (int j = 0; j < 20; ++j) e[j] = SE[(size_t)(c0 + j) * 4096 + i];
; #pragma unroll
;             for (int j = 0; j < 20; ++j) {
;                 CIN[(size_t)(c0 + j) * 4096 + i] = make_float2(sr, si);
;                 const float nr = a.x * sr - a.y * si + e[j].x, ni = a.x * si + a.y * sr + e[j].y;
;                 sr = nr; si = ni;
;             }
	v_pk_add_f32 v[10:11], v[16:17], v[14:15]
	s_mov_b64 s[12:13], vcc
	v_add_co_u32_e32 v14, vcc, 0x3a2fa000, v2
	global_store_dwordx2 v[6:7], v[10:11], off offset:1024
	s_nop 0
	v_addc_co_u32_e32 v15, vcc, 0, v3, vcc
	global_load_dwordx2 v[14:15], v[14:15], off offset:1024
	v_add_co_u32_e32 v16, vcc, 0x3ab22000, v2
	s_mov_b64 s[4:5], vcc
	v_add_co_u32_e32 v22, vcc, 0x3a302000, v2
	v_pk_mul_f32 v[6:7], v[4:5], v[10:11] op_sel:[1,0]
	s_nop 0
	v_addc_co_u32_e32 v23, vcc, 0, v3, vcc
	global_load_dwordx2 v[22:23], v[22:23], off offset:1024
	v_add_co_u32_e32 v24, vcc, 0x3ab2a000, v2
	s_mov_b64 s[8:9], vcc
	v_add_co_u32_e32 v26, vcc, 0x3a30a000, v2
	v_pk_fma_f32 v[40:41], v[4:5], v[10:11], v[6:7] op_sel:[0,0,1] op_sel_hi:[1,1,0] neg_lo:[0,0,1] neg_hi:[0,0,1]
	s_nop 0
	v_addc_co_u32_e32 v27, vcc, 0, v3, vcc
	global_load_dwordx2 v[26:27], v[26:27], off offset:1024
	v_add_co_u32_e32 v28, vcc, 0x3ab32000, v2
	s_mov_b64 s[10:11], vcc
	v_add_co_u32_e32 v30, vcc, 0x3a312000, v2
	v_pk_fma_f32 v[6:7], v[4:5], v[10:11], v[6:7] op_sel:[0,0,1] op_sel_hi:[0,1,0]
	s_nop 0
	v_addc_co_u32_e32 v31, vcc, 0, v3, vcc
	global_load_dwordx2 v[30:31], v[30:31], off offset:1024
	v_add_co_u32_e32 v32, vcc, 0x3ab3a000, v2
	s_mov_b64 s[0:1], vcc
	v_add_co_u32_e32 v34, vcc, 0x3a31a000, v2
	v_mov_b32_e32 v41, v7
	s_nop 0
	v_addc_co_u32_e32 v35, vcc, 0, v3, vcc
	global_load_dwordx2 v[34:35], v[34:35], off offset:1024
	v_add_co_u32_e32 v36, vcc, 0x3ab42000, v2
	s_mov_b64 s[14:15], vcc
	v_add_co_u32_e32 v38, vcc, 0x3a322000, v2
	s_waitcnt vmcnt(8)
	v_pk_add_f32 v[6:7], v[8:9], v[40:41]
	v_addc_co_u32_e32 v39, vcc, 0, v3, vcc
	global_load_dwordx2 v[38:39], v[38:39], off offset:1024
	v_addc_co_u32_e64 v19, vcc, 0, v3, s[6:7]
	v_pk_mul_f32 v[8:9], v[4:5], v[6:7] op_sel:[1,0]
	global_store_dwordx2 v[18:19], v[6:7], off offset:1024
	v_pk_fma_f32 v[10:11], v[4:5], v[6:7], v[8:9] op_sel:[0,0,1] op_sel_hi:[1,1,0] neg_lo:[0,0,1] neg_hi:[0,0,1]
	v_pk_fma_f32 v[6:7], v[4:5], v[6:7], v[8:9] op_sel:[0,0,1] op_sel_hi:[0,1,0]
	v_addc_co_u32_e64 v13, vcc, 0, v3, s[12:13]
	v_mov_b32_e32 v11, v7
	v_add_co_u32_e32 v8, vcc, 0x3ab4a000, v2
	s_waitcnt vmcnt(9)
	v_pk_add_f32 v[6:7], v[10:11], v[20:21]
	s_mov_b64 s[6:7], vcc
	v_add_co_u32_e32 v10, vcc, 0x3a32a000, v2
	global_store_dwordx2 v[12:13], v[6:7], off offset:1024
	s_nop 0
	v_addc_co_u32_e32 v11, vcc, 0, v3, vcc
	global_load_dwordx2 v[10:11], v[10:11], off offset:1024
	v_add_co_u32_e32 v18, vcc, 0x3ab52000, v2
	s_mov_b64 s[12:13], vcc
	v_add_co_u32_e32 v20, vcc, 0x3a332000, v2
	v_pk_mul_f32 v[12:13], v[4:5], v[6:7] op_sel:[1,1] op_sel_hi:[0,1]
	s_nop 0
	v_addc_co_u32_e32 v21, vcc, 0, v3, vcc
	global_load_dwordx2 v[20:21], v[20:21], off offset:1024
	v_pk_fma_f32 v[40:41], v[4:5], v[6:7], v[12:13] neg_lo:[0,0,1] neg_hi:[0,0,1]
	v_pk_fma_f32 v[6:7], v[4:5], v[6:7], v[12:13] op_sel_hi:[1,0,1]
	v_addc_co_u32_e64 v17, vcc, 0, v3, s[4:5]
	v_mov_b32_e32 v41, v7
	s_waitcnt vmcnt(9)
	v_pk_add_f32 v[6:7], v[14:15], v[40:41]
	global_store_dwordx2 v[16:17], v[6:7], off offset:1024
	v_pk_mul_f32 v[12:13], v[4:5], v[6:7] op_sel:[1,0]
	v_addc_co_u32_e64 v25, vcc, 0, v3, s[8:9]
	v_pk_fma_f32 v[14:15], v[4:5], v[6:7], v[12:13] op_sel:[0,0,1] op_sel_hi:[1,1,0] neg_lo:[0,0,1] neg_hi:[0,0,1]
	v_pk_fma_f32 v[6:7], v[4:5], v[6:7], v[12:13] op_sel:[0,0,1] op_sel_hi:[0,1,0]
	v_mov_b32_e32 v15, v7
	s_waitcnt vmcnt(9)
	v_pk_add_f32 v[6:7], v[22:23], v[14:15]
	global_store_dwordx2 v[24:25], v[6:7], off offset:1024
	v_pk_mul_f32 v[12:13], v[4:5], v[6:7] op_sel:[1,0]
	v_addc_co_u32_e64 v29, vcc, 0, v3, s[10:11]
	v_pk_fma_f32 v[14:15], v[4:5], v[6:7], v[12:13] op_sel:[0,0,1] op_sel_hi:[1,1,0] neg_lo:[0,0,1] neg_hi:[0,0,1]
	v_pk_fma_f32 v[6:7], v[4:5], v[6:7], v[12:13] op_sel:[0,0,1] op_sel_hi:[0,1,0]
	v_mov_b32_e32 v15, v7
	s_waitcnt vmcnt(9)
	v_pk_add_f32 v[6:7], v[26:27], v[14:15]
	global_store_dwordx2 v[28:29], v[6:7], off offset:1024
	v_pk_mul_f32 v[12:13], v[4:5], v[6:7] op_sel:[1,0]
	v_addc_co_u32_e64 v33, vcc, 0, v3, s[0:1]
	v_pk_fma_f32 v[14:15], v[4:5], v[6:7], v[12:13] op_sel:[0,0,1] op_sel_hi:[1,1,0] neg_lo:[0,0,1] neg_hi:[0,0,1]
	v_pk_fma_f32 v[6:7], v[4:5], v[6:7], v[12:13] op_sel:[0,0,1] op_sel_hi:[0,1,0]
	v_mov_b32_e32 v15, v7
	s_waitcnt vmcnt(9)
	v_pk_add_f32 v[6:7], v[30:31], v[14:15]
	global_store_dwordx2 v[32:33], v[6:7], off offset:1024
	v_pk_mul_f32 v[12:13], v[4:5], v[6:7] op_sel:[1,0]
	v_addc_co_u32_e64 v37, vcc, 0, v3, s[14:15]
	v_pk_fma_f32 v[14:15], v[4:5], v[6:7], v[12:13] op_sel:[0,0,1] op_sel_hi:[1,1,0] neg_lo:[0,0,1] neg_hi:[0,0,1]
	v_pk_fma_f32 v[6:7], v[4:5], v[6:7], v[12:13] op_sel:[0,0,1] op_sel_hi:[0,1,0]
	v_mov_b32_e32 v15, v7
	s_waitcnt vmcnt(9)
	v_pk_add_f32 v[6:7], v[34:35], v[14:15]
	global_store_dwordx2 v[36:37], v[6:7], off offset:1024
	v_pk_mul_f32 v[12:13], v[4:5], v[6:7] op_sel:[1,0]
	v_addc_co_u32_e64 v9, vcc, 0, v3, s[6:7]
	v_pk_fma_f32 v[14:15], v[4:5], v[6:7], v[12:13] op_sel:[0,0,1] op_sel_hi:[1,1,0] neg_lo:[0,0,1] neg_hi:[0,0,1]
	v_pk_fma_f32 v[6:7], v[4:5], v[6:7], v[12:13] op_sel:[0,0,1] op_sel_hi:[0,1,0]
	v_mov_b32_e32 v15, v7
	s_waitcnt vmcnt(9)
	v_pk_add_f32 v[6:7], v[38:39], v[14:15]
	global_store_dwordx2 v[8:9], v[6:7], off offset:1024
	v_pk_mul_f32 v[8:9], v[4:5], v[6:7] op_sel:[1,0]
	s_nop 0
	v_pk_fma_f32 v[12:13], v[4:5], v[6:7], v[8:9] op_sel:[0,0,1] op_sel_hi:[1,1,0] neg_lo:[0,0,1] neg_hi:[0,0,1]
	v_pk_fma_f32 v[6:7], v[4:5], v[6:7], v[8:9] op_sel:[0,0,1] op_sel_hi:[0,1,0]
	v_add_co_u32_e32 v6, vcc, 0x3ab5a000, v2
	s_mov_b64 s[0:1], vcc
	v_add_co_u32_e32 v8, vcc, 0x3a33a000, v2
	v_mov_b32_e32 v13, v7
	s_nop 0
	v_addc_co_u32_e32 v9, vcc, 0, v3, vcc
	global_load_dwordx2 v[8:9], v[8:9], off offset:1024
	v_add_co_u32_e32 v14, vcc, 0x3ab62000, v2
	s_mov_b64 s[6:7], vcc
	v_add_co_u32_e32 v16, vcc, 0x3a342000, v2
	s_waitcnt vmcnt(8)
; __device__ __forceinline__ void phase_s5b_gqa(const Params& P, unsigned char* smraw, int bid, int nb) {
;     ...
;         float sr = 0.f, si = 0.f;
;         for (int c0 = 0; c0 < 260; c0 += 20) {
;             float2 e[20];
; #pragma unroll
;             for (int j = 0; j < 20; ++j) e[j] = SE[(size_t)(c0 + j) * 4096 + i];
; #pragma unroll
;             for (int j = 0; j < 20; ++j) {
;                 CIN[(size_t)(c0 + j) * 4096 + i] = make_float2(sr, si);
;                 const float nr = a.x * sr - a.y * si + e[j].x, ni = a.x * si + a.y * sr + e[j].y;
;                 sr = nr; si = ni;
;             }
	v_pk_add_f32 v[10:11], v[10:11], v[12:13]
	v_addc_co_u32_e32 v17, vcc, 0, v3, vcc
	global_load_dwordx2 v[16:17], v[16:17], off offset:1024
	v_addc_co_u32_e64 v19, vcc, 0, v3, s[12:13]
	v_pk_mul_f32 v[12:13], v[4:5], v[10:11] op_sel:[1,0]
	global_store_dwordx2 v[18:19], v[10:11], off offset:1024
	v_pk_fma_f32 v[18:19], v[4:5], v[10:11], v[12:13] op_sel:[0,0,1] op_sel_hi:[1,1,0] neg_lo:[0,0,1] neg_hi:[0,0,1]
	v_pk_fma_f32 v[10:11], v[4:5], v[10:11], v[12:13] op_sel:[0,0,1] op_sel_hi:[0,1,0]
	v_addc_co_u32_e64 v7, vcc, 0, v3, s[0:1]
	v_mov_b32_e32 v19, v11
	v_add_co_u32_e32 v12, vcc, 0x3ab6a000, v2
	s_waitcnt vmcnt(9)
	v_pk_add_f32 v[10:11], v[20:21], v[18:19]
	s_mov_b64 s[12:13], vcc
	v_add_co_u32_e32 v18, vcc, 0x3a34a000, v2
	global_store_dwordx2 v[6:7], v[10:11], off offset:1024
	s_nop 0
	v_addc_co_u32_e32 v19, vcc, 0, v3, vcc
	global_load_dwordx2 v[18:19], v[18:19], off offset:1024
	v_add_co_u32_e32 v20, vcc, 0x3ab72000, v2
	s_mov_b64 s[4:5], vcc
	v_add_co_u32_e32 v22, vcc, 0x3a352000, v2
	v_pk_mul_f32 v[6:7], v[4:5], v[10:11] op_sel:[1,0]
	s_nop 0
	v_addc_co_u32_e32 v23, vcc, 0, v3, vcc
	global_load_dwordx2 v[22:23], v[22:23], off offset:1024
	v_add_co_u32_e32 v24, vcc, 0x3ab7a000, v2
	s_mov_b64 s[8:9], vcc
	v_add_co_u32_e32 v26, vcc, 0x3a35a000, v2
	v_pk_fma_f32 v[40:41], v[4:5], v[10:11], v[6:7] op_sel:[0,0,1] op_sel_hi:[1,1,0] neg_lo:[0,0,1] neg_hi:[0,0,1]
	s_nop 0
	v_addc_co_u32_e32 v27, vcc, 0, v3, vcc
	global_load_dwordx2 v[26:27], v[26:27], off offset:1024
	v_add_co_u32_e32 v28, vcc, 0x3ab82000, v2
	s_mov_b64 s[10:11], vcc
	v_add_co_u32_e32 v30, vcc, 0x3a362000, v2
	v_pk_fma_f32 v[6:7], v[4:5], v[10:11], v[6:7] op_sel:[0,0,1] op_sel_hi:[0,1,0]
	s_nop 0
	v_addc_co_u32_e32 v31, vcc, 0, v3, vcc
	global_load_dwordx2 v[30:31], v[30:31], off offset:1024
	v_add_co_u32_e32 v32, vcc, 0x3ab8a000, v2
	s_mov_b64 s[0:1], vcc
	v_add_co_u32_e32 v34, vcc, 0x3a36a000, v2
	v_mov_b32_e32 v41, v7
	s_nop 0
	v_addc_co_u32_e32 v35, vcc, 0, v3, vcc
	global_load_dwordx2 v[34:35], v[34:35], off offset:1024
	v_add_co_u32_e32 v36, vcc, 0x3ab92000, v2
	s_mov_b64 s[14:15], vcc
	v_add_co_u32_e32 v38, vcc, 0x3a372000, v2
	s_waitcnt vmcnt(8)
	v_pk_add_f32 v[6:7], v[8:9], v[40:41]
	v_addc_co_u32_e32 v39, vcc, 0, v3, vcc
	global_load_dwordx2 v[38:39], v[38:39], off offset:1024
	v_addc_co_u32_e64 v15, vcc, 0, v3, s[6:7]
	v_pk_mul_f32 v[8:9], v[4:5], v[6:7] op_sel:[1,0]
	global_store_dwordx2 v[14:15], v[6:7], off offset:1024
	v_pk_fma_f32 v[10:11], v[4:5], v[6:7], v[8:9] op_sel:[0,0,1] op_sel_hi:[1,1,0] neg_lo:[0,0,1] neg_hi:[0,0,1]
	v_pk_fma_f32 v[6:7], v[4:5], v[6:7], v[8:9] op_sel:[0,0,1] op_sel_hi:[0,1,0]
	v_addc_co_u32_e64 v13, vcc, 0, v3, s[12:13]
	v_mov_b32_e32 v11, v7
	v_add_co_u32_e32 v8, vcc, 0x3ab9a000, v2
	s_waitcnt vmcnt(9)
	v_pk_add_f32 v[6:7], v[16:17], v[10:11]
	s_mov_b64 s[6:7], vcc
	v_add_co_u32_e32 v10, vcc, 0x3a37a000, v2
	global_store_dwordx2 v[12:13], v[6:7], off offset:1024
	s_nop 0
	v_addc_co_u32_e32 v11, vcc, 0, v3, vcc
	global_load_dwordx2 v[10:11], v[10:11], off offset:1024
	v_add_co_u32_e32 v14, vcc, 0x3aba2000, v2
	s_mov_b64 s[12:13], vcc
	v_add_co_u32_e32 v16, vcc, 0x3a382000, v2
	v_pk_mul_f32 v[12:13], v[4:5], v[6:7] op_sel:[1,0]
	s_nop 0
	v_addc_co_u32_e32 v17, vcc, 0, v3, vcc
	global_load_dwordx2 v[16:17], v[16:17], off offset:1024
	v_pk_fma_f32 v[40:41], v[4:5], v[6:7], v[12:13] op_sel:[0,0,1] op_sel_hi:[1,1,0] neg_lo:[0,0,1] neg_hi:[0,0,1]
	v_pk_fma_f32 v[6:7], v[4:5], v[6:7], v[12:13] op_sel:[0,0,1] op_sel_hi:[0,1,0]
	v_mov_b32_e32 v41, v7
	s_waitcnt vmcnt(9)
	v_pk_add_f32 v[6:7], v[18:19], v[40:41]
	v_addc_co_u32_e64 v21, vcc, 0, v3, s[4:5]
	v_pk_mul_f32 v[12:13], v[4:5], v[6:7] op_sel:[1,0]
	global_store_dwordx2 v[20:21], v[6:7], off offset:1024
	v_pk_fma_f32 v[18:19], v[4:5], v[6:7], v[12:13] op_sel:[0,0,1] op_sel_hi:[1,1,0] neg_lo:[0,0,1] neg_hi:[0,0,1]
	v_pk_fma_f32 v[6:7], v[4:5], v[6:7], v[12:13] op_sel:[0,0,1] op_sel_hi:[0,1,0]
	v_mov_b32_e32 v19, v7
	s_waitcnt vmcnt(9)
	v_pk_add_f32 v[6:7], v[22:23], v[18:19]
	v_addc_co_u32_e64 v25, vcc, 0, v3, s[8:9]
	v_pk_mul_f32 v[12:13], v[4:5], v[6:7] op_sel:[1,0]
	global_store_dwordx2 v[24:25], v[6:7], off offset:1024
	v_pk_fma_f32 v[18:19], v[4:5], v[6:7], v[12:13] op_sel:[0,0,1] op_sel_hi:[1,1,0] neg_lo:[0,0,1] neg_hi:[0,0,1]
	v_pk_fma_f32 v[6:7], v[4:5], v[6:7], v[12:13] op_sel:[0,0,1] op_sel_hi:[0,1,0]
	v_mov_b32_e32 v19, v7
	s_waitcnt vmcnt(9)
	v_pk_add_f32 v[6:7], v[26:27], v[18:19]
	v_addc_co_u32_e64 v29, vcc, 0, v3, s[10:11]
	v_pk_mul_f32 v[12:13], v[4:5], v[6:7] op_sel:[1,0]
	global_store_dwordx2 v[28:29], v[6:7], off offset:1024
	v_pk_fma_f32 v[18:19], v[4:5], v[6:7], v[12:13] op_sel:[0,0,1] op_sel_hi:[1,1,0] neg_lo:[0,0,1] neg_hi:[0,0,1]
	v_pk_fma_f32 v[6:7], v[4:5], v[6:7], v[12:13] op_sel:[0,0,1] op_sel_hi:[0,1,0]
	v_mov_b32_e32 v19, v7
	s_waitcnt vmcnt(9)
	v_pk_add_f32 v[6:7], v[30:31], v[18:19]
	v_addc_co_u32_e64 v33, vcc, 0, v3, s[0:1]
	v_pk_mul_f32 v[12:13], v[4:5], v[6:7] op_sel:[1,0]
	global_store_dwordx2 v[32:33], v[6:7], off offset:1024
	v_pk_fma_f32 v[18:19], v[4:5], v[6:7], v[12:13] op_sel:[0,0,1] op_sel_hi:[1,1,0] neg_lo:[0,0,1] neg_hi:[0,0,1]
	v_pk_fma_f32 v[6:7], v[4:5], v[6:7], v[12:13] op_sel:[0,0,1] op_sel_hi:[0,1,0]
	v_mov_b32_e32 v19, v7
	s_waitcnt vmcnt(9)
	v_pk_add_f32 v[6:7], v[34:35], v[18:19]
	v_addc_co_u32_e64 v37, vcc, 0, v3, s[14:15]
	v_pk_mul_f32 v[12:13], v[4:5], v[6:7] op_sel:[1,0]
	global_store_dwordx2 v[36:37], v[6:7], off offset:1024
	v_pk_fma_f32 v[18:19], v[4:5], v[6:7], v[12:13] op_sel:[0,0,1] op_sel_hi:[1,1,0] neg_lo:[0,0,1] neg_hi:[0,0,1]
	v_pk_fma_f32 v[6:7], v[4:5], v[6:7], v[12:13] op_sel:[0,0,1] op_sel_hi:[0,1,0]
	v_mov_b32_e32 v19, v7
	v_addc_co_u32_e64 v9, vcc, 0, v3, s[6:7]
	s_waitcnt vmcnt(9)
; __device__ __forceinline__ void phase_s5b_gqa(const Params& P, unsigned char* smraw, int bid, int nb) {
;     ...
;         float sr = 0.f, si = 0.f;
;         for (int c0 = 0; c0 < 260; c0 += 20) {
;             float2 e[20];
; #pragma unroll
;             for (int j = 0; j < 20; ++j) e[j] = SE[(size_t)(c0 + j) * 4096 + i];
; #pragma unroll
;             for (int j = 0; j < 20; ++j) {
;                 CIN[(size_t)(c0 + j) * 4096 + i] = make_float2(sr, si);
;                 const float nr = a.x * sr - a.y * si + e[j].x, ni = a.x * si + a.y * sr + e[j].y;
;                 sr = nr; si = ni;
;             }
	v_pk_add_f32 v[6:7], v[38:39], v[18:19]
	global_store_dwordx2 v[8:9], v[6:7], off offset:1024
	v_pk_mul_f32 v[8:9], v[4:5], v[6:7] op_sel:[1,0]
	s_nop 0
	v_pk_fma_f32 v[12:13], v[4:5], v[6:7], v[8:9] op_sel:[0,0,1] op_sel_hi:[1,1,0] neg_lo:[0,0,1] neg_hi:[0,0,1]
	v_pk_fma_f32 v[6:7], v[4:5], v[6:7], v[8:9] op_sel:[0,0,1] op_sel_hi:[0,1,0]
	v_add_co_u32_e32 v6, vcc, 0x3abaa000, v2
	s_mov_b64 s[0:1], vcc
	v_add_co_u32_e32 v8, vcc, 0x3a38a000, v2
	v_mov_b32_e32 v13, v7
	s_nop 0
	v_addc_co_u32_e32 v9, vcc, 0, v3, vcc
	global_load_dwordx2 v[8:9], v[8:9], off offset:1024
	v_add_co_u32_e32 v18, vcc, 0x3abb2000, v2
	s_mov_b64 s[6:7], vcc
	v_add_co_u32_e32 v20, vcc, 0x3a392000, v2
	s_waitcnt vmcnt(8)
	v_pk_add_f32 v[10:11], v[10:11], v[12:13]
	v_addc_co_u32_e32 v21, vcc, 0, v3, vcc
	global_load_dwordx2 v[20:21], v[20:21], off offset:1024
	v_addc_co_u32_e64 v15, vcc, 0, v3, s[12:13]
	v_pk_mul_f32 v[12:13], v[4:5], v[10:11] op_sel:[1,0]
	global_store_dwordx2 v[14:15], v[10:11], off offset:1024
	v_pk_fma_f32 v[14:15], v[4:5], v[10:11], v[12:13] op_sel:[0,0,1] op_sel_hi:[1,1,0] neg_lo:[0,0,1] neg_hi:[0,0,1]
	v_pk_fma_f32 v[10:11], v[4:5], v[10:11], v[12:13] op_sel:[0,0,1] op_sel_hi:[0,1,0]
	v_addc_co_u32_e64 v7, vcc, 0, v3, s[0:1]
	v_mov_b32_e32 v15, v11
	v_add_co_u32_e32 v12, vcc, 0x3abba000, v2
	s_waitcnt vmcnt(9)
	v_pk_add_f32 v[10:11], v[16:17], v[14:15]
	s_mov_b64 s[12:13], vcc
	v_add_co_u32_e32 v14, vcc, 0x3a39a000, v2
	global_store_dwordx2 v[6:7], v[10:11], off offset:1024
	s_nop 0
	v_addc_co_u32_e32 v15, vcc, 0, v3, vcc
	global_load_dwordx2 v[14:15], v[14:15], off offset:1024
	v_add_co_u32_e32 v16, vcc, 0x3abc2000, v2
	s_mov_b64 s[4:5], vcc
	v_add_co_u32_e32 v22, vcc, 0x3a3a2000, v2
	v_pk_mul_f32 v[6:7], v[4:5], v[10:11] op_sel:[1,0]
	s_nop 0
	v_addc_co_u32_e32 v23, vcc, 0, v3, vcc
	global_load_dwordx2 v[22:23], v[22:23], off offset:1024
	v_add_co_u32_e32 v24, vcc, 0x3abca000, v2
	s_mov_b64 s[8:9], vcc
	v_add_co_u32_e32 v26, vcc, 0x3a3aa000, v2
	v_pk_fma_f32 v[40:41], v[4:5], v[10:11], v[6:7] op_sel:[0,0,1] op_sel_hi:[1,1,0] neg_lo:[0,0,1] neg_hi:[0,0,1]
	s_nop 0
	v_addc_co_u32_e32 v27, vcc, 0, v3, vcc
	global_load_dwordx2 v[26:27], v[26:27], off offset:1024
	v_add_co_u32_e32 v28, vcc, 0x3abd2000, v2
	s_mov_b64 s[10:11], vcc
	v_add_co_u32_e32 v30, vcc, 0x3a3b2000, v2
	v_pk_fma_f32 v[6:7], v[4:5], v[10:11], v[6:7] op_sel:[0,0,1] op_sel_hi:[0,1,0]
	s_nop 0
	v_addc_co_u32_e32 v31, vcc, 0, v3, vcc
	global_load_dwordx2 v[30:31], v[30:31], off offset:1024
	v_add_co_u32_e32 v32, vcc, 0x3abda000, v2
	s_mov_b64 s[0:1], vcc
	v_add_co_u32_e32 v34, vcc, 0x3a3ba000, v2
	v_mov_b32_e32 v41, v7
	s_nop 0
	v_addc_co_u32_e32 v35, vcc, 0, v3, vcc
	global_load_dwordx2 v[34:35], v[34:35], off offset:1024
	v_add_co_u32_e32 v36, vcc, 0x3abe2000, v2
	s_mov_b64 s[14:15], vcc
	v_add_co_u32_e32 v38, vcc, 0x3a3c2000, v2
	s_waitcnt vmcnt(8)
	v_pk_add_f32 v[6:7], v[8:9], v[40:41]
	v_addc_co_u32_e32 v39, vcc, 0, v3, vcc
	global_load_dwordx2 v[38:39], v[38:39], off offset:1024
	v_addc_co_u32_e64 v19, vcc, 0, v3, s[6:7]
	v_pk_mul_f32 v[8:9], v[4:5], v[6:7] op_sel:[1,0]
	global_store_dwordx2 v[18:19], v[6:7], off offset:1024
	v_pk_fma_f32 v[10:11], v[4:5], v[6:7], v[8:9] op_sel:[0,0,1] op_sel_hi:[1,1,0] neg_lo:[0,0,1] neg_hi:[0,0,1]
	v_pk_fma_f32 v[6:7], v[4:5], v[6:7], v[8:9] op_sel:[0,0,1] op_sel_hi:[0,1,0]
	v_addc_co_u32_e64 v13, vcc, 0, v3, s[12:13]
	v_mov_b32_e32 v11, v7
	v_add_co_u32_e32 v8, vcc, 0x3abea000, v2
	s_waitcnt vmcnt(9)
	v_pk_add_f32 v[6:7], v[10:11], v[20:21]
	s_mov_b64 s[6:7], vcc
	v_add_co_u32_e32 v10, vcc, 0x3a3ca000, v2
	global_store_dwordx2 v[12:13], v[6:7], off offset:1024
	s_nop 0
	v_addc_co_u32_e32 v11, vcc, 0, v3, vcc
	global_load_dwordx2 v[10:11], v[10:11], off offset:1024
	v_add_co_u32_e32 v18, vcc, 0x3abf2000, v2
	s_mov_b64 s[12:13], vcc
	v_add_co_u32_e32 v20, vcc, 0x3a3d2000, v2
	v_pk_mul_f32 v[12:13], v[4:5], v[6:7] op_sel:[1,1] op_sel_hi:[0,1]
	s_nop 0
	v_addc_co_u32_e32 v21, vcc, 0, v3, vcc
	global_load_dwordx2 v[20:21], v[20:21], off offset:1024
	v_pk_fma_f32 v[40:41], v[4:5], v[6:7], v[12:13] neg_lo:[0,0,1] neg_hi:[0,0,1]
	v_pk_fma_f32 v[6:7], v[4:5], v[6:7], v[12:13] op_sel_hi:[1,0,1]
	v_addc_co_u32_e64 v17, vcc, 0, v3, s[4:5]
	v_mov_b32_e32 v41, v7
	s_waitcnt vmcnt(9)
	v_pk_add_f32 v[6:7], v[14:15], v[40:41]
	global_store_dwordx2 v[16:17], v[6:7], off offset:1024
	v_pk_mul_f32 v[12:13], v[4:5], v[6:7] op_sel:[1,0]
	v_addc_co_u32_e64 v25, vcc, 0, v3, s[8:9]
	v_pk_fma_f32 v[14:15], v[4:5], v[6:7], v[12:13] op_sel:[0,0,1] op_sel_hi:[1,1,0] neg_lo:[0,0,1] neg_hi:[0,0,1]
	v_pk_fma_f32 v[6:7], v[4:5], v[6:7], v[12:13] op_sel:[0,0,1] op_sel_hi:[0,1,0]
	v_mov_b32_e32 v15, v7
	s_waitcnt vmcnt(9)
	v_pk_add_f32 v[6:7], v[22:23], v[14:15]
	global_store_dwordx2 v[24:25], v[6:7], off offset:1024
	v_pk_mul_f32 v[12:13], v[4:5], v[6:7] op_sel:[1,0]
	v_addc_co_u32_e64 v29, vcc, 0, v3, s[10:11]
	v_pk_fma_f32 v[14:15], v[4:5], v[6:7], v[12:13] op_sel:[0,0,1] op_sel_hi:[1,1,0] neg_lo:[0,0,1] neg_hi:[0,0,1]
	v_pk_fma_f32 v[6:7], v[4:5], v[6:7], v[12:13] op_sel:[0,0,1] op_sel_hi:[0,1,0]
	v_mov_b32_e32 v15, v7
	s_waitcnt vmcnt(9)
	v_pk_add_f32 v[6:7], v[26:27], v[14:15]
	global_store_dwordx2 v[28:29], v[6:7], off offset:1024
	v_pk_mul_f32 v[12:13], v[4:5], v[6:7] op_sel:[1,0]
	v_addc_co_u32_e64 v33, vcc, 0, v3, s[0:1]
	v_pk_fma_f32 v[14:15], v[4:5], v[6:7], v[12:13] op_sel:[0,0,1] op_sel_hi:[1,1,0] neg_lo:[0,0,1] neg_hi:[0,0,1]
	v_pk_fma_f32 v[6:7], v[4:5], v[6:7], v[12:13] op_sel:[0,0,1] op_sel_hi:[0,1,0]
	v_mov_b32_e32 v15, v7
	s_waitcnt vmcnt(9)
; __device__ __forceinline__ void phase_s5b_gqa(const Params& P, unsigned char* smraw, int bid, int nb) {
;     ...
;         float sr = 0.f, si = 0.f;
;         for (int c0 = 0; c0 < 260; c0 += 20) {
;             float2 e[20];
; #pragma unroll
;             for (int j = 0; j < 20; ++j) e[j] = SE[(size_t)(c0 + j) * 4096 + i];
; #pragma unroll
;             for (int j = 0; j < 20; ++j) {
;                 CIN[(size_t)(c0 + j) * 4096 + i] = make_float2(sr, si);
;                 const float nr = a.x * sr - a.y * si + e[j].x, ni = a.x * si + a.y * sr + e[j].y;
;                 sr = nr; si = ni;
;             }
	v_pk_add_f32 v[6:7], v[30:31], v[14:15]
	global_store_dwordx2 v[32:33], v[6:7], off offset:1024
	v_pk_mul_f32 v[12:13], v[4:5], v[6:7] op_sel:[1,0]
	v_addc_co_u32_e64 v37, vcc, 0, v3, s[14:15]
	v_pk_fma_f32 v[14:15], v[4:5], v[6:7], v[12:13] op_sel:[0,0,1] op_sel_hi:[1,1,0] neg_lo:[0,0,1] neg_hi:[0,0,1]
	v_pk_fma_f32 v[6:7], v[4:5], v[6:7], v[12:13] op_sel:[0,0,1] op_sel_hi:[0,1,0]
	v_mov_b32_e32 v15, v7
	s_waitcnt vmcnt(9)
	v_pk_add_f32 v[6:7], v[34:35], v[14:15]
	global_store_dwordx2 v[36:37], v[6:7], off offset:1024
	v_pk_mul_f32 v[12:13], v[4:5], v[6:7] op_sel:[1,0]
	v_addc_co_u32_e64 v9, vcc, 0, v3, s[6:7]
	v_pk_fma_f32 v[14:15], v[4:5], v[6:7], v[12:13] op_sel:[0,0,1] op_sel_hi:[1,1,0] neg_lo:[0,0,1] neg_hi:[0,0,1]
	v_pk_fma_f32 v[6:7], v[4:5], v[6:7], v[12:13] op_sel:[0,0,1] op_sel_hi:[0,1,0]
	v_mov_b32_e32 v15, v7
	s_waitcnt vmcnt(9)
	v_pk_add_f32 v[6:7], v[38:39], v[14:15]
	global_store_dwordx2 v[8:9], v[6:7], off offset:1024
	v_pk_mul_f32 v[8:9], v[4:5], v[6:7] op_sel:[1,0]
	s_nop 0
	v_pk_fma_f32 v[12:13], v[4:5], v[6:7], v[8:9] op_sel:[0,0,1] op_sel_hi:[1,1,0] neg_lo:[0,0,1] neg_hi:[0,0,1]
	v_pk_fma_f32 v[6:7], v[4:5], v[6:7], v[8:9] op_sel:[0,0,1] op_sel_hi:[0,1,0]
	v_add_co_u32_e32 v6, vcc, 0x3abfa000, v2
	s_mov_b64 s[0:1], vcc
	v_add_co_u32_e32 v8, vcc, 0x3a3da000, v2
	v_mov_b32_e32 v13, v7
	s_nop 0
	v_addc_co_u32_e32 v9, vcc, 0, v3, vcc
	global_load_dwordx2 v[8:9], v[8:9], off offset:1024
	v_add_co_u32_e32 v14, vcc, 0x3ac02000, v2
	s_mov_b64 s[6:7], vcc
	v_add_co_u32_e32 v16, vcc, 0x3a3e2000, v2
	s_waitcnt vmcnt(8)
	v_pk_add_f32 v[10:11], v[10:11], v[12:13]
	v_addc_co_u32_e32 v17, vcc, 0, v3, vcc
	global_load_dwordx2 v[16:17], v[16:17], off offset:1024
	v_addc_co_u32_e64 v19, vcc, 0, v3, s[12:13]
	v_pk_mul_f32 v[12:13], v[4:5], v[10:11] op_sel:[1,0]
	global_store_dwordx2 v[18:19], v[10:11], off offset:1024
	v_pk_fma_f32 v[18:19], v[4:5], v[10:11], v[12:13] op_sel:[0,0,1] op_sel_hi:[1,1,0] neg_lo:[0,0,1] neg_hi:[0,0,1]
	v_pk_fma_f32 v[10:11], v[4:5], v[10:11], v[12:13] op_sel:[0,0,1] op_sel_hi:[0,1,0]
	v_addc_co_u32_e64 v7, vcc, 0, v3, s[0:1]
	v_mov_b32_e32 v19, v11
	v_add_co_u32_e32 v12, vcc, 0x3ac0a000, v2
	s_waitcnt vmcnt(9)
	v_pk_add_f32 v[10:11], v[20:21], v[18:19]
	s_mov_b64 s[12:13], vcc
	v_add_co_u32_e32 v18, vcc, 0x3a3ea000, v2
	global_store_dwordx2 v[6:7], v[10:11], off offset:1024
	s_nop 0
	v_addc_co_u32_e32 v19, vcc, 0, v3, vcc
	global_load_dwordx2 v[18:19], v[18:19], off offset:1024
	v_add_co_u32_e32 v20, vcc, 0x3ac12000, v2
	s_mov_b64 s[4:5], vcc
	v_add_co_u32_e32 v22, vcc, 0x3a3f2000, v2
	v_pk_mul_f32 v[6:7], v[4:5], v[10:11] op_sel:[1,0]
	s_nop 0
	v_addc_co_u32_e32 v23, vcc, 0, v3, vcc
	global_load_dwordx2 v[22:23], v[22:23], off offset:1024
	v_add_co_u32_e32 v24, vcc, 0x3ac1a000, v2
	s_mov_b64 s[8:9], vcc
	v_add_co_u32_e32 v26, vcc, 0x3a3fa000, v2
	v_pk_fma_f32 v[40:41], v[4:5], v[10:11], v[6:7] op_sel:[0,0,1] op_sel_hi:[1,1,0] neg_lo:[0,0,1] neg_hi:[0,0,1]
	s_nop 0
	v_addc_co_u32_e32 v27, vcc, 0, v3, vcc
	global_load_dwordx2 v[26:27], v[26:27], off offset:1024
	v_add_co_u32_e32 v28, vcc, 0x3ac22000, v2
	s_mov_b64 s[10:11], vcc
	v_add_co_u32_e32 v30, vcc, 0x3a402000, v2
	v_pk_fma_f32 v[6:7], v[4:5], v[10:11], v[6:7] op_sel:[0,0,1] op_sel_hi:[0,1,0]
	s_nop 0
	v_addc_co_u32_e32 v31, vcc, 0, v3, vcc
	global_load_dwordx2 v[30:31], v[30:31], off offset:1024
	v_add_co_u32_e32 v32, vcc, 0x3ac2a000, v2
	s_mov_b64 s[0:1], vcc
	v_add_co_u32_e32 v34, vcc, 0x3a40a000, v2
	v_mov_b32_e32 v41, v7
	s_nop 0
	v_addc_co_u32_e32 v35, vcc, 0, v3, vcc
	global_load_dwordx2 v[34:35], v[34:35], off offset:1024
	v_add_co_u32_e32 v36, vcc, 0x3ac32000, v2
	s_mov_b64 s[14:15], vcc
	v_add_co_u32_e32 v38, vcc, 0x3a412000, v2
	s_waitcnt vmcnt(8)
	v_pk_add_f32 v[6:7], v[8:9], v[40:41]
	v_addc_co_u32_e32 v39, vcc, 0, v3, vcc
	global_load_dwordx2 v[38:39], v[38:39], off offset:1024
	v_addc_co_u32_e64 v15, vcc, 0, v3, s[6:7]
	v_pk_mul_f32 v[8:9], v[4:5], v[6:7] op_sel:[1,0]
	global_store_dwordx2 v[14:15], v[6:7], off offset:1024
	v_pk_fma_f32 v[10:11], v[4:5], v[6:7], v[8:9] op_sel:[0,0,1] op_sel_hi:[1,1,0] neg_lo:[0,0,1] neg_hi:[0,0,1]
	v_pk_fma_f32 v[6:7], v[4:5], v[6:7], v[8:9] op_sel:[0,0,1] op_sel_hi:[0,1,0]
	v_addc_co_u32_e64 v13, vcc, 0, v3, s[12:13]
	v_mov_b32_e32 v11, v7
	v_add_co_u32_e32 v8, vcc, 0x3ac3a000, v2
	s_waitcnt vmcnt(9)
	v_pk_add_f32 v[6:7], v[16:17], v[10:11]
	s_mov_b64 s[6:7], vcc
	v_add_co_u32_e32 v10, vcc, 0x3a41a000, v2
	global_store_dwordx2 v[12:13], v[6:7], off offset:1024
	s_nop 0
	v_addc_co_u32_e32 v11, vcc, 0, v3, vcc
	global_load_dwordx2 v[10:11], v[10:11], off offset:1024
	v_add_co_u32_e32 v14, vcc, 0x3ac42000, v2
	s_mov_b64 s[12:13], vcc
	v_add_co_u32_e32 v16, vcc, 0x3a422000, v2
	v_pk_mul_f32 v[12:13], v[4:5], v[6:7] op_sel:[1,0]
	s_nop 0
	v_addc_co_u32_e32 v17, vcc, 0, v3, vcc
	global_load_dwordx2 v[16:17], v[16:17], off offset:1024
	v_pk_fma_f32 v[40:41], v[4:5], v[6:7], v[12:13] op_sel:[0,0,1] op_sel_hi:[1,1,0] neg_lo:[0,0,1] neg_hi:[0,0,1]
	v_pk_fma_f32 v[6:7], v[4:5], v[6:7], v[12:13] op_sel:[0,0,1] op_sel_hi:[0,1,0]
	v_mov_b32_e32 v41, v7
	s_waitcnt vmcnt(9)
	v_pk_add_f32 v[6:7], v[18:19], v[40:41]
	v_addc_co_u32_e64 v21, vcc, 0, v3, s[4:5]
	v_pk_mul_f32 v[12:13], v[4:5], v[6:7] op_sel:[1,0]
	global_store_dwordx2 v[20:21], v[6:7], off offset:1024
	v_pk_fma_f32 v[18:19], v[4:5], v[6:7], v[12:13] op_sel:[0,0,1] op_sel_hi:[1,1,0] neg_lo:[0,0,1] neg_hi:[0,0,1]
	v_pk_fma_f32 v[6:7], v[4:5], v[6:7], v[12:13] op_sel:[0,0,1] op_sel_hi:[0,1,0]
	v_mov_b32_e32 v19, v7
	s_waitcnt vmcnt(9)
; __device__ __forceinline__ void phase_s5b_gqa(const Params& P, unsigned char* smraw, int bid, int nb) {
;     ...
;         float sr = 0.f, si = 0.f;
;         for (int c0 = 0; c0 < 260; c0 += 20) {
;             float2 e[20];
; #pragma unroll
;             for (int j = 0; j < 20; ++j) e[j] = SE[(size_t)(c0 + j) * 4096 + i];
; #pragma unroll
;             for (int j = 0; j < 20; ++j) {
;                 CIN[(size_t)(c0 + j) * 4096 + i] = make_float2(sr, si);
;                 const float nr = a.x * sr - a.y * si + e[j].x, ni = a.x * si + a.y * sr + e[j].y;
;                 sr = nr; si = ni;
;             }
	v_pk_add_f32 v[6:7], v[22:23], v[18:19]
	v_addc_co_u32_e64 v25, vcc, 0, v3, s[8:9]
	v_pk_mul_f32 v[12:13], v[4:5], v[6:7] op_sel:[1,0]
	global_store_dwordx2 v[24:25], v[6:7], off offset:1024
	v_pk_fma_f32 v[18:19], v[4:5], v[6:7], v[12:13] op_sel:[0,0,1] op_sel_hi:[1,1,0] neg_lo:[0,0,1] neg_hi:[0,0,1]
	v_pk_fma_f32 v[6:7], v[4:5], v[6:7], v[12:13] op_sel:[0,0,1] op_sel_hi:[0,1,0]
	v_mov_b32_e32 v19, v7
	s_waitcnt vmcnt(9)
	v_pk_add_f32 v[6:7], v[26:27], v[18:19]
	v_addc_co_u32_e64 v29, vcc, 0, v3, s[10:11]
	v_pk_mul_f32 v[12:13], v[4:5], v[6:7] op_sel:[1,0]
	global_store_dwordx2 v[28:29], v[6:7], off offset:1024
	v_pk_fma_f32 v[18:19], v[4:5], v[6:7], v[12:13] op_sel:[0,0,1] op_sel_hi:[1,1,0] neg_lo:[0,0,1] neg_hi:[0,0,1]
	v_pk_fma_f32 v[6:7], v[4:5], v[6:7], v[12:13] op_sel:[0,0,1] op_sel_hi:[0,1,0]
	v_mov_b32_e32 v19, v7
	s_waitcnt vmcnt(9)
	v_pk_add_f32 v[6:7], v[30:31], v[18:19]
	v_addc_co_u32_e64 v33, vcc, 0, v3, s[0:1]
	v_pk_mul_f32 v[12:13], v[4:5], v[6:7] op_sel:[1,0]
	global_store_dwordx2 v[32:33], v[6:7], off offset:1024
	v_pk_fma_f32 v[18:19], v[4:5], v[6:7], v[12:13] op_sel:[0,0,1] op_sel_hi:[1,1,0] neg_lo:[0,0,1] neg_hi:[0,0,1]
	v_pk_fma_f32 v[6:7], v[4:5], v[6:7], v[12:13] op_sel:[0,0,1] op_sel_hi:[0,1,0]
	v_mov_b32_e32 v19, v7
	s_waitcnt vmcnt(9)
	v_pk_add_f32 v[6:7], v[34:35], v[18:19]
	v_addc_co_u32_e64 v37, vcc, 0, v3, s[14:15]
	v_pk_mul_f32 v[12:13], v[4:5], v[6:7] op_sel:[1,0]
	global_store_dwordx2 v[36:37], v[6:7], off offset:1024
	v_pk_fma_f32 v[18:19], v[4:5], v[6:7], v[12:13] op_sel:[0,0,1] op_sel_hi:[1,1,0] neg_lo:[0,0,1] neg_hi:[0,0,1]
	v_pk_fma_f32 v[6:7], v[4:5], v[6:7], v[12:13] op_sel:[0,0,1] op_sel_hi:[0,1,0]
	v_mov_b32_e32 v19, v7
	v_addc_co_u32_e64 v9, vcc, 0, v3, s[6:7]
	s_waitcnt vmcnt(9)
	v_pk_add_f32 v[6:7], v[38:39], v[18:19]
	global_store_dwordx2 v[8:9], v[6:7], off offset:1024
	v_pk_mul_f32 v[8:9], v[4:5], v[6:7] op_sel:[1,0]
	s_nop 0
	v_pk_fma_f32 v[12:13], v[4:5], v[6:7], v[8:9] op_sel:[0,0,1] op_sel_hi:[1,1,0] neg_lo:[0,0,1] neg_hi:[0,0,1]
	v_pk_fma_f32 v[6:7], v[4:5], v[6:7], v[8:9] op_sel:[0,0,1] op_sel_hi:[0,1,0]
	v_add_co_u32_e32 v6, vcc, 0x3ac4a000, v2
	s_mov_b64 s[0:1], vcc
	v_add_co_u32_e32 v8, vcc, 0x3a42a000, v2
	v_mov_b32_e32 v13, v7
	s_nop 0
	v_addc_co_u32_e32 v9, vcc, 0, v3, vcc
	global_load_dwordx2 v[8:9], v[8:9], off offset:1024
	v_add_co_u32_e32 v18, vcc, 0x3ac52000, v2
	s_mov_b64 s[6:7], vcc
	v_add_co_u32_e32 v20, vcc, 0x3a432000, v2
	s_waitcnt vmcnt(8)
	v_pk_add_f32 v[10:11], v[10:11], v[12:13]
	v_addc_co_u32_e32 v21, vcc, 0, v3, vcc
	global_load_dwordx2 v[20:21], v[20:21], off offset:1024
	v_addc_co_u32_e64 v15, vcc, 0, v3, s[12:13]
	v_pk_mul_f32 v[12:13], v[4:5], v[10:11] op_sel:[1,0]
	global_store_dwordx2 v[14:15], v[10:11], off offset:1024
	v_pk_fma_f32 v[14:15], v[4:5], v[10:11], v[12:13] op_sel:[0,0,1] op_sel_hi:[1,1,0] neg_lo:[0,0,1] neg_hi:[0,0,1]
	v_pk_fma_f32 v[10:11], v[4:5], v[10:11], v[12:13] op_sel:[0,0,1] op_sel_hi:[0,1,0]
	v_addc_co_u32_e64 v7, vcc, 0, v3, s[0:1]
	v_mov_b32_e32 v15, v11
	v_add_co_u32_e32 v12, vcc, 0x3ac5a000, v2
	s_waitcnt vmcnt(9)
	v_pk_add_f32 v[10:11], v[16:17], v[14:15]
	s_mov_b64 s[12:13], vcc
	v_add_co_u32_e32 v14, vcc, 0x3a43a000, v2
	global_store_dwordx2 v[6:7], v[10:11], off offset:1024
	s_nop 0
	v_addc_co_u32_e32 v15, vcc, 0, v3, vcc
	global_load_dwordx2 v[14:15], v[14:15], off offset:1024
	v_add_co_u32_e32 v16, vcc, 0x3ac62000, v2
	s_mov_b64 s[4:5], vcc
	v_add_co_u32_e32 v22, vcc, 0x3a442000, v2
	v_pk_mul_f32 v[6:7], v[4:5], v[10:11] op_sel:[1,0]
	s_nop 0
	v_addc_co_u32_e32 v23, vcc, 0, v3, vcc
	global_load_dwordx2 v[22:23], v[22:23], off offset:1024
	v_add_co_u32_e32 v24, vcc, 0x3ac6a000, v2
	s_mov_b64 s[8:9], vcc
	v_add_co_u32_e32 v26, vcc, 0x3a44a000, v2
	v_pk_fma_f32 v[40:41], v[4:5], v[10:11], v[6:7] op_sel:[0,0,1] op_sel_hi:[1,1,0] neg_lo:[0,0,1] neg_hi:[0,0,1]
	s_nop 0
	v_addc_co_u32_e32 v27, vcc, 0, v3, vcc
	global_load_dwordx2 v[26:27], v[26:27], off offset:1024
	v_add_co_u32_e32 v28, vcc, 0x3ac72000, v2
	s_mov_b64 s[10:11], vcc
	v_add_co_u32_e32 v30, vcc, 0x3a452000, v2
	v_pk_fma_f32 v[6:7], v[4:5], v[10:11], v[6:7] op_sel:[0,0,1] op_sel_hi:[0,1,0]
	s_nop 0
	v_addc_co_u32_e32 v31, vcc, 0, v3, vcc
	global_load_dwordx2 v[30:31], v[30:31], off offset:1024
	v_add_co_u32_e32 v32, vcc, 0x3ac7a000, v2
	s_mov_b64 s[0:1], vcc
	v_add_co_u32_e32 v34, vcc, 0x3a45a000, v2
	v_mov_b32_e32 v41, v7
	s_nop 0
	v_addc_co_u32_e32 v35, vcc, 0, v3, vcc
	global_load_dwordx2 v[34:35], v[34:35], off offset:1024
	v_add_co_u32_e32 v36, vcc, 0x3ac82000, v2
	s_mov_b64 s[14:15], vcc
	v_add_co_u32_e32 v38, vcc, 0x3a462000, v2
	s_waitcnt vmcnt(8)
	v_pk_add_f32 v[6:7], v[8:9], v[40:41]
	v_addc_co_u32_e32 v39, vcc, 0, v3, vcc
	global_load_dwordx2 v[38:39], v[38:39], off offset:1024
	v_addc_co_u32_e64 v19, vcc, 0, v3, s[6:7]
	v_pk_mul_f32 v[8:9], v[4:5], v[6:7] op_sel:[1,0]
	global_store_dwordx2 v[18:19], v[6:7], off offset:1024
	v_pk_fma_f32 v[10:11], v[4:5], v[6:7], v[8:9] op_sel:[0,0,1] op_sel_hi:[1,1,0] neg_lo:[0,0,1] neg_hi:[0,0,1]
	v_pk_fma_f32 v[6:7], v[4:5], v[6:7], v[8:9] op_sel:[0,0,1] op_sel_hi:[0,1,0]
	v_addc_co_u32_e64 v13, vcc, 0, v3, s[12:13]
	v_mov_b32_e32 v11, v7
	v_add_co_u32_e32 v8, vcc, 0x3ac8a000, v2
	s_waitcnt vmcnt(9)
	v_pk_add_f32 v[6:7], v[10:11], v[20:21]
	s_mov_b64 s[6:7], vcc
	v_add_co_u32_e32 v10, vcc, 0x3a46a000, v2
	global_store_dwordx2 v[12:13], v[6:7], off offset:1024
	s_nop 0
	v_addc_co_u32_e32 v11, vcc, 0, v3, vcc
	global_load_dwordx2 v[10:11], v[10:11], off offset:1024
	v_add_co_u32_e32 v18, vcc, 0x3ac92000, v2
	s_mov_b64 s[12:13], vcc
	v_add_co_u32_e32 v20, vcc, 0x3a472000, v2
	v_pk_mul_f32 v[12:13], v[4:5], v[6:7] op_sel:[1,1] op_sel_hi:[0,1]
	s_nop 0
	v_addc_co_u32_e32 v21, vcc, 0, v3, vcc
	global_load_dwordx2 v[20:21], v[20:21], off offset:1024
	v_pk_fma_f32 v[40:41], v[4:5], v[6:7], v[12:13] neg_lo:[0,0,1] neg_hi:[0,0,1]
	v_pk_fma_f32 v[6:7], v[4:5], v[6:7], v[12:13] op_sel_hi:[1,0,1]
	v_addc_co_u32_e64 v17, vcc, 0, v3, s[4:5]
	v_mov_b32_e32 v41, v7
	s_waitcnt vmcnt(9)
; __device__ __forceinline__ void phase_s5b_gqa(const Params& P, unsigned char* smraw, int bid, int nb) {
;     ...
;         float sr = 0.f, si = 0.f;
;         for (int c0 = 0; c0 < 260; c0 += 20) {
;             float2 e[20];
; #pragma unroll
;             for (int j = 0; j < 20; ++j) e[j] = SE[(size_t)(c0 + j) * 4096 + i];
; #pragma unroll
;             for (int j = 0; j < 20; ++j) {
;                 CIN[(size_t)(c0 + j) * 4096 + i] = make_float2(sr, si);
;                 const float nr = a.x * sr - a.y * si + e[j].x, ni = a.x * si + a.y * sr + e[j].y;
;                 sr = nr; si = ni;
;             }
	v_pk_add_f32 v[6:7], v[14:15], v[40:41]
	global_store_dwordx2 v[16:17], v[6:7], off offset:1024
	v_pk_mul_f32 v[12:13], v[4:5], v[6:7] op_sel:[1,0]
	v_addc_co_u32_e64 v25, vcc, 0, v3, s[8:9]
	v_pk_fma_f32 v[14:15], v[4:5], v[6:7], v[12:13] op_sel:[0,0,1] op_sel_hi:[1,1,0] neg_lo:[0,0,1] neg_hi:[0,0,1]
	v_pk_fma_f32 v[6:7], v[4:5], v[6:7], v[12:13] op_sel:[0,0,1] op_sel_hi:[0,1,0]
	v_mov_b32_e32 v15, v7
	s_waitcnt vmcnt(9)
	v_pk_add_f32 v[6:7], v[22:23], v[14:15]
	global_store_dwordx2 v[24:25], v[6:7], off offset:1024
	v_pk_mul_f32 v[12:13], v[4:5], v[6:7] op_sel:[1,0]
	v_addc_co_u32_e64 v29, vcc, 0, v3, s[10:11]
	v_pk_fma_f32 v[14:15], v[4:5], v[6:7], v[12:13] op_sel:[0,0,1] op_sel_hi:[1,1,0] neg_lo:[0,0,1] neg_hi:[0,0,1]
	v_pk_fma_f32 v[6:7], v[4:5], v[6:7], v[12:13] op_sel:[0,0,1] op_sel_hi:[0,1,0]
	v_mov_b32_e32 v15, v7
	s_waitcnt vmcnt(9)
	v_pk_add_f32 v[6:7], v[26:27], v[14:15]
	global_store_dwordx2 v[28:29], v[6:7], off offset:1024
	v_pk_mul_f32 v[12:13], v[4:5], v[6:7] op_sel:[1,0]
	v_addc_co_u32_e64 v33, vcc, 0, v3, s[0:1]
	v_pk_fma_f32 v[14:15], v[4:5], v[6:7], v[12:13] op_sel:[0,0,1] op_sel_hi:[1,1,0] neg_lo:[0,0,1] neg_hi:[0,0,1]
	v_pk_fma_f32 v[6:7], v[4:5], v[6:7], v[12:13] op_sel:[0,0,1] op_sel_hi:[0,1,0]
	v_mov_b32_e32 v15, v7
	s_waitcnt vmcnt(9)
	v_pk_add_f32 v[6:7], v[30:31], v[14:15]
	global_store_dwordx2 v[32:33], v[6:7], off offset:1024
	v_pk_mul_f32 v[12:13], v[4:5], v[6:7] op_sel:[1,0]
	v_addc_co_u32_e64 v37, vcc, 0, v3, s[14:15]
	v_pk_fma_f32 v[14:15], v[4:5], v[6:7], v[12:13] op_sel:[0,0,1] op_sel_hi:[1,1,0] neg_lo:[0,0,1] neg_hi:[0,0,1]
	v_pk_fma_f32 v[6:7], v[4:5], v[6:7], v[12:13] op_sel:[0,0,1] op_sel_hi:[0,1,0]
	v_mov_b32_e32 v15, v7
	s_waitcnt vmcnt(9)
	v_pk_add_f32 v[6:7], v[34:35], v[14:15]
	global_store_dwordx2 v[36:37], v[6:7], off offset:1024
	v_pk_mul_f32 v[12:13], v[4:5], v[6:7] op_sel:[1,0]
	v_addc_co_u32_e64 v9, vcc, 0, v3, s[6:7]
	v_pk_fma_f32 v[14:15], v[4:5], v[6:7], v[12:13] op_sel:[0,0,1] op_sel_hi:[1,1,0] neg_lo:[0,0,1] neg_hi:[0,0,1]
	v_pk_fma_f32 v[6:7], v[4:5], v[6:7], v[12:13] op_sel:[0,0,1] op_sel_hi:[0,1,0]
	v_mov_b32_e32 v15, v7
	s_waitcnt vmcnt(9)
	v_pk_add_f32 v[6:7], v[38:39], v[14:15]
	global_store_dwordx2 v[8:9], v[6:7], off offset:1024
	v_pk_mul_f32 v[8:9], v[4:5], v[6:7] op_sel:[1,0]
	s_nop 0
	v_pk_fma_f32 v[12:13], v[4:5], v[6:7], v[8:9] op_sel:[0,0,1] op_sel_hi:[1,1,0] neg_lo:[0,0,1] neg_hi:[0,0,1]
	v_pk_fma_f32 v[6:7], v[4:5], v[6:7], v[8:9] op_sel:[0,0,1] op_sel_hi:[0,1,0]
	v_add_co_u32_e32 v6, vcc, 0x3ac9a000, v2
	s_mov_b64 s[0:1], vcc
	v_add_co_u32_e32 v8, vcc, 0x3a47a000, v2
	v_mov_b32_e32 v13, v7
	s_nop 0
	v_addc_co_u32_e32 v9, vcc, 0, v3, vcc
	global_load_dwordx2 v[8:9], v[8:9], off offset:1024
	v_add_co_u32_e32 v14, vcc, 0x3aca2000, v2
	s_mov_b64 s[6:7], vcc
	v_add_co_u32_e32 v16, vcc, 0x3a482000, v2
	s_waitcnt vmcnt(8)
	v_pk_add_f32 v[10:11], v[10:11], v[12:13]
	v_addc_co_u32_e32 v17, vcc, 0, v3, vcc
	global_load_dwordx2 v[16:17], v[16:17], off offset:1024
	v_addc_co_u32_e64 v19, vcc, 0, v3, s[12:13]
	v_pk_mul_f32 v[12:13], v[4:5], v[10:11] op_sel:[1,0]
	global_store_dwordx2 v[18:19], v[10:11], off offset:1024
	v_pk_fma_f32 v[18:19], v[4:5], v[10:11], v[12:13] op_sel:[0,0,1] op_sel_hi:[1,1,0] neg_lo:[0,0,1] neg_hi:[0,0,1]
	v_pk_fma_f32 v[10:11], v[4:5], v[10:11], v[12:13] op_sel:[0,0,1] op_sel_hi:[0,1,0]
	v_addc_co_u32_e64 v7, vcc, 0, v3, s[0:1]
	v_mov_b32_e32 v19, v11
	v_add_co_u32_e32 v12, vcc, 0x3acaa000, v2
	s_waitcnt vmcnt(9)
	v_pk_add_f32 v[10:11], v[20:21], v[18:19]
	s_mov_b64 s[12:13], vcc
	v_add_co_u32_e32 v18, vcc, 0x3a48a000, v2
	global_store_dwordx2 v[6:7], v[10:11], off offset:1024
	s_nop 0
	v_addc_co_u32_e32 v19, vcc, 0, v3, vcc
	global_load_dwordx2 v[18:19], v[18:19], off offset:1024
	v_add_co_u32_e32 v20, vcc, 0x3acb2000, v2
	s_mov_b64 s[4:5], vcc
	v_add_co_u32_e32 v22, vcc, 0x3a492000, v2
	v_pk_mul_f32 v[6:7], v[4:5], v[10:11] op_sel:[1,0]
	s_nop 0
	v_addc_co_u32_e32 v23, vcc, 0, v3, vcc
	global_load_dwordx2 v[22:23], v[22:23], off offset:1024
	v_add_co_u32_e32 v24, vcc, 0x3acba000, v2
	s_mov_b64 s[8:9], vcc
	v_add_co_u32_e32 v26, vcc, 0x3a49a000, v2
	v_pk_fma_f32 v[40:41], v[4:5], v[10:11], v[6:7] op_sel:[0,0,1] op_sel_hi:[1,1,0] neg_lo:[0,0,1] neg_hi:[0,0,1]
	s_nop 0
	v_addc_co_u32_e32 v27, vcc, 0, v3, vcc
	global_load_dwordx2 v[26:27], v[26:27], off offset:1024
	v_add_co_u32_e32 v28, vcc, 0x3acc2000, v2
	s_mov_b64 s[10:11], vcc
	v_add_co_u32_e32 v30, vcc, 0x3a4a2000, v2
	v_pk_fma_f32 v[6:7], v[4:5], v[10:11], v[6:7] op_sel:[0,0,1] op_sel_hi:[0,1,0]
	s_nop 0
	v_addc_co_u32_e32 v31, vcc, 0, v3, vcc
	global_load_dwordx2 v[30:31], v[30:31], off offset:1024
	v_add_co_u32_e32 v32, vcc, 0x3acca000, v2
	s_mov_b64 s[0:1], vcc
	v_add_co_u32_e32 v34, vcc, 0x3a4aa000, v2
	v_mov_b32_e32 v41, v7
	s_nop 0
	v_addc_co_u32_e32 v35, vcc, 0, v3, vcc
	global_load_dwordx2 v[34:35], v[34:35], off offset:1024
	v_add_co_u32_e32 v36, vcc, 0x3acd2000, v2
	s_mov_b64 s[14:15], vcc
	v_add_co_u32_e32 v38, vcc, 0x3a4b2000, v2
	s_waitcnt vmcnt(8)
	v_pk_add_f32 v[6:7], v[8:9], v[40:41]
	v_addc_co_u32_e32 v39, vcc, 0, v3, vcc
	global_load_dwordx2 v[38:39], v[38:39], off offset:1024
	v_addc_co_u32_e64 v15, vcc, 0, v3, s[6:7]
	v_pk_mul_f32 v[8:9], v[4:5], v[6:7] op_sel:[1,0]
	global_store_dwordx2 v[14:15], v[6:7], off offset:1024
	v_pk_fma_f32 v[10:11], v[4:5], v[6:7], v[8:9] op_sel:[0,0,1] op_sel_hi:[1,1,0] neg_lo:[0,0,1] neg_hi:[0,0,1]
	v_pk_fma_f32 v[6:7], v[4:5], v[6:7], v[8:9] op_sel:[0,0,1] op_sel_hi:[0,1,0]
	v_addc_co_u32_e64 v13, vcc, 0, v3, s[12:13]
	v_mov_b32_e32 v11, v7
	v_add_co_u32_e32 v8, vcc, 0x3acda000, v2
	s_waitcnt vmcnt(9)
; __device__ __forceinline__ void phase_s5b_gqa(const Params& P, unsigned char* smraw, int bid, int nb) {
;     ...
;         float sr = 0.f, si = 0.f;
;         for (int c0 = 0; c0 < 260; c0 += 20) {
;             float2 e[20];
; #pragma unroll
;             for (int j = 0; j < 20; ++j) e[j] = SE[(size_t)(c0 + j) * 4096 + i];
; #pragma unroll
;             for (int j = 0; j < 20; ++j) {
;                 CIN[(size_t)(c0 + j) * 4096 + i] = make_float2(sr, si);
;                 const float nr = a.x * sr - a.y * si + e[j].x, ni = a.x * si + a.y * sr + e[j].y;
;                 sr = nr; si = ni;
;             }
	v_pk_add_f32 v[6:7], v[16:17], v[10:11]
	s_mov_b64 s[6:7], vcc
	v_add_co_u32_e32 v10, vcc, 0x3a4ba000, v2
	global_store_dwordx2 v[12:13], v[6:7], off offset:1024
	s_nop 0
	v_addc_co_u32_e32 v11, vcc, 0, v3, vcc
	global_load_dwordx2 v[10:11], v[10:11], off offset:1024
	v_add_co_u32_e32 v14, vcc, 0x3ace2000, v2
	s_mov_b64 s[12:13], vcc
	v_add_co_u32_e32 v16, vcc, 0x3a4c2000, v2
	v_pk_mul_f32 v[12:13], v[4:5], v[6:7] op_sel:[1,0]
	s_nop 0
	v_addc_co_u32_e32 v17, vcc, 0, v3, vcc
	global_load_dwordx2 v[16:17], v[16:17], off offset:1024
	v_pk_fma_f32 v[40:41], v[4:5], v[6:7], v[12:13] op_sel:[0,0,1] op_sel_hi:[1,1,0] neg_lo:[0,0,1] neg_hi:[0,0,1]
	v_pk_fma_f32 v[6:7], v[4:5], v[6:7], v[12:13] op_sel:[0,0,1] op_sel_hi:[0,1,0]
	v_mov_b32_e32 v41, v7
	s_waitcnt vmcnt(9)
	v_pk_add_f32 v[6:7], v[18:19], v[40:41]
	v_addc_co_u32_e64 v21, vcc, 0, v3, s[4:5]
	v_pk_mul_f32 v[12:13], v[4:5], v[6:7] op_sel:[1,0]
	global_store_dwordx2 v[20:21], v[6:7], off offset:1024
	v_pk_fma_f32 v[18:19], v[4:5], v[6:7], v[12:13] op_sel:[0,0,1] op_sel_hi:[1,1,0] neg_lo:[0,0,1] neg_hi:[0,0,1]
	v_pk_fma_f32 v[6:7], v[4:5], v[6:7], v[12:13] op_sel:[0,0,1] op_sel_hi:[0,1,0]
	v_mov_b32_e32 v19, v7
	s_waitcnt vmcnt(9)
	v_pk_add_f32 v[6:7], v[22:23], v[18:19]
	v_addc_co_u32_e64 v25, vcc, 0, v3, s[8:9]
	v_pk_mul_f32 v[12:13], v[4:5], v[6:7] op_sel:[1,0]
	global_store_dwordx2 v[24:25], v[6:7], off offset:1024
	v_pk_fma_f32 v[18:19], v[4:5], v[6:7], v[12:13] op_sel:[0,0,1] op_sel_hi:[1,1,0] neg_lo:[0,0,1] neg_hi:[0,0,1]
	v_pk_fma_f32 v[6:7], v[4:5], v[6:7], v[12:13] op_sel:[0,0,1] op_sel_hi:[0,1,0]
	v_mov_b32_e32 v19, v7
	s_waitcnt vmcnt(9)
	v_pk_add_f32 v[6:7], v[26:27], v[18:19]
	v_addc_co_u32_e64 v29, vcc, 0, v3, s[10:11]
	v_pk_mul_f32 v[12:13], v[4:5], v[6:7] op_sel:[1,0]
	global_store_dwordx2 v[28:29], v[6:7], off offset:1024
	v_pk_fma_f32 v[18:19], v[4:5], v[6:7], v[12:13] op_sel:[0,0,1] op_sel_hi:[1,1,0] neg_lo:[0,0,1] neg_hi:[0,0,1]
	v_pk_fma_f32 v[6:7], v[4:5], v[6:7], v[12:13] op_sel:[0,0,1] op_sel_hi:[0,1,0]
	v_mov_b32_e32 v19, v7
	s_waitcnt vmcnt(9)
	v_pk_add_f32 v[6:7], v[30:31], v[18:19]
	v_addc_co_u32_e64 v33, vcc, 0, v3, s[0:1]
	v_pk_mul_f32 v[12:13], v[4:5], v[6:7] op_sel:[1,0]
	global_store_dwordx2 v[32:33], v[6:7], off offset:1024
	v_pk_fma_f32 v[18:19], v[4:5], v[6:7], v[12:13] op_sel:[0,0,1] op_sel_hi:[1,1,0] neg_lo:[0,0,1] neg_hi:[0,0,1]
	v_pk_fma_f32 v[6:7], v[4:5], v[6:7], v[12:13] op_sel:[0,0,1] op_sel_hi:[0,1,0]
	v_mov_b32_e32 v19, v7
	s_waitcnt vmcnt(9)
	v_pk_add_f32 v[6:7], v[34:35], v[18:19]
	v_addc_co_u32_e64 v37, vcc, 0, v3, s[14:15]
	v_pk_mul_f32 v[12:13], v[4:5], v[6:7] op_sel:[1,0]
	global_store_dwordx2 v[36:37], v[6:7], off offset:1024
	v_pk_fma_f32 v[18:19], v[4:5], v[6:7], v[12:13] op_sel:[0,0,1] op_sel_hi:[1,1,0] neg_lo:[0,0,1] neg_hi:[0,0,1]
	v_pk_fma_f32 v[6:7], v[4:5], v[6:7], v[12:13] op_sel:[0,0,1] op_sel_hi:[0,1,0]
	v_mov_b32_e32 v19, v7
	v_addc_co_u32_e64 v9, vcc, 0, v3, s[6:7]
	s_waitcnt vmcnt(9)
	v_pk_add_f32 v[6:7], v[38:39], v[18:19]
	global_store_dwordx2 v[8:9], v[6:7], off offset:1024
	v_pk_mul_f32 v[8:9], v[4:5], v[6:7] op_sel:[1,0]
	s_nop 0
	v_pk_fma_f32 v[12:13], v[4:5], v[6:7], v[8:9] op_sel:[0,0,1] op_sel_hi:[1,1,0] neg_lo:[0,0,1] neg_hi:[0,0,1]
	v_pk_fma_f32 v[6:7], v[4:5], v[6:7], v[8:9] op_sel:[0,0,1] op_sel_hi:[0,1,0]
	v_add_co_u32_e32 v6, vcc, 0x3acea000, v2
	s_mov_b64 s[0:1], vcc
	v_add_co_u32_e32 v8, vcc, 0x3a4ca000, v2
	v_mov_b32_e32 v13, v7
	s_nop 0
	v_addc_co_u32_e32 v9, vcc, 0, v3, vcc
	global_load_dwordx2 v[8:9], v[8:9], off offset:1024
	v_add_co_u32_e32 v18, vcc, 0x3acf2000, v2
	s_mov_b64 s[6:7], vcc
	v_add_co_u32_e32 v20, vcc, 0x3a4d2000, v2
	s_waitcnt vmcnt(8)
	v_pk_add_f32 v[10:11], v[10:11], v[12:13]
	v_addc_co_u32_e32 v21, vcc, 0, v3, vcc
	global_load_dwordx2 v[20:21], v[20:21], off offset:1024
	v_addc_co_u32_e64 v15, vcc, 0, v3, s[12:13]
	v_pk_mul_f32 v[12:13], v[4:5], v[10:11] op_sel:[1,0]
	global_store_dwordx2 v[14:15], v[10:11], off offset:1024
	v_pk_fma_f32 v[14:15], v[4:5], v[10:11], v[12:13] op_sel:[0,0,1] op_sel_hi:[1,1,0] neg_lo:[0,0,1] neg_hi:[0,0,1]
	v_pk_fma_f32 v[10:11], v[4:5], v[10:11], v[12:13] op_sel:[0,0,1] op_sel_hi:[0,1,0]
	v_addc_co_u32_e64 v7, vcc, 0, v3, s[0:1]
	v_mov_b32_e32 v15, v11
	v_add_co_u32_e32 v12, vcc, 0x3acfa000, v2
	s_waitcnt vmcnt(9)
	v_pk_add_f32 v[10:11], v[16:17], v[14:15]
	s_mov_b64 s[12:13], vcc
	v_add_co_u32_e32 v14, vcc, 0x3a4da000, v2
	global_store_dwordx2 v[6:7], v[10:11], off offset:1024
	s_nop 0
	v_addc_co_u32_e32 v15, vcc, 0, v3, vcc
	global_load_dwordx2 v[14:15], v[14:15], off offset:1024
	v_add_co_u32_e32 v16, vcc, 0x3ad02000, v2
	s_mov_b64 s[4:5], vcc
	v_add_co_u32_e32 v22, vcc, 0x3a4e2000, v2
	v_pk_mul_f32 v[6:7], v[4:5], v[10:11] op_sel:[1,0]
	s_nop 0
	v_addc_co_u32_e32 v23, vcc, 0, v3, vcc
	global_load_dwordx2 v[22:23], v[22:23], off offset:1024
	v_add_co_u32_e32 v24, vcc, 0x3ad0a000, v2
	s_mov_b64 s[8:9], vcc
	v_add_co_u32_e32 v26, vcc, 0x3a4ea000, v2
	v_pk_fma_f32 v[40:41], v[4:5], v[10:11], v[6:7] op_sel:[0,0,1] op_sel_hi:[1,1,0] neg_lo:[0,0,1] neg_hi:[0,0,1]
	s_nop 0
	v_addc_co_u32_e32 v27, vcc, 0, v3, vcc
	global_load_dwordx2 v[26:27], v[26:27], off offset:1024
	v_add_co_u32_e32 v28, vcc, 0x3ad12000, v2
	s_mov_b64 s[10:11], vcc
	v_add_co_u32_e32 v30, vcc, 0x3a4f2000, v2
	v_pk_fma_f32 v[6:7], v[4:5], v[10:11], v[6:7] op_sel:[0,0,1] op_sel_hi:[0,1,0]
	s_nop 0
	v_addc_co_u32_e32 v31, vcc, 0, v3, vcc
	global_load_dwordx2 v[30:31], v[30:31], off offset:1024
	v_add_co_u32_e32 v32, vcc, 0x3ad1a000, v2
	s_mov_b64 s[0:1], vcc
	v_add_co_u32_e32 v34, vcc, 0x3a4fa000, v2
	v_mov_b32_e32 v41, v7
	s_nop 0
	v_addc_co_u32_e32 v35, vcc, 0, v3, vcc
	global_load_dwordx2 v[34:35], v[34:35], off offset:1024
	v_add_co_u32_e32 v36, vcc, 0x3ad22000, v2
	s_mov_b64 s[14:15], vcc
	v_add_co_u32_e32 v38, vcc, 0x3a502000, v2
	s_waitcnt vmcnt(8)
; __device__ __forceinline__ void phase_s5b_gqa(const Params& P, unsigned char* smraw, int bid, int nb) {
;     ...
;         float sr = 0.f, si = 0.f;
;         for (int c0 = 0; c0 < 260; c0 += 20) {
;             float2 e[20];
; #pragma unroll
;             for (int j = 0; j < 20; ++j) e[j] = SE[(size_t)(c0 + j) * 4096 + i];
; #pragma unroll
;             for (int j = 0; j < 20; ++j) {
;                 CIN[(size_t)(c0 + j) * 4096 + i] = make_float2(sr, si);
;                 const float nr = a.x * sr - a.y * si + e[j].x, ni = a.x * si + a.y * sr + e[j].y;
;                 sr = nr; si = ni;
;             }
	v_pk_add_f32 v[6:7], v[8:9], v[40:41]
	v_addc_co_u32_e32 v39, vcc, 0, v3, vcc
	global_load_dwordx2 v[38:39], v[38:39], off offset:1024
	v_addc_co_u32_e64 v19, vcc, 0, v3, s[6:7]
	v_pk_mul_f32 v[8:9], v[4:5], v[6:7] op_sel:[1,0]
	global_store_dwordx2 v[18:19], v[6:7], off offset:1024
	v_pk_fma_f32 v[10:11], v[4:5], v[6:7], v[8:9] op_sel:[0,0,1] op_sel_hi:[1,1,0] neg_lo:[0,0,1] neg_hi:[0,0,1]
	v_pk_fma_f32 v[6:7], v[4:5], v[6:7], v[8:9] op_sel:[0,0,1] op_sel_hi:[0,1,0]
	v_addc_co_u32_e64 v13, vcc, 0, v3, s[12:13]
	v_mov_b32_e32 v11, v7
	v_add_co_u32_e32 v8, vcc, 0x3ad2a000, v2
	s_waitcnt vmcnt(9)
	v_pk_add_f32 v[6:7], v[10:11], v[20:21]
	s_mov_b64 s[6:7], vcc
	v_add_co_u32_e32 v10, vcc, 0x3a50a000, v2
	global_store_dwordx2 v[12:13], v[6:7], off offset:1024
	s_nop 0
	v_addc_co_u32_e32 v11, vcc, 0, v3, vcc
	global_load_dwordx2 v[10:11], v[10:11], off offset:1024
	v_add_co_u32_e32 v18, vcc, 0x3ad32000, v2
	s_mov_b64 s[12:13], vcc
	v_add_co_u32_e32 v20, vcc, 0x3a512000, v2
	v_pk_mul_f32 v[12:13], v[4:5], v[6:7] op_sel:[1,1] op_sel_hi:[0,1]
	s_nop 0
	v_addc_co_u32_e32 v21, vcc, 0, v3, vcc
	global_load_dwordx2 v[20:21], v[20:21], off offset:1024
	v_pk_fma_f32 v[40:41], v[4:5], v[6:7], v[12:13] neg_lo:[0,0,1] neg_hi:[0,0,1]
	v_pk_fma_f32 v[6:7], v[4:5], v[6:7], v[12:13] op_sel_hi:[1,0,1]
	v_addc_co_u32_e64 v17, vcc, 0, v3, s[4:5]
	v_mov_b32_e32 v41, v7
	s_waitcnt vmcnt(9)
	v_pk_add_f32 v[6:7], v[14:15], v[40:41]
	global_store_dwordx2 v[16:17], v[6:7], off offset:1024
	v_pk_mul_f32 v[12:13], v[4:5], v[6:7] op_sel:[1,0]
	v_addc_co_u32_e64 v25, vcc, 0, v3, s[8:9]
	v_pk_fma_f32 v[14:15], v[4:5], v[6:7], v[12:13] op_sel:[0,0,1] op_sel_hi:[1,1,0] neg_lo:[0,0,1] neg_hi:[0,0,1]
	v_pk_fma_f32 v[6:7], v[4:5], v[6:7], v[12:13] op_sel:[0,0,1] op_sel_hi:[0,1,0]
	v_mov_b32_e32 v15, v7
	s_waitcnt vmcnt(9)
	v_pk_add_f32 v[6:7], v[22:23], v[14:15]
	global_store_dwordx2 v[24:25], v[6:7], off offset:1024
	v_pk_mul_f32 v[12:13], v[4:5], v[6:7] op_sel:[1,0]
	v_addc_co_u32_e64 v29, vcc, 0, v3, s[10:11]
	v_pk_fma_f32 v[14:15], v[4:5], v[6:7], v[12:13] op_sel:[0,0,1] op_sel_hi:[1,1,0] neg_lo:[0,0,1] neg_hi:[0,0,1]
	v_pk_fma_f32 v[6:7], v[4:5], v[6:7], v[12:13] op_sel:[0,0,1] op_sel_hi:[0,1,0]
	v_mov_b32_e32 v15, v7
	s_waitcnt vmcnt(9)
	v_pk_add_f32 v[6:7], v[26:27], v[14:15]
	global_store_dwordx2 v[28:29], v[6:7], off offset:1024
	v_pk_mul_f32 v[12:13], v[4:5], v[6:7] op_sel:[1,0]
	v_addc_co_u32_e64 v33, vcc, 0, v3, s[0:1]
	v_pk_fma_f32 v[14:15], v[4:5], v[6:7], v[12:13] op_sel:[0,0,1] op_sel_hi:[1,1,0] neg_lo:[0,0,1] neg_hi:[0,0,1]
	v_pk_fma_f32 v[6:7], v[4:5], v[6:7], v[12:13] op_sel:[0,0,1] op_sel_hi:[0,1,0]
	v_mov_b32_e32 v15, v7
	s_waitcnt vmcnt(9)
	v_pk_add_f32 v[6:7], v[30:31], v[14:15]
	global_store_dwordx2 v[32:33], v[6:7], off offset:1024
	v_pk_mul_f32 v[12:13], v[4:5], v[6:7] op_sel:[1,0]
	v_addc_co_u32_e64 v37, vcc, 0, v3, s[14:15]
	v_pk_fma_f32 v[14:15], v[4:5], v[6:7], v[12:13] op_sel:[0,0,1] op_sel_hi:[1,1,0] neg_lo:[0,0,1] neg_hi:[0,0,1]
	v_pk_fma_f32 v[6:7], v[4:5], v[6:7], v[12:13] op_sel:[0,0,1] op_sel_hi:[0,1,0]
	v_mov_b32_e32 v15, v7
	s_waitcnt vmcnt(9)
	v_pk_add_f32 v[6:7], v[34:35], v[14:15]
	global_store_dwordx2 v[36:37], v[6:7], off offset:1024
	v_pk_mul_f32 v[12:13], v[4:5], v[6:7] op_sel:[1,0]
	v_addc_co_u32_e64 v9, vcc, 0, v3, s[6:7]
	v_pk_fma_f32 v[14:15], v[4:5], v[6:7], v[12:13] op_sel:[0,0,1] op_sel_hi:[1,1,0] neg_lo:[0,0,1] neg_hi:[0,0,1]
	v_pk_fma_f32 v[6:7], v[4:5], v[6:7], v[12:13] op_sel:[0,0,1] op_sel_hi:[0,1,0]
	v_mov_b32_e32 v15, v7
	s_waitcnt vmcnt(9)
	v_pk_add_f32 v[6:7], v[38:39], v[14:15]
	global_store_dwordx2 v[8:9], v[6:7], off offset:1024
	v_pk_mul_f32 v[8:9], v[4:5], v[6:7] op_sel:[1,0]
	s_nop 0
	v_pk_fma_f32 v[12:13], v[4:5], v[6:7], v[8:9] op_sel:[0,0,1] op_sel_hi:[1,1,0] neg_lo:[0,0,1] neg_hi:[0,0,1]
	v_pk_fma_f32 v[6:7], v[4:5], v[6:7], v[8:9] op_sel:[0,0,1] op_sel_hi:[0,1,0]
	v_add_co_u32_e32 v6, vcc, 0x3ad3a000, v2
	s_mov_b64 s[0:1], vcc
	v_add_co_u32_e32 v8, vcc, 0x3a51a000, v2
	v_mov_b32_e32 v13, v7
	s_nop 0
	v_addc_co_u32_e32 v9, vcc, 0, v3, vcc
	global_load_dwordx2 v[8:9], v[8:9], off offset:1024
	v_add_co_u32_e32 v14, vcc, 0x3ad42000, v2
	s_mov_b64 s[6:7], vcc
	v_add_co_u32_e32 v16, vcc, 0x3a522000, v2
	s_waitcnt vmcnt(8)
	v_pk_add_f32 v[10:11], v[10:11], v[12:13]
	v_addc_co_u32_e32 v17, vcc, 0, v3, vcc
	global_load_dwordx2 v[16:17], v[16:17], off offset:1024
	v_addc_co_u32_e64 v19, vcc, 0, v3, s[12:13]
	v_pk_mul_f32 v[12:13], v[4:5], v[10:11] op_sel:[1,0]
	global_store_dwordx2 v[18:19], v[10:11], off offset:1024
	v_pk_fma_f32 v[18:19], v[4:5], v[10:11], v[12:13] op_sel:[0,0,1] op_sel_hi:[1,1,0] neg_lo:[0,0,1] neg_hi:[0,0,1]
	v_pk_fma_f32 v[10:11], v[4:5], v[10:11], v[12:13] op_sel:[0,0,1] op_sel_hi:[0,1,0]
	v_addc_co_u32_e64 v7, vcc, 0, v3, s[0:1]
	v_mov_b32_e32 v19, v11
	v_add_co_u32_e32 v12, vcc, 0x3ad4a000, v2
	s_waitcnt vmcnt(9)
	v_pk_add_f32 v[10:11], v[20:21], v[18:19]
	s_mov_b64 s[12:13], vcc
	v_add_co_u32_e32 v18, vcc, 0x3a52a000, v2
	global_store_dwordx2 v[6:7], v[10:11], off offset:1024
	s_nop 0
	v_addc_co_u32_e32 v19, vcc, 0, v3, vcc
	global_load_dwordx2 v[18:19], v[18:19], off offset:1024
	v_add_co_u32_e32 v20, vcc, 0x3ad52000, v2
	s_mov_b64 s[4:5], vcc
	v_add_co_u32_e32 v22, vcc, 0x3a532000, v2
	v_pk_mul_f32 v[6:7], v[4:5], v[10:11] op_sel:[1,0]
	s_nop 0
	v_addc_co_u32_e32 v23, vcc, 0, v3, vcc
	global_load_dwordx2 v[22:23], v[22:23], off offset:1024
	v_add_co_u32_e32 v24, vcc, 0x3ad5a000, v2
	s_mov_b64 s[8:9], vcc
	v_add_co_u32_e32 v26, vcc, 0x3a53a000, v2
	v_pk_fma_f32 v[40:41], v[4:5], v[10:11], v[6:7] op_sel:[0,0,1] op_sel_hi:[1,1,0] neg_lo:[0,0,1] neg_hi:[0,0,1]
	s_nop 0
	v_addc_co_u32_e32 v27, vcc, 0, v3, vcc
	global_load_dwordx2 v[26:27], v[26:27], off offset:1024
	v_add_co_u32_e32 v28, vcc, 0x3ad62000, v2
	s_mov_b64 s[10:11], vcc
	v_add_co_u32_e32 v30, vcc, 0x3a542000, v2
	v_pk_fma_f32 v[6:7], v[4:5], v[10:11], v[6:7] op_sel:[0,0,1] op_sel_hi:[0,1,0]
	s_nop 0
	v_addc_co_u32_e32 v31, vcc, 0, v3, vcc
	global_load_dwordx2 v[30:31], v[30:31], off offset:1024
	v_add_co_u32_e32 v32, vcc, 0x3ad6a000, v2
	s_mov_b64 s[0:1], vcc
	v_add_co_u32_e32 v34, vcc, 0x3a54a000, v2
	v_mov_b32_e32 v41, v7
	s_nop 0
	v_addc_co_u32_e32 v35, vcc, 0, v3, vcc
	global_load_dwordx2 v[34:35], v[34:35], off offset:1024
	v_add_co_u32_e32 v36, vcc, 0x3ad72000, v2
	s_mov_b64 s[14:15], vcc
	v_add_co_u32_e32 v38, vcc, 0x3a552000, v2
	s_waitcnt vmcnt(8)
; __device__ __forceinline__ void phase_s5b_gqa(const Params& P, unsigned char* smraw, int bid, int nb) {
;     ...
;         float sr = 0.f, si = 0.f;
;         for (int c0 = 0; c0 < 260; c0 += 20) {
;             float2 e[20];
; #pragma unroll
;             for (int j = 0; j < 20; ++j) e[j] = SE[(size_t)(c0 + j) * 4096 + i];
; #pragma unroll
;             for (int j = 0; j < 20; ++j) {
;                 CIN[(size_t)(c0 + j) * 4096 + i] = make_float2(sr, si);
;                 const float nr = a.x * sr - a.y * si + e[j].x, ni = a.x * si + a.y * sr + e[j].y;
;                 sr = nr; si = ni;
;             }
	v_pk_add_f32 v[6:7], v[8:9], v[40:41]
	v_addc_co_u32_e32 v39, vcc, 0, v3, vcc
	global_load_dwordx2 v[38:39], v[38:39], off offset:1024
	v_addc_co_u32_e64 v15, vcc, 0, v3, s[6:7]
	v_pk_mul_f32 v[8:9], v[4:5], v[6:7] op_sel:[1,0]
	global_store_dwordx2 v[14:15], v[6:7], off offset:1024
	v_pk_fma_f32 v[10:11], v[4:5], v[6:7], v[8:9] op_sel:[0,0,1] op_sel_hi:[1,1,0] neg_lo:[0,0,1] neg_hi:[0,0,1]
	v_pk_fma_f32 v[6:7], v[4:5], v[6:7], v[8:9] op_sel:[0,0,1] op_sel_hi:[0,1,0]
	v_addc_co_u32_e64 v13, vcc, 0, v3, s[12:13]
	v_mov_b32_e32 v11, v7
	v_add_co_u32_e32 v8, vcc, 0x3ad7a000, v2
	s_waitcnt vmcnt(9)
	v_pk_add_f32 v[6:7], v[16:17], v[10:11]
	s_mov_b64 s[6:7], vcc
	v_add_co_u32_e32 v10, vcc, 0x3a55a000, v2
	global_store_dwordx2 v[12:13], v[6:7], off offset:1024
	s_nop 0
	v_addc_co_u32_e32 v11, vcc, 0, v3, vcc
	global_load_dwordx2 v[10:11], v[10:11], off offset:1024
	v_add_co_u32_e32 v14, vcc, 0x3ad82000, v2
	s_mov_b64 s[12:13], vcc
	v_add_co_u32_e32 v16, vcc, 0x3a562000, v2
	v_pk_mul_f32 v[12:13], v[4:5], v[6:7] op_sel:[1,0]
	s_nop 0
	v_addc_co_u32_e32 v17, vcc, 0, v3, vcc
	global_load_dwordx2 v[16:17], v[16:17], off offset:1024
	v_pk_fma_f32 v[40:41], v[4:5], v[6:7], v[12:13] op_sel:[0,0,1] op_sel_hi:[1,1,0] neg_lo:[0,0,1] neg_hi:[0,0,1]
	v_pk_fma_f32 v[6:7], v[4:5], v[6:7], v[12:13] op_sel:[0,0,1] op_sel_hi:[0,1,0]
	v_mov_b32_e32 v41, v7
	s_waitcnt vmcnt(9)
	v_pk_add_f32 v[6:7], v[18:19], v[40:41]
	v_addc_co_u32_e64 v21, vcc, 0, v3, s[4:5]
	v_pk_mul_f32 v[12:13], v[4:5], v[6:7] op_sel:[1,0]
	global_store_dwordx2 v[20:21], v[6:7], off offset:1024
	v_pk_fma_f32 v[18:19], v[4:5], v[6:7], v[12:13] op_sel:[0,0,1] op_sel_hi:[1,1,0] neg_lo:[0,0,1] neg_hi:[0,0,1]
	v_pk_fma_f32 v[6:7], v[4:5], v[6:7], v[12:13] op_sel:[0,0,1] op_sel_hi:[0,1,0]
	v_mov_b32_e32 v19, v7
	s_waitcnt vmcnt(9)
	v_pk_add_f32 v[6:7], v[22:23], v[18:19]
	v_addc_co_u32_e64 v25, vcc, 0, v3, s[8:9]
	v_pk_mul_f32 v[12:13], v[4:5], v[6:7] op_sel:[1,0]
	global_store_dwordx2 v[24:25], v[6:7], off offset:1024
	v_pk_fma_f32 v[18:19], v[4:5], v[6:7], v[12:13] op_sel:[0,0,1] op_sel_hi:[1,1,0] neg_lo:[0,0,1] neg_hi:[0,0,1]
	v_pk_fma_f32 v[6:7], v[4:5], v[6:7], v[12:13] op_sel:[0,0,1] op_sel_hi:[0,1,0]
	v_mov_b32_e32 v19, v7
	s_waitcnt vmcnt(9)
	v_pk_add_f32 v[6:7], v[26:27], v[18:19]
	v_addc_co_u32_e64 v29, vcc, 0, v3, s[10:11]
	v_pk_mul_f32 v[12:13], v[4:5], v[6:7] op_sel:[1,0]
	global_store_dwordx2 v[28:29], v[6:7], off offset:1024
	v_pk_fma_f32 v[18:19], v[4:5], v[6:7], v[12:13] op_sel:[0,0,1] op_sel_hi:[1,1,0] neg_lo:[0,0,1] neg_hi:[0,0,1]
	v_pk_fma_f32 v[6:7], v[4:5], v[6:7], v[12:13] op_sel:[0,0,1] op_sel_hi:[0,1,0]
	v_mov_b32_e32 v19, v7
	s_waitcnt vmcnt(9)
	v_pk_add_f32 v[6:7], v[30:31], v[18:19]
	v_addc_co_u32_e64 v33, vcc, 0, v3, s[0:1]
	v_pk_mul_f32 v[12:13], v[4:5], v[6:7] op_sel:[1,0]
	global_store_dwordx2 v[32:33], v[6:7], off offset:1024
	v_pk_fma_f32 v[18:19], v[4:5], v[6:7], v[12:13] op_sel:[0,0,1] op_sel_hi:[1,1,0] neg_lo:[0,0,1] neg_hi:[0,0,1]
	v_pk_fma_f32 v[6:7], v[4:5], v[6:7], v[12:13] op_sel:[0,0,1] op_sel_hi:[0,1,0]
	v_mov_b32_e32 v19, v7
	s_waitcnt vmcnt(9)
	v_pk_add_f32 v[6:7], v[34:35], v[18:19]
	v_addc_co_u32_e64 v37, vcc, 0, v3, s[14:15]
	v_pk_mul_f32 v[12:13], v[4:5], v[6:7] op_sel:[1,0]
	global_store_dwordx2 v[36:37], v[6:7], off offset:1024
	v_pk_fma_f32 v[18:19], v[4:5], v[6:7], v[12:13] op_sel:[0,0,1] op_sel_hi:[1,1,0] neg_lo:[0,0,1] neg_hi:[0,0,1]
	v_pk_fma_f32 v[6:7], v[4:5], v[6:7], v[12:13] op_sel:[0,0,1] op_sel_hi:[0,1,0]
	v_mov_b32_e32 v19, v7
	v_addc_co_u32_e64 v9, vcc, 0, v3, s[6:7]
	s_waitcnt vmcnt(9)
	v_pk_add_f32 v[6:7], v[38:39], v[18:19]
	global_store_dwordx2 v[8:9], v[6:7], off offset:1024
	v_pk_mul_f32 v[8:9], v[4:5], v[6:7] op_sel:[1,0]
	s_nop 0
	v_pk_fma_f32 v[12:13], v[4:5], v[6:7], v[8:9] op_sel:[0,0,1] op_sel_hi:[1,1,0] neg_lo:[0,0,1] neg_hi:[0,0,1]
	v_pk_fma_f32 v[6:7], v[4:5], v[6:7], v[8:9] op_sel:[0,0,1] op_sel_hi:[0,1,0]
	v_add_co_u32_e32 v6, vcc, 0x3ad8a000, v2
	s_mov_b64 s[0:1], vcc
	v_add_co_u32_e32 v8, vcc, 0x3a56a000, v2
	v_mov_b32_e32 v13, v7
	s_nop 0
	v_addc_co_u32_e32 v9, vcc, 0, v3, vcc
	global_load_dwordx2 v[8:9], v[8:9], off offset:1024
	v_add_co_u32_e32 v18, vcc, 0x3ad92000, v2
	s_mov_b64 s[6:7], vcc
	v_add_co_u32_e32 v20, vcc, 0x3a572000, v2
	s_waitcnt vmcnt(8)
	v_pk_add_f32 v[10:11], v[10:11], v[12:13]
	v_addc_co_u32_e32 v21, vcc, 0, v3, vcc
	global_load_dwordx2 v[20:21], v[20:21], off offset:1024
	v_addc_co_u32_e64 v15, vcc, 0, v3, s[12:13]
	v_pk_mul_f32 v[12:13], v[4:5], v[10:11] op_sel:[1,0]
	global_store_dwordx2 v[14:15], v[10:11], off offset:1024
	v_pk_fma_f32 v[14:15], v[4:5], v[10:11], v[12:13] op_sel:[0,0,1] op_sel_hi:[1,1,0] neg_lo:[0,0,1] neg_hi:[0,0,1]
	v_pk_fma_f32 v[10:11], v[4:5], v[10:11], v[12:13] op_sel:[0,0,1] op_sel_hi:[0,1,0]
	v_addc_co_u32_e64 v7, vcc, 0, v3, s[0:1]
	v_mov_b32_e32 v15, v11
	v_add_co_u32_e32 v12, vcc, 0x3ad9a000, v2
	s_waitcnt vmcnt(9)
; __device__ __forceinline__ void phase_s5b_gqa(const Params& P, unsigned char* smraw, int bid, int nb) {
;     ...
;         float sr = 0.f, si = 0.f;
;         for (int c0 = 0; c0 < 260; c0 += 20) {
;             float2 e[20];
; #pragma unroll
;             for (int j = 0; j < 20; ++j) e[j] = SE[(size_t)(c0 + j) * 4096 + i];
; #pragma unroll
;             for (int j = 0; j < 20; ++j) {
;                 CIN[(size_t)(c0 + j) * 4096 + i] = make_float2(sr, si);
;                 const float nr = a.x * sr - a.y * si + e[j].x, ni = a.x * si + a.y * sr + e[j].y;
;                 sr = nr; si = ni;
;             }
	v_pk_add_f32 v[10:11], v[16:17], v[14:15]
	s_mov_b64 s[12:13], vcc
	v_add_co_u32_e32 v14, vcc, 0x3a57a000, v2
	global_store_dwordx2 v[6:7], v[10:11], off offset:1024
	s_nop 0
	v_addc_co_u32_e32 v15, vcc, 0, v3, vcc
	global_load_dwordx2 v[14:15], v[14:15], off offset:1024
	v_add_co_u32_e32 v16, vcc, 0x3ada2000, v2
	s_mov_b64 s[4:5], vcc
	v_add_co_u32_e32 v22, vcc, 0x3a582000, v2
	v_pk_mul_f32 v[6:7], v[4:5], v[10:11] op_sel:[1,0]
	s_nop 0
	v_addc_co_u32_e32 v23, vcc, 0, v3, vcc
	global_load_dwordx2 v[22:23], v[22:23], off offset:1024
	v_add_co_u32_e32 v24, vcc, 0x3adaa000, v2
	s_mov_b64 s[8:9], vcc
	v_add_co_u32_e32 v26, vcc, 0x3a58a000, v2
	v_pk_fma_f32 v[40:41], v[4:5], v[10:11], v[6:7] op_sel:[0,0,1] op_sel_hi:[1,1,0] neg_lo:[0,0,1] neg_hi:[0,0,1]
	s_nop 0
	v_addc_co_u32_e32 v27, vcc, 0, v3, vcc
	global_load_dwordx2 v[26:27], v[26:27], off offset:1024
	v_add_co_u32_e32 v28, vcc, 0x3adb2000, v2
	s_mov_b64 s[10:11], vcc
	v_add_co_u32_e32 v30, vcc, 0x3a592000, v2
	v_pk_fma_f32 v[6:7], v[4:5], v[10:11], v[6:7] op_sel:[0,0,1] op_sel_hi:[0,1,0]
	s_nop 0
	v_addc_co_u32_e32 v31, vcc, 0, v3, vcc
	global_load_dwordx2 v[30:31], v[30:31], off offset:1024
	v_add_co_u32_e32 v32, vcc, 0x3adba000, v2
	s_mov_b64 s[0:1], vcc
	v_add_co_u32_e32 v34, vcc, 0x3a59a000, v2
	v_mov_b32_e32 v41, v7
	s_nop 0
	v_addc_co_u32_e32 v35, vcc, 0, v3, vcc
	global_load_dwordx2 v[34:35], v[34:35], off offset:1024
	v_add_co_u32_e32 v36, vcc, 0x3adc2000, v2
	s_mov_b64 s[14:15], vcc
	v_add_co_u32_e32 v38, vcc, 0x3a5a2000, v2
	s_waitcnt vmcnt(8)
	v_pk_add_f32 v[6:7], v[8:9], v[40:41]
	v_addc_co_u32_e32 v39, vcc, 0, v3, vcc
	global_load_dwordx2 v[38:39], v[38:39], off offset:1024
	v_addc_co_u32_e64 v19, vcc, 0, v3, s[6:7]
	v_pk_mul_f32 v[8:9], v[4:5], v[6:7] op_sel:[1,0]
	global_store_dwordx2 v[18:19], v[6:7], off offset:1024
	v_pk_fma_f32 v[10:11], v[4:5], v[6:7], v[8:9] op_sel:[0,0,1] op_sel_hi:[1,1,0] neg_lo:[0,0,1] neg_hi:[0,0,1]
	v_pk_fma_f32 v[6:7], v[4:5], v[6:7], v[8:9] op_sel:[0,0,1] op_sel_hi:[0,1,0]
	v_addc_co_u32_e64 v13, vcc, 0, v3, s[12:13]
	v_mov_b32_e32 v11, v7
	v_add_co_u32_e32 v8, vcc, 0x3adca000, v2
	s_waitcnt vmcnt(9)
	v_pk_add_f32 v[6:7], v[10:11], v[20:21]
	s_mov_b64 s[6:7], vcc
	v_add_co_u32_e32 v10, vcc, 0x3a5aa000, v2
	global_store_dwordx2 v[12:13], v[6:7], off offset:1024
	s_nop 0
	v_addc_co_u32_e32 v11, vcc, 0, v3, vcc
	global_load_dwordx2 v[10:11], v[10:11], off offset:1024
	v_add_co_u32_e32 v18, vcc, 0x3add2000, v2
	s_mov_b64 s[12:13], vcc
	v_add_co_u32_e32 v20, vcc, 0x3a5b2000, v2
	v_pk_mul_f32 v[12:13], v[4:5], v[6:7] op_sel:[1,1] op_sel_hi:[0,1]
	s_nop 0
	v_addc_co_u32_e32 v21, vcc, 0, v3, vcc
	global_load_dwordx2 v[20:21], v[20:21], off offset:1024
	v_pk_fma_f32 v[40:41], v[4:5], v[6:7], v[12:13] neg_lo:[0,0,1] neg_hi:[0,0,1]
	v_pk_fma_f32 v[6:7], v[4:5], v[6:7], v[12:13] op_sel_hi:[1,0,1]
	v_addc_co_u32_e64 v17, vcc, 0, v3, s[4:5]
	v_mov_b32_e32 v41, v7
	s_waitcnt vmcnt(9)
	v_pk_add_f32 v[6:7], v[14:15], v[40:41]
	global_store_dwordx2 v[16:17], v[6:7], off offset:1024
	v_pk_mul_f32 v[12:13], v[4:5], v[6:7] op_sel:[1,0]
	v_addc_co_u32_e64 v25, vcc, 0, v3, s[8:9]
	v_pk_fma_f32 v[14:15], v[4:5], v[6:7], v[12:13] op_sel:[0,0,1] op_sel_hi:[1,1,0] neg_lo:[0,0,1] neg_hi:[0,0,1]
	v_pk_fma_f32 v[6:7], v[4:5], v[6:7], v[12:13] op_sel:[0,0,1] op_sel_hi:[0,1,0]
	v_mov_b32_e32 v15, v7
	s_waitcnt vmcnt(9)
	v_pk_add_f32 v[6:7], v[22:23], v[14:15]
	global_store_dwordx2 v[24:25], v[6:7], off offset:1024
	v_pk_mul_f32 v[12:13], v[4:5], v[6:7] op_sel:[1,0]
	v_addc_co_u32_e64 v29, vcc, 0, v3, s[10:11]
	v_pk_fma_f32 v[14:15], v[4:5], v[6:7], v[12:13] op_sel:[0,0,1] op_sel_hi:[1,1,0] neg_lo:[0,0,1] neg_hi:[0,0,1]
	v_pk_fma_f32 v[6:7], v[4:5], v[6:7], v[12:13] op_sel:[0,0,1] op_sel_hi:[0,1,0]
	v_mov_b32_e32 v15, v7
	s_waitcnt vmcnt(9)
	v_pk_add_f32 v[6:7], v[26:27], v[14:15]
	global_store_dwordx2 v[28:29], v[6:7], off offset:1024
	v_pk_mul_f32 v[12:13], v[4:5], v[6:7] op_sel:[1,0]
	v_addc_co_u32_e64 v33, vcc, 0, v3, s[0:1]
	v_pk_fma_f32 v[14:15], v[4:5], v[6:7], v[12:13] op_sel:[0,0,1] op_sel_hi:[1,1,0] neg_lo:[0,0,1] neg_hi:[0,0,1]
	v_pk_fma_f32 v[6:7], v[4:5], v[6:7], v[12:13] op_sel:[0,0,1] op_sel_hi:[0,1,0]
	v_mov_b32_e32 v15, v7
	s_waitcnt vmcnt(9)
	v_pk_add_f32 v[6:7], v[30:31], v[14:15]
	global_store_dwordx2 v[32:33], v[6:7], off offset:1024
	v_pk_mul_f32 v[12:13], v[4:5], v[6:7] op_sel:[1,0]
	v_addc_co_u32_e64 v37, vcc, 0, v3, s[14:15]
	v_pk_fma_f32 v[14:15], v[4:5], v[6:7], v[12:13] op_sel:[0,0,1] op_sel_hi:[1,1,0] neg_lo:[0,0,1] neg_hi:[0,0,1]
	v_pk_fma_f32 v[6:7], v[4:5], v[6:7], v[12:13] op_sel:[0,0,1] op_sel_hi:[0,1,0]
	v_mov_b32_e32 v15, v7
	s_waitcnt vmcnt(9)
	v_pk_add_f32 v[6:7], v[34:35], v[14:15]
	global_store_dwordx2 v[36:37], v[6:7], off offset:1024
	v_pk_mul_f32 v[12:13], v[4:5], v[6:7] op_sel:[1,0]
	v_addc_co_u32_e64 v9, vcc, 0, v3, s[6:7]
	v_pk_fma_f32 v[14:15], v[4:5], v[6:7], v[12:13] op_sel:[0,0,1] op_sel_hi:[1,1,0] neg_lo:[0,0,1] neg_hi:[0,0,1]
	v_pk_fma_f32 v[6:7], v[4:5], v[6:7], v[12:13] op_sel:[0,0,1] op_sel_hi:[0,1,0]
	v_mov_b32_e32 v15, v7
	s_waitcnt vmcnt(9)
	v_pk_add_f32 v[6:7], v[38:39], v[14:15]
	global_store_dwordx2 v[8:9], v[6:7], off offset:1024
	v_pk_mul_f32 v[8:9], v[4:5], v[6:7] op_sel:[1,0]
	s_nop 0
	v_pk_fma_f32 v[12:13], v[4:5], v[6:7], v[8:9] op_sel:[0,0,1] op_sel_hi:[1,1,0] neg_lo:[0,0,1] neg_hi:[0,0,1]
	v_pk_fma_f32 v[6:7], v[4:5], v[6:7], v[8:9] op_sel:[0,0,1] op_sel_hi:[0,1,0]
	v_add_co_u32_e32 v6, vcc, 0x3adda000, v2
	s_mov_b64 s[0:1], vcc
	v_add_co_u32_e32 v8, vcc, 0x3a5ba000, v2
	v_mov_b32_e32 v13, v7
	s_nop 0
	v_addc_co_u32_e32 v9, vcc, 0, v3, vcc
	global_load_dwordx2 v[8:9], v[8:9], off offset:1024
	v_add_co_u32_e32 v14, vcc, 0x3ade2000, v2
	s_mov_b64 s[6:7], vcc
	v_add_co_u32_e32 v16, vcc, 0x3a5c2000, v2
	s_waitcnt vmcnt(8)
; __device__ __forceinline__ void phase_s5b_gqa(const Params& P, unsigned char* smraw, int bid, int nb) {
;     ...
;         float sr = 0.f, si = 0.f;
;         for (int c0 = 0; c0 < 260; c0 += 20) {
;             float2 e[20];
; #pragma unroll
;             for (int j = 0; j < 20; ++j) e[j] = SE[(size_t)(c0 + j) * 4096 + i];
; #pragma unroll
;             for (int j = 0; j < 20; ++j) {
;                 CIN[(size_t)(c0 + j) * 4096 + i] = make_float2(sr, si);
;                 const float nr = a.x * sr - a.y * si + e[j].x, ni = a.x * si + a.y * sr + e[j].y;
;                 sr = nr; si = ni;
;             }
	v_pk_add_f32 v[10:11], v[10:11], v[12:13]
	v_addc_co_u32_e32 v17, vcc, 0, v3, vcc
	global_load_dwordx2 v[16:17], v[16:17], off offset:1024
	v_addc_co_u32_e64 v19, vcc, 0, v3, s[12:13]
	v_pk_mul_f32 v[12:13], v[4:5], v[10:11] op_sel:[1,0]
	global_store_dwordx2 v[18:19], v[10:11], off offset:1024
	v_pk_fma_f32 v[18:19], v[4:5], v[10:11], v[12:13] op_sel:[0,0,1] op_sel_hi:[1,1,0] neg_lo:[0,0,1] neg_hi:[0,0,1]
	v_pk_fma_f32 v[10:11], v[4:5], v[10:11], v[12:13] op_sel:[0,0,1] op_sel_hi:[0,1,0]
	v_addc_co_u32_e64 v7, vcc, 0, v3, s[0:1]
	v_mov_b32_e32 v19, v11
	v_add_co_u32_e32 v12, vcc, 0x3adea000, v2
	s_waitcnt vmcnt(9)
	v_pk_add_f32 v[10:11], v[20:21], v[18:19]
	s_mov_b64 s[12:13], vcc
	v_add_co_u32_e32 v18, vcc, 0x3a5ca000, v2
	global_store_dwordx2 v[6:7], v[10:11], off offset:1024
	s_nop 0
	v_addc_co_u32_e32 v19, vcc, 0, v3, vcc
	global_load_dwordx2 v[18:19], v[18:19], off offset:1024
	v_add_co_u32_e32 v20, vcc, 0x3adf2000, v2
	s_mov_b64 s[4:5], vcc
	v_add_co_u32_e32 v22, vcc, 0x3a5d2000, v2
	v_pk_mul_f32 v[6:7], v[4:5], v[10:11] op_sel:[1,0]
	s_nop 0
	v_addc_co_u32_e32 v23, vcc, 0, v3, vcc
	global_load_dwordx2 v[22:23], v[22:23], off offset:1024
	v_add_co_u32_e32 v24, vcc, 0x3adfa000, v2
	s_mov_b64 s[8:9], vcc
	v_add_co_u32_e32 v26, vcc, 0x3a5da000, v2
	v_pk_fma_f32 v[40:41], v[4:5], v[10:11], v[6:7] op_sel:[0,0,1] op_sel_hi:[1,1,0] neg_lo:[0,0,1] neg_hi:[0,0,1]
	s_nop 0
	v_addc_co_u32_e32 v27, vcc, 0, v3, vcc
	global_load_dwordx2 v[26:27], v[26:27], off offset:1024
	v_add_co_u32_e32 v28, vcc, 0x3ae02000, v2
	s_mov_b64 s[10:11], vcc
	v_add_co_u32_e32 v30, vcc, 0x3a5e2000, v2
	v_pk_fma_f32 v[6:7], v[4:5], v[10:11], v[6:7] op_sel:[0,0,1] op_sel_hi:[0,1,0]
	s_nop 0
	v_addc_co_u32_e32 v31, vcc, 0, v3, vcc
	global_load_dwordx2 v[30:31], v[30:31], off offset:1024
	v_add_co_u32_e32 v32, vcc, 0x3ae0a000, v2
	s_mov_b64 s[0:1], vcc
	v_add_co_u32_e32 v34, vcc, 0x3a5ea000, v2
	v_mov_b32_e32 v41, v7
	s_nop 0
	v_addc_co_u32_e32 v35, vcc, 0, v3, vcc
	global_load_dwordx2 v[34:35], v[34:35], off offset:1024
	v_add_co_u32_e32 v36, vcc, 0x3ae12000, v2
	s_mov_b64 s[14:15], vcc
	v_add_co_u32_e32 v38, vcc, 0x3a5f2000, v2
	s_waitcnt vmcnt(8)
	v_pk_add_f32 v[6:7], v[8:9], v[40:41]
	v_addc_co_u32_e32 v39, vcc, 0, v3, vcc
	global_load_dwordx2 v[38:39], v[38:39], off offset:1024
	v_addc_co_u32_e64 v15, vcc, 0, v3, s[6:7]
	v_pk_mul_f32 v[8:9], v[4:5], v[6:7] op_sel:[1,0]
	global_store_dwordx2 v[14:15], v[6:7], off offset:1024
	v_pk_fma_f32 v[10:11], v[4:5], v[6:7], v[8:9] op_sel:[0,0,1] op_sel_hi:[1,1,0] neg_lo:[0,0,1] neg_hi:[0,0,1]
	v_pk_fma_f32 v[6:7], v[4:5], v[6:7], v[8:9] op_sel:[0,0,1] op_sel_hi:[0,1,0]
	v_addc_co_u32_e64 v13, vcc, 0, v3, s[12:13]
	v_mov_b32_e32 v11, v7
	v_add_co_u32_e32 v8, vcc, 0x3ae1a000, v2
	s_waitcnt vmcnt(9)
	v_pk_add_f32 v[6:7], v[16:17], v[10:11]
	s_mov_b64 s[6:7], vcc
	v_add_co_u32_e32 v10, vcc, 0x3a5fa000, v2
	global_store_dwordx2 v[12:13], v[6:7], off offset:1024
	s_nop 0
	v_addc_co_u32_e32 v11, vcc, 0, v3, vcc
	global_load_dwordx2 v[10:11], v[10:11], off offset:1024
	v_add_co_u32_e32 v14, vcc, 0x3ae22000, v2
	s_mov_b64 s[12:13], vcc
	v_add_co_u32_e32 v16, vcc, 0x3a602000, v2
	v_pk_mul_f32 v[12:13], v[4:5], v[6:7] op_sel:[1,0]
	s_nop 0
	v_addc_co_u32_e32 v17, vcc, 0, v3, vcc
	global_load_dwordx2 v[16:17], v[16:17], off offset:1024
	v_pk_fma_f32 v[40:41], v[4:5], v[6:7], v[12:13] op_sel:[0,0,1] op_sel_hi:[1,1,0] neg_lo:[0,0,1] neg_hi:[0,0,1]
	v_pk_fma_f32 v[6:7], v[4:5], v[6:7], v[12:13] op_sel:[0,0,1] op_sel_hi:[0,1,0]
	v_mov_b32_e32 v41, v7
	s_waitcnt vmcnt(9)
	v_pk_add_f32 v[6:7], v[18:19], v[40:41]
	v_addc_co_u32_e64 v21, vcc, 0, v3, s[4:5]
	v_pk_mul_f32 v[12:13], v[4:5], v[6:7] op_sel:[1,0]
	global_store_dwordx2 v[20:21], v[6:7], off offset:1024
	v_pk_fma_f32 v[18:19], v[4:5], v[6:7], v[12:13] op_sel:[0,0,1] op_sel_hi:[1,1,0] neg_lo:[0,0,1] neg_hi:[0,0,1]
	v_pk_fma_f32 v[6:7], v[4:5], v[6:7], v[12:13] op_sel:[0,0,1] op_sel_hi:[0,1,0]
	v_mov_b32_e32 v19, v7
	s_waitcnt vmcnt(9)
	v_pk_add_f32 v[6:7], v[22:23], v[18:19]
	v_addc_co_u32_e64 v25, vcc, 0, v3, s[8:9]
	v_pk_mul_f32 v[12:13], v[4:5], v[6:7] op_sel:[1,0]
	global_store_dwordx2 v[24:25], v[6:7], off offset:1024
	v_pk_fma_f32 v[18:19], v[4:5], v[6:7], v[12:13] op_sel:[0,0,1] op_sel_hi:[1,1,0] neg_lo:[0,0,1] neg_hi:[0,0,1]
	v_pk_fma_f32 v[6:7], v[4:5], v[6:7], v[12:13] op_sel:[0,0,1] op_sel_hi:[0,1,0]
	v_mov_b32_e32 v19, v7
	s_waitcnt vmcnt(9)
	v_pk_add_f32 v[6:7], v[26:27], v[18:19]
	v_addc_co_u32_e64 v29, vcc, 0, v3, s[10:11]
	v_pk_mul_f32 v[12:13], v[4:5], v[6:7] op_sel:[1,0]
	global_store_dwordx2 v[28:29], v[6:7], off offset:1024
	v_pk_fma_f32 v[18:19], v[4:5], v[6:7], v[12:13] op_sel:[0,0,1] op_sel_hi:[1,1,0] neg_lo:[0,0,1] neg_hi:[0,0,1]
	v_pk_fma_f32 v[6:7], v[4:5], v[6:7], v[12:13] op_sel:[0,0,1] op_sel_hi:[0,1,0]
	v_mov_b32_e32 v19, v7
	s_waitcnt vmcnt(9)
	v_pk_add_f32 v[6:7], v[30:31], v[18:19]
	v_addc_co_u32_e64 v33, vcc, 0, v3, s[0:1]
	v_pk_mul_f32 v[12:13], v[4:5], v[6:7] op_sel:[1,0]
	global_store_dwordx2 v[32:33], v[6:7], off offset:1024
	v_pk_fma_f32 v[18:19], v[4:5], v[6:7], v[12:13] op_sel:[0,0,1] op_sel_hi:[1,1,0] neg_lo:[0,0,1] neg_hi:[0,0,1]
	v_pk_fma_f32 v[6:7], v[4:5], v[6:7], v[12:13] op_sel:[0,0,1] op_sel_hi:[0,1,0]
	v_mov_b32_e32 v19, v7
	s_waitcnt vmcnt(9)
	v_pk_add_f32 v[6:7], v[34:35], v[18:19]
	v_addc_co_u32_e64 v37, vcc, 0, v3, s[14:15]
	v_pk_mul_f32 v[12:13], v[4:5], v[6:7] op_sel:[1,0]
	global_store_dwordx2 v[36:37], v[6:7], off offset:1024
	v_pk_fma_f32 v[18:19], v[4:5], v[6:7], v[12:13] op_sel:[0,0,1] op_sel_hi:[1,1,0] neg_lo:[0,0,1] neg_hi:[0,0,1]
	v_pk_fma_f32 v[6:7], v[4:5], v[6:7], v[12:13] op_sel:[0,0,1] op_sel_hi:[0,1,0]
	v_mov_b32_e32 v19, v7
	v_addc_co_u32_e64 v9, vcc, 0, v3, s[6:7]
	s_waitcnt vmcnt(9)
; __device__ __forceinline__ void phase_s5b_gqa(const Params& P, unsigned char* smraw, int bid, int nb) {
;     ...
;         float sr = 0.f, si = 0.f;
;         for (int c0 = 0; c0 < 260; c0 += 20) {
;             float2 e[20];
; #pragma unroll
;             for (int j = 0; j < 20; ++j) e[j] = SE[(size_t)(c0 + j) * 4096 + i];
; #pragma unroll
;             for (int j = 0; j < 20; ++j) {
;                 CIN[(size_t)(c0 + j) * 4096 + i] = make_float2(sr, si);
;                 const float nr = a.x * sr - a.y * si + e[j].x, ni = a.x * si + a.y * sr + e[j].y;
;                 sr = nr; si = ni;
;             }
	v_pk_add_f32 v[6:7], v[38:39], v[18:19]
	global_store_dwordx2 v[8:9], v[6:7], off offset:1024
	v_pk_mul_f32 v[8:9], v[4:5], v[6:7] op_sel:[1,0]
	s_nop 0
	v_pk_fma_f32 v[12:13], v[4:5], v[6:7], v[8:9] op_sel:[0,0,1] op_sel_hi:[1,1,0] neg_lo:[0,0,1] neg_hi:[0,0,1]
	v_pk_fma_f32 v[6:7], v[4:5], v[6:7], v[8:9] op_sel:[0,0,1] op_sel_hi:[0,1,0]
	v_add_co_u32_e32 v6, vcc, 0x3ae2a000, v2
	s_mov_b64 s[0:1], vcc
	v_add_co_u32_e32 v8, vcc, 0x3a60a000, v2
	v_mov_b32_e32 v13, v7
	s_nop 0
	v_addc_co_u32_e32 v9, vcc, 0, v3, vcc
	global_load_dwordx2 v[8:9], v[8:9], off offset:1024
	v_add_co_u32_e32 v18, vcc, 0x3ae32000, v2
	s_mov_b64 s[6:7], vcc
	v_add_co_u32_e32 v20, vcc, 0x3a612000, v2
	s_waitcnt vmcnt(8)
	v_pk_add_f32 v[10:11], v[10:11], v[12:13]
	v_addc_co_u32_e32 v21, vcc, 0, v3, vcc
	global_load_dwordx2 v[20:21], v[20:21], off offset:1024
	v_addc_co_u32_e64 v15, vcc, 0, v3, s[12:13]
	v_pk_mul_f32 v[12:13], v[4:5], v[10:11] op_sel:[1,0]
	global_store_dwordx2 v[14:15], v[10:11], off offset:1024
	v_pk_fma_f32 v[14:15], v[4:5], v[10:11], v[12:13] op_sel:[0,0,1] op_sel_hi:[1,1,0] neg_lo:[0,0,1] neg_hi:[0,0,1]
	v_pk_fma_f32 v[10:11], v[4:5], v[10:11], v[12:13] op_sel:[0,0,1] op_sel_hi:[0,1,0]
	v_addc_co_u32_e64 v7, vcc, 0, v3, s[0:1]
	v_mov_b32_e32 v15, v11
	v_add_co_u32_e32 v12, vcc, 0x3ae3a000, v2
	s_waitcnt vmcnt(9)
	v_pk_add_f32 v[10:11], v[16:17], v[14:15]
	s_mov_b64 s[12:13], vcc
	v_add_co_u32_e32 v14, vcc, 0x3a61a000, v2
	global_store_dwordx2 v[6:7], v[10:11], off offset:1024
	s_nop 0
	v_addc_co_u32_e32 v15, vcc, 0, v3, vcc
	global_load_dwordx2 v[14:15], v[14:15], off offset:1024
	v_add_co_u32_e32 v16, vcc, 0x3ae42000, v2
	s_mov_b64 s[4:5], vcc
	v_add_co_u32_e32 v22, vcc, 0x3a622000, v2
	v_pk_mul_f32 v[6:7], v[4:5], v[10:11] op_sel:[1,0]
	s_nop 0
	v_addc_co_u32_e32 v23, vcc, 0, v3, vcc
	global_load_dwordx2 v[22:23], v[22:23], off offset:1024
	v_add_co_u32_e32 v24, vcc, 0x3ae4a000, v2
	s_mov_b64 s[8:9], vcc
	v_add_co_u32_e32 v26, vcc, 0x3a62a000, v2
	v_pk_fma_f32 v[40:41], v[4:5], v[10:11], v[6:7] op_sel:[0,0,1] op_sel_hi:[1,1,0] neg_lo:[0,0,1] neg_hi:[0,0,1]
	s_nop 0
	v_addc_co_u32_e32 v27, vcc, 0, v3, vcc
	global_load_dwordx2 v[26:27], v[26:27], off offset:1024
	v_add_co_u32_e32 v28, vcc, 0x3ae52000, v2
	s_mov_b64 s[10:11], vcc
	v_add_co_u32_e32 v30, vcc, 0x3a632000, v2
	v_pk_fma_f32 v[6:7], v[4:5], v[10:11], v[6:7] op_sel:[0,0,1] op_sel_hi:[0,1,0]
	s_nop 0
	v_addc_co_u32_e32 v31, vcc, 0, v3, vcc
	global_load_dwordx2 v[30:31], v[30:31], off offset:1024
	v_add_co_u32_e32 v32, vcc, 0x3ae5a000, v2
	s_mov_b64 s[0:1], vcc
	v_add_co_u32_e32 v34, vcc, 0x3a63a000, v2
	v_mov_b32_e32 v41, v7
	s_nop 0
	v_addc_co_u32_e32 v35, vcc, 0, v3, vcc
	global_load_dwordx2 v[34:35], v[34:35], off offset:1024
	v_add_co_u32_e32 v36, vcc, 0x3ae62000, v2
	s_mov_b64 s[14:15], vcc
	v_add_co_u32_e32 v38, vcc, 0x3a642000, v2
	s_waitcnt vmcnt(8)
	v_pk_add_f32 v[6:7], v[8:9], v[40:41]
	v_addc_co_u32_e32 v39, vcc, 0, v3, vcc
	global_load_dwordx2 v[38:39], v[38:39], off offset:1024
	v_addc_co_u32_e64 v19, vcc, 0, v3, s[6:7]
	v_pk_mul_f32 v[8:9], v[4:5], v[6:7] op_sel:[1,0]
	global_store_dwordx2 v[18:19], v[6:7], off offset:1024
	v_pk_fma_f32 v[10:11], v[4:5], v[6:7], v[8:9] op_sel:[0,0,1] op_sel_hi:[1,1,0] neg_lo:[0,0,1] neg_hi:[0,0,1]
	v_pk_fma_f32 v[6:7], v[4:5], v[6:7], v[8:9] op_sel:[0,0,1] op_sel_hi:[0,1,0]
	v_addc_co_u32_e64 v13, vcc, 0, v3, s[12:13]
	v_mov_b32_e32 v11, v7
	v_add_co_u32_e32 v8, vcc, 0x3ae6a000, v2
	s_waitcnt vmcnt(9)
	v_pk_add_f32 v[6:7], v[10:11], v[20:21]
	s_mov_b64 s[6:7], vcc
	v_add_co_u32_e32 v10, vcc, 0x3a64a000, v2
	global_store_dwordx2 v[12:13], v[6:7], off offset:1024
	s_nop 0
	v_addc_co_u32_e32 v11, vcc, 0, v3, vcc
	global_load_dwordx2 v[10:11], v[10:11], off offset:1024
	v_add_co_u32_e32 v18, vcc, 0x3ae72000, v2
	s_mov_b64 s[12:13], vcc
	v_add_co_u32_e32 v20, vcc, 0x3a652000, v2
	v_pk_mul_f32 v[12:13], v[4:5], v[6:7] op_sel:[1,1] op_sel_hi:[0,1]
	s_nop 0
	v_addc_co_u32_e32 v21, vcc, 0, v3, vcc
	global_load_dwordx2 v[20:21], v[20:21], off offset:1024
	v_pk_fma_f32 v[40:41], v[4:5], v[6:7], v[12:13] neg_lo:[0,0,1] neg_hi:[0,0,1]
	v_pk_fma_f32 v[6:7], v[4:5], v[6:7], v[12:13] op_sel_hi:[1,0,1]
	v_addc_co_u32_e64 v17, vcc, 0, v3, s[4:5]
	v_mov_b32_e32 v41, v7
	s_waitcnt vmcnt(9)
	v_pk_add_f32 v[6:7], v[14:15], v[40:41]
	global_store_dwordx2 v[16:17], v[6:7], off offset:1024
	v_pk_mul_f32 v[12:13], v[4:5], v[6:7] op_sel:[1,0]
	v_addc_co_u32_e64 v25, vcc, 0, v3, s[8:9]
	v_pk_fma_f32 v[14:15], v[4:5], v[6:7], v[12:13] op_sel:[0,0,1] op_sel_hi:[1,1,0] neg_lo:[0,0,1] neg_hi:[0,0,1]
	v_pk_fma_f32 v[6:7], v[4:5], v[6:7], v[12:13] op_sel:[0,0,1] op_sel_hi:[0,1,0]
	v_mov_b32_e32 v15, v7
	s_waitcnt vmcnt(9)
	v_pk_add_f32 v[6:7], v[22:23], v[14:15]
	global_store_dwordx2 v[24:25], v[6:7], off offset:1024
	v_pk_mul_f32 v[12:13], v[4:5], v[6:7] op_sel:[1,0]
	v_addc_co_u32_e64 v29, vcc, 0, v3, s[10:11]
	v_pk_fma_f32 v[14:15], v[4:5], v[6:7], v[12:13] op_sel:[0,0,1] op_sel_hi:[1,1,0] neg_lo:[0,0,1] neg_hi:[0,0,1]
	v_pk_fma_f32 v[6:7], v[4:5], v[6:7], v[12:13] op_sel:[0,0,1] op_sel_hi:[0,1,0]
	v_mov_b32_e32 v15, v7
	s_waitcnt vmcnt(9)
	v_pk_add_f32 v[6:7], v[26:27], v[14:15]
	global_store_dwordx2 v[28:29], v[6:7], off offset:1024
	v_pk_mul_f32 v[12:13], v[4:5], v[6:7] op_sel:[1,0]
	v_addc_co_u32_e64 v33, vcc, 0, v3, s[0:1]
	v_pk_fma_f32 v[14:15], v[4:5], v[6:7], v[12:13] op_sel:[0,0,1] op_sel_hi:[1,1,0] neg_lo:[0,0,1] neg_hi:[0,0,1]
	v_pk_fma_f32 v[6:7], v[4:5], v[6:7], v[12:13] op_sel:[0,0,1] op_sel_hi:[0,1,0]
	v_mov_b32_e32 v15, v7
	s_waitcnt vmcnt(9)
; __device__ __forceinline__ void phase_s5b_gqa(const Params& P, unsigned char* smraw, int bid, int nb) {
;     ...
;         float sr = 0.f, si = 0.f;
;         for (int c0 = 0; c0 < 260; c0 += 20) {
;             float2 e[20];
; #pragma unroll
;             for (int j = 0; j < 20; ++j) e[j] = SE[(size_t)(c0 + j) * 4096 + i];
; #pragma unroll
;             for (int j = 0; j < 20; ++j) {
;                 CIN[(size_t)(c0 + j) * 4096 + i] = make_float2(sr, si);
;                 const float nr = a.x * sr - a.y * si + e[j].x, ni = a.x * si + a.y * sr + e[j].y;
;                 sr = nr; si = ni;
;             }
	v_pk_add_f32 v[6:7], v[30:31], v[14:15]
	global_store_dwordx2 v[32:33], v[6:7], off offset:1024
	v_pk_mul_f32 v[12:13], v[4:5], v[6:7] op_sel:[1,0]
	v_addc_co_u32_e64 v37, vcc, 0, v3, s[14:15]
	v_pk_fma_f32 v[14:15], v[4:5], v[6:7], v[12:13] op_sel:[0,0,1] op_sel_hi:[1,1,0] neg_lo:[0,0,1] neg_hi:[0,0,1]
	v_pk_fma_f32 v[6:7], v[4:5], v[6:7], v[12:13] op_sel:[0,0,1] op_sel_hi:[0,1,0]
	v_mov_b32_e32 v15, v7
	s_waitcnt vmcnt(9)
	v_pk_add_f32 v[6:7], v[34:35], v[14:15]
	global_store_dwordx2 v[36:37], v[6:7], off offset:1024
	v_pk_mul_f32 v[12:13], v[4:5], v[6:7] op_sel:[1,0]
	v_addc_co_u32_e64 v9, vcc, 0, v3, s[6:7]
	v_pk_fma_f32 v[14:15], v[4:5], v[6:7], v[12:13] op_sel:[0,0,1] op_sel_hi:[1,1,0] neg_lo:[0,0,1] neg_hi:[0,0,1]
	v_pk_fma_f32 v[6:7], v[4:5], v[6:7], v[12:13] op_sel:[0,0,1] op_sel_hi:[0,1,0]
	v_mov_b32_e32 v15, v7
	s_waitcnt vmcnt(9)
	v_pk_add_f32 v[6:7], v[38:39], v[14:15]
	global_store_dwordx2 v[8:9], v[6:7], off offset:1024
	v_pk_mul_f32 v[8:9], v[4:5], v[6:7] op_sel:[1,0]
	s_nop 0
	v_pk_fma_f32 v[12:13], v[4:5], v[6:7], v[8:9] op_sel:[0,0,1] op_sel_hi:[1,1,0] neg_lo:[0,0,1] neg_hi:[0,0,1]
	v_pk_fma_f32 v[6:7], v[4:5], v[6:7], v[8:9] op_sel:[0,0,1] op_sel_hi:[0,1,0]
	v_add_co_u32_e32 v6, vcc, 0x3ae7a000, v2
	s_mov_b64 s[0:1], vcc
	v_add_co_u32_e32 v8, vcc, 0x3a65a000, v2
	v_mov_b32_e32 v13, v7
	s_nop 0
	v_addc_co_u32_e32 v9, vcc, 0, v3, vcc
	global_load_dwordx2 v[8:9], v[8:9], off offset:1024
	v_add_co_u32_e32 v14, vcc, 0x3ae82000, v2
	s_mov_b64 s[6:7], vcc
	v_add_co_u32_e32 v16, vcc, 0x3a662000, v2
	s_waitcnt vmcnt(8)
	v_pk_add_f32 v[10:11], v[10:11], v[12:13]
	v_addc_co_u32_e32 v17, vcc, 0, v3, vcc
	global_load_dwordx2 v[16:17], v[16:17], off offset:1024
	v_addc_co_u32_e64 v19, vcc, 0, v3, s[12:13]
	v_pk_mul_f32 v[12:13], v[4:5], v[10:11] op_sel:[1,0]
	global_store_dwordx2 v[18:19], v[10:11], off offset:1024
	v_pk_fma_f32 v[18:19], v[4:5], v[10:11], v[12:13] op_sel:[0,0,1] op_sel_hi:[1,1,0] neg_lo:[0,0,1] neg_hi:[0,0,1]
	v_pk_fma_f32 v[10:11], v[4:5], v[10:11], v[12:13] op_sel:[0,0,1] op_sel_hi:[0,1,0]
	v_addc_co_u32_e64 v7, vcc, 0, v3, s[0:1]
	v_mov_b32_e32 v19, v11
	v_add_co_u32_e32 v12, vcc, 0x3ae8a000, v2
	s_waitcnt vmcnt(9)
	v_pk_add_f32 v[10:11], v[20:21], v[18:19]
	s_mov_b64 s[12:13], vcc
	v_add_co_u32_e32 v18, vcc, 0x3a66a000, v2
	global_store_dwordx2 v[6:7], v[10:11], off offset:1024
	s_nop 0
	v_addc_co_u32_e32 v19, vcc, 0, v3, vcc
	global_load_dwordx2 v[18:19], v[18:19], off offset:1024
	v_add_co_u32_e32 v20, vcc, 0x3ae92000, v2
	s_mov_b64 s[4:5], vcc
	v_add_co_u32_e32 v22, vcc, 0x3a672000, v2
	v_pk_mul_f32 v[6:7], v[4:5], v[10:11] op_sel:[1,0]
	s_nop 0
	v_addc_co_u32_e32 v23, vcc, 0, v3, vcc
	global_load_dwordx2 v[22:23], v[22:23], off offset:1024
	v_add_co_u32_e32 v24, vcc, 0x3ae9a000, v2
	s_mov_b64 s[8:9], vcc
	v_add_co_u32_e32 v26, vcc, 0x3a67a000, v2
	v_pk_fma_f32 v[40:41], v[4:5], v[10:11], v[6:7] op_sel:[0,0,1] op_sel_hi:[1,1,0] neg_lo:[0,0,1] neg_hi:[0,0,1]
	s_nop 0
	v_addc_co_u32_e32 v27, vcc, 0, v3, vcc
	global_load_dwordx2 v[26:27], v[26:27], off offset:1024
	v_add_co_u32_e32 v28, vcc, 0x3aea2000, v2
	s_mov_b64 s[10:11], vcc
	v_add_co_u32_e32 v30, vcc, 0x3a682000, v2
	v_pk_fma_f32 v[6:7], v[4:5], v[10:11], v[6:7] op_sel:[0,0,1] op_sel_hi:[0,1,0]
	s_nop 0
	v_addc_co_u32_e32 v31, vcc, 0, v3, vcc
	global_load_dwordx2 v[30:31], v[30:31], off offset:1024
	v_add_co_u32_e32 v32, vcc, 0x3aeaa000, v2
	s_mov_b64 s[0:1], vcc
	v_add_co_u32_e32 v34, vcc, 0x3a68a000, v2
	v_mov_b32_e32 v41, v7
	s_nop 0
	v_addc_co_u32_e32 v35, vcc, 0, v3, vcc
	global_load_dwordx2 v[34:35], v[34:35], off offset:1024
	v_add_co_u32_e32 v36, vcc, 0x3aeb2000, v2
	s_mov_b64 s[14:15], vcc
	v_add_co_u32_e32 v38, vcc, 0x3a692000, v2
	s_waitcnt vmcnt(8)
	v_pk_add_f32 v[6:7], v[8:9], v[40:41]
	v_addc_co_u32_e32 v39, vcc, 0, v3, vcc
	global_load_dwordx2 v[38:39], v[38:39], off offset:1024
	v_addc_co_u32_e64 v15, vcc, 0, v3, s[6:7]
	v_pk_mul_f32 v[8:9], v[4:5], v[6:7] op_sel:[1,0]
	global_store_dwordx2 v[14:15], v[6:7], off offset:1024
	v_pk_fma_f32 v[10:11], v[4:5], v[6:7], v[8:9] op_sel:[0,0,1] op_sel_hi:[1,1,0] neg_lo:[0,0,1] neg_hi:[0,0,1]
	v_pk_fma_f32 v[6:7], v[4:5], v[6:7], v[8:9] op_sel:[0,0,1] op_sel_hi:[0,1,0]
	v_addc_co_u32_e64 v13, vcc, 0, v3, s[12:13]
	v_mov_b32_e32 v11, v7
	v_add_co_u32_e32 v8, vcc, 0x3aeba000, v2
	s_waitcnt vmcnt(9)
	v_pk_add_f32 v[6:7], v[16:17], v[10:11]
	s_mov_b64 s[6:7], vcc
	v_add_co_u32_e32 v10, vcc, 0x3a69a000, v2
	global_store_dwordx2 v[12:13], v[6:7], off offset:1024
	s_nop 0
	v_addc_co_u32_e32 v11, vcc, 0, v3, vcc
	global_load_dwordx2 v[10:11], v[10:11], off offset:1024
	v_add_co_u32_e32 v14, vcc, 0x3aec2000, v2
	s_mov_b64 s[12:13], vcc
	v_add_co_u32_e32 v16, vcc, 0x3a6a2000, v2
	v_pk_mul_f32 v[12:13], v[4:5], v[6:7] op_sel:[1,0]
	s_nop 0
	v_addc_co_u32_e32 v17, vcc, 0, v3, vcc
	global_load_dwordx2 v[16:17], v[16:17], off offset:1024
	v_pk_fma_f32 v[40:41], v[4:5], v[6:7], v[12:13] op_sel:[0,0,1] op_sel_hi:[1,1,0] neg_lo:[0,0,1] neg_hi:[0,0,1]
	v_pk_fma_f32 v[6:7], v[4:5], v[6:7], v[12:13] op_sel:[0,0,1] op_sel_hi:[0,1,0]
	v_mov_b32_e32 v41, v7
	s_waitcnt vmcnt(9)
	v_pk_add_f32 v[6:7], v[18:19], v[40:41]
	v_addc_co_u32_e64 v21, vcc, 0, v3, s[4:5]
	v_pk_mul_f32 v[12:13], v[4:5], v[6:7] op_sel:[1,0]
	global_store_dwordx2 v[20:21], v[6:7], off offset:1024
	v_pk_fma_f32 v[18:19], v[4:5], v[6:7], v[12:13] op_sel:[0,0,1] op_sel_hi:[1,1,0] neg_lo:[0,0,1] neg_hi:[0,0,1]
	v_pk_fma_f32 v[6:7], v[4:5], v[6:7], v[12:13] op_sel:[0,0,1] op_sel_hi:[0,1,0]
	v_mov_b32_e32 v19, v7
	s_waitcnt vmcnt(9)
; __device__ __forceinline__ void phase_s5b_gqa(const Params& P, unsigned char* smraw, int bid, int nb) {
;     ...
;         float sr = 0.f, si = 0.f;
;         for (int c0 = 0; c0 < 260; c0 += 20) {
;             float2 e[20];
; #pragma unroll
;             for (int j = 0; j < 20; ++j) e[j] = SE[(size_t)(c0 + j) * 4096 + i];
; #pragma unroll
;             for (int j = 0; j < 20; ++j) {
;                 CIN[(size_t)(c0 + j) * 4096 + i] = make_float2(sr, si);
;                 const float nr = a.x * sr - a.y * si + e[j].x, ni = a.x * si + a.y * sr + e[j].y;
;                 sr = nr; si = ni;
;             }
	v_pk_add_f32 v[6:7], v[22:23], v[18:19]
	v_addc_co_u32_e64 v25, vcc, 0, v3, s[8:9]
	v_pk_mul_f32 v[12:13], v[4:5], v[6:7] op_sel:[1,0]
	global_store_dwordx2 v[24:25], v[6:7], off offset:1024
	v_pk_fma_f32 v[18:19], v[4:5], v[6:7], v[12:13] op_sel:[0,0,1] op_sel_hi:[1,1,0] neg_lo:[0,0,1] neg_hi:[0,0,1]
	v_pk_fma_f32 v[6:7], v[4:5], v[6:7], v[12:13] op_sel:[0,0,1] op_sel_hi:[0,1,0]
	v_mov_b32_e32 v19, v7
	s_waitcnt vmcnt(9)
	v_pk_add_f32 v[6:7], v[26:27], v[18:19]
	v_addc_co_u32_e64 v29, vcc, 0, v3, s[10:11]
	v_pk_mul_f32 v[12:13], v[4:5], v[6:7] op_sel:[1,0]
	global_store_dwordx2 v[28:29], v[6:7], off offset:1024
	v_pk_fma_f32 v[18:19], v[4:5], v[6:7], v[12:13] op_sel:[0,0,1] op_sel_hi:[1,1,0] neg_lo:[0,0,1] neg_hi:[0,0,1]
	v_pk_fma_f32 v[6:7], v[4:5], v[6:7], v[12:13] op_sel:[0,0,1] op_sel_hi:[0,1,0]
	v_mov_b32_e32 v19, v7
	s_waitcnt vmcnt(9)
	v_pk_add_f32 v[6:7], v[30:31], v[18:19]
	v_addc_co_u32_e64 v33, vcc, 0, v3, s[0:1]
	v_pk_mul_f32 v[12:13], v[4:5], v[6:7] op_sel:[1,0]
	global_store_dwordx2 v[32:33], v[6:7], off offset:1024
	v_pk_fma_f32 v[18:19], v[4:5], v[6:7], v[12:13] op_sel:[0,0,1] op_sel_hi:[1,1,0] neg_lo:[0,0,1] neg_hi:[0,0,1]
	v_pk_fma_f32 v[6:7], v[4:5], v[6:7], v[12:13] op_sel:[0,0,1] op_sel_hi:[0,1,0]
	v_mov_b32_e32 v19, v7
	s_waitcnt vmcnt(9)
	v_pk_add_f32 v[6:7], v[34:35], v[18:19]
	v_addc_co_u32_e64 v37, vcc, 0, v3, s[14:15]
	v_pk_mul_f32 v[12:13], v[4:5], v[6:7] op_sel:[1,0]
	global_store_dwordx2 v[36:37], v[6:7], off offset:1024
	v_pk_fma_f32 v[18:19], v[4:5], v[6:7], v[12:13] op_sel:[0,0,1] op_sel_hi:[1,1,0] neg_lo:[0,0,1] neg_hi:[0,0,1]
	v_pk_fma_f32 v[6:7], v[4:5], v[6:7], v[12:13] op_sel:[0,0,1] op_sel_hi:[0,1,0]
	v_mov_b32_e32 v19, v7
	v_addc_co_u32_e64 v9, vcc, 0, v3, s[6:7]
	s_waitcnt vmcnt(9)
	v_pk_add_f32 v[6:7], v[38:39], v[18:19]
	global_store_dwordx2 v[8:9], v[6:7], off offset:1024
	v_pk_mul_f32 v[8:9], v[4:5], v[6:7] op_sel:[1,0]
	s_nop 0
	v_pk_fma_f32 v[12:13], v[4:5], v[6:7], v[8:9] op_sel:[0,0,1] op_sel_hi:[1,1,0] neg_lo:[0,0,1] neg_hi:[0,0,1]
	v_pk_fma_f32 v[6:7], v[4:5], v[6:7], v[8:9] op_sel:[0,0,1] op_sel_hi:[0,1,0]
	v_add_co_u32_e32 v6, vcc, 0x3aeca000, v2
	s_mov_b64 s[0:1], vcc
	v_add_co_u32_e32 v8, vcc, 0x3a6aa000, v2
	v_mov_b32_e32 v13, v7
	s_nop 0
	v_addc_co_u32_e32 v9, vcc, 0, v3, vcc
	global_load_dwordx2 v[8:9], v[8:9], off offset:1024
	v_add_co_u32_e32 v18, vcc, 0x3aed2000, v2
	s_mov_b64 s[6:7], vcc
	v_add_co_u32_e32 v20, vcc, 0x3a6b2000, v2
	s_waitcnt vmcnt(8)
	v_pk_add_f32 v[10:11], v[10:11], v[12:13]
	v_addc_co_u32_e32 v21, vcc, 0, v3, vcc
	global_load_dwordx2 v[20:21], v[20:21], off offset:1024
	v_addc_co_u32_e64 v15, vcc, 0, v3, s[12:13]
	v_pk_mul_f32 v[12:13], v[4:5], v[10:11] op_sel:[1,0]
	global_store_dwordx2 v[14:15], v[10:11], off offset:1024
	v_pk_fma_f32 v[14:15], v[4:5], v[10:11], v[12:13] op_sel:[0,0,1] op_sel_hi:[1,1,0] neg_lo:[0,0,1] neg_hi:[0,0,1]
	v_pk_fma_f32 v[10:11], v[4:5], v[10:11], v[12:13] op_sel:[0,0,1] op_sel_hi:[0,1,0]
	v_addc_co_u32_e64 v7, vcc, 0, v3, s[0:1]
	v_mov_b32_e32 v15, v11
	v_add_co_u32_e32 v12, vcc, 0x3aeda000, v2
	s_waitcnt vmcnt(9)
	v_pk_add_f32 v[10:11], v[16:17], v[14:15]
	s_mov_b64 s[12:13], vcc
	v_add_co_u32_e32 v14, vcc, 0x3a6ba000, v2
	global_store_dwordx2 v[6:7], v[10:11], off offset:1024
	s_nop 0
	v_addc_co_u32_e32 v15, vcc, 0, v3, vcc
	global_load_dwordx2 v[14:15], v[14:15], off offset:1024
	v_add_co_u32_e32 v16, vcc, 0x3aee2000, v2
	s_mov_b64 s[4:5], vcc
	v_add_co_u32_e32 v22, vcc, 0x3a6c2000, v2
	v_pk_mul_f32 v[6:7], v[4:5], v[10:11] op_sel:[1,0]
	s_nop 0
	v_addc_co_u32_e32 v23, vcc, 0, v3, vcc
	global_load_dwordx2 v[22:23], v[22:23], off offset:1024
	v_add_co_u32_e32 v24, vcc, 0x3aeea000, v2
	s_mov_b64 s[8:9], vcc
	v_add_co_u32_e32 v26, vcc, 0x3a6ca000, v2
	v_pk_fma_f32 v[40:41], v[4:5], v[10:11], v[6:7] op_sel:[0,0,1] op_sel_hi:[1,1,0] neg_lo:[0,0,1] neg_hi:[0,0,1]
	s_nop 0
	v_addc_co_u32_e32 v27, vcc, 0, v3, vcc
	global_load_dwordx2 v[26:27], v[26:27], off offset:1024
	v_add_co_u32_e32 v28, vcc, 0x3aef2000, v2
	s_mov_b64 s[10:11], vcc
	v_add_co_u32_e32 v30, vcc, 0x3a6d2000, v2
	v_pk_fma_f32 v[6:7], v[4:5], v[10:11], v[6:7] op_sel:[0,0,1] op_sel_hi:[0,1,0]
	s_nop 0
	v_addc_co_u32_e32 v31, vcc, 0, v3, vcc
	global_load_dwordx2 v[30:31], v[30:31], off offset:1024
	v_add_co_u32_e32 v32, vcc, 0x3aefa000, v2
	s_mov_b64 s[0:1], vcc
	v_add_co_u32_e32 v34, vcc, 0x3a6da000, v2
	v_mov_b32_e32 v41, v7
	s_nop 0
	v_addc_co_u32_e32 v35, vcc, 0, v3, vcc
	global_load_dwordx2 v[34:35], v[34:35], off offset:1024
	v_add_co_u32_e32 v36, vcc, 0x3af02000, v2
	s_mov_b64 s[14:15], vcc
	v_add_co_u32_e32 v38, vcc, 0x3a6e2000, v2
	s_waitcnt vmcnt(8)
	v_pk_add_f32 v[6:7], v[8:9], v[40:41]
	v_addc_co_u32_e32 v39, vcc, 0, v3, vcc
	global_load_dwordx2 v[38:39], v[38:39], off offset:1024
	v_addc_co_u32_e64 v19, vcc, 0, v3, s[6:7]
	v_pk_mul_f32 v[8:9], v[4:5], v[6:7] op_sel:[1,0]
	global_store_dwordx2 v[18:19], v[6:7], off offset:1024
	v_pk_fma_f32 v[10:11], v[4:5], v[6:7], v[8:9] op_sel:[0,0,1] op_sel_hi:[1,1,0] neg_lo:[0,0,1] neg_hi:[0,0,1]
	v_pk_fma_f32 v[6:7], v[4:5], v[6:7], v[8:9] op_sel:[0,0,1] op_sel_hi:[0,1,0]
	v_addc_co_u32_e64 v13, vcc, 0, v3, s[12:13]
	v_mov_b32_e32 v11, v7
	v_add_co_u32_e32 v8, vcc, 0x3af0a000, v2
	s_waitcnt vmcnt(9)
	v_pk_add_f32 v[6:7], v[10:11], v[20:21]
	s_mov_b64 s[6:7], vcc
	v_add_co_u32_e32 v10, vcc, 0x3a6ea000, v2
	global_store_dwordx2 v[12:13], v[6:7], off offset:1024
	s_nop 0
	v_addc_co_u32_e32 v11, vcc, 0, v3, vcc
	global_load_dwordx2 v[10:11], v[10:11], off offset:1024
	v_add_co_u32_e32 v18, vcc, 0x3af12000, v2
	s_mov_b64 s[12:13], vcc
	v_add_co_u32_e32 v20, vcc, 0x3a6f2000, v2
	v_pk_mul_f32 v[12:13], v[4:5], v[6:7] op_sel:[1,1] op_sel_hi:[0,1]
	s_nop 0
	v_addc_co_u32_e32 v21, vcc, 0, v3, vcc
	global_load_dwordx2 v[20:21], v[20:21], off offset:1024
	v_pk_fma_f32 v[40:41], v[4:5], v[6:7], v[12:13] neg_lo:[0,0,1] neg_hi:[0,0,1]
	v_pk_fma_f32 v[6:7], v[4:5], v[6:7], v[12:13] op_sel_hi:[1,0,1]
	v_addc_co_u32_e64 v17, vcc, 0, v3, s[4:5]
	v_mov_b32_e32 v41, v7
	s_waitcnt vmcnt(9)
; __device__ __forceinline__ void phase_s5b_gqa(const Params& P, unsigned char* smraw, int bid, int nb) {
;     ...
;         float sr = 0.f, si = 0.f;
;         for (int c0 = 0; c0 < 260; c0 += 20) {
;             float2 e[20];
; #pragma unroll
;             for (int j = 0; j < 20; ++j) e[j] = SE[(size_t)(c0 + j) * 4096 + i];
; #pragma unroll
;             for (int j = 0; j < 20; ++j) {
;                 CIN[(size_t)(c0 + j) * 4096 + i] = make_float2(sr, si);
;                 const float nr = a.x * sr - a.y * si + e[j].x, ni = a.x * si + a.y * sr + e[j].y;
;                 sr = nr; si = ni;
;             }
	v_pk_add_f32 v[6:7], v[14:15], v[40:41]
	global_store_dwordx2 v[16:17], v[6:7], off offset:1024
	v_pk_mul_f32 v[12:13], v[4:5], v[6:7] op_sel:[1,0]
	v_addc_co_u32_e64 v25, vcc, 0, v3, s[8:9]
	v_pk_fma_f32 v[14:15], v[4:5], v[6:7], v[12:13] op_sel:[0,0,1] op_sel_hi:[1,1,0] neg_lo:[0,0,1] neg_hi:[0,0,1]
	v_pk_fma_f32 v[6:7], v[4:5], v[6:7], v[12:13] op_sel:[0,0,1] op_sel_hi:[0,1,0]
	v_mov_b32_e32 v15, v7
	s_waitcnt vmcnt(9)
	v_pk_add_f32 v[6:7], v[22:23], v[14:15]
	global_store_dwordx2 v[24:25], v[6:7], off offset:1024
	v_pk_mul_f32 v[12:13], v[4:5], v[6:7] op_sel:[1,0]
	v_addc_co_u32_e64 v29, vcc, 0, v3, s[10:11]
	v_pk_fma_f32 v[14:15], v[4:5], v[6:7], v[12:13] op_sel:[0,0,1] op_sel_hi:[1,1,0] neg_lo:[0,0,1] neg_hi:[0,0,1]
	v_pk_fma_f32 v[6:7], v[4:5], v[6:7], v[12:13] op_sel:[0,0,1] op_sel_hi:[0,1,0]
	v_mov_b32_e32 v15, v7
	s_waitcnt vmcnt(9)
	v_pk_add_f32 v[6:7], v[26:27], v[14:15]
	global_store_dwordx2 v[28:29], v[6:7], off offset:1024
	v_pk_mul_f32 v[12:13], v[4:5], v[6:7] op_sel:[1,0]
	v_addc_co_u32_e64 v33, vcc, 0, v3, s[0:1]
	v_pk_fma_f32 v[14:15], v[4:5], v[6:7], v[12:13] op_sel:[0,0,1] op_sel_hi:[1,1,0] neg_lo:[0,0,1] neg_hi:[0,0,1]
	v_pk_fma_f32 v[6:7], v[4:5], v[6:7], v[12:13] op_sel:[0,0,1] op_sel_hi:[0,1,0]
	v_mov_b32_e32 v15, v7
	s_waitcnt vmcnt(9)
	v_pk_add_f32 v[6:7], v[30:31], v[14:15]
	global_store_dwordx2 v[32:33], v[6:7], off offset:1024
	v_pk_mul_f32 v[12:13], v[4:5], v[6:7] op_sel:[1,0]
	v_addc_co_u32_e64 v37, vcc, 0, v3, s[14:15]
	v_pk_fma_f32 v[14:15], v[4:5], v[6:7], v[12:13] op_sel:[0,0,1] op_sel_hi:[1,1,0] neg_lo:[0,0,1] neg_hi:[0,0,1]
	v_pk_fma_f32 v[6:7], v[4:5], v[6:7], v[12:13] op_sel:[0,0,1] op_sel_hi:[0,1,0]
	v_mov_b32_e32 v15, v7
	s_waitcnt vmcnt(9)
	v_pk_add_f32 v[6:7], v[34:35], v[14:15]
	global_store_dwordx2 v[36:37], v[6:7], off offset:1024
	v_pk_mul_f32 v[12:13], v[4:5], v[6:7] op_sel:[1,0]
	v_addc_co_u32_e64 v9, vcc, 0, v3, s[6:7]
	v_pk_fma_f32 v[14:15], v[4:5], v[6:7], v[12:13] op_sel:[0,0,1] op_sel_hi:[1,1,0] neg_lo:[0,0,1] neg_hi:[0,0,1]
	v_pk_fma_f32 v[6:7], v[4:5], v[6:7], v[12:13] op_sel:[0,0,1] op_sel_hi:[0,1,0]
	v_mov_b32_e32 v15, v7
	s_waitcnt vmcnt(9)
	v_pk_add_f32 v[6:7], v[38:39], v[14:15]
	global_store_dwordx2 v[8:9], v[6:7], off offset:1024
	v_pk_mul_f32 v[8:9], v[4:5], v[6:7] op_sel:[1,0]
	s_nop 0
	v_pk_fma_f32 v[12:13], v[4:5], v[6:7], v[8:9] op_sel:[0,0,1] op_sel_hi:[1,1,0] neg_lo:[0,0,1] neg_hi:[0,0,1]
	v_pk_fma_f32 v[6:7], v[4:5], v[6:7], v[8:9] op_sel:[0,0,1] op_sel_hi:[0,1,0]
	v_add_co_u32_e32 v6, vcc, 0x3af1a000, v2
	s_mov_b64 s[0:1], vcc
	v_add_co_u32_e32 v8, vcc, 0x3a6fa000, v2
	v_mov_b32_e32 v13, v7
	s_nop 0
	v_addc_co_u32_e32 v9, vcc, 0, v3, vcc
	global_load_dwordx2 v[8:9], v[8:9], off offset:1024
	v_add_co_u32_e32 v14, vcc, 0x3af22000, v2
	s_mov_b64 s[6:7], vcc
	v_add_co_u32_e32 v16, vcc, 0x3a702000, v2
	s_waitcnt vmcnt(8)
	v_pk_add_f32 v[10:11], v[10:11], v[12:13]
	v_addc_co_u32_e32 v17, vcc, 0, v3, vcc
	global_load_dwordx2 v[16:17], v[16:17], off offset:1024
	v_addc_co_u32_e64 v19, vcc, 0, v3, s[12:13]
	v_pk_mul_f32 v[12:13], v[4:5], v[10:11] op_sel:[1,0]
	global_store_dwordx2 v[18:19], v[10:11], off offset:1024
	v_pk_fma_f32 v[18:19], v[4:5], v[10:11], v[12:13] op_sel:[0,0,1] op_sel_hi:[1,1,0] neg_lo:[0,0,1] neg_hi:[0,0,1]
	v_pk_fma_f32 v[10:11], v[4:5], v[10:11], v[12:13] op_sel:[0,0,1] op_sel_hi:[0,1,0]
	v_addc_co_u32_e64 v7, vcc, 0, v3, s[0:1]
	v_mov_b32_e32 v19, v11
	v_add_co_u32_e32 v12, vcc, 0x3af2a000, v2
	s_waitcnt vmcnt(9)
	v_pk_add_f32 v[10:11], v[20:21], v[18:19]
	s_mov_b64 s[12:13], vcc
	v_add_co_u32_e32 v18, vcc, 0x3a70a000, v2
	global_store_dwordx2 v[6:7], v[10:11], off offset:1024
	s_nop 0
	v_addc_co_u32_e32 v19, vcc, 0, v3, vcc
	global_load_dwordx2 v[18:19], v[18:19], off offset:1024
	v_add_co_u32_e32 v20, vcc, 0x3af32000, v2
	s_mov_b64 s[4:5], vcc
	v_add_co_u32_e32 v22, vcc, 0x3a712000, v2
	v_pk_mul_f32 v[6:7], v[4:5], v[10:11] op_sel:[1,0]
	s_nop 0
	v_addc_co_u32_e32 v23, vcc, 0, v3, vcc
	global_load_dwordx2 v[22:23], v[22:23], off offset:1024
	v_add_co_u32_e32 v24, vcc, 0x3af3a000, v2
	s_mov_b64 s[8:9], vcc
	v_add_co_u32_e32 v26, vcc, 0x3a71a000, v2
	v_pk_fma_f32 v[40:41], v[4:5], v[10:11], v[6:7] op_sel:[0,0,1] op_sel_hi:[1,1,0] neg_lo:[0,0,1] neg_hi:[0,0,1]
	s_nop 0
	v_addc_co_u32_e32 v27, vcc, 0, v3, vcc
	global_load_dwordx2 v[26:27], v[26:27], off offset:1024
	v_add_co_u32_e32 v28, vcc, 0x3af42000, v2
	s_mov_b64 s[10:11], vcc
	v_add_co_u32_e32 v30, vcc, 0x3a722000, v2
	v_pk_fma_f32 v[6:7], v[4:5], v[10:11], v[6:7] op_sel:[0,0,1] op_sel_hi:[0,1,0]
	s_nop 0
	v_addc_co_u32_e32 v31, vcc, 0, v3, vcc
	global_load_dwordx2 v[30:31], v[30:31], off offset:1024
	v_add_co_u32_e32 v32, vcc, 0x3af4a000, v2
	s_mov_b64 s[0:1], vcc
	v_add_co_u32_e32 v34, vcc, 0x3a72a000, v2
	v_mov_b32_e32 v41, v7
	s_nop 0
	v_addc_co_u32_e32 v35, vcc, 0, v3, vcc
	global_load_dwordx2 v[34:35], v[34:35], off offset:1024
	v_add_co_u32_e32 v36, vcc, 0x3af52000, v2
	s_mov_b64 s[14:15], vcc
	v_add_co_u32_e32 v38, vcc, 0x3a732000, v2
	s_waitcnt vmcnt(8)
	v_pk_add_f32 v[6:7], v[8:9], v[40:41]
	v_addc_co_u32_e32 v39, vcc, 0, v3, vcc
	global_load_dwordx2 v[38:39], v[38:39], off offset:1024
	v_addc_co_u32_e64 v15, vcc, 0, v3, s[6:7]
	v_pk_mul_f32 v[8:9], v[4:5], v[6:7] op_sel:[1,0]
	global_store_dwordx2 v[14:15], v[6:7], off offset:1024
	v_pk_fma_f32 v[10:11], v[4:5], v[6:7], v[8:9] op_sel:[0,0,1] op_sel_hi:[1,1,0] neg_lo:[0,0,1] neg_hi:[0,0,1]
	v_pk_fma_f32 v[6:7], v[4:5], v[6:7], v[8:9] op_sel:[0,0,1] op_sel_hi:[0,1,0]
	v_addc_co_u32_e64 v13, vcc, 0, v3, s[12:13]
	v_mov_b32_e32 v11, v7
	v_add_co_u32_e32 v8, vcc, 0x3af5a000, v2
	s_waitcnt vmcnt(9)
; __device__ __forceinline__ void phase_s5b_gqa(const Params& P, unsigned char* smraw, int bid, int nb) {
;     ...
;         float sr = 0.f, si = 0.f;
;         for (int c0 = 0; c0 < 260; c0 += 20) {
;             float2 e[20];
; #pragma unroll
;             for (int j = 0; j < 20; ++j) e[j] = SE[(size_t)(c0 + j) * 4096 + i];
; #pragma unroll
;             for (int j = 0; j < 20; ++j) {
;                 CIN[(size_t)(c0 + j) * 4096 + i] = make_float2(sr, si);
;                 const float nr = a.x * sr - a.y * si + e[j].x, ni = a.x * si + a.y * sr + e[j].y;
;                 sr = nr; si = ni;
;             }
	v_pk_add_f32 v[6:7], v[16:17], v[10:11]
	s_mov_b64 s[6:7], vcc
	v_add_co_u32_e32 v10, vcc, 0x3a73a000, v2
	global_store_dwordx2 v[12:13], v[6:7], off offset:1024
	s_nop 0
	v_addc_co_u32_e32 v11, vcc, 0, v3, vcc
	global_load_dwordx2 v[10:11], v[10:11], off offset:1024
	v_add_co_u32_e32 v14, vcc, 0x3af62000, v2
	s_mov_b64 s[12:13], vcc
	v_add_co_u32_e32 v16, vcc, 0x3a742000, v2
	v_pk_mul_f32 v[12:13], v[4:5], v[6:7] op_sel:[1,0]
	s_nop 0
	v_addc_co_u32_e32 v17, vcc, 0, v3, vcc
	global_load_dwordx2 v[16:17], v[16:17], off offset:1024
	v_pk_fma_f32 v[40:41], v[4:5], v[6:7], v[12:13] op_sel:[0,0,1] op_sel_hi:[1,1,0] neg_lo:[0,0,1] neg_hi:[0,0,1]
	v_pk_fma_f32 v[6:7], v[4:5], v[6:7], v[12:13] op_sel:[0,0,1] op_sel_hi:[0,1,0]
	v_mov_b32_e32 v41, v7
	s_waitcnt vmcnt(9)
	v_pk_add_f32 v[6:7], v[18:19], v[40:41]
	v_addc_co_u32_e64 v21, vcc, 0, v3, s[4:5]
	v_pk_mul_f32 v[12:13], v[4:5], v[6:7] op_sel:[1,0]
	global_store_dwordx2 v[20:21], v[6:7], off offset:1024
	v_pk_fma_f32 v[18:19], v[4:5], v[6:7], v[12:13] op_sel:[0,0,1] op_sel_hi:[1,1,0] neg_lo:[0,0,1] neg_hi:[0,0,1]
	v_pk_fma_f32 v[6:7], v[4:5], v[6:7], v[12:13] op_sel:[0,0,1] op_sel_hi:[0,1,0]
	v_mov_b32_e32 v19, v7
	s_waitcnt vmcnt(9)
	v_pk_add_f32 v[6:7], v[22:23], v[18:19]
	v_addc_co_u32_e64 v25, vcc, 0, v3, s[8:9]
	v_pk_mul_f32 v[12:13], v[4:5], v[6:7] op_sel:[1,0]
	global_store_dwordx2 v[24:25], v[6:7], off offset:1024
	v_pk_fma_f32 v[18:19], v[4:5], v[6:7], v[12:13] op_sel:[0,0,1] op_sel_hi:[1,1,0] neg_lo:[0,0,1] neg_hi:[0,0,1]
	v_pk_fma_f32 v[6:7], v[4:5], v[6:7], v[12:13] op_sel:[0,0,1] op_sel_hi:[0,1,0]
	v_mov_b32_e32 v19, v7
	s_waitcnt vmcnt(9)
	v_pk_add_f32 v[6:7], v[26:27], v[18:19]
	v_addc_co_u32_e64 v29, vcc, 0, v3, s[10:11]
	v_pk_mul_f32 v[12:13], v[4:5], v[6:7] op_sel:[1,0]
	global_store_dwordx2 v[28:29], v[6:7], off offset:1024
	v_pk_fma_f32 v[18:19], v[4:5], v[6:7], v[12:13] op_sel:[0,0,1] op_sel_hi:[1,1,0] neg_lo:[0,0,1] neg_hi:[0,0,1]
	v_pk_fma_f32 v[6:7], v[4:5], v[6:7], v[12:13] op_sel:[0,0,1] op_sel_hi:[0,1,0]
	v_mov_b32_e32 v19, v7
	s_waitcnt vmcnt(9)
	v_pk_add_f32 v[6:7], v[30:31], v[18:19]
	v_addc_co_u32_e64 v33, vcc, 0, v3, s[0:1]
	v_pk_mul_f32 v[12:13], v[4:5], v[6:7] op_sel:[1,0]
	global_store_dwordx2 v[32:33], v[6:7], off offset:1024
	v_pk_fma_f32 v[18:19], v[4:5], v[6:7], v[12:13] op_sel:[0,0,1] op_sel_hi:[1,1,0] neg_lo:[0,0,1] neg_hi:[0,0,1]
	v_pk_fma_f32 v[6:7], v[4:5], v[6:7], v[12:13] op_sel:[0,0,1] op_sel_hi:[0,1,0]
	v_mov_b32_e32 v19, v7
	s_waitcnt vmcnt(9)
	v_pk_add_f32 v[6:7], v[34:35], v[18:19]
	v_addc_co_u32_e64 v37, vcc, 0, v3, s[14:15]
	v_pk_mul_f32 v[12:13], v[4:5], v[6:7] op_sel:[1,0]
	global_store_dwordx2 v[36:37], v[6:7], off offset:1024
	v_pk_fma_f32 v[18:19], v[4:5], v[6:7], v[12:13] op_sel:[0,0,1] op_sel_hi:[1,1,0] neg_lo:[0,0,1] neg_hi:[0,0,1]
	v_pk_fma_f32 v[6:7], v[4:5], v[6:7], v[12:13] op_sel:[0,0,1] op_sel_hi:[0,1,0]
	v_mov_b32_e32 v19, v7
	v_addc_co_u32_e64 v9, vcc, 0, v3, s[6:7]
	s_waitcnt vmcnt(9)
	v_pk_add_f32 v[6:7], v[38:39], v[18:19]
	global_store_dwordx2 v[8:9], v[6:7], off offset:1024
	v_pk_mul_f32 v[8:9], v[4:5], v[6:7] op_sel:[1,0]
	s_nop 0
	v_pk_fma_f32 v[12:13], v[4:5], v[6:7], v[8:9] op_sel:[0,0,1] op_sel_hi:[1,1,0] neg_lo:[0,0,1] neg_hi:[0,0,1]
	v_pk_fma_f32 v[6:7], v[4:5], v[6:7], v[8:9] op_sel:[0,0,1] op_sel_hi:[0,1,0]
	v_add_co_u32_e32 v6, vcc, 0x3af6a000, v2
	s_mov_b64 s[0:1], vcc
	v_add_co_u32_e32 v8, vcc, 0x3a74a000, v2
	v_mov_b32_e32 v13, v7
	s_nop 0
	v_addc_co_u32_e32 v9, vcc, 0, v3, vcc
	global_load_dwordx2 v[8:9], v[8:9], off offset:1024
	v_add_co_u32_e32 v18, vcc, 0x3af72000, v2
	s_mov_b64 s[6:7], vcc
	v_add_co_u32_e32 v20, vcc, 0x3a752000, v2
	s_waitcnt vmcnt(8)
	v_pk_add_f32 v[10:11], v[10:11], v[12:13]
	v_addc_co_u32_e32 v21, vcc, 0, v3, vcc
	global_load_dwordx2 v[20:21], v[20:21], off offset:1024
	v_addc_co_u32_e64 v15, vcc, 0, v3, s[12:13]
	v_pk_mul_f32 v[12:13], v[4:5], v[10:11] op_sel:[1,0]
	global_store_dwordx2 v[14:15], v[10:11], off offset:1024
	v_pk_fma_f32 v[14:15], v[4:5], v[10:11], v[12:13] op_sel:[0,0,1] op_sel_hi:[1,1,0] neg_lo:[0,0,1] neg_hi:[0,0,1]
	v_pk_fma_f32 v[10:11], v[4:5], v[10:11], v[12:13] op_sel:[0,0,1] op_sel_hi:[0,1,0]
	v_addc_co_u32_e64 v7, vcc, 0, v3, s[0:1]
	v_mov_b32_e32 v15, v11
	v_add_co_u32_e32 v12, vcc, 0x3af7a000, v2
	s_waitcnt vmcnt(9)
	v_pk_add_f32 v[10:11], v[16:17], v[14:15]
	s_mov_b64 s[12:13], vcc
	v_add_co_u32_e32 v14, vcc, 0x3a75a000, v2
	global_store_dwordx2 v[6:7], v[10:11], off offset:1024
	s_nop 0
	v_addc_co_u32_e32 v15, vcc, 0, v3, vcc
	global_load_dwordx2 v[14:15], v[14:15], off offset:1024
	v_add_co_u32_e32 v16, vcc, 0x3af82000, v2
	s_mov_b64 s[4:5], vcc
	v_add_co_u32_e32 v22, vcc, 0x3a762000, v2
	v_pk_mul_f32 v[6:7], v[4:5], v[10:11] op_sel:[1,0]
	s_nop 0
	v_addc_co_u32_e32 v23, vcc, 0, v3, vcc
	global_load_dwordx2 v[22:23], v[22:23], off offset:1024
	v_add_co_u32_e32 v24, vcc, 0x3af8a000, v2
	s_mov_b64 s[8:9], vcc
	v_add_co_u32_e32 v26, vcc, 0x3a76a000, v2
	v_pk_fma_f32 v[40:41], v[4:5], v[10:11], v[6:7] op_sel:[0,0,1] op_sel_hi:[1,1,0] neg_lo:[0,0,1] neg_hi:[0,0,1]
	s_nop 0
	v_addc_co_u32_e32 v27, vcc, 0, v3, vcc
	global_load_dwordx2 v[26:27], v[26:27], off offset:1024
	v_add_co_u32_e32 v28, vcc, 0x3af92000, v2
	s_mov_b64 s[10:11], vcc
	v_add_co_u32_e32 v30, vcc, 0x3a772000, v2
	v_pk_fma_f32 v[6:7], v[4:5], v[10:11], v[6:7] op_sel:[0,0,1] op_sel_hi:[0,1,0]
	s_nop 0
	v_addc_co_u32_e32 v31, vcc, 0, v3, vcc
	global_load_dwordx2 v[30:31], v[30:31], off offset:1024
	v_add_co_u32_e32 v32, vcc, 0x3af9a000, v2
	s_mov_b64 s[0:1], vcc
	v_add_co_u32_e32 v34, vcc, 0x3a77a000, v2
	v_mov_b32_e32 v41, v7
	s_nop 0
	v_addc_co_u32_e32 v35, vcc, 0, v3, vcc
	global_load_dwordx2 v[34:35], v[34:35], off offset:1024
	v_add_co_u32_e32 v36, vcc, 0x3afa2000, v2
	s_mov_b64 s[14:15], vcc
	v_add_co_u32_e32 v38, vcc, 0x3a782000, v2
	s_waitcnt vmcnt(8)
; __device__ __forceinline__ void phase_s5b_gqa(const Params& P, unsigned char* smraw, int bid, int nb) {
;     ...
;         float sr = 0.f, si = 0.f;
;         for (int c0 = 0; c0 < 260; c0 += 20) {
;             float2 e[20];
; #pragma unroll
;             for (int j = 0; j < 20; ++j) e[j] = SE[(size_t)(c0 + j) * 4096 + i];
; #pragma unroll
;             for (int j = 0; j < 20; ++j) {
;                 CIN[(size_t)(c0 + j) * 4096 + i] = make_float2(sr, si);
;                 const float nr = a.x * sr - a.y * si + e[j].x, ni = a.x * si + a.y * sr + e[j].y;
;                 sr = nr; si = ni;
;             }
	v_pk_add_f32 v[6:7], v[8:9], v[40:41]
	v_addc_co_u32_e32 v39, vcc, 0, v3, vcc
	global_load_dwordx2 v[38:39], v[38:39], off offset:1024
	v_addc_co_u32_e64 v19, vcc, 0, v3, s[6:7]
	v_pk_mul_f32 v[8:9], v[4:5], v[6:7] op_sel:[1,0]
	global_store_dwordx2 v[18:19], v[6:7], off offset:1024
	v_pk_fma_f32 v[10:11], v[4:5], v[6:7], v[8:9] op_sel:[0,0,1] op_sel_hi:[1,1,0] neg_lo:[0,0,1] neg_hi:[0,0,1]
	v_pk_fma_f32 v[6:7], v[4:5], v[6:7], v[8:9] op_sel:[0,0,1] op_sel_hi:[0,1,0]
	v_addc_co_u32_e64 v13, vcc, 0, v3, s[12:13]
	v_mov_b32_e32 v11, v7
	v_add_co_u32_e32 v8, vcc, 0x3afaa000, v2
	s_waitcnt vmcnt(9)
	v_pk_add_f32 v[6:7], v[10:11], v[20:21]
	s_mov_b64 s[6:7], vcc
	v_add_co_u32_e32 v10, vcc, 0x3a78a000, v2
	global_store_dwordx2 v[12:13], v[6:7], off offset:1024
	s_nop 0
	v_addc_co_u32_e32 v11, vcc, 0, v3, vcc
	global_load_dwordx2 v[10:11], v[10:11], off offset:1024
	v_add_co_u32_e32 v18, vcc, 0x3afb2000, v2
	s_mov_b64 s[12:13], vcc
	v_add_co_u32_e32 v20, vcc, 0x3a792000, v2
	v_pk_mul_f32 v[12:13], v[4:5], v[6:7] op_sel:[1,1] op_sel_hi:[0,1]
	s_nop 0
	v_addc_co_u32_e32 v21, vcc, 0, v3, vcc
	global_load_dwordx2 v[20:21], v[20:21], off offset:1024
	v_pk_fma_f32 v[40:41], v[4:5], v[6:7], v[12:13] neg_lo:[0,0,1] neg_hi:[0,0,1]
	v_pk_fma_f32 v[6:7], v[4:5], v[6:7], v[12:13] op_sel_hi:[1,0,1]
	v_addc_co_u32_e64 v17, vcc, 0, v3, s[4:5]
	v_mov_b32_e32 v41, v7
	s_waitcnt vmcnt(9)
	v_pk_add_f32 v[6:7], v[14:15], v[40:41]
	global_store_dwordx2 v[16:17], v[6:7], off offset:1024
	v_pk_mul_f32 v[12:13], v[4:5], v[6:7] op_sel:[1,0]
	v_addc_co_u32_e64 v25, vcc, 0, v3, s[8:9]
	v_pk_fma_f32 v[14:15], v[4:5], v[6:7], v[12:13] op_sel:[0,0,1] op_sel_hi:[1,1,0] neg_lo:[0,0,1] neg_hi:[0,0,1]
	v_pk_fma_f32 v[6:7], v[4:5], v[6:7], v[12:13] op_sel:[0,0,1] op_sel_hi:[0,1,0]
	v_mov_b32_e32 v15, v7
	s_waitcnt vmcnt(9)
	v_pk_add_f32 v[6:7], v[22:23], v[14:15]
	global_store_dwordx2 v[24:25], v[6:7], off offset:1024
	v_pk_mul_f32 v[12:13], v[4:5], v[6:7] op_sel:[1,0]
	v_addc_co_u32_e64 v29, vcc, 0, v3, s[10:11]
	v_pk_fma_f32 v[14:15], v[4:5], v[6:7], v[12:13] op_sel:[0,0,1] op_sel_hi:[1,1,0] neg_lo:[0,0,1] neg_hi:[0,0,1]
	v_pk_fma_f32 v[6:7], v[4:5], v[6:7], v[12:13] op_sel:[0,0,1] op_sel_hi:[0,1,0]
	v_mov_b32_e32 v15, v7
	s_waitcnt vmcnt(9)
	v_pk_add_f32 v[6:7], v[26:27], v[14:15]
	global_store_dwordx2 v[28:29], v[6:7], off offset:1024
	v_pk_mul_f32 v[12:13], v[4:5], v[6:7] op_sel:[1,0]
	v_addc_co_u32_e64 v33, vcc, 0, v3, s[0:1]
	v_pk_fma_f32 v[14:15], v[4:5], v[6:7], v[12:13] op_sel:[0,0,1] op_sel_hi:[1,1,0] neg_lo:[0,0,1] neg_hi:[0,0,1]
	v_pk_fma_f32 v[6:7], v[4:5], v[6:7], v[12:13] op_sel:[0,0,1] op_sel_hi:[0,1,0]
	v_mov_b32_e32 v15, v7
	s_waitcnt vmcnt(9)
	v_pk_add_f32 v[6:7], v[30:31], v[14:15]
	global_store_dwordx2 v[32:33], v[6:7], off offset:1024
	v_pk_mul_f32 v[12:13], v[4:5], v[6:7] op_sel:[1,0]
	v_addc_co_u32_e64 v37, vcc, 0, v3, s[14:15]
	v_pk_fma_f32 v[14:15], v[4:5], v[6:7], v[12:13] op_sel:[0,0,1] op_sel_hi:[1,1,0] neg_lo:[0,0,1] neg_hi:[0,0,1]
	v_pk_fma_f32 v[6:7], v[4:5], v[6:7], v[12:13] op_sel:[0,0,1] op_sel_hi:[0,1,0]
	v_mov_b32_e32 v15, v7
	s_waitcnt vmcnt(9)
	v_pk_add_f32 v[6:7], v[34:35], v[14:15]
	global_store_dwordx2 v[36:37], v[6:7], off offset:1024
	v_pk_mul_f32 v[12:13], v[4:5], v[6:7] op_sel:[1,0]
	v_addc_co_u32_e64 v9, vcc, 0, v3, s[6:7]
	v_pk_fma_f32 v[14:15], v[4:5], v[6:7], v[12:13] op_sel:[0,0,1] op_sel_hi:[1,1,0] neg_lo:[0,0,1] neg_hi:[0,0,1]
	v_pk_fma_f32 v[6:7], v[4:5], v[6:7], v[12:13] op_sel:[0,0,1] op_sel_hi:[0,1,0]
	v_mov_b32_e32 v15, v7
	s_waitcnt vmcnt(9)
	v_pk_add_f32 v[6:7], v[38:39], v[14:15]
	global_store_dwordx2 v[8:9], v[6:7], off offset:1024
	v_pk_mul_f32 v[8:9], v[4:5], v[6:7] op_sel:[1,0]
	s_nop 0
	v_pk_fma_f32 v[12:13], v[4:5], v[6:7], v[8:9] op_sel:[0,0,1] op_sel_hi:[1,1,0] neg_lo:[0,0,1] neg_hi:[0,0,1]
	v_pk_fma_f32 v[6:7], v[4:5], v[6:7], v[8:9] op_sel:[0,0,1] op_sel_hi:[0,1,0]
	v_add_co_u32_e32 v6, vcc, 0x3afba000, v2
	s_mov_b64 s[0:1], vcc
	v_add_co_u32_e32 v8, vcc, 0x3a79a000, v2
	v_mov_b32_e32 v13, v7
	s_nop 0
	v_addc_co_u32_e32 v9, vcc, 0, v3, vcc
	global_load_dwordx2 v[8:9], v[8:9], off offset:1024
	v_add_co_u32_e32 v14, vcc, 0x3afc2000, v2
	s_mov_b64 s[6:7], vcc
	v_add_co_u32_e32 v16, vcc, 0x3a7a2000, v2
	s_waitcnt vmcnt(8)
	v_pk_add_f32 v[10:11], v[10:11], v[12:13]
	v_addc_co_u32_e32 v17, vcc, 0, v3, vcc
	global_load_dwordx2 v[16:17], v[16:17], off offset:1024
	v_addc_co_u32_e64 v19, vcc, 0, v3, s[12:13]
	v_pk_mul_f32 v[12:13], v[4:5], v[10:11] op_sel:[1,0]
	global_store_dwordx2 v[18:19], v[10:11], off offset:1024
	v_pk_fma_f32 v[18:19], v[4:5], v[10:11], v[12:13] op_sel:[0,0,1] op_sel_hi:[1,1,0] neg_lo:[0,0,1] neg_hi:[0,0,1]
	v_pk_fma_f32 v[10:11], v[4:5], v[10:11], v[12:13] op_sel:[0,0,1] op_sel_hi:[0,1,0]
	v_addc_co_u32_e64 v7, vcc, 0, v3, s[0:1]
	v_mov_b32_e32 v19, v11
	v_add_co_u32_e32 v12, vcc, 0x3afca000, v2
	s_waitcnt vmcnt(9)
	v_pk_add_f32 v[10:11], v[20:21], v[18:19]
	s_mov_b64 s[12:13], vcc
	v_add_co_u32_e32 v18, vcc, 0x3a7aa000, v2
	global_store_dwordx2 v[6:7], v[10:11], off offset:1024
	s_nop 0
	v_addc_co_u32_e32 v19, vcc, 0, v3, vcc
	global_load_dwordx2 v[18:19], v[18:19], off offset:1024
	v_add_co_u32_e32 v20, vcc, 0x3afd2000, v2
	s_mov_b64 s[4:5], vcc
	v_add_co_u32_e32 v22, vcc, 0x3a7b2000, v2
	v_pk_mul_f32 v[6:7], v[4:5], v[10:11] op_sel:[1,0]
	s_nop 0
	v_addc_co_u32_e32 v23, vcc, 0, v3, vcc
	global_load_dwordx2 v[22:23], v[22:23], off offset:1024
	v_add_co_u32_e32 v24, vcc, 0x3afda000, v2
	s_mov_b64 s[8:9], vcc
	v_add_co_u32_e32 v26, vcc, 0x3a7ba000, v2
	v_pk_fma_f32 v[40:41], v[4:5], v[10:11], v[6:7] op_sel:[0,0,1] op_sel_hi:[1,1,0] neg_lo:[0,0,1] neg_hi:[0,0,1]
	s_nop 0
	v_addc_co_u32_e32 v27, vcc, 0, v3, vcc
	global_load_dwordx2 v[26:27], v[26:27], off offset:1024
	v_add_co_u32_e32 v28, vcc, 0x3afe2000, v2
	s_mov_b64 s[10:11], vcc
	v_add_co_u32_e32 v30, vcc, 0x3a7c2000, v2
	v_pk_fma_f32 v[6:7], v[4:5], v[10:11], v[6:7] op_sel:[0,0,1] op_sel_hi:[0,1,0]
	s_nop 0
	v_addc_co_u32_e32 v31, vcc, 0, v3, vcc
	global_load_dwordx2 v[30:31], v[30:31], off offset:1024
	v_add_co_u32_e32 v32, vcc, 0x3afea000, v2
	s_mov_b64 s[0:1], vcc
	v_add_co_u32_e32 v34, vcc, 0x3a7ca000, v2
	v_mov_b32_e32 v41, v7
	s_nop 0
	v_addc_co_u32_e32 v35, vcc, 0, v3, vcc
	global_load_dwordx2 v[34:35], v[34:35], off offset:1024
	v_add_co_u32_e32 v36, vcc, 0x3aff2000, v2
	s_mov_b64 s[14:15], vcc
	v_add_co_u32_e32 v38, vcc, 0x3a7d2000, v2
	s_waitcnt vmcnt(8)
; __device__ __forceinline__ void phase_s5b_gqa(const Params& P, unsigned char* smraw, int bid, int nb) {
;     ...
;         float sr = 0.f, si = 0.f;
;         for (int c0 = 0; c0 < 260; c0 += 20) {
;             float2 e[20];
; #pragma unroll
;             for (int j = 0; j < 20; ++j) e[j] = SE[(size_t)(c0 + j) * 4096 + i];
; #pragma unroll
;             for (int j = 0; j < 20; ++j) {
;                 CIN[(size_t)(c0 + j) * 4096 + i] = make_float2(sr, si);
;                 const float nr = a.x * sr - a.y * si + e[j].x, ni = a.x * si + a.y * sr + e[j].y;
;                 sr = nr; si = ni;
;             }
	v_pk_add_f32 v[6:7], v[8:9], v[40:41]
	v_addc_co_u32_e32 v39, vcc, 0, v3, vcc
	global_load_dwordx2 v[38:39], v[38:39], off offset:1024
	v_addc_co_u32_e64 v15, vcc, 0, v3, s[6:7]
	v_pk_mul_f32 v[8:9], v[4:5], v[6:7] op_sel:[1,0]
	global_store_dwordx2 v[14:15], v[6:7], off offset:1024
	v_pk_fma_f32 v[10:11], v[4:5], v[6:7], v[8:9] op_sel:[0,0,1] op_sel_hi:[1,1,0] neg_lo:[0,0,1] neg_hi:[0,0,1]
	v_pk_fma_f32 v[6:7], v[4:5], v[6:7], v[8:9] op_sel:[0,0,1] op_sel_hi:[0,1,0]
	v_addc_co_u32_e64 v13, vcc, 0, v3, s[12:13]
	v_mov_b32_e32 v11, v7
	v_add_co_u32_e32 v8, vcc, 0x3affa000, v2
	s_waitcnt vmcnt(9)
	v_pk_add_f32 v[6:7], v[16:17], v[10:11]
	s_mov_b64 s[6:7], vcc
	v_add_co_u32_e32 v10, vcc, 0x3a7da000, v2
	global_store_dwordx2 v[12:13], v[6:7], off offset:1024
	s_nop 0
	v_addc_co_u32_e32 v11, vcc, 0, v3, vcc
	global_load_dwordx2 v[10:11], v[10:11], off offset:1024
	v_add_co_u32_e32 v14, vcc, 0x3b002000, v2
	s_mov_b64 s[12:13], vcc
	v_add_co_u32_e32 v16, vcc, 0x3a7e2000, v2
	v_pk_mul_f32 v[12:13], v[4:5], v[6:7] op_sel:[1,0]
	s_nop 0
	v_addc_co_u32_e32 v17, vcc, 0, v3, vcc
	global_load_dwordx2 v[16:17], v[16:17], off offset:1024
	v_pk_fma_f32 v[40:41], v[4:5], v[6:7], v[12:13] op_sel:[0,0,1] op_sel_hi:[1,1,0] neg_lo:[0,0,1] neg_hi:[0,0,1]
	v_pk_fma_f32 v[6:7], v[4:5], v[6:7], v[12:13] op_sel:[0,0,1] op_sel_hi:[0,1,0]
	v_mov_b32_e32 v41, v7
	s_waitcnt vmcnt(9)
	v_pk_add_f32 v[6:7], v[18:19], v[40:41]
	v_addc_co_u32_e64 v21, vcc, 0, v3, s[4:5]
	v_pk_mul_f32 v[12:13], v[4:5], v[6:7] op_sel:[1,0]
	global_store_dwordx2 v[20:21], v[6:7], off offset:1024
	v_pk_fma_f32 v[18:19], v[4:5], v[6:7], v[12:13] op_sel:[0,0,1] op_sel_hi:[1,1,0] neg_lo:[0,0,1] neg_hi:[0,0,1]
	v_pk_fma_f32 v[6:7], v[4:5], v[6:7], v[12:13] op_sel:[0,0,1] op_sel_hi:[0,1,0]
	v_mov_b32_e32 v19, v7
	s_waitcnt vmcnt(9)
	v_pk_add_f32 v[6:7], v[22:23], v[18:19]
	v_addc_co_u32_e64 v25, vcc, 0, v3, s[8:9]
	v_pk_mul_f32 v[12:13], v[4:5], v[6:7] op_sel:[1,0]
	global_store_dwordx2 v[24:25], v[6:7], off offset:1024
	v_pk_fma_f32 v[18:19], v[4:5], v[6:7], v[12:13] op_sel:[0,0,1] op_sel_hi:[1,1,0] neg_lo:[0,0,1] neg_hi:[0,0,1]
	v_pk_fma_f32 v[6:7], v[4:5], v[6:7], v[12:13] op_sel:[0,0,1] op_sel_hi:[0,1,0]
	v_mov_b32_e32 v19, v7
	s_waitcnt vmcnt(9)
	v_pk_add_f32 v[6:7], v[26:27], v[18:19]
	v_addc_co_u32_e64 v29, vcc, 0, v3, s[10:11]
	v_pk_mul_f32 v[12:13], v[4:5], v[6:7] op_sel:[1,0]
	global_store_dwordx2 v[28:29], v[6:7], off offset:1024
	v_pk_fma_f32 v[18:19], v[4:5], v[6:7], v[12:13] op_sel:[0,0,1] op_sel_hi:[1,1,0] neg_lo:[0,0,1] neg_hi:[0,0,1]
	v_pk_fma_f32 v[6:7], v[4:5], v[6:7], v[12:13] op_sel:[0,0,1] op_sel_hi:[0,1,0]
	v_mov_b32_e32 v19, v7
	s_waitcnt vmcnt(9)
	v_pk_add_f32 v[6:7], v[30:31], v[18:19]
	v_addc_co_u32_e64 v33, vcc, 0, v3, s[0:1]
	v_pk_mul_f32 v[12:13], v[4:5], v[6:7] op_sel:[1,0]
	global_store_dwordx2 v[32:33], v[6:7], off offset:1024
	v_pk_fma_f32 v[18:19], v[4:5], v[6:7], v[12:13] op_sel:[0,0,1] op_sel_hi:[1,1,0] neg_lo:[0,0,1] neg_hi:[0,0,1]
	v_pk_fma_f32 v[6:7], v[4:5], v[6:7], v[12:13] op_sel:[0,0,1] op_sel_hi:[0,1,0]
	v_mov_b32_e32 v19, v7
	s_waitcnt vmcnt(9)
	v_pk_add_f32 v[6:7], v[34:35], v[18:19]
	v_addc_co_u32_e64 v37, vcc, 0, v3, s[14:15]
	v_pk_mul_f32 v[12:13], v[4:5], v[6:7] op_sel:[1,0]
	global_store_dwordx2 v[36:37], v[6:7], off offset:1024
	v_pk_fma_f32 v[18:19], v[4:5], v[6:7], v[12:13] op_sel:[0,0,1] op_sel_hi:[1,1,0] neg_lo:[0,0,1] neg_hi:[0,0,1]
	v_pk_fma_f32 v[6:7], v[4:5], v[6:7], v[12:13] op_sel:[0,0,1] op_sel_hi:[0,1,0]
	v_mov_b32_e32 v19, v7
	v_addc_co_u32_e64 v9, vcc, 0, v3, s[6:7]
	s_waitcnt vmcnt(9)
	v_pk_add_f32 v[6:7], v[38:39], v[18:19]
	global_store_dwordx2 v[8:9], v[6:7], off offset:1024
	v_pk_mul_f32 v[8:9], v[4:5], v[6:7] op_sel:[1,0]
	s_nop 0
	v_pk_fma_f32 v[12:13], v[4:5], v[6:7], v[8:9] op_sel:[0,0,1] op_sel_hi:[1,1,0] neg_lo:[0,0,1] neg_hi:[0,0,1]
	v_pk_fma_f32 v[6:7], v[4:5], v[6:7], v[8:9] op_sel:[0,0,1] op_sel_hi:[0,1,0]
	v_add_co_u32_e32 v6, vcc, 0x3b00a000, v2
	s_mov_b64 s[0:1], vcc
	v_add_co_u32_e32 v8, vcc, 0x3a7ea000, v2
	v_mov_b32_e32 v13, v7
	s_nop 0
	v_addc_co_u32_e32 v9, vcc, 0, v3, vcc
	global_load_dwordx2 v[8:9], v[8:9], off offset:1024
	v_add_co_u32_e32 v18, vcc, 0x3b012000, v2
	s_mov_b64 s[6:7], vcc
	v_add_co_u32_e32 v20, vcc, 0x3a7f2000, v2
	s_waitcnt vmcnt(8)
	v_pk_add_f32 v[10:11], v[10:11], v[12:13]
	v_addc_co_u32_e32 v21, vcc, 0, v3, vcc
	global_load_dwordx2 v[20:21], v[20:21], off offset:1024
	v_addc_co_u32_e64 v15, vcc, 0, v3, s[12:13]
	v_pk_mul_f32 v[12:13], v[4:5], v[10:11] op_sel:[1,0]
	global_store_dwordx2 v[14:15], v[10:11], off offset:1024
	v_pk_fma_f32 v[14:15], v[4:5], v[10:11], v[12:13] op_sel:[0,0,1] op_sel_hi:[1,1,0] neg_lo:[0,0,1] neg_hi:[0,0,1]
	v_pk_fma_f32 v[10:11], v[4:5], v[10:11], v[12:13] op_sel:[0,0,1] op_sel_hi:[0,1,0]
	v_addc_co_u32_e64 v7, vcc, 0, v3, s[0:1]
	v_mov_b32_e32 v15, v11
	v_add_co_u32_e32 v12, vcc, 0x3b01a000, v2
	s_waitcnt vmcnt(9)
; __device__ __forceinline__ void phase_s5b_gqa(const Params& P, unsigned char* smraw, int bid, int nb) {
;     ...
;         float sr = 0.f, si = 0.f;
;         for (int c0 = 0; c0 < 260; c0 += 20) {
;             float2 e[20];
; #pragma unroll
;             for (int j = 0; j < 20; ++j) e[j] = SE[(size_t)(c0 + j) * 4096 + i];
; #pragma unroll
;             for (int j = 0; j < 20; ++j) {
;                 CIN[(size_t)(c0 + j) * 4096 + i] = make_float2(sr, si);
;                 const float nr = a.x * sr - a.y * si + e[j].x, ni = a.x * si + a.y * sr + e[j].y;
;                 sr = nr; si = ni;
;             }
	v_pk_add_f32 v[10:11], v[16:17], v[14:15]
	s_mov_b64 s[12:13], vcc
	v_add_co_u32_e32 v14, vcc, 0x3a7fa000, v2
	global_store_dwordx2 v[6:7], v[10:11], off offset:1024
	s_nop 0
	v_addc_co_u32_e32 v15, vcc, 0, v3, vcc
	global_load_dwordx2 v[14:15], v[14:15], off offset:1024
	v_add_co_u32_e32 v16, vcc, 0x3b022000, v2
	s_mov_b64 s[4:5], vcc
	v_add_co_u32_e32 v22, vcc, 0x3a802000, v2
	v_pk_mul_f32 v[6:7], v[4:5], v[10:11] op_sel:[1,0]
	s_nop 0
	v_addc_co_u32_e32 v23, vcc, 0, v3, vcc
	global_load_dwordx2 v[22:23], v[22:23], off offset:1024
	v_add_co_u32_e32 v24, vcc, 0x3b02a000, v2
	s_mov_b64 s[8:9], vcc
	v_add_co_u32_e32 v26, vcc, 0x3a80a000, v2
	v_pk_fma_f32 v[40:41], v[4:5], v[10:11], v[6:7] op_sel:[0,0,1] op_sel_hi:[1,1,0] neg_lo:[0,0,1] neg_hi:[0,0,1]
	s_nop 0
	v_addc_co_u32_e32 v27, vcc, 0, v3, vcc
	global_load_dwordx2 v[26:27], v[26:27], off offset:1024
	v_add_co_u32_e32 v28, vcc, 0x3b032000, v2
	s_mov_b64 s[10:11], vcc
	v_add_co_u32_e32 v30, vcc, 0x3a812000, v2
	v_pk_fma_f32 v[6:7], v[4:5], v[10:11], v[6:7] op_sel:[0,0,1] op_sel_hi:[0,1,0]
	s_nop 0
	v_addc_co_u32_e32 v31, vcc, 0, v3, vcc
	global_load_dwordx2 v[30:31], v[30:31], off offset:1024
	v_add_co_u32_e32 v32, vcc, 0x3b03a000, v2
	s_mov_b64 s[0:1], vcc
	v_add_co_u32_e32 v34, vcc, 0x3a81a000, v2
	v_mov_b32_e32 v41, v7
	s_nop 0
	v_addc_co_u32_e32 v35, vcc, 0, v3, vcc
	global_load_dwordx2 v[34:35], v[34:35], off offset:1024
	v_add_co_u32_e32 v36, vcc, 0x3b042000, v2
	s_mov_b64 s[14:15], vcc
	v_add_co_u32_e32 v38, vcc, 0x3a822000, v2
	s_waitcnt vmcnt(8)
	v_pk_add_f32 v[6:7], v[8:9], v[40:41]
	v_addc_co_u32_e32 v39, vcc, 0, v3, vcc
	global_load_dwordx2 v[38:39], v[38:39], off offset:1024
	v_addc_co_u32_e64 v19, vcc, 0, v3, s[6:7]
	v_pk_mul_f32 v[8:9], v[4:5], v[6:7] op_sel:[1,0]
	global_store_dwordx2 v[18:19], v[6:7], off offset:1024
	v_pk_fma_f32 v[10:11], v[4:5], v[6:7], v[8:9] op_sel:[0,0,1] op_sel_hi:[1,1,0] neg_lo:[0,0,1] neg_hi:[0,0,1]
	v_pk_fma_f32 v[6:7], v[4:5], v[6:7], v[8:9] op_sel:[0,0,1] op_sel_hi:[0,1,0]
	v_addc_co_u32_e64 v13, vcc, 0, v3, s[12:13]
	v_mov_b32_e32 v11, v7
	v_add_co_u32_e32 v8, vcc, 0x3b04a000, v2
	s_waitcnt vmcnt(9)
	v_pk_add_f32 v[6:7], v[10:11], v[20:21]
	s_mov_b64 s[6:7], vcc
	v_add_co_u32_e32 v10, vcc, 0x3a82a000, v2
	global_store_dwordx2 v[12:13], v[6:7], off offset:1024
	s_nop 0
	v_addc_co_u32_e32 v11, vcc, 0, v3, vcc
	global_load_dwordx2 v[10:11], v[10:11], off offset:1024
	v_add_co_u32_e32 v18, vcc, 0x3b052000, v2
	s_mov_b64 s[12:13], vcc
	v_add_co_u32_e32 v20, vcc, 0x3a832000, v2
	v_pk_mul_f32 v[12:13], v[4:5], v[6:7] op_sel:[1,1] op_sel_hi:[0,1]
	s_nop 0
	v_addc_co_u32_e32 v21, vcc, 0, v3, vcc
	global_load_dwordx2 v[20:21], v[20:21], off offset:1024
	v_pk_fma_f32 v[40:41], v[4:5], v[6:7], v[12:13] neg_lo:[0,0,1] neg_hi:[0,0,1]
	v_pk_fma_f32 v[6:7], v[4:5], v[6:7], v[12:13] op_sel_hi:[1,0,1]
	v_addc_co_u32_e64 v17, vcc, 0, v3, s[4:5]
	v_mov_b32_e32 v41, v7
	s_waitcnt vmcnt(9)
	v_pk_add_f32 v[6:7], v[14:15], v[40:41]
	global_store_dwordx2 v[16:17], v[6:7], off offset:1024
	v_pk_mul_f32 v[12:13], v[4:5], v[6:7] op_sel:[1,0]
	v_addc_co_u32_e64 v25, vcc, 0, v3, s[8:9]
	v_pk_fma_f32 v[14:15], v[4:5], v[6:7], v[12:13] op_sel:[0,0,1] op_sel_hi:[1,1,0] neg_lo:[0,0,1] neg_hi:[0,0,1]
	v_pk_fma_f32 v[6:7], v[4:5], v[6:7], v[12:13] op_sel:[0,0,1] op_sel_hi:[0,1,0]
	v_mov_b32_e32 v15, v7
	s_waitcnt vmcnt(9)
	v_pk_add_f32 v[6:7], v[22:23], v[14:15]
	global_store_dwordx2 v[24:25], v[6:7], off offset:1024
	v_pk_mul_f32 v[12:13], v[4:5], v[6:7] op_sel:[1,0]
	v_addc_co_u32_e64 v29, vcc, 0, v3, s[10:11]
	v_pk_fma_f32 v[14:15], v[4:5], v[6:7], v[12:13] op_sel:[0,0,1] op_sel_hi:[1,1,0] neg_lo:[0,0,1] neg_hi:[0,0,1]
	v_pk_fma_f32 v[6:7], v[4:5], v[6:7], v[12:13] op_sel:[0,0,1] op_sel_hi:[0,1,0]
	v_mov_b32_e32 v15, v7
	s_waitcnt vmcnt(9)
	v_pk_add_f32 v[6:7], v[26:27], v[14:15]
	global_store_dwordx2 v[28:29], v[6:7], off offset:1024
	v_pk_mul_f32 v[12:13], v[4:5], v[6:7] op_sel:[1,0]
	v_addc_co_u32_e64 v33, vcc, 0, v3, s[0:1]
	v_pk_fma_f32 v[14:15], v[4:5], v[6:7], v[12:13] op_sel:[0,0,1] op_sel_hi:[1,1,0] neg_lo:[0,0,1] neg_hi:[0,0,1]
	v_pk_fma_f32 v[6:7], v[4:5], v[6:7], v[12:13] op_sel:[0,0,1] op_sel_hi:[0,1,0]
	v_mov_b32_e32 v15, v7
	s_waitcnt vmcnt(9)
	v_pk_add_f32 v[6:7], v[30:31], v[14:15]
	global_store_dwordx2 v[32:33], v[6:7], off offset:1024
	v_pk_mul_f32 v[12:13], v[4:5], v[6:7] op_sel:[1,0]
	v_addc_co_u32_e64 v37, vcc, 0, v3, s[14:15]
	v_pk_fma_f32 v[14:15], v[4:5], v[6:7], v[12:13] op_sel:[0,0,1] op_sel_hi:[1,1,0] neg_lo:[0,0,1] neg_hi:[0,0,1]
	v_pk_fma_f32 v[6:7], v[4:5], v[6:7], v[12:13] op_sel:[0,0,1] op_sel_hi:[0,1,0]
	v_mov_b32_e32 v15, v7
	s_waitcnt vmcnt(9)
	v_pk_add_f32 v[6:7], v[34:35], v[14:15]
	global_store_dwordx2 v[36:37], v[6:7], off offset:1024
	v_pk_mul_f32 v[12:13], v[4:5], v[6:7] op_sel:[1,0]
	v_addc_co_u32_e64 v9, vcc, 0, v3, s[6:7]
	v_pk_fma_f32 v[14:15], v[4:5], v[6:7], v[12:13] op_sel:[0,0,1] op_sel_hi:[1,1,0] neg_lo:[0,0,1] neg_hi:[0,0,1]
	v_pk_fma_f32 v[6:7], v[4:5], v[6:7], v[12:13] op_sel:[0,0,1] op_sel_hi:[0,1,0]
	v_mov_b32_e32 v15, v7
	s_waitcnt vmcnt(9)
	v_pk_add_f32 v[6:7], v[38:39], v[14:15]
	global_store_dwordx2 v[8:9], v[6:7], off offset:1024
	v_pk_mul_f32 v[8:9], v[4:5], v[6:7] op_sel:[1,0]
	s_nop 0
	v_pk_fma_f32 v[12:13], v[4:5], v[6:7], v[8:9] op_sel:[0,0,1] op_sel_hi:[1,1,0] neg_lo:[0,0,1] neg_hi:[0,0,1]
	v_pk_fma_f32 v[6:7], v[4:5], v[6:7], v[8:9] op_sel:[0,0,1] op_sel_hi:[0,1,0]
	v_add_co_u32_e32 v6, vcc, 0x3b05a000, v2
	s_mov_b64 s[0:1], vcc
	v_add_co_u32_e32 v8, vcc, 0x3a83a000, v2
	v_mov_b32_e32 v13, v7
	s_nop 0
	v_addc_co_u32_e32 v9, vcc, 0, v3, vcc
	global_load_dwordx2 v[8:9], v[8:9], off offset:1024
	v_add_co_u32_e32 v14, vcc, 0x3b062000, v2
	s_mov_b64 s[6:7], vcc
	v_add_co_u32_e32 v16, vcc, 0x3a842000, v2
	s_waitcnt vmcnt(8)
; __device__ __forceinline__ void phase_s5b_gqa(const Params& P, unsigned char* smraw, int bid, int nb) {
;     ...
;         float sr = 0.f, si = 0.f;
;         for (int c0 = 0; c0 < 260; c0 += 20) {
;             float2 e[20];
; #pragma unroll
;             for (int j = 0; j < 20; ++j) e[j] = SE[(size_t)(c0 + j) * 4096 + i];
; #pragma unroll
;             for (int j = 0; j < 20; ++j) {
;                 CIN[(size_t)(c0 + j) * 4096 + i] = make_float2(sr, si);
;                 const float nr = a.x * sr - a.y * si + e[j].x, ni = a.x * si + a.y * sr + e[j].y;
;                 sr = nr; si = ni;
;             }
	v_pk_add_f32 v[10:11], v[10:11], v[12:13]
	v_addc_co_u32_e32 v17, vcc, 0, v3, vcc
	global_load_dwordx2 v[16:17], v[16:17], off offset:1024
	v_addc_co_u32_e64 v19, vcc, 0, v3, s[12:13]
	v_pk_mul_f32 v[12:13], v[4:5], v[10:11] op_sel:[1,0]
	global_store_dwordx2 v[18:19], v[10:11], off offset:1024
	v_pk_fma_f32 v[18:19], v[4:5], v[10:11], v[12:13] op_sel:[0,0,1] op_sel_hi:[1,1,0] neg_lo:[0,0,1] neg_hi:[0,0,1]
	v_pk_fma_f32 v[10:11], v[4:5], v[10:11], v[12:13] op_sel:[0,0,1] op_sel_hi:[0,1,0]
	v_addc_co_u32_e64 v7, vcc, 0, v3, s[0:1]
	v_mov_b32_e32 v19, v11
	v_add_co_u32_e32 v12, vcc, 0x3b06a000, v2
	s_waitcnt vmcnt(9)
	v_pk_add_f32 v[10:11], v[20:21], v[18:19]
	s_mov_b64 s[12:13], vcc
	v_add_co_u32_e32 v18, vcc, 0x3a84a000, v2
	global_store_dwordx2 v[6:7], v[10:11], off offset:1024
	s_nop 0
	v_addc_co_u32_e32 v19, vcc, 0, v3, vcc
	global_load_dwordx2 v[18:19], v[18:19], off offset:1024
	v_add_co_u32_e32 v20, vcc, 0x3b072000, v2
	s_mov_b64 s[4:5], vcc
	v_add_co_u32_e32 v22, vcc, 0x3a852000, v2
	v_pk_mul_f32 v[6:7], v[4:5], v[10:11] op_sel:[1,0]
	s_nop 0
	v_addc_co_u32_e32 v23, vcc, 0, v3, vcc
	global_load_dwordx2 v[22:23], v[22:23], off offset:1024
	v_add_co_u32_e32 v24, vcc, 0x3b07a000, v2
	s_mov_b64 s[8:9], vcc
	v_add_co_u32_e32 v26, vcc, 0x3a85a000, v2
	v_pk_fma_f32 v[40:41], v[4:5], v[10:11], v[6:7] op_sel:[0,0,1] op_sel_hi:[1,1,0] neg_lo:[0,0,1] neg_hi:[0,0,1]
	s_nop 0
	v_addc_co_u32_e32 v27, vcc, 0, v3, vcc
	global_load_dwordx2 v[26:27], v[26:27], off offset:1024
	v_add_co_u32_e32 v28, vcc, 0x3b082000, v2
	s_mov_b64 s[10:11], vcc
	v_add_co_u32_e32 v30, vcc, 0x3a862000, v2
	v_pk_fma_f32 v[6:7], v[4:5], v[10:11], v[6:7] op_sel:[0,0,1] op_sel_hi:[0,1,0]
	s_nop 0
	v_addc_co_u32_e32 v31, vcc, 0, v3, vcc
	global_load_dwordx2 v[30:31], v[30:31], off offset:1024
	v_add_co_u32_e32 v32, vcc, 0x3b08a000, v2
	s_mov_b64 s[0:1], vcc
	v_add_co_u32_e32 v34, vcc, 0x3a86a000, v2
	v_mov_b32_e32 v41, v7
	s_nop 0
	v_addc_co_u32_e32 v35, vcc, 0, v3, vcc
	global_load_dwordx2 v[34:35], v[34:35], off offset:1024
	v_add_co_u32_e32 v36, vcc, 0x3b092000, v2
	s_mov_b64 s[14:15], vcc
	v_add_co_u32_e32 v38, vcc, 0x3a872000, v2
	s_waitcnt vmcnt(8)
	v_pk_add_f32 v[6:7], v[8:9], v[40:41]
	v_addc_co_u32_e32 v39, vcc, 0, v3, vcc
	global_load_dwordx2 v[38:39], v[38:39], off offset:1024
	v_addc_co_u32_e64 v15, vcc, 0, v3, s[6:7]
	v_pk_mul_f32 v[8:9], v[4:5], v[6:7] op_sel:[1,0]
	global_store_dwordx2 v[14:15], v[6:7], off offset:1024
	v_pk_fma_f32 v[10:11], v[4:5], v[6:7], v[8:9] op_sel:[0,0,1] op_sel_hi:[1,1,0] neg_lo:[0,0,1] neg_hi:[0,0,1]
	v_pk_fma_f32 v[6:7], v[4:5], v[6:7], v[8:9] op_sel:[0,0,1] op_sel_hi:[0,1,0]
	v_addc_co_u32_e64 v13, vcc, 0, v3, s[12:13]
	v_mov_b32_e32 v11, v7
	v_add_co_u32_e32 v8, vcc, 0x3b09a000, v2
	s_waitcnt vmcnt(9)
	v_pk_add_f32 v[6:7], v[16:17], v[10:11]
	s_mov_b64 s[6:7], vcc
	v_add_co_u32_e32 v10, vcc, 0x3a87a000, v2
	global_store_dwordx2 v[12:13], v[6:7], off offset:1024
	s_nop 0
	v_addc_co_u32_e32 v11, vcc, 0, v3, vcc
	global_load_dwordx2 v[10:11], v[10:11], off offset:1024
	v_add_co_u32_e32 v14, vcc, 0x3b0a2000, v2
	s_mov_b64 s[12:13], vcc
	v_add_co_u32_e32 v16, vcc, 0x3a882000, v2
	v_pk_mul_f32 v[12:13], v[4:5], v[6:7] op_sel:[1,0]
	s_nop 0
	v_addc_co_u32_e32 v17, vcc, 0, v3, vcc
	global_load_dwordx2 v[16:17], v[16:17], off offset:1024
	v_pk_fma_f32 v[40:41], v[4:5], v[6:7], v[12:13] op_sel:[0,0,1] op_sel_hi:[1,1,0] neg_lo:[0,0,1] neg_hi:[0,0,1]
	v_pk_fma_f32 v[6:7], v[4:5], v[6:7], v[12:13] op_sel:[0,0,1] op_sel_hi:[0,1,0]
	v_mov_b32_e32 v41, v7
	s_waitcnt vmcnt(9)
	v_pk_add_f32 v[6:7], v[18:19], v[40:41]
	v_addc_co_u32_e64 v21, vcc, 0, v3, s[4:5]
	v_pk_mul_f32 v[12:13], v[4:5], v[6:7] op_sel:[1,0]
	global_store_dwordx2 v[20:21], v[6:7], off offset:1024
	v_pk_fma_f32 v[18:19], v[4:5], v[6:7], v[12:13] op_sel:[0,0,1] op_sel_hi:[1,1,0] neg_lo:[0,0,1] neg_hi:[0,0,1]
	v_pk_fma_f32 v[6:7], v[4:5], v[6:7], v[12:13] op_sel:[0,0,1] op_sel_hi:[0,1,0]
	v_mov_b32_e32 v19, v7
	s_waitcnt vmcnt(9)
	v_pk_add_f32 v[6:7], v[22:23], v[18:19]
	v_addc_co_u32_e64 v25, vcc, 0, v3, s[8:9]
	v_pk_mul_f32 v[12:13], v[4:5], v[6:7] op_sel:[1,0]
	global_store_dwordx2 v[24:25], v[6:7], off offset:1024
	v_pk_fma_f32 v[18:19], v[4:5], v[6:7], v[12:13] op_sel:[0,0,1] op_sel_hi:[1,1,0] neg_lo:[0,0,1] neg_hi:[0,0,1]
	v_pk_fma_f32 v[6:7], v[4:5], v[6:7], v[12:13] op_sel:[0,0,1] op_sel_hi:[0,1,0]
	v_mov_b32_e32 v19, v7
	s_waitcnt vmcnt(9)
	v_pk_add_f32 v[6:7], v[26:27], v[18:19]
	v_addc_co_u32_e64 v29, vcc, 0, v3, s[10:11]
	v_pk_mul_f32 v[12:13], v[4:5], v[6:7] op_sel:[1,0]
	global_store_dwordx2 v[28:29], v[6:7], off offset:1024
	v_pk_fma_f32 v[18:19], v[4:5], v[6:7], v[12:13] op_sel:[0,0,1] op_sel_hi:[1,1,0] neg_lo:[0,0,1] neg_hi:[0,0,1]
	v_pk_fma_f32 v[6:7], v[4:5], v[6:7], v[12:13] op_sel:[0,0,1] op_sel_hi:[0,1,0]
	v_mov_b32_e32 v19, v7
	s_waitcnt vmcnt(9)
	v_pk_add_f32 v[6:7], v[30:31], v[18:19]
	v_addc_co_u32_e64 v33, vcc, 0, v3, s[0:1]
	v_pk_mul_f32 v[12:13], v[4:5], v[6:7] op_sel:[1,0]
	global_store_dwordx2 v[32:33], v[6:7], off offset:1024
	v_pk_fma_f32 v[18:19], v[4:5], v[6:7], v[12:13] op_sel:[0,0,1] op_sel_hi:[1,1,0] neg_lo:[0,0,1] neg_hi:[0,0,1]
	v_pk_fma_f32 v[6:7], v[4:5], v[6:7], v[12:13] op_sel:[0,0,1] op_sel_hi:[0,1,0]
	v_mov_b32_e32 v19, v7
	s_waitcnt vmcnt(9)
	v_pk_add_f32 v[6:7], v[34:35], v[18:19]
	v_addc_co_u32_e64 v37, vcc, 0, v3, s[14:15]
	v_pk_mul_f32 v[12:13], v[4:5], v[6:7] op_sel:[1,0]
	global_store_dwordx2 v[36:37], v[6:7], off offset:1024
	v_pk_fma_f32 v[18:19], v[4:5], v[6:7], v[12:13] op_sel:[0,0,1] op_sel_hi:[1,1,0] neg_lo:[0,0,1] neg_hi:[0,0,1]
	v_pk_fma_f32 v[6:7], v[4:5], v[6:7], v[12:13] op_sel:[0,0,1] op_sel_hi:[0,1,0]
	v_mov_b32_e32 v19, v7
	v_addc_co_u32_e64 v9, vcc, 0, v3, s[6:7]
	s_waitcnt vmcnt(9)
; __device__ __forceinline__ void phase_s5b_gqa(const Params& P, unsigned char* smraw, int bid, int nb) {
;     ...
;         for (int c0 = 0; c0 < 260; c0 += 20) {
;             float2 e[20];
; #pragma unroll
;             for (int j = 0; j < 20; ++j) e[j] = SE[(size_t)(c0 + j) * 4096 + i];
; #pragma unroll
;             for (int j = 0; j < 20; ++j) {
;                 CIN[(size_t)(c0 + j) * 4096 + i] = make_float2(sr, si);
;                 const float nr = a.x * sr - a.y * si + e[j].x, ni = a.x * si + a.y * sr + e[j].y;
;                 sr = nr; si = ni;
;             }
	v_pk_add_f32 v[6:7], v[38:39], v[18:19]
	global_store_dwordx2 v[8:9], v[6:7], off offset:1024
	v_pk_mul_f32 v[8:9], v[4:5], v[6:7] op_sel:[1,0]
	s_nop 0
	v_pk_fma_f32 v[12:13], v[4:5], v[6:7], v[8:9] op_sel:[0,0,1] op_sel_hi:[1,1,0] neg_lo:[0,0,1] neg_hi:[0,0,1]
	v_pk_fma_f32 v[6:7], v[4:5], v[6:7], v[8:9] op_sel:[0,0,1] op_sel_hi:[0,1,0]
	v_add_co_u32_e32 v6, vcc, 0x3b0aa000, v2
	s_mov_b64 s[0:1], vcc
	v_add_co_u32_e32 v8, vcc, 0x3a88a000, v2
	v_mov_b32_e32 v13, v7
	s_nop 0
	v_addc_co_u32_e32 v9, vcc, 0, v3, vcc
	global_load_dwordx2 v[8:9], v[8:9], off offset:1024
	v_add_co_u32_e32 v18, vcc, 0x3b0b2000, v2
	s_mov_b64 s[6:7], vcc
	v_add_co_u32_e32 v20, vcc, 0x3a892000, v2
	s_waitcnt vmcnt(8)
	v_pk_add_f32 v[10:11], v[10:11], v[12:13]
	v_addc_co_u32_e32 v21, vcc, 0, v3, vcc
	global_load_dwordx2 v[20:21], v[20:21], off offset:1024
	v_addc_co_u32_e64 v15, vcc, 0, v3, s[12:13]
	v_pk_mul_f32 v[12:13], v[4:5], v[10:11] op_sel:[1,0]
	global_store_dwordx2 v[14:15], v[10:11], off offset:1024
	v_pk_fma_f32 v[14:15], v[4:5], v[10:11], v[12:13] op_sel:[0,0,1] op_sel_hi:[1,1,0] neg_lo:[0,0,1] neg_hi:[0,0,1]
	v_pk_fma_f32 v[10:11], v[4:5], v[10:11], v[12:13] op_sel:[0,0,1] op_sel_hi:[0,1,0]
	v_addc_co_u32_e64 v7, vcc, 0, v3, s[0:1]
	v_mov_b32_e32 v15, v11
	v_add_co_u32_e32 v12, vcc, 0x3b0ba000, v2
	s_waitcnt vmcnt(9)
	v_pk_add_f32 v[10:11], v[16:17], v[14:15]
	s_mov_b64 s[12:13], vcc
	v_add_co_u32_e32 v14, vcc, 0x3a89a000, v2
	global_store_dwordx2 v[6:7], v[10:11], off offset:1024
	s_nop 0
	v_addc_co_u32_e32 v15, vcc, 0, v3, vcc
	v_add_co_u32_e32 v16, vcc, 0x3b0c2000, v2
	s_mov_b64 s[4:5], vcc
	v_add_co_u32_e32 v22, vcc, 0x3a8a2000, v2
	v_pk_mul_f32 v[6:7], v[4:5], v[10:11] op_sel:[1,0]
	s_nop 0
	v_addc_co_u32_e32 v23, vcc, 0, v3, vcc
	global_load_dwordx2 v[22:23], v[22:23], off offset:1024
	v_add_co_u32_e32 v24, vcc, 0x3b0ca000, v2
	global_load_dwordx2 v[14:15], v[14:15], off offset:1024
	s_mov_b64 s[8:9], vcc
	v_add_co_u32_e32 v26, vcc, 0x3a8aa000, v2
	v_pk_fma_f32 v[40:41], v[4:5], v[10:11], v[6:7] op_sel:[0,0,1] op_sel_hi:[1,1,0] neg_lo:[0,0,1] neg_hi:[0,0,1]
	s_nop 0
	v_addc_co_u32_e32 v27, vcc, 0, v3, vcc
	global_load_dwordx2 v[26:27], v[26:27], off offset:1024
	v_add_co_u32_e32 v28, vcc, 0x3b0d2000, v2
	s_mov_b64 s[10:11], vcc
	v_add_co_u32_e32 v30, vcc, 0x3a8b2000, v2
	v_pk_fma_f32 v[6:7], v[4:5], v[10:11], v[6:7] op_sel:[0,0,1] op_sel_hi:[0,1,0]
	s_nop 0
	v_addc_co_u32_e32 v31, vcc, 0, v3, vcc
	global_load_dwordx2 v[30:31], v[30:31], off offset:1024
	v_add_co_u32_e32 v32, vcc, 0x3b0da000, v2
	s_mov_b64 s[0:1], vcc
	v_add_co_u32_e32 v34, vcc, 0x3a8ba000, v2
	v_mov_b32_e32 v41, v7
	s_nop 0
	v_addc_co_u32_e32 v35, vcc, 0, v3, vcc
	global_load_dwordx2 v[34:35], v[34:35], off offset:1024
	v_add_co_u32_e32 v36, vcc, 0x3b0e2000, v2
	s_mov_b64 s[14:15], vcc
	v_add_co_u32_e32 v38, vcc, 0x3a8c2000, v2
	s_waitcnt vmcnt(8)
	v_pk_add_f32 v[6:7], v[8:9], v[40:41]
	v_addc_co_u32_e32 v39, vcc, 0, v3, vcc
	global_load_dwordx2 v[38:39], v[38:39], off offset:1024
	v_addc_co_u32_e64 v19, vcc, 0, v3, s[6:7]
	v_pk_mul_f32 v[8:9], v[4:5], v[6:7] op_sel:[1,0]
	global_store_dwordx2 v[18:19], v[6:7], off offset:1024
	v_pk_fma_f32 v[10:11], v[4:5], v[6:7], v[8:9] op_sel:[0,0,1] op_sel_hi:[1,1,0] neg_lo:[0,0,1] neg_hi:[0,0,1]
	v_pk_fma_f32 v[6:7], v[4:5], v[6:7], v[8:9] op_sel:[0,0,1] op_sel_hi:[0,1,0]
	v_addc_co_u32_e64 v13, vcc, 0, v3, s[12:13]
	v_mov_b32_e32 v11, v7
	v_add_co_u32_e32 v8, vcc, 0x3b0ea000, v2
	s_waitcnt vmcnt(9)
	v_pk_add_f32 v[6:7], v[10:11], v[20:21]
	s_mov_b64 s[6:7], vcc
	v_add_co_u32_e32 v10, vcc, 0x3a8ca000, v2
	global_store_dwordx2 v[12:13], v[6:7], off offset:1024
	s_nop 0
	v_addc_co_u32_e32 v11, vcc, 0, v3, vcc
	global_load_dwordx2 v[10:11], v[10:11], off offset:1024
	v_add_co_u32_e32 v18, vcc, 0x3b0f2000, v2
	s_mov_b64 s[12:13], vcc
	v_add_co_u32_e32 v20, vcc, 0x3a8d2000, v2
	v_pk_mul_f32 v[12:13], v[4:5], v[6:7] op_sel:[1,1] op_sel_hi:[0,1]
	s_nop 0
	v_addc_co_u32_e32 v21, vcc, 0, v3, vcc
	global_load_dwordx2 v[20:21], v[20:21], off offset:1024
	v_pk_fma_f32 v[40:41], v[4:5], v[6:7], v[12:13] neg_lo:[0,0,1] neg_hi:[0,0,1]
	v_pk_fma_f32 v[6:7], v[4:5], v[6:7], v[12:13] op_sel_hi:[1,0,1]
	v_addc_co_u32_e64 v17, vcc, 0, v3, s[4:5]
	v_mov_b32_e32 v41, v7
	v_addc_co_u32_e64 v25, vcc, 0, v3, s[8:9]
	s_waitcnt vmcnt(8)
	v_pk_add_f32 v[6:7], v[14:15], v[40:41]
	global_store_dwordx2 v[16:17], v[6:7], off offset:1024
	v_pk_mul_f32 v[12:13], v[4:5], v[6:7] op_sel:[1,0]
	v_addc_co_u32_e64 v29, vcc, 0, v3, s[10:11]
	v_pk_fma_f32 v[14:15], v[4:5], v[6:7], v[12:13] op_sel:[0,0,1] op_sel_hi:[1,1,0] neg_lo:[0,0,1] neg_hi:[0,0,1]
	v_pk_fma_f32 v[6:7], v[4:5], v[6:7], v[12:13] op_sel:[0,0,1] op_sel_hi:[0,1,0]
	v_mov_b32_e32 v15, v7
	v_pk_add_f32 v[6:7], v[22:23], v[14:15]
	global_store_dwordx2 v[24:25], v[6:7], off offset:1024
	v_pk_mul_f32 v[12:13], v[4:5], v[6:7] op_sel:[1,0]
	v_addc_co_u32_e64 v33, vcc, 0, v3, s[0:1]
	v_pk_fma_f32 v[14:15], v[4:5], v[6:7], v[12:13] op_sel:[0,0,1] op_sel_hi:[1,1,0] neg_lo:[0,0,1] neg_hi:[0,0,1]
	v_pk_fma_f32 v[6:7], v[4:5], v[6:7], v[12:13] op_sel:[0,0,1] op_sel_hi:[0,1,0]
	v_mov_b32_e32 v15, v7
	s_waitcnt vmcnt(9)
	v_pk_add_f32 v[6:7], v[26:27], v[14:15]
	global_store_dwordx2 v[28:29], v[6:7], off offset:1024
	v_pk_mul_f32 v[12:13], v[4:5], v[6:7] op_sel:[1,0]
	v_addc_co_u32_e64 v37, vcc, 0, v3, s[14:15]
	v_pk_fma_f32 v[14:15], v[4:5], v[6:7], v[12:13] op_sel:[0,0,1] op_sel_hi:[1,1,0] neg_lo:[0,0,1] neg_hi:[0,0,1]
	v_pk_fma_f32 v[6:7], v[4:5], v[6:7], v[12:13] op_sel:[0,0,1] op_sel_hi:[0,1,0]
	v_mov_b32_e32 v15, v7
	s_waitcnt vmcnt(9)
; __device__ __forceinline__ void phase_s5b_gqa(const Params& P, unsigned char* smraw, int bid, int nb) {
;     ...
;         for (int c0 = 0; c0 < 260; c0 += 20) {
;             float2 e[20];
; #pragma unroll
;             for (int j = 0; j < 20; ++j) e[j] = SE[(size_t)(c0 + j) * 4096 + i];
; #pragma unroll
;             for (int j = 0; j < 20; ++j) {
;                 CIN[(size_t)(c0 + j) * 4096 + i] = make_float2(sr, si);
;                 const float nr = a.x * sr - a.y * si + e[j].x, ni = a.x * si + a.y * sr + e[j].y;
;                 sr = nr; si = ni;
;             }
	v_pk_add_f32 v[6:7], v[30:31], v[14:15]
	global_store_dwordx2 v[32:33], v[6:7], off offset:1024
	v_pk_mul_f32 v[12:13], v[4:5], v[6:7] op_sel:[1,0]
	v_addc_co_u32_e64 v9, vcc, 0, v3, s[6:7]
	v_pk_fma_f32 v[14:15], v[4:5], v[6:7], v[12:13] op_sel:[0,0,1] op_sel_hi:[1,1,0] neg_lo:[0,0,1] neg_hi:[0,0,1]
	v_pk_fma_f32 v[6:7], v[4:5], v[6:7], v[12:13] op_sel:[0,0,1] op_sel_hi:[0,1,0]
	v_mov_b32_e32 v15, v7
	s_waitcnt vmcnt(9)
	v_pk_add_f32 v[6:7], v[34:35], v[14:15]
	global_store_dwordx2 v[36:37], v[6:7], off offset:1024
	v_pk_mul_f32 v[12:13], v[4:5], v[6:7] op_sel:[1,0]
	s_nop 0
	v_pk_fma_f32 v[14:15], v[4:5], v[6:7], v[12:13] op_sel:[0,0,1] op_sel_hi:[1,1,0] neg_lo:[0,0,1] neg_hi:[0,0,1]
	v_pk_fma_f32 v[6:7], v[4:5], v[6:7], v[12:13] op_sel:[0,0,1] op_sel_hi:[0,1,0]
	v_mov_b32_e32 v15, v7
	s_waitcnt vmcnt(9)
	v_pk_add_f32 v[6:7], v[38:39], v[14:15]
	global_store_dwordx2 v[8:9], v[6:7], off offset:1024
	v_pk_mul_f32 v[8:9], v[4:5], v[6:7] op_sel:[1,0]
	s_nop 0
	v_pk_fma_f32 v[12:13], v[4:5], v[6:7], v[8:9] op_sel:[0,0,1] op_sel_hi:[1,1,0] neg_lo:[0,0,1] neg_hi:[0,0,1]
	v_pk_fma_f32 v[6:7], v[4:5], v[6:7], v[8:9] op_sel:[0,0,1] op_sel_hi:[0,1,0]
	v_add_co_u32_e32 v6, vcc, 0x3b0fa000, v2
	s_mov_b64 s[0:1], vcc
	v_add_co_u32_e32 v8, vcc, 0x3a8da000, v2
	v_mov_b32_e32 v13, v7
	s_nop 0
	v_addc_co_u32_e32 v9, vcc, 0, v3, vcc
	v_add_co_u32_e32 v14, vcc, 0x3b102000, v2
	s_mov_b64 s[4:5], vcc
	v_add_co_u32_e32 v16, vcc, 0x3a8e2000, v2
	s_waitcnt vmcnt(7)
	v_pk_add_f32 v[10:11], v[10:11], v[12:13]
	v_addc_co_u32_e32 v17, vcc, 0, v3, vcc
	global_load_dwordx2 v[8:9], v[8:9], off offset:1024
	s_nop 0
	global_load_dwordx2 v[16:17], v[16:17], off offset:1024
	v_addc_co_u32_e64 v19, vcc, 0, v3, s[12:13]
	v_pk_mul_f32 v[12:13], v[4:5], v[10:11] op_sel:[1,0]
	global_store_dwordx2 v[18:19], v[10:11], off offset:1024
	v_pk_fma_f32 v[18:19], v[4:5], v[10:11], v[12:13] op_sel:[0,0,1] op_sel_hi:[1,1,0] neg_lo:[0,0,1] neg_hi:[0,0,1]
	v_pk_fma_f32 v[10:11], v[4:5], v[10:11], v[12:13] op_sel:[0,0,1] op_sel_hi:[0,1,0]
	v_addc_co_u32_e64 v7, vcc, 0, v3, s[0:1]
	v_mov_b32_e32 v19, v11
	v_add_co_u32_e32 v12, vcc, 0x3b10a000, v2
	s_waitcnt vmcnt(9)
	v_pk_add_f32 v[10:11], v[20:21], v[18:19]
	s_mov_b64 s[8:9], vcc
	v_add_co_u32_e32 v18, vcc, 0x3a8ea000, v2
	global_store_dwordx2 v[6:7], v[10:11], off offset:1024
	s_nop 0
	v_addc_co_u32_e32 v19, vcc, 0, v3, vcc
	global_load_dwordx2 v[18:19], v[18:19], off offset:1024
	v_add_co_u32_e32 v20, vcc, 0x3b112000, v2
	s_mov_b64 s[6:7], vcc
	v_add_co_u32_e32 v22, vcc, 0x3a8f2000, v2
	v_pk_mul_f32 v[6:7], v[4:5], v[10:11] op_sel:[1,0]
	s_nop 0
	v_addc_co_u32_e32 v23, vcc, 0, v3, vcc
	global_load_dwordx2 v[22:23], v[22:23], off offset:1024
	v_add_co_u32_e32 v24, vcc, 0x3b11a000, v2
	s_mov_b64 s[12:13], vcc
	v_add_co_u32_e32 v26, vcc, 0x3a8fa000, v2
	v_pk_fma_f32 v[40:41], v[4:5], v[10:11], v[6:7] op_sel:[0,0,1] op_sel_hi:[1,1,0] neg_lo:[0,0,1] neg_hi:[0,0,1]
	s_nop 0
	v_addc_co_u32_e32 v27, vcc, 0, v3, vcc
	global_load_dwordx2 v[26:27], v[26:27], off offset:1024
	v_add_co_u32_e32 v28, vcc, 0x3b122000, v2
	s_mov_b64 s[10:11], vcc
	v_add_co_u32_e32 v30, vcc, 0x3a902000, v2
	v_pk_fma_f32 v[6:7], v[4:5], v[10:11], v[6:7] op_sel:[0,0,1] op_sel_hi:[0,1,0]
	s_nop 0
	v_addc_co_u32_e32 v31, vcc, 0, v3, vcc
	global_load_dwordx2 v[30:31], v[30:31], off offset:1024
	v_add_co_u32_e32 v32, vcc, 0x3b12a000, v2
	s_mov_b64 s[0:1], vcc
	v_add_co_u32_e32 v34, vcc, 0x3a90a000, v2
	v_mov_b32_e32 v41, v7
	s_nop 0
	v_addc_co_u32_e32 v35, vcc, 0, v3, vcc
	global_load_dwordx2 v[34:35], v[34:35], off offset:1024
	v_add_co_u32_e32 v36, vcc, 0x3b132000, v2
	s_mov_b64 s[14:15], vcc
	v_add_co_u32_e32 v38, vcc, 0x3a912000, v2
	s_waitcnt vmcnt(8)
; __device__ __forceinline__ void phase_s5b_gqa(const Params& P, unsigned char* smraw, int bid, int nb) {
;     ...
;         for (int c0 = 0; c0 < 260; c0 += 20) {
;             float2 e[20];
; #pragma unroll
;             for (int j = 0; j < 20; ++j) e[j] = SE[(size_t)(c0 + j) * 4096 + i];
; #pragma unroll
;             for (int j = 0; j < 20; ++j) {
;                 CIN[(size_t)(c0 + j) * 4096 + i] = make_float2(sr, si);
;                 const float nr = a.x * sr - a.y * si + e[j].x, ni = a.x * si + a.y * sr + e[j].y;
;                 sr = nr; si = ni;
;             }
;         }
;     }
	v_pk_add_f32 v[6:7], v[8:9], v[40:41]
	v_addc_co_u32_e32 v39, vcc, 0, v3, vcc
	global_load_dwordx2 v[38:39], v[38:39], off offset:1024
	v_add_co_u32_e32 v42, vcc, 0x3b13a000, v2
	s_mov_b64 s[16:17], vcc
	v_add_co_u32_e32 v44, vcc, 0x3a91a000, v2
	v_pk_mul_f32 v[8:9], v[4:5], v[6:7] op_sel:[1,0]
	s_nop 0
	v_addc_co_u32_e32 v45, vcc, 0, v3, vcc
	global_load_dwordx2 v[44:45], v[44:45], off offset:1024
	v_add_co_u32_e32 v46, vcc, 0x3b142000, v2
	s_mov_b64 s[18:19], vcc
	v_add_co_u32_e32 v48, vcc, 0x3a922000, v2
	v_pk_fma_f32 v[10:11], v[4:5], v[6:7], v[8:9] op_sel:[0,0,1] op_sel_hi:[1,1,0] neg_lo:[0,0,1] neg_hi:[0,0,1]
	s_nop 0
	v_addc_co_u32_e32 v49, vcc, 0, v3, vcc
	global_load_dwordx2 v[48:49], v[48:49], off offset:1024
	v_addc_co_u32_e64 v15, vcc, 0, v3, s[4:5]
	global_store_dwordx2 v[14:15], v[6:7], off offset:1024
	v_pk_fma_f32 v[6:7], v[4:5], v[6:7], v[8:9] op_sel:[0,0,1] op_sel_hi:[0,1,0]
	v_mov_b32_e32 v11, v7
	s_waitcnt vmcnt(11)
	v_pk_add_f32 v[6:7], v[16:17], v[10:11]
	v_addc_co_u32_e64 v13, vcc, 0, v3, s[8:9]
	v_pk_mul_f32 v[8:9], v[4:5], v[6:7] op_sel:[1,0]
	global_store_dwordx2 v[12:13], v[6:7], off offset:1024
	v_pk_fma_f32 v[10:11], v[4:5], v[6:7], v[8:9] op_sel:[0,0,1] op_sel_hi:[1,1,0] neg_lo:[0,0,1] neg_hi:[0,0,1]
	v_pk_fma_f32 v[6:7], v[4:5], v[6:7], v[8:9] op_sel:[0,0,1] op_sel_hi:[0,1,0]
	v_mov_b32_e32 v11, v7
	s_waitcnt vmcnt(9)
	v_pk_add_f32 v[6:7], v[18:19], v[10:11]
	v_addc_co_u32_e64 v21, vcc, 0, v3, s[6:7]
	v_pk_mul_f32 v[8:9], v[4:5], v[6:7] op_sel:[1,0]
	global_store_dwordx2 v[20:21], v[6:7], off offset:1024
	v_pk_fma_f32 v[10:11], v[4:5], v[6:7], v[8:9] op_sel:[0,0,1] op_sel_hi:[1,1,0] neg_lo:[0,0,1] neg_hi:[0,0,1]
	v_pk_fma_f32 v[6:7], v[4:5], v[6:7], v[8:9] op_sel:[0,0,1] op_sel_hi:[0,1,0]
	v_mov_b32_e32 v11, v7
	s_waitcnt vmcnt(9)
	v_pk_add_f32 v[6:7], v[22:23], v[10:11]
	v_addc_co_u32_e64 v25, vcc, 0, v3, s[12:13]
	v_pk_mul_f32 v[8:9], v[4:5], v[6:7] op_sel:[1,0]
	global_store_dwordx2 v[24:25], v[6:7], off offset:1024
	v_pk_fma_f32 v[10:11], v[4:5], v[6:7], v[8:9] op_sel:[0,0,1] op_sel_hi:[1,1,0] neg_lo:[0,0,1] neg_hi:[0,0,1]
	v_pk_fma_f32 v[6:7], v[4:5], v[6:7], v[8:9] op_sel:[0,0,1] op_sel_hi:[0,1,0]
	v_mov_b32_e32 v11, v7
	s_waitcnt vmcnt(9)
	v_pk_add_f32 v[6:7], v[26:27], v[10:11]
	v_addc_co_u32_e64 v29, vcc, 0, v3, s[10:11]
	v_pk_mul_f32 v[8:9], v[4:5], v[6:7] op_sel:[1,0]
	global_store_dwordx2 v[28:29], v[6:7], off offset:1024
	v_pk_fma_f32 v[10:11], v[4:5], v[6:7], v[8:9] op_sel:[0,0,1] op_sel_hi:[1,1,0] neg_lo:[0,0,1] neg_hi:[0,0,1]
	v_pk_fma_f32 v[6:7], v[4:5], v[6:7], v[8:9] op_sel:[0,0,1] op_sel_hi:[0,1,0]
	v_mov_b32_e32 v11, v7
	s_waitcnt vmcnt(9)
	v_pk_add_f32 v[6:7], v[30:31], v[10:11]
	v_addc_co_u32_e64 v33, vcc, 0, v3, s[0:1]
	v_pk_mul_f32 v[8:9], v[4:5], v[6:7] op_sel:[1,0]
	global_store_dwordx2 v[32:33], v[6:7], off offset:1024
	v_pk_fma_f32 v[10:11], v[4:5], v[6:7], v[8:9] op_sel:[0,0,1] op_sel_hi:[1,1,0] neg_lo:[0,0,1] neg_hi:[0,0,1]
	v_pk_fma_f32 v[6:7], v[4:5], v[6:7], v[8:9] op_sel:[0,0,1] op_sel_hi:[0,1,0]
	v_mov_b32_e32 v11, v7
	s_waitcnt vmcnt(9)
	v_pk_add_f32 v[6:7], v[34:35], v[10:11]
	v_addc_co_u32_e64 v37, vcc, 0, v3, s[14:15]
	v_pk_mul_f32 v[8:9], v[4:5], v[6:7] op_sel:[1,0]
	global_store_dwordx2 v[36:37], v[6:7], off offset:1024
	v_pk_fma_f32 v[10:11], v[4:5], v[6:7], v[8:9] op_sel:[0,0,1] op_sel_hi:[1,1,0] neg_lo:[0,0,1] neg_hi:[0,0,1]
	v_pk_fma_f32 v[6:7], v[4:5], v[6:7], v[8:9] op_sel:[0,0,1] op_sel_hi:[0,1,0]
	v_mov_b32_e32 v11, v7
	v_addc_co_u32_e64 v43, vcc, 0, v3, s[16:17]
	v_add_co_u32_e32 v12, vcc, 0x3b14a000, v2
	s_waitcnt vmcnt(9)
	v_pk_add_f32 v[6:7], v[38:39], v[10:11]
	s_nop 0
	v_pk_mul_f32 v[8:9], v[4:5], v[6:7] op_sel:[1,0]
	global_store_dwordx2 v[42:43], v[6:7], off offset:1024
	v_pk_fma_f32 v[10:11], v[4:5], v[6:7], v[8:9] op_sel:[0,0,1] op_sel_hi:[1,1,0] neg_lo:[0,0,1] neg_hi:[0,0,1]
	v_pk_fma_f32 v[6:7], v[4:5], v[6:7], v[8:9] op_sel:[0,0,1] op_sel_hi:[0,1,0]
	v_mov_b32_e32 v11, v7
	v_addc_co_u32_e32 v13, vcc, 0, v3, vcc
	v_addc_co_u32_e64 v47, vcc, 0, v3, s[18:19]
	s_waitcnt vmcnt(9)
	v_pk_add_f32 v[6:7], v[44:45], v[10:11]
	global_store_dwordx2 v[46:47], v[6:7], off offset:1024
	v_pk_mul_f32 v[8:9], v[4:5], v[6:7] op_sel:[1,0]
	s_nop 0
	v_pk_fma_f32 v[10:11], v[4:5], v[6:7], v[8:9] op_sel:[0,0,1] op_sel_hi:[1,1,0] neg_lo:[0,0,1] neg_hi:[0,0,1]
	v_pk_fma_f32 v[2:3], v[4:5], v[6:7], v[8:9] op_sel:[0,0,1] op_sel_hi:[0,1,0]
	v_mov_b32_e32 v11, v3
	s_waitcnt vmcnt(9)
	v_pk_add_f32 v[2:3], v[48:49], v[10:11]
	global_store_dwordx2 v[12:13], v[2:3], off offset:1024
.Lscan_skip:
	s_mov_b64 exec, s[98:99]

;     __device__ __forceinline__ void mainloop(bfr* smem, const AL& al, const BL& bl) {
;     ...
;             for (int kt = 0; kt < nk; kt += 6) {
;                 G_STEP3(0, 1, sa0, sb0, 2, 2);
;                 G_STEP3(1, 2, sa1, sb1, 0, 2);
;                 G_STEP3(2, 0, sa0, sb0, 1, 2);
;                 G_STEP3(3, 1, sa1, sb1, 2, 2);
;                 G_STEP3(4, 2, sa0, sb0, 0, 2);
;                 G_STEP3(5, 0, sa1, sb1, 1, 2);
;             }
.LBB0_2575:
	s_or_b64 exec, exec, s[2:3]
	v_add_co_u32_e32 v130, vcc, 0xf8000, v220
	s_nop 1
	v_addc_co_u32_e32 v131, vcc, 0, v221, vcc
	global_load_dwordx4 v[138:141], v[130:131], off
	global_load_dwordx4 v[142:145], v[130:131], off offset:1024
	global_load_dwordx4 v[134:137], v[130:131], off offset:2048
	s_nop 0
	global_load_dwordx4 v[130:133], v[130:131], off offset:3072
	v_mfma_f32_32x32x16_bf16 v[34:49], v[170:173], v[190:193], v[34:49]
	ds_read_b128 v[146:149], v227 offset:17968
	v_mfma_f32_32x32x16_bf16 v[18:33], v[174:177], v[182:185], v[18:33]
	ds_read_b64_tr_b16 v[182:183], v229
	ds_read_b64_tr_b16 v[184:185], v229 offset:2304
	v_mfma_f32_32x32x16_bf16 v[2:17], v[174:177], v[190:193], v[2:17]
	s_waitcnt lgkmcnt(10)
	v_mfma_f32_32x32x16_bf16 v[82:97], v[158:161], v[178:181], v[82:97]
	ds_read_b128 v[154:157], v227 offset:20528
	ds_read_b64_tr_b16 v[198:199], v230 offset:64
	ds_read_b64_tr_b16 v[200:201], v230 offset:2368
	s_waitcnt lgkmcnt(3)
	s_barrier
	v_mfma_f32_32x32x16_bf16 v[66:81], v[158:161], v[186:189], v[66:81]
	ds_read_b128 v[158:161], v227 offset:30736
	v_mfma_f32_32x32x16_bf16 v[50:65], v[162:165], v[178:181], v[50:65]
	v_mfma_f32_32x32x16_bf16 v[34:49], v[162:165], v[186:189], v[34:49]
	ds_read_b128 v[162:165], v227 offset:33296
	v_mfma_f32_32x32x16_bf16 v[18:33], v[166:169], v[178:181], v[18:33]
	ds_read_b64_tr_b16 v[190:191], v232
	ds_read_b64_tr_b16 v[192:193], v232 offset:2304
	v_mfma_f32_32x32x16_bf16 v[2:17], v[166:169], v[186:189], v[2:17]
	ds_read_b128 v[166:169], v227 offset:35856
	ds_read_b64_tr_b16 v[194:195], v232 offset:64
	ds_read_b64_tr_b16 v[196:197], v232 offset:2368
	v_mfma_f32_32x32x16_bf16 v[82:97], v[150:153], v[182:185], v[82:97]
	s_waitcnt vmcnt(9)
	ds_write_b128 v222, v[106:109] offset:16
	s_and_saveexec_b64 s[2:3], s[4:5]
	ds_write_b128 v223, v[98:101] offset:10256
	s_or_b64 exec, exec, s[2:3]
	s_waitcnt lgkmcnt(9)
	v_mfma_f32_32x32x16_bf16 v[66:81], v[150:153], v[198:201], v[66:81]
	ds_read_b128 v[170:173], v227 offset:30768
	s_waitcnt vmcnt(8)
	v_cvt_pk_bf16_f32 v150, v118, v119
	v_cvt_pk_bf16_f32 v151, v120, v121
	s_waitcnt vmcnt(7)
	v_cvt_pk_bf16_f32 v152, v122, v123
	v_cvt_pk_bf16_f32 v153, v124, v125
	ds_write2_b64 v205, v[150:151], v[152:153] offset0:130 offset1:202
	s_waitcnt vmcnt(6)
	v_cvt_pk_bf16_f32 v150, v110, v111
	v_cvt_pk_bf16_f32 v151, v112, v113
	s_waitcnt vmcnt(5)
	v_cvt_pk_bf16_f32 v152, v114, v115
	v_cvt_pk_bf16_f32 v153, v116, v117
	ds_write2_b64 v206, v[150:151], v[152:153] offset0:18 offset1:90
	v_mfma_f32_32x32x16_bf16 v[50:65], v[146:149], v[182:185], v[50:65]
	v_mfma_f32_32x32x16_bf16 v[34:49], v[146:149], v[198:201], v[34:49]
	ds_read_b128 v[174:177], v227 offset:33328
	v_mfma_f32_32x32x16_bf16 v[18:33], v[154:157], v[182:185], v[18:33]
	ds_read_b64_tr_b16 v[182:183], v233
	ds_read_b64_tr_b16 v[184:185], v233 offset:2304
	v_mfma_f32_32x32x16_bf16 v[2:17], v[154:157], v[198:201], v[2:17]
	s_waitcnt lgkmcnt(10)
	v_mfma_f32_32x32x16_bf16 v[82:97], v[158:161], v[190:193], v[82:97]
	ds_read_b128 v[178:181], v227 offset:35888
	ds_read_b64_tr_b16 v[186:187], v234 offset:64
	ds_read_b64_tr_b16 v[188:189], v234 offset:2368
	s_waitcnt lgkmcnt(3)
	s_barrier
; __device__ __forceinline__ void moe_unit(const int* pre, const int* lpre, int x, int lb, int& e, int& rb) {
;     if (lb < lpre[32]) {
;         int lo = 0, hi = 32;
;         while (hi - lo > 1) { const int mid = (lo + hi) >> 1; if (lpre[mid] <= lb) lo = mid; else hi = mid; }
;         e = x + 8 * lo; rb = lb - lpre[lo];
;     } else { e = 256; rb = (lb - lpre[32]) * 8 + x; }
	v_mfma_f32_32x32x16_bf16 v[66:81], v[158:161], v[194:197], v[66:81]
	ds_read_b128 v[154:157], v227 offset:16
	v_mfma_f32_32x32x16_bf16 v[50:65], v[162:165], v[190:193], v[50:65]
	v_mfma_f32_32x32x16_bf16 v[34:49], v[162:165], v[194:197], v[34:49]
	ds_read_b128 v[158:161], v227 offset:2576
	v_mfma_f32_32x32x16_bf16 v[18:33], v[166:169], v[190:193], v[18:33]
	ds_read_b64_tr_b16 v[162:163], v235 offset:46096
	ds_read_b64_tr_b16 v[164:165], v235 offset:48400
	v_mfma_f32_32x32x16_bf16 v[2:17], v[166:169], v[194:197], v[2:17]
	ds_read_b128 v[146:149], v227 offset:5136
	ds_read_b64_tr_b16 v[150:151], v235 offset:46160
	ds_read_b64_tr_b16 v[152:153], v235 offset:48464
	v_mfma_f32_32x32x16_bf16 v[82:97], v[170:173], v[182:185], v[82:97]
	s_waitcnt vmcnt(4)
	ds_write_b128 v222, v[126:129] offset:15376
	s_and_saveexec_b64 s[2:3], s[4:5]
	ds_write_b128 v223, v[102:105] offset:25616
	s_or_b64 exec, exec, s[2:3]
	s_waitcnt lgkmcnt(9)
	v_mfma_f32_32x32x16_bf16 v[66:81], v[170:173], v[186:189], v[66:81]
	ds_read_b128 v[166:169], v227 offset:48
	s_waitcnt vmcnt(3)
	v_cvt_pk_bf16_f32 v170, v138, v139
	v_cvt_pk_bf16_f32 v171, v140, v141
	s_waitcnt vmcnt(2)
	v_cvt_pk_bf16_f32 v172, v142, v143
	v_cvt_pk_bf16_f32 v173, v144, v145
	ds_write2_b64 v226, v[170:171], v[172:173] offset1:72
	s_waitcnt vmcnt(1)
	v_cvt_pk_bf16_f32 v170, v134, v135
	v_cvt_pk_bf16_f32 v171, v136, v137
	s_waitcnt vmcnt(0)
	v_cvt_pk_bf16_f32 v172, v130, v131
	v_cvt_pk_bf16_f32 v173, v132, v133
	ds_write2_b64 v226, v[170:171], v[172:173] offset0:144 offset1:216
	v_mfma_f32_32x32x16_bf16 v[50:65], v[174:177], v[182:185], v[50:65]
	v_mfma_f32_32x32x16_bf16 v[34:49], v[174:177], v[186:189], v[34:49]
	ds_read_b128 v[170:173], v227 offset:2608
	v_mfma_f32_32x32x16_bf16 v[18:33], v[178:181], v[182:185], v[18:33]
	ds_read_b64_tr_b16 v[174:175], v235 offset:55312
	ds_read_b64_tr_b16 v[176:177], v235 offset:57616
	v_mfma_f32_32x32x16_bf16 v[2:17], v[178:181], v[186:189], v[2:17]
	s_waitcnt lgkmcnt(10)
	v_mfma_f32_32x32x16_bf16 v[82:97], v[154:157], v[162:165], v[82:97]
	ds_read_b128 v[178:181], v227 offset:5168
	ds_read_b64_tr_b16 v[182:183], v235 offset:55376
	ds_read_b64_tr_b16 v[184:185], v235 offset:57680
	s_waitcnt lgkmcnt(3)
	s_barrier
	v_mfma_f32_32x32x16_bf16 v[66:81], v[154:157], v[150:153], v[66:81]
	ds_read_b128 v[154:157], v227 offset:15376
	v_mfma_f32_32x32x16_bf16 v[50:65], v[158:161], v[162:165], v[50:65]
	v_mfma_f32_32x32x16_bf16 v[34:49], v[158:161], v[150:153], v[34:49]
	ds_read_b128 v[158:161], v227 offset:17936
	v_mfma_f32_32x32x16_bf16 v[18:33], v[146:149], v[162:165], v[18:33]
	ds_read_b64_tr_b16 v[162:163], v228
	ds_read_b64_tr_b16 v[164:165], v228 offset:2304
	v_mfma_f32_32x32x16_bf16 v[2:17], v[146:149], v[150:153], v[2:17]
	ds_read_b128 v[146:149], v227 offset:20496
	ds_read_b64_tr_b16 v[150:151], v228 offset:64
	ds_read_b64_tr_b16 v[152:153], v228 offset:2368
	v_mfma_f32_32x32x16_bf16 v[82:97], v[166:169], v[174:177], v[82:97]
	s_waitcnt lgkmcnt(7)
	v_mfma_f32_32x32x16_bf16 v[66:81], v[166:169], v[182:185], v[66:81]
	ds_read_b128 v[166:169], v227 offset:15408
	v_mfma_f32_32x32x16_bf16 v[50:65], v[170:173], v[174:177], v[50:65]
	v_mfma_f32_32x32x16_bf16 v[34:49], v[170:173], v[182:185], v[34:49]
	ds_read_b128 v[170:173], v227 offset:17968
	v_mfma_f32_32x32x16_bf16 v[18:33], v[178:181], v[174:177], v[18:33]
	ds_read_b64_tr_b16 v[174:175], v229
	ds_read_b64_tr_b16 v[176:177], v229 offset:2304
	v_mfma_f32_32x32x16_bf16 v[2:17], v[178:181], v[182:185], v[2:17]
	s_waitcnt lgkmcnt(7)
	v_mfma_f32_32x32x16_bf16 v[82:97], v[154:157], v[162:165], v[82:97]
	ds_read_b128 v[178:181], v227 offset:20528
	ds_read_b64_tr_b16 v[182:183], v230 offset:64
	ds_read_b64_tr_b16 v[184:185], v230 offset:2368
	s_waitcnt lgkmcnt(3)
	s_barrier
	v_mfma_f32_32x32x16_bf16 v[66:81], v[154:157], v[150:153], v[66:81]
	v_mfma_f32_32x32x16_bf16 v[50:65], v[158:161], v[162:165], v[50:65]
	v_mfma_f32_32x32x16_bf16 v[34:49], v[158:161], v[150:153], v[34:49]
	v_mfma_f32_32x32x16_bf16 v[18:33], v[146:149], v[162:165], v[18:33]
	v_mfma_f32_32x32x16_bf16 v[2:17], v[146:149], v[150:153], v[2:17]
	v_mfma_f32_32x32x16_bf16 v[82:97], v[166:169], v[174:177], v[82:97]
	s_waitcnt lgkmcnt(0)
	v_mfma_f32_32x32x16_bf16 v[66:81], v[166:169], v[182:185], v[66:81]
	v_mfma_f32_32x32x16_bf16 v[50:65], v[170:173], v[174:177], v[50:65]
	v_mfma_f32_32x32x16_bf16 v[34:49], v[170:173], v[182:185], v[34:49]
	v_mfma_f32_32x32x16_bf16 v[18:33], v[178:181], v[174:177], v[18:33]
	v_mfma_f32_32x32x16_bf16 v[2:17], v[178:181], v[182:185], v[2:17]
	s_add_i32 s21, s21, s23
	s_cmp_ge_i32 s21, s22
	s_cselect_b64 s[2:3], -1, 0
	s_and_b64 vcc, exec, s[2:3]
	s_barrier
	s_cbranch_vccnz .LBB0_2597
	v_mov_b32_e32 v106, s35
	ds_read_b32 v106, v106
	s_ashr_i32 s0, s21, 1
	s_waitcnt lgkmcnt(0)
	v_cmp_ge_i32_e32 vcc, s0, v106
	s_cbranch_vccz .LBB0_2582
	v_sub_u32_e32 v106, s0, v106
	v_lshlrev_b32_e32 v106, 3, v106
	v_or_b32_e32 v146, s20, v106
	s_movk_i32 s14, 0x100
	s_cbranch_execz .LBB0_2583
	s_branch .LBB0_2586

.LBB0_2718:
	s_or_b64 exec, exec, s[12:13]
	v_add_co_u32_e32 v122, vcc, 0x80000, v212
	s_nop 1
	v_addc_co_u32_e32 v123, vcc, 0, v213, vcc
	v_add_co_u32_e32 v124, vcc, 0x81000, v212
	s_nop 1
	v_addc_co_u32_e32 v125, vcc, 0, v213, vcc
	v_add_co_u32_e32 v142, vcc, 0x82000, v212
	global_load_dwordx4 v[134:137], v[122:123], off
	s_nop 0
	global_load_dwordx4 v[122:125], v[124:125], off
	v_addc_co_u32_e32 v143, vcc, 0, v213, vcc
	v_add_co_u32_e32 v144, vcc, 0x83000, v212
	s_nop 1
	v_addc_co_u32_e32 v145, vcc, 0, v213, vcc
	global_load_dwordx4 v[150:153], v[142:143], off
	s_nop 0
	global_load_dwordx4 v[142:145], v[144:145], off
	v_mfma_f32_32x32x16_bf16 v[34:49], v[158:161], v[178:181], v[34:49]
	ds_read_b128 v[158:161], v218 offset:17968
	v_mfma_f32_32x32x16_bf16 v[18:33], v[162:165], v[182:185], v[18:33]
	ds_read_b64_tr_b16 v[182:183], v220
	ds_read_b64_tr_b16 v[184:185], v220 offset:2304
	v_mfma_f32_32x32x16_bf16 v[2:17], v[162:165], v[178:181], v[2:17]
	s_waitcnt lgkmcnt(10)
	v_mfma_f32_32x32x16_bf16 v[82:97], v[166:169], v[174:177], v[82:97]
	ds_read_b128 v[162:165], v218 offset:20528
	ds_read_b64_tr_b16 v[194:195], v221 offset:64
	ds_read_b64_tr_b16 v[196:197], v221 offset:2368
	s_waitcnt lgkmcnt(3)
	s_barrier
	v_mfma_f32_32x32x16_bf16 v[66:81], v[166:169], v[154:157], v[66:81]
	ds_read_b128 v[166:169], v218 offset:30736
	v_mfma_f32_32x32x16_bf16 v[50:65], v[170:173], v[174:177], v[50:65]
	v_mfma_f32_32x32x16_bf16 v[34:49], v[170:173], v[154:157], v[34:49]
	ds_read_b128 v[170:173], v218 offset:33296
	v_mfma_f32_32x32x16_bf16 v[18:33], v[138:141], v[174:177], v[18:33]
	ds_read_b64_tr_b16 v[178:179], v223
	ds_read_b64_tr_b16 v[180:181], v223 offset:2304
	v_mfma_f32_32x32x16_bf16 v[2:17], v[138:141], v[154:157], v[2:17]
	ds_read_b128 v[174:177], v218 offset:35856
	ds_read_b64_tr_b16 v[190:191], v223 offset:64
	ds_read_b64_tr_b16 v[192:193], v223 offset:2368
	v_mfma_f32_32x32x16_bf16 v[82:97], v[146:149], v[182:185], v[82:97]
	s_waitcnt vmcnt(9)
	ds_write_b128 v214, v[110:113] offset:16
	s_and_saveexec_b64 s[12:13], s[4:5]
	ds_write_b128 v215, v[102:105] offset:10256
	s_or_b64 exec, exec, s[12:13]
	s_waitcnt lgkmcnt(9)
	v_mfma_f32_32x32x16_bf16 v[66:81], v[146:149], v[194:197], v[66:81]
	ds_read_b128 v[110:113], v218 offset:30768
	s_waitcnt vmcnt(8)
	v_cvt_pk_bf16_f32 v118, v118, v119
	v_cvt_pk_bf16_f32 v119, v120, v121
	s_waitcnt vmcnt(7)
	v_cvt_pk_bf16_f32 v114, v114, v115
	v_cvt_pk_bf16_f32 v115, v116, v117
	ds_write2_b64 v198, v[118:119], v[114:115] offset0:130 offset1:202
	s_waitcnt vmcnt(6)
	v_cvt_pk_bf16_f32 v114, v130, v131
	v_cvt_pk_bf16_f32 v115, v132, v133
	s_waitcnt vmcnt(5)
	v_cvt_pk_bf16_f32 v116, v126, v127
	v_cvt_pk_bf16_f32 v117, v128, v129
	ds_write2_b64 v209, v[114:115], v[116:117] offset0:18 offset1:90
	v_mfma_f32_32x32x16_bf16 v[50:65], v[158:161], v[182:185], v[50:65]
	global_load_dwordx4 v[126:129], v[200:201], off offset:320
	s_and_saveexec_b64 s[12:13], s[4:5]
	s_cbranch_execz .LBB0_2722
	global_load_dwordx4 v[102:105], v[202:203], off offset:320
.LBB0_2722:
	s_or_b64 exec, exec, s[12:13]
	v_add_co_u32_e32 v114, vcc, 0xa0000, v212
	s_nop 1
	v_addc_co_u32_e32 v115, vcc, 0, v213, vcc
	v_add_co_u32_e32 v116, vcc, 0xa1000, v212
	s_nop 1
	v_addc_co_u32_e32 v117, vcc, 0, v213, vcc
	global_load_dwordx4 v[138:141], v[114:115], off
	global_load_dwordx4 v[130:133], v[116:117], off
	v_add_co_u32_e32 v114, vcc, 0xa2000, v212
	s_nop 1
	v_addc_co_u32_e32 v115, vcc, 0, v213, vcc
	v_add_co_u32_e32 v116, vcc, 0xa3000, v212
	s_nop 1
	v_addc_co_u32_e32 v117, vcc, 0, v213, vcc
	global_load_dwordx4 v[154:157], v[114:115], off
	global_load_dwordx4 v[146:149], v[116:117], off
	v_mfma_f32_32x32x16_bf16 v[34:49], v[158:161], v[194:197], v[34:49]
	ds_read_b128 v[158:161], v218 offset:33328
	v_mfma_f32_32x32x16_bf16 v[18:33], v[162:165], v[182:185], v[18:33]
	ds_read_b64_tr_b16 v[186:187], v224
	ds_read_b64_tr_b16 v[188:189], v224 offset:2304
	v_mfma_f32_32x32x16_bf16 v[2:17], v[162:165], v[194:197], v[2:17]
	s_waitcnt lgkmcnt(10)
	v_mfma_f32_32x32x16_bf16 v[82:97], v[166:169], v[178:181], v[82:97]
	ds_read_b128 v[162:165], v218 offset:35888
	ds_read_b64_tr_b16 v[194:195], v225 offset:64
	ds_read_b64_tr_b16 v[196:197], v225 offset:2368
	s_waitcnt lgkmcnt(3)
	s_barrier
	v_mfma_f32_32x32x16_bf16 v[66:81], v[166:169], v[190:193], v[66:81]
	ds_read_b128 v[166:169], v218 offset:16
	v_mfma_f32_32x32x16_bf16 v[50:65], v[170:173], v[178:181], v[50:65]
	v_mfma_f32_32x32x16_bf16 v[34:49], v[170:173], v[190:193], v[34:49]
	ds_read_b128 v[170:173], v218 offset:2576
	v_mfma_f32_32x32x16_bf16 v[18:33], v[174:177], v[178:181], v[18:33]
	ds_read_b64_tr_b16 v[182:183], v226 offset:46096
	ds_read_b64_tr_b16 v[184:185], v226 offset:48400
	v_mfma_f32_32x32x16_bf16 v[2:17], v[174:177], v[190:193], v[2:17]
	ds_read_b128 v[174:177], v218 offset:5136
	ds_read_b64_tr_b16 v[190:191], v226 offset:46160
	ds_read_b64_tr_b16 v[192:193], v226 offset:48464
	v_mfma_f32_32x32x16_bf16 v[82:97], v[110:113], v[186:189], v[82:97]
	s_waitcnt vmcnt(9)
	ds_write_b128 v214, v[106:109] offset:15376
	s_and_saveexec_b64 s[12:13], s[4:5]
	ds_write_b128 v215, v[98:101] offset:25616
	s_or_b64 exec, exec, s[12:13]
	s_waitcnt lgkmcnt(9)
	v_mfma_f32_32x32x16_bf16 v[66:81], v[110:113], v[194:197], v[66:81]
	ds_read_b128 v[178:181], v218 offset:48
	s_waitcnt vmcnt(8)
	v_cvt_pk_bf16_f32 v106, v134, v135
	v_cvt_pk_bf16_f32 v107, v136, v137
	s_waitcnt vmcnt(7)
	v_cvt_pk_bf16_f32 v108, v122, v123
	v_cvt_pk_bf16_f32 v109, v124, v125
	ds_write2_b64 v217, v[106:107], v[108:109] offset1:72
	s_waitcnt vmcnt(6)
	v_cvt_pk_bf16_f32 v106, v150, v151
	v_cvt_pk_bf16_f32 v107, v152, v153
	s_waitcnt vmcnt(5)
	v_cvt_pk_bf16_f32 v108, v142, v143
	v_cvt_pk_bf16_f32 v109, v144, v145
	ds_write2_b64 v217, v[106:107], v[108:109] offset0:144 offset1:216
	v_mfma_f32_32x32x16_bf16 v[50:65], v[158:161], v[186:189], v[50:65]
	global_load_dwordx4 v[106:109], v[200:201], off offset:384
	s_and_saveexec_b64 s[12:13], s[4:5]
	s_cbranch_execz .LBB0_2726
	global_load_dwordx4 v[98:101], v[202:203], off offset:384
.LBB0_2726:
	s_or_b64 exec, exec, s[12:13]
	v_add_co_u32_e32 v110, vcc, 0xc0000, v212
	s_nop 1
	v_addc_co_u32_e32 v111, vcc, 0, v213, vcc
	v_add_co_u32_e32 v112, vcc, 0xc1000, v212
	s_nop 1
	v_addc_co_u32_e32 v113, vcc, 0, v213, vcc
	v_add_co_u32_e32 v114, vcc, 0xc2000, v212
	global_load_dwordx4 v[118:121], v[110:111], off
	s_nop 0
	global_load_dwordx4 v[110:113], v[112:113], off
	v_addc_co_u32_e32 v115, vcc, 0, v213, vcc
	v_add_co_u32_e32 v122, vcc, 0xc3000, v212
	s_nop 1
	v_addc_co_u32_e32 v123, vcc, 0, v213, vcc
	global_load_dwordx4 v[114:117], v[114:115], off
	s_nop 0
	global_load_dwordx4 v[122:125], v[122:123], off
	v_mfma_f32_32x32x16_bf16 v[34:49], v[158:161], v[194:197], v[34:49]
	ds_read_b128 v[158:161], v218 offset:2608
	v_mfma_f32_32x32x16_bf16 v[18:33], v[162:165], v[186:189], v[18:33]
	ds_read_b64_tr_b16 v[186:187], v226 offset:55312
	ds_read_b64_tr_b16 v[188:189], v226 offset:57616
	v_mfma_f32_32x32x16_bf16 v[2:17], v[162:165], v[194:197], v[2:17]
	s_waitcnt lgkmcnt(10)
	v_mfma_f32_32x32x16_bf16 v[82:97], v[166:169], v[182:185], v[82:97]
	ds_read_b128 v[162:165], v218 offset:5168
	ds_read_b64_tr_b16 v[194:195], v226 offset:55376
	ds_read_b64_tr_b16 v[196:197], v226 offset:57680
	s_waitcnt lgkmcnt(3)
	s_barrier
	v_mfma_f32_32x32x16_bf16 v[66:81], v[166:169], v[190:193], v[66:81]
	ds_read_b128 v[166:169], v218 offset:15376
	v_mfma_f32_32x32x16_bf16 v[50:65], v[170:173], v[182:185], v[50:65]
	v_mfma_f32_32x32x16_bf16 v[34:49], v[170:173], v[190:193], v[34:49]
	ds_read_b128 v[170:173], v218 offset:17936
	v_mfma_f32_32x32x16_bf16 v[18:33], v[174:177], v[182:185], v[18:33]
	ds_read_b64_tr_b16 v[182:183], v219
	ds_read_b64_tr_b16 v[184:185], v219 offset:2304
	v_mfma_f32_32x32x16_bf16 v[2:17], v[174:177], v[190:193], v[2:17]
	ds_read_b128 v[174:177], v218 offset:20496
	ds_read_b64_tr_b16 v[190:191], v219 offset:64
	ds_read_b64_tr_b16 v[192:193], v219 offset:2368
	v_mfma_f32_32x32x16_bf16 v[82:97], v[178:181], v[186:189], v[82:97]
	s_waitcnt vmcnt(9)
	ds_write_b128 v214, v[126:129] offset:30736
	s_and_saveexec_b64 s[12:13], s[4:5]
	ds_write_b128 v215, v[102:105] offset:40976
	s_or_b64 exec, exec, s[12:13]
	s_waitcnt lgkmcnt(9)
	v_mfma_f32_32x32x16_bf16 v[66:81], v[178:181], v[194:197], v[66:81]
	ds_read_b128 v[150:153], v218 offset:15408
	s_waitcnt vmcnt(8)
	v_cvt_pk_bf16_f32 v126, v138, v139
	v_cvt_pk_bf16_f32 v127, v140, v141
	s_waitcnt vmcnt(7)
	v_cvt_pk_bf16_f32 v128, v130, v131
	v_cvt_pk_bf16_f32 v129, v132, v133
	ds_write2_b64 v222, v[126:127], v[128:129] offset1:72
	s_waitcnt vmcnt(6)
	v_cvt_pk_bf16_f32 v126, v154, v155
	v_cvt_pk_bf16_f32 v127, v156, v157
	s_waitcnt vmcnt(5)
	v_cvt_pk_bf16_f32 v128, v146, v147
	v_cvt_pk_bf16_f32 v129, v148, v149
	ds_write2_b64 v222, v[126:127], v[128:129] offset0:144 offset1:216
	v_mfma_f32_32x32x16_bf16 v[50:65], v[158:161], v[186:189], v[50:65]
	global_load_dwordx4 v[126:129], v[200:201], off offset:448
	s_and_saveexec_b64 s[12:13], s[4:5]
	s_cbranch_execz .LBB0_2730
	global_load_dwordx4 v[102:105], v[202:203], off offset:448
.LBB0_2730:
	s_or_b64 exec, exec, s[12:13]
	v_add_co_u32_e32 v130, vcc, 0xe0000, v212
	s_nop 1
	v_addc_co_u32_e32 v131, vcc, 0, v213, vcc
	v_add_co_u32_e32 v134, vcc, 0xe1000, v212
	s_nop 1
	v_addc_co_u32_e32 v135, vcc, 0, v213, vcc
	v_add_co_u32_e32 v138, vcc, 0xe2000, v212
	global_load_dwordx4 v[130:133], v[130:131], off
	s_nop 0
	global_load_dwordx4 v[134:137], v[134:135], off
	v_addc_co_u32_e32 v139, vcc, 0, v213, vcc
	v_add_co_u32_e32 v142, vcc, 0xe3000, v212
	s_nop 1
	v_addc_co_u32_e32 v143, vcc, 0, v213, vcc
	global_load_dwordx4 v[138:141], v[138:139], off
	s_nop 0
	global_load_dwordx4 v[142:145], v[142:143], off
	v_mfma_f32_32x32x16_bf16 v[34:49], v[158:161], v[194:197], v[34:49]
	ds_read_b128 v[146:149], v218 offset:17968
	v_mfma_f32_32x32x16_bf16 v[18:33], v[162:165], v[186:189], v[18:33]
	ds_read_b64_tr_b16 v[178:179], v220
	ds_read_b64_tr_b16 v[180:181], v220 offset:2304
	v_mfma_f32_32x32x16_bf16 v[2:17], v[162:165], v[194:197], v[2:17]
	s_waitcnt lgkmcnt(10)
	v_mfma_f32_32x32x16_bf16 v[82:97], v[166:169], v[182:185], v[82:97]
	ds_read_b128 v[154:157], v218 offset:20528
	ds_read_b64_tr_b16 v[194:195], v221 offset:64
	ds_read_b64_tr_b16 v[196:197], v221 offset:2368
	s_waitcnt lgkmcnt(3)
	s_barrier
	v_mfma_f32_32x32x16_bf16 v[66:81], v[166:169], v[190:193], v[66:81]
	ds_read_b128 v[158:161], v218 offset:30736
	v_mfma_f32_32x32x16_bf16 v[50:65], v[170:173], v[182:185], v[50:65]
	v_mfma_f32_32x32x16_bf16 v[34:49], v[170:173], v[190:193], v[34:49]
	ds_read_b128 v[162:165], v218 offset:33296
	v_mfma_f32_32x32x16_bf16 v[18:33], v[174:177], v[182:185], v[18:33]
	ds_read_b64_tr_b16 v[182:183], v223
	ds_read_b64_tr_b16 v[184:185], v223 offset:2304
	v_mfma_f32_32x32x16_bf16 v[2:17], v[174:177], v[190:193], v[2:17]
	ds_read_b128 v[166:169], v218 offset:35856
	ds_read_b64_tr_b16 v[186:187], v223 offset:64
	ds_read_b64_tr_b16 v[188:189], v223 offset:2368
	v_mfma_f32_32x32x16_bf16 v[82:97], v[150:153], v[178:181], v[82:97]
	s_waitcnt vmcnt(9)
	ds_write_b128 v214, v[106:109] offset:16
	s_and_saveexec_b64 s[12:13], s[4:5]
	ds_write_b128 v215, v[98:101] offset:10256
	s_or_b64 exec, exec, s[12:13]
	s_waitcnt lgkmcnt(9)
	v_mfma_f32_32x32x16_bf16 v[66:81], v[150:153], v[194:197], v[66:81]
	ds_read_b128 v[170:173], v218 offset:30768
	s_waitcnt vmcnt(8)
	v_cvt_pk_bf16_f32 v150, v118, v119
	v_cvt_pk_bf16_f32 v151, v120, v121
	s_waitcnt vmcnt(7)
	v_cvt_pk_bf16_f32 v152, v110, v111
	v_cvt_pk_bf16_f32 v153, v112, v113
	ds_write2_b64 v198, v[150:151], v[152:153] offset0:130 offset1:202
	s_waitcnt vmcnt(6)
	v_cvt_pk_bf16_f32 v150, v114, v115
	v_cvt_pk_bf16_f32 v151, v116, v117
	s_waitcnt vmcnt(5)
	v_cvt_pk_bf16_f32 v152, v122, v123
	v_cvt_pk_bf16_f32 v153, v124, v125
	ds_write2_b64 v209, v[150:151], v[152:153] offset0:18 offset1:90
	v_mfma_f32_32x32x16_bf16 v[50:65], v[146:149], v[178:181], v[50:65]
	v_mfma_f32_32x32x16_bf16 v[34:49], v[146:149], v[194:197], v[34:49]
	ds_read_b128 v[174:177], v218 offset:33328
	v_mfma_f32_32x32x16_bf16 v[18:33], v[154:157], v[178:181], v[18:33]
	ds_read_b64_tr_b16 v[178:179], v224
	ds_read_b64_tr_b16 v[180:181], v224 offset:2304
	v_mfma_f32_32x32x16_bf16 v[2:17], v[154:157], v[194:197], v[2:17]
	s_waitcnt lgkmcnt(10)
	v_mfma_f32_32x32x16_bf16 v[82:97], v[158:161], v[182:185], v[82:97]
	ds_read_b128 v[190:193], v218 offset:35888
	ds_read_b64_tr_b16 v[194:195], v225 offset:64
	ds_read_b64_tr_b16 v[196:197], v225 offset:2368
	s_waitcnt lgkmcnt(3)
	s_barrier
; __device__ __forceinline__ void moe_unit(const int* pre, const int* lpre, int x, int lb, int& e, int& rb) {
;     if (lb < lpre[32]) {
;         int lo = 0, hi = 32;
;         while (hi - lo > 1) { const int mid = (lo + hi) >> 1; if (lpre[mid] <= lb) lo = mid; else hi = mid; }
;         e = x + 8 * lo; rb = lb - lpre[lo];
;     } else { e = 256; rb = (lb - lpre[32]) * 8 + x; }
	v_mfma_f32_32x32x16_bf16 v[66:81], v[158:161], v[186:189], v[66:81]
	ds_read_b128 v[154:157], v218 offset:16
	v_mfma_f32_32x32x16_bf16 v[50:65], v[162:165], v[182:185], v[50:65]
	v_mfma_f32_32x32x16_bf16 v[34:49], v[162:165], v[186:189], v[34:49]
	ds_read_b128 v[158:161], v218 offset:2576
	v_mfma_f32_32x32x16_bf16 v[18:33], v[166:169], v[182:185], v[18:33]
	ds_read_b64_tr_b16 v[162:163], v226 offset:46096
	ds_read_b64_tr_b16 v[164:165], v226 offset:48400
	v_mfma_f32_32x32x16_bf16 v[2:17], v[166:169], v[186:189], v[2:17]
	ds_read_b128 v[146:149], v218 offset:5136
	ds_read_b64_tr_b16 v[150:151], v226 offset:46160
	ds_read_b64_tr_b16 v[152:153], v226 offset:48464
	v_mfma_f32_32x32x16_bf16 v[82:97], v[170:173], v[178:181], v[82:97]
	s_waitcnt vmcnt(4)
	ds_write_b128 v214, v[126:129] offset:15376
	s_and_saveexec_b64 s[12:13], s[4:5]
	ds_write_b128 v215, v[102:105] offset:25616
	s_or_b64 exec, exec, s[12:13]
	s_waitcnt lgkmcnt(9)
	v_mfma_f32_32x32x16_bf16 v[66:81], v[170:173], v[194:197], v[66:81]
	ds_read_b128 v[166:169], v218 offset:48
	s_waitcnt vmcnt(3)
	v_cvt_pk_bf16_f32 v170, v130, v131
	v_cvt_pk_bf16_f32 v171, v132, v133
	s_waitcnt vmcnt(2)
	v_cvt_pk_bf16_f32 v172, v134, v135
	v_cvt_pk_bf16_f32 v173, v136, v137
	ds_write2_b64 v217, v[170:171], v[172:173] offset1:72
	s_waitcnt vmcnt(1)
	v_cvt_pk_bf16_f32 v170, v138, v139
	v_cvt_pk_bf16_f32 v171, v140, v141
	s_waitcnt vmcnt(0)
	v_cvt_pk_bf16_f32 v172, v142, v143
	v_cvt_pk_bf16_f32 v173, v144, v145
	ds_write2_b64 v217, v[170:171], v[172:173] offset0:144 offset1:216
	v_mfma_f32_32x32x16_bf16 v[50:65], v[174:177], v[178:181], v[50:65]
	v_mfma_f32_32x32x16_bf16 v[34:49], v[174:177], v[194:197], v[34:49]
	ds_read_b128 v[170:173], v218 offset:2608
	v_mfma_f32_32x32x16_bf16 v[18:33], v[190:193], v[178:181], v[18:33]
	ds_read_b64_tr_b16 v[174:175], v226 offset:55312
	ds_read_b64_tr_b16 v[176:177], v226 offset:57616
	v_mfma_f32_32x32x16_bf16 v[2:17], v[190:193], v[194:197], v[2:17]
	s_waitcnt lgkmcnt(10)
	v_mfma_f32_32x32x16_bf16 v[82:97], v[154:157], v[162:165], v[82:97]
	ds_read_b128 v[178:181], v218 offset:5168
	ds_read_b64_tr_b16 v[182:183], v226 offset:55376
	ds_read_b64_tr_b16 v[184:185], v226 offset:57680
	s_waitcnt lgkmcnt(3)
	s_barrier
	v_mfma_f32_32x32x16_bf16 v[66:81], v[154:157], v[150:153], v[66:81]
	ds_read_b128 v[154:157], v218 offset:15376
	v_mfma_f32_32x32x16_bf16 v[50:65], v[158:161], v[162:165], v[50:65]
	v_mfma_f32_32x32x16_bf16 v[34:49], v[158:161], v[150:153], v[34:49]
	ds_read_b128 v[158:161], v218 offset:17936
	v_mfma_f32_32x32x16_bf16 v[18:33], v[146:149], v[162:165], v[18:33]
	ds_read_b64_tr_b16 v[162:163], v219
	ds_read_b64_tr_b16 v[164:165], v219 offset:2304
	v_mfma_f32_32x32x16_bf16 v[2:17], v[146:149], v[150:153], v[2:17]
	ds_read_b128 v[146:149], v218 offset:20496
	ds_read_b64_tr_b16 v[150:151], v219 offset:64
	ds_read_b64_tr_b16 v[152:153], v219 offset:2368
	v_mfma_f32_32x32x16_bf16 v[82:97], v[166:169], v[174:177], v[82:97]
	s_waitcnt lgkmcnt(7)
	v_mfma_f32_32x32x16_bf16 v[66:81], v[166:169], v[182:185], v[66:81]
	ds_read_b128 v[166:169], v218 offset:15408
	v_mfma_f32_32x32x16_bf16 v[50:65], v[170:173], v[174:177], v[50:65]
	v_mfma_f32_32x32x16_bf16 v[34:49], v[170:173], v[182:185], v[34:49]
	ds_read_b128 v[170:173], v218 offset:17968
	v_mfma_f32_32x32x16_bf16 v[18:33], v[178:181], v[174:177], v[18:33]
	ds_read_b64_tr_b16 v[174:175], v220
	ds_read_b64_tr_b16 v[176:177], v220 offset:2304
	v_mfma_f32_32x32x16_bf16 v[2:17], v[178:181], v[182:185], v[2:17]
	s_waitcnt lgkmcnt(7)
	v_mfma_f32_32x32x16_bf16 v[82:97], v[154:157], v[162:165], v[82:97]
	ds_read_b128 v[178:181], v218 offset:20528
	ds_read_b64_tr_b16 v[182:183], v221 offset:64
	ds_read_b64_tr_b16 v[184:185], v221 offset:2368
	s_waitcnt lgkmcnt(3)
	s_barrier
	v_mfma_f32_32x32x16_bf16 v[66:81], v[154:157], v[150:153], v[66:81]
	v_mfma_f32_32x32x16_bf16 v[50:65], v[158:161], v[162:165], v[50:65]
	v_mfma_f32_32x32x16_bf16 v[34:49], v[158:161], v[150:153], v[34:49]
	v_mfma_f32_32x32x16_bf16 v[18:33], v[146:149], v[162:165], v[18:33]
	v_mfma_f32_32x32x16_bf16 v[2:17], v[146:149], v[150:153], v[2:17]
	v_mfma_f32_32x32x16_bf16 v[82:97], v[166:169], v[174:177], v[82:97]
	s_waitcnt lgkmcnt(0)
	v_mfma_f32_32x32x16_bf16 v[66:81], v[166:169], v[182:185], v[66:81]
	v_mfma_f32_32x32x16_bf16 v[50:65], v[170:173], v[174:177], v[50:65]
	v_mfma_f32_32x32x16_bf16 v[34:49], v[170:173], v[182:185], v[34:49]
	v_mfma_f32_32x32x16_bf16 v[18:33], v[178:181], v[174:177], v[18:33]
	v_mfma_f32_32x32x16_bf16 v[2:17], v[178:181], v[182:185], v[2:17]
	s_add_i32 s23, s23, s27
	s_cmp_ge_i32 s23, s24
	s_cselect_b64 s[12:13], -1, 0
	s_and_b64 vcc, exec, s[12:13]
	s_barrier
	s_cbranch_vccnz .LBB0_2755
	v_mov_b32_e32 v106, s31
	ds_read_b32 v106, v106
	s_ashr_i32 s0, s23, 2
	s_waitcnt lgkmcnt(0)
	v_cmp_ge_i32_e32 vcc, s0, v106
	s_cbranch_vccz .LBB0_2737
	v_sub_u32_e32 v106, s0, v106
	v_lshlrev_b32_e32 v106, 3, v106
	v_or_b32_e32 v108, s22, v106
	s_movk_i32 s14, 0x100
	s_cbranch_execz .LBB0_2738
	s_branch .LBB0_2741
